# baseline (speedup 1.0000x reference)
.LE_cdone1:
	s_waitcnt lgkmcnt(0)
	s_barrier
	v_mov_b32_e32 v252, 0x20600
	ds_read_b32 v200, v252
	ds_read_b32 v201, v252 offset:4
	ds_read_b32 v202, v252 offset:8
	s_waitcnt lgkmcnt(0)
	s_nop 1
	v_readfirstlane_b32 s31, v200
	v_readfirstlane_b32 s29, v201
	v_readfirstlane_b32 s30, v202
	s_nop 3
	s_barrier
	s_lshl_b32 s49, s29, 19
	s_lshl_b32 s64, s32, 13
	s_add_u32 s49, s49, s64
	s_mov_b32 s51, s64
	s_add_u32 s52, s51, 0x0
	s_add_u32 s53, s51, 0x1000
	s_add_u32 s54, s51, 0x8000
	s_add_u32 s55, s51, 0x9000
	s_add_u32 s56, s51, 0x10000
	s_add_u32 s57, s51, 0x11000
	s_add_u32 s58, s51, 0x18000
	s_add_u32 s59, s51, 0x19000
	s_lshl_b32 s64, s29, 8
	s_lshl_b32 s65, s30, 1
	s_add_u32 s64, s64, s65
	s_lshr_b32 s65, s32, 1
	s_add_u32 s64, s64, s65
	s_lshl_b32 s64, s64, 11
	s_and_b32 s65, s32, 1
	s_lshl_b32 s65, s65, 9
	s_add_u32 s50, s64, s65
	s_sub_u32 s60, s28, 1
	s_lshl_b32 s64, s30, 2
	s_add_u32 s64, s64, s32
	s_lshl_b32 s64, s64, 16
	s_add_u32 s44, s4, s64
	s_addc_u32 s45, s5, 0
	global_load_dwordx4 a[0:3], v192, s[44:45] offset:0
	global_load_dwordx4 a[4:7], v192, s[44:45] offset:1024
	global_load_dwordx4 a[8:11], v192, s[44:45] offset:2048
	global_load_dwordx4 a[12:15], v192, s[44:45] offset:3072
	s_add_u32 s44, s44, 0x1000
	s_addc_u32 s45, s45, 0
	global_load_dwordx4 a[16:19], v192, s[44:45] offset:0
	global_load_dwordx4 a[20:23], v192, s[44:45] offset:1024
	global_load_dwordx4 a[24:27], v192, s[44:45] offset:2048
	global_load_dwordx4 a[28:31], v192, s[44:45] offset:3072
	s_add_u32 s44, s44, 0x1000
	s_addc_u32 s45, s45, 0
	global_load_dwordx4 a[32:35], v192, s[44:45] offset:0
	global_load_dwordx4 a[36:39], v192, s[44:45] offset:1024
	global_load_dwordx4 a[40:43], v192, s[44:45] offset:2048
	global_load_dwordx4 a[44:47], v192, s[44:45] offset:3072
	s_add_u32 s44, s44, 0x1000
	s_addc_u32 s45, s45, 0
	global_load_dwordx4 a[48:51], v192, s[44:45] offset:0
	global_load_dwordx4 a[52:55], v192, s[44:45] offset:1024
	global_load_dwordx4 a[56:59], v192, s[44:45] offset:2048
	global_load_dwordx4 a[60:63], v192, s[44:45] offset:3072
	s_add_u32 s44, s44, 0x1000
	s_addc_u32 s45, s45, 0
	global_load_dwordx4 a[64:67], v192, s[44:45] offset:0
	global_load_dwordx4 a[68:71], v192, s[44:45] offset:1024
	global_load_dwordx4 a[72:75], v192, s[44:45] offset:2048
	global_load_dwordx4 a[76:79], v192, s[44:45] offset:3072
	s_add_u32 s44, s44, 0x1000
	s_addc_u32 s45, s45, 0
	global_load_dwordx4 a[80:83], v192, s[44:45] offset:0
	global_load_dwordx4 a[84:87], v192, s[44:45] offset:1024
	global_load_dwordx4 a[88:91], v192, s[44:45] offset:2048
	global_load_dwordx4 a[92:95], v192, s[44:45] offset:3072
	s_add_u32 s44, s44, 0x1000
	s_addc_u32 s45, s45, 0
	global_load_dwordx4 a[96:99], v192, s[44:45] offset:0
	global_load_dwordx4 a[100:103], v192, s[44:45] offset:1024
	global_load_dwordx4 a[104:107], v192, s[44:45] offset:2048
	global_load_dwordx4 a[108:111], v192, s[44:45] offset:3072
	s_add_u32 s44, s44, 0x1000
	s_addc_u32 s45, s45, 0
	global_load_dwordx4 a[112:115], v192, s[44:45] offset:0
	global_load_dwordx4 a[116:119], v192, s[44:45] offset:1024
	global_load_dwordx4 a[120:123], v192, s[44:45] offset:2048
	global_load_dwordx4 a[124:127], v192, s[44:45] offset:3072
	s_add_u32 s44, s44, 0x1000
	s_addc_u32 s45, s45, 0
	s_waitcnt vmcnt(16)
	global_load_dwordx4 a[128:131], v192, s[44:45] offset:0
	global_load_dwordx4 a[132:135], v192, s[44:45] offset:1024
	global_load_dwordx4 a[136:139], v192, s[44:45] offset:2048
	global_load_dwordx4 a[140:143], v192, s[44:45] offset:3072
	s_add_u32 s44, s44, 0x1000
	s_addc_u32 s45, s45, 0
	global_load_dwordx4 a[144:147], v192, s[44:45] offset:0
	global_load_dwordx4 a[148:151], v192, s[44:45] offset:1024
	global_load_dwordx4 a[152:155], v192, s[44:45] offset:2048
	global_load_dwordx4 a[156:159], v192, s[44:45] offset:3072
	s_add_u32 s44, s44, 0x1000
	s_addc_u32 s45, s45, 0
	global_load_dwordx4 a[160:163], v192, s[44:45] offset:0
	global_load_dwordx4 a[164:167], v192, s[44:45] offset:1024
	global_load_dwordx4 a[168:171], v192, s[44:45] offset:2048
	global_load_dwordx4 a[172:175], v192, s[44:45] offset:3072
	s_add_u32 s44, s44, 0x1000
	s_addc_u32 s45, s45, 0
	global_load_dwordx4 a[176:179], v192, s[44:45] offset:0
	global_load_dwordx4 a[180:183], v192, s[44:45] offset:1024
	global_load_dwordx4 a[184:187], v192, s[44:45] offset:2048
	global_load_dwordx4 a[188:191], v192, s[44:45] offset:3072
	s_add_u32 s44, s44, 0x1000
	s_addc_u32 s45, s45, 0
	global_load_dwordx4 a[192:195], v192, s[44:45] offset:0
	global_load_dwordx4 a[196:199], v192, s[44:45] offset:1024
	global_load_dwordx4 a[200:203], v192, s[44:45] offset:2048
	global_load_dwordx4 a[204:207], v192, s[44:45] offset:3072
	s_add_u32 s44, s44, 0x1000
	s_addc_u32 s45, s45, 0
	global_load_dwordx4 a[208:211], v192, s[44:45] offset:0
	global_load_dwordx4 a[212:215], v192, s[44:45] offset:1024
	global_load_dwordx4 a[216:219], v192, s[44:45] offset:2048
	global_load_dwordx4 a[220:223], v192, s[44:45] offset:3072
	s_add_u32 s44, s44, 0x1000
	s_addc_u32 s45, s45, 0
	global_load_dwordx4 a[224:227], v192, s[44:45] offset:0
	global_load_dwordx4 a[228:231], v192, s[44:45] offset:1024
	global_load_dwordx4 a[232:235], v192, s[44:45] offset:2048
	global_load_dwordx4 a[236:239], v192, s[44:45] offset:3072
	s_add_u32 s44, s44, 0x1000
	s_addc_u32 s45, s45, 0
	global_load_dwordx4 a[240:243], v192, s[44:45] offset:0
	global_load_dwordx4 a[244:247], v192, s[44:45] offset:1024
	global_load_dwordx4 a[248:251], v192, s[44:45] offset:2048
	global_load_dwordx4 a[252:255], v192, s[44:45] offset:3072
	s_add_u32 s44, s44, 0x1000
	s_addc_u32 s45, s45, 0
	v_mov_b32_e32 v128, 0
	v_mov_b32_e32 v129, 0
	v_mov_b32_e32 v130, 0
	v_mov_b32_e32 v131, 0
	v_mov_b32_e32 v132, 0
	v_mov_b32_e32 v133, 0
	v_mov_b32_e32 v134, 0
	v_mov_b32_e32 v135, 0
	v_mov_b32_e32 v136, 0
	v_mov_b32_e32 v137, 0
	v_mov_b32_e32 v138, 0
	v_mov_b32_e32 v139, 0
	v_mov_b32_e32 v140, 0
	v_mov_b32_e32 v141, 0
	v_mov_b32_e32 v142, 0
	v_mov_b32_e32 v143, 0
	v_mov_b32_e32 v144, 0
	v_mov_b32_e32 v145, 0
	v_mov_b32_e32 v146, 0
	v_mov_b32_e32 v147, 0
	v_mov_b32_e32 v148, 0
	v_mov_b32_e32 v149, 0
	v_mov_b32_e32 v150, 0
	v_mov_b32_e32 v151, 0
	v_mov_b32_e32 v152, 0
	v_mov_b32_e32 v153, 0
	v_mov_b32_e32 v154, 0
	v_mov_b32_e32 v155, 0
	v_mov_b32_e32 v156, 0
	v_mov_b32_e32 v157, 0
	v_mov_b32_e32 v158, 0
	v_mov_b32_e32 v159, 0
	s_lshl_b32 s64, s30, 5
	s_lshl_b32 s65, s32, 3
	s_add_u32 s64, s64, s65
	v_lshlrev_b32_e32 v255, 2, v254
	v_add_u32_e32 v255, s64, v255
	v_lshl_add_u32 v248, s32, 1, v254
	v_mul_u32_u24_e32 v248, 192, v248
	v_add_u32_e32 v248, 0x20000, v248
	v_lshlrev_b32_e32 v249, 3, v253
	v_lshlrev_b32_e32 v250, 12, v253
	v_lshl_add_u32 v250, v254, 4, v250
	v_lshlrev_b32_e32 v200, 3, v255
	v_lshlrev_b32_e32 v201, 2, v255
	v_add_u32_e32 v202, 0x0, v200
	v_add_u32_e32 v203, 0x0, v201
	global_load_dwordx4 v[204:207], v202, s[14:15]
	global_load_dwordx4 v[208:211], v202, s[14:15] offset:16
	global_load_dwordx4 v[212:215], v203, s[16:17]
	s_waitcnt vmcnt(0)
	s_mov_b32 s65, 0xbfb8aa3b
	v_mul_f32_e32 v204, s65, v204
	v_mul_f32_e32 v205, s65, v205
	v_mul_f32_e32 v206, s65, v206
	v_mul_f32_e32 v207, s65, v207
	v_mul_f32_e32 v208, s65, v208
	v_mul_f32_e32 v209, s65, v209
	v_mul_f32_e32 v210, s65, v210
	v_mul_f32_e32 v211, s65, v211
	v_mul_f32_e32 v212, s65, v212
	v_mul_f32_e32 v213, s65, v213
	v_mul_f32_e32 v214, s65, v214
	v_mul_f32_e32 v215, s65, v215
	ds_write_b128 v248, v[204:207] offset:0
	ds_write_b128 v248, v[208:211] offset:16
	ds_write_b128 v248, v[212:215] offset:32
	s_waitcnt lgkmcnt(0)
	v_add_u32_e32 v202, 0x2000, v200
	v_add_u32_e32 v203, 0x1000, v201
	global_load_dwordx4 v[204:207], v202, s[14:15]
	global_load_dwordx4 v[208:211], v202, s[14:15] offset:16
	global_load_dwordx4 v[212:215], v203, s[16:17]
	s_waitcnt vmcnt(0)
	s_mov_b32 s65, 0xbfb8aa3b
	v_mul_f32_e32 v204, s65, v204
	v_mul_f32_e32 v205, s65, v205
	v_mul_f32_e32 v206, s65, v206
	v_mul_f32_e32 v207, s65, v207
	v_mul_f32_e32 v208, s65, v208
	v_mul_f32_e32 v209, s65, v209
	v_mul_f32_e32 v210, s65, v210
	v_mul_f32_e32 v211, s65, v211
	v_mul_f32_e32 v212, s65, v212
	v_mul_f32_e32 v213, s65, v213
	v_mul_f32_e32 v214, s65, v214
	v_mul_f32_e32 v215, s65, v215
	ds_write_b128 v248, v[204:207] offset:48
	ds_write_b128 v248, v[208:211] offset:64
	ds_write_b128 v248, v[212:215] offset:80
	s_waitcnt lgkmcnt(0)
	v_add_u32_e32 v202, 0x4000, v200
	v_add_u32_e32 v203, 0x2000, v201
	global_load_dwordx4 v[204:207], v202, s[14:15]
	global_load_dwordx4 v[208:211], v202, s[14:15] offset:16
	global_load_dwordx4 v[212:215], v203, s[16:17]
	s_waitcnt vmcnt(0)
	s_mov_b32 s65, 0xc038aa3b
	v_mul_f32_e32 v204, s65, v204
	v_mul_f32_e32 v205, s65, v205
	v_mul_f32_e32 v206, s65, v206
	v_mul_f32_e32 v207, s65, v207
	v_mul_f32_e32 v208, s65, v208
	v_mul_f32_e32 v209, s65, v209
	v_mul_f32_e32 v210, s65, v210
	v_mul_f32_e32 v211, s65, v211
	v_mul_f32_e32 v212, s65, v212
	v_mul_f32_e32 v213, s65, v213
	v_mul_f32_e32 v214, s65, v214
	v_mul_f32_e32 v215, s65, v215
	ds_write_b128 v248, v[204:207] offset:96
	ds_write_b128 v248, v[208:211] offset:112
	ds_write_b128 v248, v[212:215] offset:128
	s_waitcnt lgkmcnt(0)
	v_add_u32_e32 v202, 0x6000, v200
	v_add_u32_e32 v203, 0x3000, v201
	global_load_dwordx4 v[204:207], v202, s[14:15]
	global_load_dwordx4 v[208:211], v202, s[14:15] offset:16
	global_load_dwordx4 v[212:215], v203, s[16:17]
	s_waitcnt vmcnt(0)
	s_mov_b32 s65, 0xbfb8aa3b
	v_mul_f32_e32 v204, s65, v204
	v_mul_f32_e32 v205, s65, v205
	v_mul_f32_e32 v206, s65, v206
	v_mul_f32_e32 v207, s65, v207
	v_mul_f32_e32 v208, s65, v208
	v_mul_f32_e32 v209, s65, v209
	v_mul_f32_e32 v210, s65, v210
	v_mul_f32_e32 v211, s65, v211
	v_mul_f32_e32 v212, s65, v212
	v_mul_f32_e32 v213, s65, v213
	v_mul_f32_e32 v214, s65, v214
	v_mul_f32_e32 v215, s65, v215
	ds_write_b128 v248, v[204:207] offset:144
	ds_write_b128 v248, v[208:211] offset:160
	ds_write_b128 v248, v[212:215] offset:176
	s_waitcnt lgkmcnt(0)
	s_lshl_b32 s65, s29, 20
	s_lshl_b32 s66, s64, 2
	s_add_u32 s65, s65, s66
	s_add_u32 s62, s26, s65
	s_addc_u32 s63, s27, 0
	s_waitcnt vmcnt(0)
	s_mov_b32 s33, 0
	s_lshl_b32 s64, s33, 11
	s_lshl_b32 s65, s29, 8
	s_add_u32 s64, s64, s65
	s_lshl_b32 s64, s64, 3
	s_add_u32 s42, s12, s64
	s_addc_u32 s43, s13, 0
	global_load_dwordx2 v[228:229], v249, s[42:43] offset:0
	global_load_dwordx2 v[230:231], v249, s[42:43] offset:256
	ds_read_b128 v[236:239], v248 offset:0
	ds_read_b128 v[240:243], v248 offset:16
	ds_read_b128 v[244:247], v248 offset:32
	ds_read_b128 v[200:203], v248 offset:48
	ds_read_b128 v[204:207], v248 offset:64
	ds_read_b128 v[208:211], v248 offset:80
	s_waitcnt lgkmcnt(3)
	s_waitcnt vmcnt(0)
	v_fma_f32 v0, v229, v237, v244
	v_fma_f32 v1, v229, v239, v245
	v_fma_f32 v2, v229, v241, v246
	v_fma_f32 v3, v229, v243, v247
	v_fmac_f32_e32 v0, v228, v236
	v_fmac_f32_e32 v1, v228, v238
	v_fmac_f32_e32 v2, v228, v240
	v_fmac_f32_e32 v3, v228, v242
	v_fma_f32 v16, v231, v237, v244
	v_fma_f32 v17, v231, v239, v245
	v_fma_f32 v18, v231, v241, v246
	v_fma_f32 v19, v231, v243, v247
	v_fmac_f32_e32 v16, v230, v236
	v_fmac_f32_e32 v17, v230, v238
	v_fmac_f32_e32 v18, v230, v240
	v_fmac_f32_e32 v19, v230, v242
	ds_read_b128 v[236:239], v248 offset:96
	ds_read_b128 v[240:243], v248 offset:112
	ds_read_b128 v[244:247], v248 offset:128
	s_waitcnt lgkmcnt(3)
	v_fma_f32 v4, v229, v201, v208
	v_fma_f32 v5, v229, v203, v209
	v_fma_f32 v6, v229, v205, v210
	v_fma_f32 v7, v229, v207, v211
	v_fmac_f32_e32 v4, v228, v200
	v_fmac_f32_e32 v5, v228, v202
	v_fmac_f32_e32 v6, v228, v204
	v_fmac_f32_e32 v7, v228, v206
	v_fma_f32 v20, v231, v201, v208
	v_fma_f32 v21, v231, v203, v209
	v_fma_f32 v22, v231, v205, v210
	v_fma_f32 v23, v231, v207, v211
	v_fmac_f32_e32 v20, v230, v200
	v_fmac_f32_e32 v21, v230, v202
	v_fmac_f32_e32 v22, v230, v204
	v_fmac_f32_e32 v23, v230, v206
	ds_read_b128 v[200:203], v248 offset:144
	ds_read_b128 v[204:207], v248 offset:160
	ds_read_b128 v[208:211], v248 offset:176
	s_waitcnt lgkmcnt(3)
	v_fma_f32 v8, v229, v237, v244
	v_fma_f32 v9, v229, v239, v245
	v_fma_f32 v10, v229, v241, v246
	v_fma_f32 v11, v229, v243, v247
	v_fmac_f32_e32 v8, v228, v236
	v_fmac_f32_e32 v9, v228, v238
	v_fmac_f32_e32 v10, v228, v240
	v_fmac_f32_e32 v11, v228, v242
	v_fma_f32 v24, v231, v237, v244
	v_fma_f32 v25, v231, v239, v245
	v_fma_f32 v26, v231, v241, v246
	v_fma_f32 v27, v231, v243, v247
	v_fmac_f32_e32 v24, v230, v236
	v_fmac_f32_e32 v25, v230, v238
	v_fmac_f32_e32 v26, v230, v240
	v_fmac_f32_e32 v27, v230, v242
	s_waitcnt lgkmcnt(0)
	v_fma_f32 v12, v229, v201, v208
	v_fma_f32 v13, v229, v203, v209
	v_fma_f32 v14, v229, v205, v210
	v_fma_f32 v15, v229, v207, v211
	v_fmac_f32_e32 v12, v228, v200
	v_fmac_f32_e32 v13, v228, v202
	v_fmac_f32_e32 v14, v228, v204
	v_fmac_f32_e32 v15, v228, v206
	v_fma_f32 v28, v231, v201, v208
	v_fma_f32 v29, v231, v203, v209
	v_fma_f32 v30, v231, v205, v210
	v_fma_f32 v31, v231, v207, v211
	v_fmac_f32_e32 v28, v230, v200
	v_fmac_f32_e32 v29, v230, v202
	v_fmac_f32_e32 v30, v230, v204
	v_fmac_f32_e32 v31, v230, v206
	s_lshl_b32 s64, s33, 11
	s_lshl_b32 s65, s29, 8
	s_add_u32 s64, s64, s65
	s_add_u32 s64, s64, 64
	s_lshl_b32 s64, s64, 3
	s_add_u32 s42, s12, s64
	s_addc_u32 s43, s13, 0
	global_load_dwordx2 v[228:229], v249, s[42:43] offset:0
	global_load_dwordx2 v[230:231], v249, s[42:43] offset:256
	ds_read_b128 v[236:239], v248 offset:0
	ds_read_b128 v[240:243], v248 offset:16
	ds_read_b128 v[244:247], v248 offset:32
	ds_read_b128 v[200:203], v248 offset:48
	ds_read_b128 v[204:207], v248 offset:64
	ds_read_b128 v[208:211], v248 offset:80
	s_waitcnt lgkmcnt(3)
	s_waitcnt vmcnt(0)
	v_fma_f32 v32, v229, v237, v244
	v_fma_f32 v33, v229, v239, v245
	v_fma_f32 v34, v229, v241, v246
	v_fma_f32 v35, v229, v243, v247
	v_fmac_f32_e32 v32, v228, v236
	v_fmac_f32_e32 v33, v228, v238
	v_fmac_f32_e32 v34, v228, v240
	v_fmac_f32_e32 v35, v228, v242
	v_fma_f32 v48, v231, v237, v244
	v_fma_f32 v49, v231, v239, v245
	v_fma_f32 v50, v231, v241, v246
	v_fma_f32 v51, v231, v243, v247
	v_fmac_f32_e32 v48, v230, v236
	v_fmac_f32_e32 v49, v230, v238
	v_fmac_f32_e32 v50, v230, v240
	v_fmac_f32_e32 v51, v230, v242
	ds_read_b128 v[236:239], v248 offset:96
	ds_read_b128 v[240:243], v248 offset:112
	ds_read_b128 v[244:247], v248 offset:128
	s_waitcnt lgkmcnt(3)
	v_fma_f32 v36, v229, v201, v208
	v_fma_f32 v37, v229, v203, v209
	v_fma_f32 v38, v229, v205, v210
	v_fma_f32 v39, v229, v207, v211
	v_fmac_f32_e32 v36, v228, v200
	v_fmac_f32_e32 v37, v228, v202
	v_fmac_f32_e32 v38, v228, v204
	v_fmac_f32_e32 v39, v228, v206
	v_fma_f32 v52, v231, v201, v208
	v_fma_f32 v53, v231, v203, v209
	v_fma_f32 v54, v231, v205, v210
	v_fma_f32 v55, v231, v207, v211
	v_fmac_f32_e32 v52, v230, v200
	v_fmac_f32_e32 v53, v230, v202
	v_fmac_f32_e32 v54, v230, v204
	v_fmac_f32_e32 v55, v230, v206
	ds_read_b128 v[200:203], v248 offset:144
	ds_read_b128 v[204:207], v248 offset:160
	ds_read_b128 v[208:211], v248 offset:176
	s_waitcnt lgkmcnt(3)
	v_fma_f32 v40, v229, v237, v244
	v_fma_f32 v41, v229, v239, v245
	v_fma_f32 v42, v229, v241, v246
	v_fma_f32 v43, v229, v243, v247
	v_fmac_f32_e32 v40, v228, v236
	v_fmac_f32_e32 v41, v228, v238
	v_fmac_f32_e32 v42, v228, v240
	v_fmac_f32_e32 v43, v228, v242
	v_fma_f32 v56, v231, v237, v244
	v_fma_f32 v57, v231, v239, v245
	v_fma_f32 v58, v231, v241, v246
	v_fma_f32 v59, v231, v243, v247
	v_fmac_f32_e32 v56, v230, v236
	v_fmac_f32_e32 v57, v230, v238
	v_fmac_f32_e32 v58, v230, v240
	v_fmac_f32_e32 v59, v230, v242
	s_waitcnt lgkmcnt(0)
	v_fma_f32 v44, v229, v201, v208
	v_fma_f32 v45, v229, v203, v209
	v_fma_f32 v46, v229, v205, v210
	v_fma_f32 v47, v229, v207, v211
	v_fmac_f32_e32 v44, v228, v200
	v_fmac_f32_e32 v45, v228, v202
	v_fmac_f32_e32 v46, v228, v204
	v_fmac_f32_e32 v47, v228, v206
	v_fma_f32 v60, v231, v201, v208
	v_fma_f32 v61, v231, v203, v209
	v_fma_f32 v62, v231, v205, v210
	v_fma_f32 v63, v231, v207, v211
	v_fmac_f32_e32 v60, v230, v200
	v_fmac_f32_e32 v61, v230, v202
	v_fmac_f32_e32 v62, v230, v204
	v_fmac_f32_e32 v63, v230, v206
	s_lshl_b32 s64, s33, 11
	s_lshl_b32 s65, s29, 8
	s_add_u32 s64, s64, s65
	s_add_u32 s64, s64, 128
	s_lshl_b32 s64, s64, 3
	s_add_u32 s42, s12, s64
	s_addc_u32 s43, s13, 0
	global_load_dwordx2 v[228:229], v249, s[42:43] offset:0
	global_load_dwordx2 v[230:231], v249, s[42:43] offset:256
	ds_read_b128 v[236:239], v248 offset:0
	ds_read_b128 v[240:243], v248 offset:16
	ds_read_b128 v[244:247], v248 offset:32
	ds_read_b128 v[200:203], v248 offset:48
	ds_read_b128 v[204:207], v248 offset:64
	ds_read_b128 v[208:211], v248 offset:80
	s_waitcnt lgkmcnt(3)
	s_waitcnt vmcnt(0)
	v_fma_f32 v64, v229, v237, v244
	v_fma_f32 v65, v229, v239, v245
	v_fma_f32 v66, v229, v241, v246
	v_fma_f32 v67, v229, v243, v247
	v_fmac_f32_e32 v64, v228, v236
	v_fmac_f32_e32 v65, v228, v238
	v_fmac_f32_e32 v66, v228, v240
	v_fmac_f32_e32 v67, v228, v242
	v_fma_f32 v80, v231, v237, v244
	v_fma_f32 v81, v231, v239, v245
	v_fma_f32 v82, v231, v241, v246
	v_fma_f32 v83, v231, v243, v247
	v_fmac_f32_e32 v80, v230, v236
	v_fmac_f32_e32 v81, v230, v238
	v_fmac_f32_e32 v82, v230, v240
	v_fmac_f32_e32 v83, v230, v242
	ds_read_b128 v[236:239], v248 offset:96
	ds_read_b128 v[240:243], v248 offset:112
	ds_read_b128 v[244:247], v248 offset:128
	s_waitcnt lgkmcnt(3)
	v_fma_f32 v68, v229, v201, v208
	v_fma_f32 v69, v229, v203, v209
	v_fma_f32 v70, v229, v205, v210
	v_fma_f32 v71, v229, v207, v211
	v_fmac_f32_e32 v68, v228, v200
	v_fmac_f32_e32 v69, v228, v202
	v_fmac_f32_e32 v70, v228, v204
	v_fmac_f32_e32 v71, v228, v206
	v_fma_f32 v84, v231, v201, v208
	v_fma_f32 v85, v231, v203, v209
	v_fma_f32 v86, v231, v205, v210
	v_fma_f32 v87, v231, v207, v211
	v_fmac_f32_e32 v84, v230, v200
	v_fmac_f32_e32 v85, v230, v202
	v_fmac_f32_e32 v86, v230, v204
	v_fmac_f32_e32 v87, v230, v206
	ds_read_b128 v[200:203], v248 offset:144
	ds_read_b128 v[204:207], v248 offset:160
	ds_read_b128 v[208:211], v248 offset:176
	s_waitcnt lgkmcnt(3)
	v_fma_f32 v72, v229, v237, v244
	v_fma_f32 v73, v229, v239, v245
	v_fma_f32 v74, v229, v241, v246
	v_fma_f32 v75, v229, v243, v247
	v_fmac_f32_e32 v72, v228, v236
	v_fmac_f32_e32 v73, v228, v238
	v_fmac_f32_e32 v74, v228, v240
	v_fmac_f32_e32 v75, v228, v242
	v_fma_f32 v88, v231, v237, v244
	v_fma_f32 v89, v231, v239, v245
	v_fma_f32 v90, v231, v241, v246
	v_fma_f32 v91, v231, v243, v247
	v_fmac_f32_e32 v88, v230, v236
	v_fmac_f32_e32 v89, v230, v238
	v_fmac_f32_e32 v90, v230, v240
	v_fmac_f32_e32 v91, v230, v242
	s_waitcnt lgkmcnt(0)
	v_fma_f32 v76, v229, v201, v208
	v_fma_f32 v77, v229, v203, v209
	v_fma_f32 v78, v229, v205, v210
	v_fma_f32 v79, v229, v207, v211
	v_fmac_f32_e32 v76, v228, v200
	v_fmac_f32_e32 v77, v228, v202
	v_fmac_f32_e32 v78, v228, v204
	v_fmac_f32_e32 v79, v228, v206
	v_fma_f32 v92, v231, v201, v208
	v_fma_f32 v93, v231, v203, v209
	v_fma_f32 v94, v231, v205, v210
	v_fma_f32 v95, v231, v207, v211
	v_fmac_f32_e32 v92, v230, v200
	v_fmac_f32_e32 v93, v230, v202
	v_fmac_f32_e32 v94, v230, v204
	v_fmac_f32_e32 v95, v230, v206
	s_lshl_b32 s64, s33, 11
	s_lshl_b32 s65, s29, 8
	s_add_u32 s64, s64, s65
	s_add_u32 s64, s64, 192
	s_lshl_b32 s64, s64, 3
	s_add_u32 s42, s12, s64
	s_addc_u32 s43, s13, 0
	global_load_dwordx2 v[228:229], v249, s[42:43] offset:0
	global_load_dwordx2 v[230:231], v249, s[42:43] offset:256
	ds_read_b128 v[236:239], v248 offset:0
	ds_read_b128 v[240:243], v248 offset:16
	ds_read_b128 v[244:247], v248 offset:32
	ds_read_b128 v[200:203], v248 offset:48
	ds_read_b128 v[204:207], v248 offset:64
	ds_read_b128 v[208:211], v248 offset:80
	s_waitcnt lgkmcnt(3)
	s_waitcnt vmcnt(0)
	v_fma_f32 v96, v229, v237, v244
	v_fma_f32 v97, v229, v239, v245
	v_fma_f32 v98, v229, v241, v246
	v_fma_f32 v99, v229, v243, v247
	v_fmac_f32_e32 v96, v228, v236
	v_fmac_f32_e32 v97, v228, v238
	v_fmac_f32_e32 v98, v228, v240
	v_fmac_f32_e32 v99, v228, v242
	v_fma_f32 v112, v231, v237, v244
	v_fma_f32 v113, v231, v239, v245
	v_fma_f32 v114, v231, v241, v246
	v_fma_f32 v115, v231, v243, v247
	v_fmac_f32_e32 v112, v230, v236
	v_fmac_f32_e32 v113, v230, v238
	v_fmac_f32_e32 v114, v230, v240
	v_fmac_f32_e32 v115, v230, v242
	ds_read_b128 v[236:239], v248 offset:96
	ds_read_b128 v[240:243], v248 offset:112
	ds_read_b128 v[244:247], v248 offset:128
	s_waitcnt lgkmcnt(3)
	v_fma_f32 v100, v229, v201, v208
	v_fma_f32 v101, v229, v203, v209
	v_fma_f32 v102, v229, v205, v210
	v_fma_f32 v103, v229, v207, v211
	v_fmac_f32_e32 v100, v228, v200
	v_fmac_f32_e32 v101, v228, v202
	v_fmac_f32_e32 v102, v228, v204
	v_fmac_f32_e32 v103, v228, v206
	v_fma_f32 v116, v231, v201, v208
	v_fma_f32 v117, v231, v203, v209
	v_fma_f32 v118, v231, v205, v210
	v_fma_f32 v119, v231, v207, v211
	v_fmac_f32_e32 v116, v230, v200
	v_fmac_f32_e32 v117, v230, v202
	v_fmac_f32_e32 v118, v230, v204
	v_fmac_f32_e32 v119, v230, v206
	ds_read_b128 v[200:203], v248 offset:144
	ds_read_b128 v[204:207], v248 offset:160
	ds_read_b128 v[208:211], v248 offset:176
	s_waitcnt lgkmcnt(3)
	v_fma_f32 v104, v229, v237, v244
	v_fma_f32 v105, v229, v239, v245
	v_fma_f32 v106, v229, v241, v246
	v_fma_f32 v107, v229, v243, v247
	v_fmac_f32_e32 v104, v228, v236
	v_fmac_f32_e32 v105, v228, v238
	v_fmac_f32_e32 v106, v228, v240
	v_fmac_f32_e32 v107, v228, v242
	v_fma_f32 v120, v231, v237, v244
	v_fma_f32 v121, v231, v239, v245
	v_fma_f32 v122, v231, v241, v246
	v_fma_f32 v123, v231, v243, v247
	v_fmac_f32_e32 v120, v230, v236
	v_fmac_f32_e32 v121, v230, v238
	v_fmac_f32_e32 v122, v230, v240
	v_fmac_f32_e32 v123, v230, v242
	s_waitcnt lgkmcnt(0)
	v_fma_f32 v108, v229, v201, v208
	v_fma_f32 v109, v229, v203, v209
	v_fma_f32 v110, v229, v205, v210
	v_fma_f32 v111, v229, v207, v211
	v_fmac_f32_e32 v108, v228, v200
	v_fmac_f32_e32 v109, v228, v202
	v_fmac_f32_e32 v110, v228, v204
	v_fmac_f32_e32 v111, v228, v206
	v_fma_f32 v124, v231, v201, v208
	v_fma_f32 v125, v231, v203, v209
	v_fma_f32 v126, v231, v205, v210
	v_fma_f32 v127, v231, v207, v211
	v_fmac_f32_e32 v124, v230, v200
	v_fmac_f32_e32 v125, v230, v202
	v_fmac_f32_e32 v126, v230, v204
	v_fmac_f32_e32 v127, v230, v206
	s_waitcnt vmcnt(0)
	s_waitcnt lgkmcnt(0)
	s_lshl_b32 s64, s33, 3
	s_add_u32 s64, s64, s29
	s_lshl_b32 s64, s64, 5
	s_add_u32 s64, s64, s30
	s_lshl_b32 s64, s64, 2
	s_add_u32 s40, s8, s64
	s_addc_u32 s41, s9, 0
	s_and_b32 s64, s33, 1
	s_lshl_b32 s64, s64, 22
	s_add_u32 s64, s64, s50
	s_add_u32 s36, s6, s64
	s_addc_u32 s37, s7, 0
	v_exp_f32_e32 v200, v0
	v_exp_f32_e32 v201, v1
	v_exp_f32_e32 v202, v2
	v_exp_f32_e32 v203, v3
	v_exp_f32_e32 v204, v4
	v_exp_f32_e32 v205, v5
	v_exp_f32_e32 v206, v6
	v_exp_f32_e32 v207, v7
	v_exp_f32_e32 v208, v8
	v_exp_f32_e32 v209, v9
	v_exp_f32_e32 v210, v10
	v_exp_f32_e32 v211, v11
	v_exp_f32_e32 v212, v12
	v_exp_f32_e32 v213, v13
	v_exp_f32_e32 v214, v14
	v_exp_f32_e32 v215, v15
	v_add_f32_e32 v200, 1.0, v200
	v_add_f32_e32 v201, 1.0, v201
	v_add_f32_e32 v202, 1.0, v202
	v_add_f32_e32 v203, 1.0, v203
	v_add_f32_e32 v204, 1.0, v204
	v_add_f32_e32 v205, 1.0, v205
	v_add_f32_e32 v206, 1.0, v206
	v_add_f32_e32 v207, 1.0, v207
	v_add_f32_e32 v208, 1.0, v208
	v_add_f32_e32 v209, 1.0, v209
	v_add_f32_e32 v210, 1.0, v210
	v_add_f32_e32 v211, 1.0, v211
	v_add_f32_e32 v212, 1.0, v212
	v_add_f32_e32 v213, 1.0, v213
	v_add_f32_e32 v214, 1.0, v214
	v_add_f32_e32 v215, 1.0, v215
	v_rcp_f32_e32 v200, v200
	v_rcp_f32_e32 v201, v201
	v_rcp_f32_e32 v202, v202
	v_rcp_f32_e32 v203, v203
	v_rcp_f32_e32 v204, v204
	v_rcp_f32_e32 v205, v205
	v_rcp_f32_e32 v206, v206
	v_rcp_f32_e32 v207, v207
	v_rcp_f32_e32 v208, v208
	v_rcp_f32_e32 v209, v209
	v_rcp_f32_e32 v210, v210
	v_rcp_f32_e32 v211, v211
	v_rcp_f32_e32 v212, v212
	v_rcp_f32_e32 v213, v213
	v_rcp_f32_e32 v214, v214
	v_rcp_f32_e32 v215, v215
	v_fmamk_f32 v208, v208, 0xc0b8aa3b, v198
	v_fmamk_f32 v209, v209, 0xc0b8aa3b, v198
	v_fmamk_f32 v210, v210, 0xc0b8aa3b, v198
	v_fmamk_f32 v211, v211, 0xc0b8aa3b, v198
	v_mul_f32_e32 v204, v204, v128
	v_mul_f32_e32 v205, v205, v129
	v_mul_f32_e32 v206, v206, v130
	v_mul_f32_e32 v207, v207, v131
	v_fma_f32 v128, v200, v208, v204
	v_fma_f32 v129, v201, v209, v205
	v_fma_f32 v130, v202, v210, v206
	v_fma_f32 v131, v203, v211, v207
	v_exp_f32_e32 v200, v128
	v_exp_f32_e32 v201, v129
	v_exp_f32_e32 v202, v130
	v_exp_f32_e32 v203, v131
	v_add_f32_e32 v200, 1.0, v200
	v_add_f32_e32 v201, 1.0, v201
	v_add_f32_e32 v202, 1.0, v202
	v_add_f32_e32 v203, 1.0, v203
	v_rcp_f32_e32 v200, v200
	v_rcp_f32_e32 v201, v201
	v_rcp_f32_e32 v202, v202
	v_rcp_f32_e32 v203, v203
	v_fma_f32 v200, v200, 2.0, -1.0
	v_fma_f32 v201, v201, 2.0, -1.0
	v_fma_f32 v202, v202, 2.0, -1.0
	v_fma_f32 v203, v203, 2.0, -1.0
	v_mul_f32_e32 v216, v212, v200
	v_mul_f32_e32 v217, v213, v201
	v_mul_f32_e32 v218, v214, v202
	v_mul_f32_e32 v219, v215, v203
	v_cvt_pk_f16_f32 v220, v216, v217
	v_cvt_pk_f16_f32 v221, v218, v219
	v_exp_f32_e32 v200, v16
	v_exp_f32_e32 v201, v17
	v_exp_f32_e32 v202, v18
	v_exp_f32_e32 v203, v19
	v_exp_f32_e32 v204, v20
	v_exp_f32_e32 v205, v21
	v_exp_f32_e32 v206, v22
	v_exp_f32_e32 v207, v23
	v_exp_f32_e32 v208, v24
	v_exp_f32_e32 v209, v25
	v_exp_f32_e32 v210, v26
	v_exp_f32_e32 v211, v27
	v_exp_f32_e32 v212, v28
	v_exp_f32_e32 v213, v29
	v_exp_f32_e32 v214, v30
	v_exp_f32_e32 v215, v31
	v_add_f32_e32 v200, 1.0, v200
	v_add_f32_e32 v201, 1.0, v201
	v_add_f32_e32 v202, 1.0, v202
	v_add_f32_e32 v203, 1.0, v203
	v_add_f32_e32 v204, 1.0, v204
	v_add_f32_e32 v205, 1.0, v205
	v_add_f32_e32 v206, 1.0, v206
	v_add_f32_e32 v207, 1.0, v207
	v_add_f32_e32 v208, 1.0, v208
	v_add_f32_e32 v209, 1.0, v209
	v_add_f32_e32 v210, 1.0, v210
	v_add_f32_e32 v211, 1.0, v211
	v_add_f32_e32 v212, 1.0, v212
	v_add_f32_e32 v213, 1.0, v213
	v_add_f32_e32 v214, 1.0, v214
	v_add_f32_e32 v215, 1.0, v215
	v_rcp_f32_e32 v200, v200
	v_rcp_f32_e32 v201, v201
	v_rcp_f32_e32 v202, v202
	v_rcp_f32_e32 v203, v203
	v_rcp_f32_e32 v204, v204
	v_rcp_f32_e32 v205, v205
	v_rcp_f32_e32 v206, v206
	v_rcp_f32_e32 v207, v207
	v_rcp_f32_e32 v208, v208
	v_rcp_f32_e32 v209, v209
	v_rcp_f32_e32 v210, v210
	v_rcp_f32_e32 v211, v211
	v_rcp_f32_e32 v212, v212
	v_rcp_f32_e32 v213, v213
	v_rcp_f32_e32 v214, v214
	v_rcp_f32_e32 v215, v215
	v_fmamk_f32 v208, v208, 0xc0b8aa3b, v198
	v_fmamk_f32 v209, v209, 0xc0b8aa3b, v198
	v_fmamk_f32 v210, v210, 0xc0b8aa3b, v198
	v_fmamk_f32 v211, v211, 0xc0b8aa3b, v198
	v_mul_f32_e32 v204, v204, v132
	v_mul_f32_e32 v205, v205, v133
	v_mul_f32_e32 v206, v206, v134
	v_mul_f32_e32 v207, v207, v135
	v_fma_f32 v132, v200, v208, v204
	v_fma_f32 v133, v201, v209, v205
	v_fma_f32 v134, v202, v210, v206
	v_fma_f32 v135, v203, v211, v207
	v_exp_f32_e32 v200, v132
	v_exp_f32_e32 v201, v133
	v_exp_f32_e32 v202, v134
	v_exp_f32_e32 v203, v135
	v_add_f32_e32 v200, 1.0, v200
	v_add_f32_e32 v201, 1.0, v201
	v_add_f32_e32 v202, 1.0, v202
	v_add_f32_e32 v203, 1.0, v203
	v_rcp_f32_e32 v200, v200
	v_rcp_f32_e32 v201, v201
	v_rcp_f32_e32 v202, v202
	v_rcp_f32_e32 v203, v203
	v_fma_f32 v200, v200, 2.0, -1.0
	v_fma_f32 v201, v201, 2.0, -1.0
	v_fma_f32 v202, v202, 2.0, -1.0
	v_fma_f32 v203, v203, 2.0, -1.0
	v_mul_f32_e32 v216, v212, v200
	v_mul_f32_e32 v217, v213, v201
	v_mul_f32_e32 v218, v214, v202
	v_mul_f32_e32 v219, v215, v203
	v_cvt_pk_f16_f32 v222, v216, v217
	v_cvt_pk_f16_f32 v223, v218, v219
	s_nop 1
	v_permlane32_swap_b32_e32 v220, v222
	v_permlane32_swap_b32_e32 v221, v223
	s_cmp_eq_u32 s31, 0
	s_cbranch_scc1 .LE_slow4
	global_store_dwordx4 v195, v[220:223], s[36:37] offset:0
	s_branch .LE_join5

.LE_join5:
	s_waitcnt vmcnt(0)
	s_barrier
	v_mov_b32_e32 v199, 1
	s_cmp_eq_u32 s31, 0
	s_cbranch_scc1 .LE_slow6
	global_store_dword v197, v199, s[40:41]
	s_branch .LE_join7

.LE_join7:
	s_and_b32 s64, s33, 1
	s_lshl_b32 s64, s64, 22
	s_add_u32 s64, s64, s50
	s_add_u32 s64, s64, 0x20000
	s_add_u32 s36, s6, s64
	s_addc_u32 s37, s7, 0
	v_exp_f32_e32 v200, v32
	v_exp_f32_e32 v201, v33
	v_exp_f32_e32 v202, v34
	v_exp_f32_e32 v203, v35
	v_exp_f32_e32 v204, v36
	v_exp_f32_e32 v205, v37
	v_exp_f32_e32 v206, v38
	v_exp_f32_e32 v207, v39
	v_exp_f32_e32 v208, v40
	v_exp_f32_e32 v209, v41
	v_exp_f32_e32 v210, v42
	v_exp_f32_e32 v211, v43
	v_exp_f32_e32 v212, v44
	v_exp_f32_e32 v213, v45
	v_exp_f32_e32 v214, v46
	v_exp_f32_e32 v215, v47
	v_add_f32_e32 v200, 1.0, v200
	v_add_f32_e32 v201, 1.0, v201
	v_add_f32_e32 v202, 1.0, v202
	v_add_f32_e32 v203, 1.0, v203
	v_add_f32_e32 v204, 1.0, v204
	v_add_f32_e32 v205, 1.0, v205
	v_add_f32_e32 v206, 1.0, v206
	v_add_f32_e32 v207, 1.0, v207
	v_add_f32_e32 v208, 1.0, v208
	v_add_f32_e32 v209, 1.0, v209
	v_add_f32_e32 v210, 1.0, v210
	v_add_f32_e32 v211, 1.0, v211
	v_add_f32_e32 v212, 1.0, v212
	v_add_f32_e32 v213, 1.0, v213
	v_add_f32_e32 v214, 1.0, v214
	v_add_f32_e32 v215, 1.0, v215
	v_rcp_f32_e32 v200, v200
	v_rcp_f32_e32 v201, v201
	v_rcp_f32_e32 v202, v202
	v_rcp_f32_e32 v203, v203
	v_rcp_f32_e32 v204, v204
	v_rcp_f32_e32 v205, v205
	v_rcp_f32_e32 v206, v206
	v_rcp_f32_e32 v207, v207
	v_rcp_f32_e32 v208, v208
	v_rcp_f32_e32 v209, v209
	v_rcp_f32_e32 v210, v210
	v_rcp_f32_e32 v211, v211
	v_rcp_f32_e32 v212, v212
	v_rcp_f32_e32 v213, v213
	v_rcp_f32_e32 v214, v214
	v_rcp_f32_e32 v215, v215
	v_fmamk_f32 v208, v208, 0xc0b8aa3b, v198
	v_fmamk_f32 v209, v209, 0xc0b8aa3b, v198
	v_fmamk_f32 v210, v210, 0xc0b8aa3b, v198
	v_fmamk_f32 v211, v211, 0xc0b8aa3b, v198
	v_mul_f32_e32 v204, v204, v136
	v_mul_f32_e32 v205, v205, v137
	v_mul_f32_e32 v206, v206, v138
	v_mul_f32_e32 v207, v207, v139
	v_fma_f32 v136, v200, v208, v204
	v_fma_f32 v137, v201, v209, v205
	v_fma_f32 v138, v202, v210, v206
	v_fma_f32 v139, v203, v211, v207
	v_exp_f32_e32 v200, v136
	v_exp_f32_e32 v201, v137
	v_exp_f32_e32 v202, v138
	v_exp_f32_e32 v203, v139
	v_add_f32_e32 v200, 1.0, v200
	v_add_f32_e32 v201, 1.0, v201
	v_add_f32_e32 v202, 1.0, v202
	v_add_f32_e32 v203, 1.0, v203
	v_rcp_f32_e32 v200, v200
	v_rcp_f32_e32 v201, v201
	v_rcp_f32_e32 v202, v202
	v_rcp_f32_e32 v203, v203
	v_fma_f32 v200, v200, 2.0, -1.0
	v_fma_f32 v201, v201, 2.0, -1.0
	v_fma_f32 v202, v202, 2.0, -1.0
	v_fma_f32 v203, v203, 2.0, -1.0
	v_mul_f32_e32 v216, v212, v200
	v_mul_f32_e32 v217, v213, v201
	v_mul_f32_e32 v218, v214, v202
	v_mul_f32_e32 v219, v215, v203
	v_cvt_pk_f16_f32 v220, v216, v217
	v_cvt_pk_f16_f32 v221, v218, v219
	v_exp_f32_e32 v200, v48
	v_exp_f32_e32 v201, v49
	v_exp_f32_e32 v202, v50
	v_exp_f32_e32 v203, v51
	v_exp_f32_e32 v204, v52
	v_exp_f32_e32 v205, v53
	v_exp_f32_e32 v206, v54
	v_exp_f32_e32 v207, v55
	v_exp_f32_e32 v208, v56
	v_exp_f32_e32 v209, v57
	v_exp_f32_e32 v210, v58
	v_exp_f32_e32 v211, v59
	v_exp_f32_e32 v212, v60
	v_exp_f32_e32 v213, v61
	v_exp_f32_e32 v214, v62
	v_exp_f32_e32 v215, v63
	v_add_f32_e32 v200, 1.0, v200
	v_add_f32_e32 v201, 1.0, v201
	v_add_f32_e32 v202, 1.0, v202
	v_add_f32_e32 v203, 1.0, v203
	v_add_f32_e32 v204, 1.0, v204
	v_add_f32_e32 v205, 1.0, v205
	v_add_f32_e32 v206, 1.0, v206
	v_add_f32_e32 v207, 1.0, v207
	v_add_f32_e32 v208, 1.0, v208
	v_add_f32_e32 v209, 1.0, v209
	v_add_f32_e32 v210, 1.0, v210
	v_add_f32_e32 v211, 1.0, v211
	v_add_f32_e32 v212, 1.0, v212
	v_add_f32_e32 v213, 1.0, v213
	v_add_f32_e32 v214, 1.0, v214
	v_add_f32_e32 v215, 1.0, v215
	v_rcp_f32_e32 v200, v200
	v_rcp_f32_e32 v201, v201
	v_rcp_f32_e32 v202, v202
	v_rcp_f32_e32 v203, v203
	v_rcp_f32_e32 v204, v204
	v_rcp_f32_e32 v205, v205
	v_rcp_f32_e32 v206, v206
	v_rcp_f32_e32 v207, v207
	v_rcp_f32_e32 v208, v208
	v_rcp_f32_e32 v209, v209
	v_rcp_f32_e32 v210, v210
	v_rcp_f32_e32 v211, v211
	v_rcp_f32_e32 v212, v212
	v_rcp_f32_e32 v213, v213
	v_rcp_f32_e32 v214, v214
	v_rcp_f32_e32 v215, v215
	v_fmamk_f32 v208, v208, 0xc0b8aa3b, v198
	v_fmamk_f32 v209, v209, 0xc0b8aa3b, v198
	v_fmamk_f32 v210, v210, 0xc0b8aa3b, v198
	v_fmamk_f32 v211, v211, 0xc0b8aa3b, v198
	v_mul_f32_e32 v204, v204, v140
	v_mul_f32_e32 v205, v205, v141
	v_mul_f32_e32 v206, v206, v142
	v_mul_f32_e32 v207, v207, v143
	v_fma_f32 v140, v200, v208, v204
	v_fma_f32 v141, v201, v209, v205
	v_fma_f32 v142, v202, v210, v206
	v_fma_f32 v143, v203, v211, v207
	v_exp_f32_e32 v200, v140
	v_exp_f32_e32 v201, v141
	v_exp_f32_e32 v202, v142
	v_exp_f32_e32 v203, v143
	v_add_f32_e32 v200, 1.0, v200
	v_add_f32_e32 v201, 1.0, v201
	v_add_f32_e32 v202, 1.0, v202
	v_add_f32_e32 v203, 1.0, v203
	v_rcp_f32_e32 v200, v200
	v_rcp_f32_e32 v201, v201
	v_rcp_f32_e32 v202, v202
	v_rcp_f32_e32 v203, v203
	v_fma_f32 v200, v200, 2.0, -1.0
	v_fma_f32 v201, v201, 2.0, -1.0
	v_fma_f32 v202, v202, 2.0, -1.0
	v_fma_f32 v203, v203, 2.0, -1.0
	v_mul_f32_e32 v216, v212, v200
	v_mul_f32_e32 v217, v213, v201
	v_mul_f32_e32 v218, v214, v202
	v_mul_f32_e32 v219, v215, v203
	v_cvt_pk_f16_f32 v222, v216, v217
	v_cvt_pk_f16_f32 v223, v218, v219
	s_nop 1
	v_permlane32_swap_b32_e32 v220, v222
	v_permlane32_swap_b32_e32 v221, v223
	s_cmp_eq_u32 s31, 0
	s_cbranch_scc1 .LE_slow8
	global_store_dwordx4 v195, v[220:223], s[36:37] offset:0
	s_branch .LE_join9

.LE_join9:
	s_waitcnt vmcnt(0)
	s_barrier
	v_mov_b32_e32 v199, 2
	s_cmp_eq_u32 s31, 0
	s_cbranch_scc1 .LE_slow10
	global_store_dword v197, v199, s[40:41]
	s_branch .LE_join11

.LE_join11:
	s_and_b32 s64, s33, 1
	s_lshl_b32 s64, s64, 22
	s_add_u32 s64, s64, s50
	s_add_u32 s64, s64, 0x40000
	s_add_u32 s36, s6, s64
	s_addc_u32 s37, s7, 0
	v_exp_f32_e32 v200, v64
	v_exp_f32_e32 v201, v65
	v_exp_f32_e32 v202, v66
	v_exp_f32_e32 v203, v67
	v_exp_f32_e32 v204, v68
	v_exp_f32_e32 v205, v69
	v_exp_f32_e32 v206, v70
	v_exp_f32_e32 v207, v71
	v_exp_f32_e32 v208, v72
	v_exp_f32_e32 v209, v73
	v_exp_f32_e32 v210, v74
	v_exp_f32_e32 v211, v75
	v_exp_f32_e32 v212, v76
	v_exp_f32_e32 v213, v77
	v_exp_f32_e32 v214, v78
	v_exp_f32_e32 v215, v79
	v_add_f32_e32 v200, 1.0, v200
	v_add_f32_e32 v201, 1.0, v201
	v_add_f32_e32 v202, 1.0, v202
	v_add_f32_e32 v203, 1.0, v203
	v_add_f32_e32 v204, 1.0, v204
	v_add_f32_e32 v205, 1.0, v205
	v_add_f32_e32 v206, 1.0, v206
	v_add_f32_e32 v207, 1.0, v207
	v_add_f32_e32 v208, 1.0, v208
	v_add_f32_e32 v209, 1.0, v209
	v_add_f32_e32 v210, 1.0, v210
	v_add_f32_e32 v211, 1.0, v211
	v_add_f32_e32 v212, 1.0, v212
	v_add_f32_e32 v213, 1.0, v213
	v_add_f32_e32 v214, 1.0, v214
	v_add_f32_e32 v215, 1.0, v215
	v_rcp_f32_e32 v200, v200
	v_rcp_f32_e32 v201, v201
	v_rcp_f32_e32 v202, v202
	v_rcp_f32_e32 v203, v203
	v_rcp_f32_e32 v204, v204
	v_rcp_f32_e32 v205, v205
	v_rcp_f32_e32 v206, v206
	v_rcp_f32_e32 v207, v207
	v_rcp_f32_e32 v208, v208
	v_rcp_f32_e32 v209, v209
	v_rcp_f32_e32 v210, v210
	v_rcp_f32_e32 v211, v211
	v_rcp_f32_e32 v212, v212
	v_rcp_f32_e32 v213, v213
	v_rcp_f32_e32 v214, v214
	v_rcp_f32_e32 v215, v215
	v_fmamk_f32 v208, v208, 0xc0b8aa3b, v198
	v_fmamk_f32 v209, v209, 0xc0b8aa3b, v198
	v_fmamk_f32 v210, v210, 0xc0b8aa3b, v198
	v_fmamk_f32 v211, v211, 0xc0b8aa3b, v198
	v_mul_f32_e32 v204, v204, v144
	v_mul_f32_e32 v205, v205, v145
	v_mul_f32_e32 v206, v206, v146
	v_mul_f32_e32 v207, v207, v147
	v_fma_f32 v144, v200, v208, v204
	v_fma_f32 v145, v201, v209, v205
	v_fma_f32 v146, v202, v210, v206
	v_fma_f32 v147, v203, v211, v207
	v_exp_f32_e32 v200, v144
	v_exp_f32_e32 v201, v145
	v_exp_f32_e32 v202, v146
	v_exp_f32_e32 v203, v147
	v_add_f32_e32 v200, 1.0, v200
	v_add_f32_e32 v201, 1.0, v201
	v_add_f32_e32 v202, 1.0, v202
	v_add_f32_e32 v203, 1.0, v203
	v_rcp_f32_e32 v200, v200
	v_rcp_f32_e32 v201, v201
	v_rcp_f32_e32 v202, v202
	v_rcp_f32_e32 v203, v203
	v_fma_f32 v200, v200, 2.0, -1.0
	v_fma_f32 v201, v201, 2.0, -1.0
	v_fma_f32 v202, v202, 2.0, -1.0
	v_fma_f32 v203, v203, 2.0, -1.0
	v_mul_f32_e32 v216, v212, v200
	v_mul_f32_e32 v217, v213, v201
	v_mul_f32_e32 v218, v214, v202
	v_mul_f32_e32 v219, v215, v203
	v_cvt_pk_f16_f32 v220, v216, v217
	v_cvt_pk_f16_f32 v221, v218, v219
	v_exp_f32_e32 v200, v80
	v_exp_f32_e32 v201, v81
	v_exp_f32_e32 v202, v82
	v_exp_f32_e32 v203, v83
	v_exp_f32_e32 v204, v84
	v_exp_f32_e32 v205, v85
	v_exp_f32_e32 v206, v86
	v_exp_f32_e32 v207, v87
	v_exp_f32_e32 v208, v88
	v_exp_f32_e32 v209, v89
	v_exp_f32_e32 v210, v90
	v_exp_f32_e32 v211, v91
	v_exp_f32_e32 v212, v92
	v_exp_f32_e32 v213, v93
	v_exp_f32_e32 v214, v94
	v_exp_f32_e32 v215, v95
	v_add_f32_e32 v200, 1.0, v200
	v_add_f32_e32 v201, 1.0, v201
	v_add_f32_e32 v202, 1.0, v202
	v_add_f32_e32 v203, 1.0, v203
	v_add_f32_e32 v204, 1.0, v204
	v_add_f32_e32 v205, 1.0, v205
	v_add_f32_e32 v206, 1.0, v206
	v_add_f32_e32 v207, 1.0, v207
	v_add_f32_e32 v208, 1.0, v208
	v_add_f32_e32 v209, 1.0, v209
	v_add_f32_e32 v210, 1.0, v210
	v_add_f32_e32 v211, 1.0, v211
	v_add_f32_e32 v212, 1.0, v212
	v_add_f32_e32 v213, 1.0, v213
	v_add_f32_e32 v214, 1.0, v214
	v_add_f32_e32 v215, 1.0, v215
	v_rcp_f32_e32 v200, v200
	v_rcp_f32_e32 v201, v201
	v_rcp_f32_e32 v202, v202
	v_rcp_f32_e32 v203, v203
	v_rcp_f32_e32 v204, v204
	v_rcp_f32_e32 v205, v205
	v_rcp_f32_e32 v206, v206
	v_rcp_f32_e32 v207, v207
	v_rcp_f32_e32 v208, v208
	v_rcp_f32_e32 v209, v209
	v_rcp_f32_e32 v210, v210
	v_rcp_f32_e32 v211, v211
	v_rcp_f32_e32 v212, v212
	v_rcp_f32_e32 v213, v213
	v_rcp_f32_e32 v214, v214
	v_rcp_f32_e32 v215, v215
	v_fmamk_f32 v208, v208, 0xc0b8aa3b, v198
	v_fmamk_f32 v209, v209, 0xc0b8aa3b, v198
	v_fmamk_f32 v210, v210, 0xc0b8aa3b, v198
	v_fmamk_f32 v211, v211, 0xc0b8aa3b, v198
	v_mul_f32_e32 v204, v204, v148
	v_mul_f32_e32 v205, v205, v149
	v_mul_f32_e32 v206, v206, v150
	v_mul_f32_e32 v207, v207, v151
	v_fma_f32 v148, v200, v208, v204
	v_fma_f32 v149, v201, v209, v205
	v_fma_f32 v150, v202, v210, v206
	v_fma_f32 v151, v203, v211, v207
	v_exp_f32_e32 v200, v148
	v_exp_f32_e32 v201, v149
	v_exp_f32_e32 v202, v150
	v_exp_f32_e32 v203, v151
	v_add_f32_e32 v200, 1.0, v200
	v_add_f32_e32 v201, 1.0, v201
	v_add_f32_e32 v202, 1.0, v202
	v_add_f32_e32 v203, 1.0, v203
	v_rcp_f32_e32 v200, v200
	v_rcp_f32_e32 v201, v201
	v_rcp_f32_e32 v202, v202
	v_rcp_f32_e32 v203, v203
	v_fma_f32 v200, v200, 2.0, -1.0
	v_fma_f32 v201, v201, 2.0, -1.0
	v_fma_f32 v202, v202, 2.0, -1.0
	v_fma_f32 v203, v203, 2.0, -1.0
	v_mul_f32_e32 v216, v212, v200
	v_mul_f32_e32 v217, v213, v201
	v_mul_f32_e32 v218, v214, v202
	v_mul_f32_e32 v219, v215, v203
	v_cvt_pk_f16_f32 v222, v216, v217
	v_cvt_pk_f16_f32 v223, v218, v219
	s_nop 1
	v_permlane32_swap_b32_e32 v220, v222
	v_permlane32_swap_b32_e32 v221, v223
	s_cmp_eq_u32 s31, 0
	s_cbranch_scc1 .LE_slow12
	global_store_dwordx4 v195, v[220:223], s[36:37] offset:0
	s_branch .LE_join13

.LE_join13:
	s_waitcnt vmcnt(0)
	s_barrier
	v_mov_b32_e32 v199, 3
	s_cmp_eq_u32 s31, 0
	s_cbranch_scc1 .LE_slow14
	global_store_dword v197, v199, s[40:41]
	s_branch .LE_join15

.LE_join15:
	s_mov_b32 s33, 1
	s_lshl_b32 s64, s33, 11
	s_lshl_b32 s65, s29, 8
	s_add_u32 s64, s64, s65
	s_lshl_b32 s64, s64, 3
	s_add_u32 s42, s12, s64
	s_addc_u32 s43, s13, 0
	global_load_dwordx2 v[228:229], v249, s[42:43] offset:0
	global_load_dwordx2 v[230:231], v249, s[42:43] offset:256
	ds_read_b128 v[236:239], v248 offset:0
	ds_read_b128 v[240:243], v248 offset:16
	ds_read_b128 v[244:247], v248 offset:32
	ds_read_b128 v[200:203], v248 offset:48
	ds_read_b128 v[204:207], v248 offset:64
	ds_read_b128 v[208:211], v248 offset:80
	s_waitcnt lgkmcnt(3)
	s_waitcnt vmcnt(0)
	v_fma_f32 v0, v229, v237, v244
	v_fma_f32 v1, v229, v239, v245
	v_fma_f32 v2, v229, v241, v246
	v_fma_f32 v3, v229, v243, v247
	v_fmac_f32_e32 v0, v228, v236
	v_fmac_f32_e32 v1, v228, v238
	v_fmac_f32_e32 v2, v228, v240
	v_fmac_f32_e32 v3, v228, v242
	v_fma_f32 v16, v231, v237, v244
	v_fma_f32 v17, v231, v239, v245
	v_fma_f32 v18, v231, v241, v246
	v_fma_f32 v19, v231, v243, v247
	v_fmac_f32_e32 v16, v230, v236
	v_fmac_f32_e32 v17, v230, v238
	v_fmac_f32_e32 v18, v230, v240
	v_fmac_f32_e32 v19, v230, v242
	ds_read_b128 v[236:239], v248 offset:96
	ds_read_b128 v[240:243], v248 offset:112
	ds_read_b128 v[244:247], v248 offset:128
	s_waitcnt lgkmcnt(3)
	v_fma_f32 v4, v229, v201, v208
	v_fma_f32 v5, v229, v203, v209
	v_fma_f32 v6, v229, v205, v210
	v_fma_f32 v7, v229, v207, v211
	v_fmac_f32_e32 v4, v228, v200
	v_fmac_f32_e32 v5, v228, v202
	v_fmac_f32_e32 v6, v228, v204
	v_fmac_f32_e32 v7, v228, v206
	v_fma_f32 v20, v231, v201, v208
	v_fma_f32 v21, v231, v203, v209
	v_fma_f32 v22, v231, v205, v210
	v_fma_f32 v23, v231, v207, v211
	v_fmac_f32_e32 v20, v230, v200
	v_fmac_f32_e32 v21, v230, v202
	v_fmac_f32_e32 v22, v230, v204
	v_fmac_f32_e32 v23, v230, v206
	ds_read_b128 v[200:203], v248 offset:144
	ds_read_b128 v[204:207], v248 offset:160
	ds_read_b128 v[208:211], v248 offset:176
	s_waitcnt lgkmcnt(3)
	v_fma_f32 v8, v229, v237, v244
	v_fma_f32 v9, v229, v239, v245
	v_fma_f32 v10, v229, v241, v246
	v_fma_f32 v11, v229, v243, v247
	v_fmac_f32_e32 v8, v228, v236
	v_fmac_f32_e32 v9, v228, v238
	v_fmac_f32_e32 v10, v228, v240
	v_fmac_f32_e32 v11, v228, v242
	v_fma_f32 v24, v231, v237, v244
	v_fma_f32 v25, v231, v239, v245
	v_fma_f32 v26, v231, v241, v246
	v_fma_f32 v27, v231, v243, v247
	v_fmac_f32_e32 v24, v230, v236
	v_fmac_f32_e32 v25, v230, v238
	v_fmac_f32_e32 v26, v230, v240
	v_fmac_f32_e32 v27, v230, v242
	s_waitcnt lgkmcnt(0)
	v_fma_f32 v12, v229, v201, v208
	v_fma_f32 v13, v229, v203, v209
	v_fma_f32 v14, v229, v205, v210
	v_fma_f32 v15, v229, v207, v211
	v_fmac_f32_e32 v12, v228, v200
	v_fmac_f32_e32 v13, v228, v202
	v_fmac_f32_e32 v14, v228, v204
	v_fmac_f32_e32 v15, v228, v206
	v_fma_f32 v28, v231, v201, v208
	v_fma_f32 v29, v231, v203, v209
	v_fma_f32 v30, v231, v205, v210
	v_fma_f32 v31, v231, v207, v211
	v_fmac_f32_e32 v28, v230, v200
	v_fmac_f32_e32 v29, v230, v202
	v_fmac_f32_e32 v30, v230, v204
	v_fmac_f32_e32 v31, v230, v206
	s_lshl_b32 s64, s33, 11
	s_lshl_b32 s65, s29, 8
	s_add_u32 s64, s64, s65
	s_add_u32 s64, s64, 64
	s_lshl_b32 s64, s64, 3
	s_add_u32 s42, s12, s64
	s_addc_u32 s43, s13, 0
	global_load_dwordx2 v[228:229], v249, s[42:43] offset:0
	global_load_dwordx2 v[230:231], v249, s[42:43] offset:256
	ds_read_b128 v[236:239], v248 offset:0
	ds_read_b128 v[240:243], v248 offset:16
	ds_read_b128 v[244:247], v248 offset:32
	ds_read_b128 v[200:203], v248 offset:48
	ds_read_b128 v[204:207], v248 offset:64
	ds_read_b128 v[208:211], v248 offset:80
	s_waitcnt lgkmcnt(3)
	s_waitcnt vmcnt(0)
	v_fma_f32 v32, v229, v237, v244
	v_fma_f32 v33, v229, v239, v245
	v_fma_f32 v34, v229, v241, v246
	v_fma_f32 v35, v229, v243, v247
	v_fmac_f32_e32 v32, v228, v236
	v_fmac_f32_e32 v33, v228, v238
	v_fmac_f32_e32 v34, v228, v240
	v_fmac_f32_e32 v35, v228, v242
	v_fma_f32 v48, v231, v237, v244
	v_fma_f32 v49, v231, v239, v245
	v_fma_f32 v50, v231, v241, v246
	v_fma_f32 v51, v231, v243, v247
	v_fmac_f32_e32 v48, v230, v236
	v_fmac_f32_e32 v49, v230, v238
	v_fmac_f32_e32 v50, v230, v240
	v_fmac_f32_e32 v51, v230, v242
	ds_read_b128 v[236:239], v248 offset:96
	ds_read_b128 v[240:243], v248 offset:112
	ds_read_b128 v[244:247], v248 offset:128
	s_waitcnt lgkmcnt(3)
	v_fma_f32 v36, v229, v201, v208
	v_fma_f32 v37, v229, v203, v209
	v_fma_f32 v38, v229, v205, v210
	v_fma_f32 v39, v229, v207, v211
	v_fmac_f32_e32 v36, v228, v200
	v_fmac_f32_e32 v37, v228, v202
	v_fmac_f32_e32 v38, v228, v204
	v_fmac_f32_e32 v39, v228, v206
	v_fma_f32 v52, v231, v201, v208
	v_fma_f32 v53, v231, v203, v209
	v_fma_f32 v54, v231, v205, v210
	v_fma_f32 v55, v231, v207, v211
	v_fmac_f32_e32 v52, v230, v200
	v_fmac_f32_e32 v53, v230, v202
	v_fmac_f32_e32 v54, v230, v204
	v_fmac_f32_e32 v55, v230, v206
	ds_read_b128 v[200:203], v248 offset:144
	ds_read_b128 v[204:207], v248 offset:160
	ds_read_b128 v[208:211], v248 offset:176
	s_waitcnt lgkmcnt(3)
	v_fma_f32 v40, v229, v237, v244
	v_fma_f32 v41, v229, v239, v245
	v_fma_f32 v42, v229, v241, v246
	v_fma_f32 v43, v229, v243, v247
	v_fmac_f32_e32 v40, v228, v236
	v_fmac_f32_e32 v41, v228, v238
	v_fmac_f32_e32 v42, v228, v240
	v_fmac_f32_e32 v43, v228, v242
	v_fma_f32 v56, v231, v237, v244
	v_fma_f32 v57, v231, v239, v245
	v_fma_f32 v58, v231, v241, v246
	v_fma_f32 v59, v231, v243, v247
	v_fmac_f32_e32 v56, v230, v236
	v_fmac_f32_e32 v57, v230, v238
	v_fmac_f32_e32 v58, v230, v240
	v_fmac_f32_e32 v59, v230, v242
	s_waitcnt lgkmcnt(0)
	v_fma_f32 v44, v229, v201, v208
	v_fma_f32 v45, v229, v203, v209
	v_fma_f32 v46, v229, v205, v210
	v_fma_f32 v47, v229, v207, v211
	v_fmac_f32_e32 v44, v228, v200
	v_fmac_f32_e32 v45, v228, v202
	v_fmac_f32_e32 v46, v228, v204
	v_fmac_f32_e32 v47, v228, v206
	v_fma_f32 v60, v231, v201, v208
	v_fma_f32 v61, v231, v203, v209
	v_fma_f32 v62, v231, v205, v210
	v_fma_f32 v63, v231, v207, v211
	v_fmac_f32_e32 v60, v230, v200
	v_fmac_f32_e32 v61, v230, v202
	v_fmac_f32_e32 v62, v230, v204
	v_fmac_f32_e32 v63, v230, v206
	s_waitcnt vmcnt(0)
	s_waitcnt lgkmcnt(0)
	s_cmp_ge_u32 s33, s28
	s_cbranch_scc1 .LE_end17
	s_sub_u32 s71, s33, 1
	s_and_b32 s64, s71, 1
	s_lshl_b32 s64, s64, 22
	s_add_u32 s64, s64, s49
	s_add_u32 s34, s6, s64
	s_addc_u32 s35, s7, 0
	s_lshl_b32 s64, s71, 3
	s_add_u32 s64, s64, s29
	s_lshl_b32 s64, s64, 7
	s_add_u32 s38, s8, s64
	s_addc_u32 s39, s9, 0

.LE_loop16:
	s_sub_u32 s71, s33, 1
	s_add_u32 s61, s33, 1
	s_min_u32 s61, s61, s60
	s_and_b32 s64, s71, 1
	s_lshl_b32 s64, s64, 22
	s_add_u32 s64, s64, s50
	s_add_u32 s64, s64, 0x60000
	s_add_u32 s36, s6, s64
	s_addc_u32 s37, s7, 0
	s_lshl_b32 s64, s71, 3
	s_add_u32 s64, s64, s29
	s_lshl_b32 s64, s64, 5
	s_add_u32 s64, s64, s30
	s_lshl_b32 s64, s64, 2
	s_add_u32 s40, s8, s64
	s_addc_u32 s41, s9, 0
	s_lshl_b32 s64, s33, 11
	s_lshl_b32 s65, s29, 8
	s_add_u32 s64, s64, s65
	s_add_u32 s64, s64, 128
	s_lshl_b32 s64, s64, 3
	s_add_u32 s42, s12, s64
	s_addc_u32 s43, s13, 0
	s_nop 11
	global_load_dwordx2 v[228:229], v249, s[42:43] offset:0
	global_load_dwordx2 v[230:231], v249, s[42:43] offset:256
	s_waitcnt lgkmcnt(6)
	v_mfma_f32_32x32x16_f16 v[0:15], a[0:3], v[160:163], v[0:15]
	ds_read_b128 v[160:163], v192 offset:8192
	v_exp_f32_e32 v200, v96
	v_mfma_f32_32x32x16_f16 v[16:31], a[0:3], v[164:167], v[16:31]
	ds_read_b128 v[164:167], v192 offset:9216
	v_exp_f32_e32 v201, v97
	v_add_f32_e32 v200, 1.0, v200
	s_waitcnt lgkmcnt(6)
	v_mfma_f32_32x32x16_f16 v[0:15], a[4:7], v[168:171], v[0:15]
	ds_read_b128 v[168:171], v192 offset:10240
	v_exp_f32_e32 v202, v98
	v_add_f32_e32 v201, 1.0, v201
	v_mfma_f32_32x32x16_f16 v[16:31], a[4:7], v[172:175], v[16:31]
	ds_read_b128 v[172:175], v192 offset:11264
	global_load_lds_dwordx4 v192, s[44:45] offset:1024 sc1
	v_exp_f32_e32 v203, v99
	v_add_f32_e32 v202, 1.0, v202
	s_waitcnt lgkmcnt(6)
	v_mfma_f32_32x32x16_f16 v[0:15], a[8:11], v[176:179], v[0:15]
	ds_read_b128 v[176:179], v192 offset:12288
	v_exp_f32_e32 v204, v100
	v_add_f32_e32 v203, 1.0, v203
	v_mfma_f32_32x32x16_f16 v[16:31], a[8:11], v[180:183], v[16:31]
	ds_read_b128 v[180:183], v192 offset:13312
	v_exp_f32_e32 v205, v101
	v_add_f32_e32 v204, 1.0, v204
	s_waitcnt lgkmcnt(6)
	v_mfma_f32_32x32x16_f16 v[0:15], a[12:15], v[184:187], v[0:15]
	ds_read_b128 v[184:187], v192 offset:14336
	v_exp_f32_e32 v206, v102
	v_add_f32_e32 v205, 1.0, v205
	v_mfma_f32_32x32x16_f16 v[16:31], a[12:15], v[188:191], v[16:31]
	ds_read_b128 v[188:191], v192 offset:15360
	global_load_lds_dwordx4 v192, s[44:45] offset:2048 sc1
	v_exp_f32_e32 v207, v103
	v_add_f32_e32 v206, 1.0, v206
	s_waitcnt lgkmcnt(6)
	v_mfma_f32_32x32x16_f16 v[0:15], a[16:19], v[160:163], v[0:15]
	ds_read_b128 v[160:163], v192 offset:16384
	v_exp_f32_e32 v208, v104
	v_add_f32_e32 v207, 1.0, v207
	v_mfma_f32_32x32x16_f16 v[16:31], a[16:19], v[164:167], v[16:31]
	ds_read_b128 v[164:167], v192 offset:17408
	v_exp_f32_e32 v209, v105
	v_add_f32_e32 v208, 1.0, v208
	s_waitcnt lgkmcnt(6)
	v_mfma_f32_32x32x16_f16 v[0:15], a[20:23], v[168:171], v[0:15]
	ds_read_b128 v[168:171], v192 offset:18432
	v_exp_f32_e32 v210, v106
	v_add_f32_e32 v209, 1.0, v209
	v_mfma_f32_32x32x16_f16 v[16:31], a[20:23], v[172:175], v[16:31]
	ds_read_b128 v[172:175], v192 offset:19456
	global_load_lds_dwordx4 v192, s[44:45] offset:3072 sc1
	v_exp_f32_e32 v211, v107
	v_add_f32_e32 v210, 1.0, v210
	s_waitcnt lgkmcnt(6)
	v_mfma_f32_32x32x16_f16 v[0:15], a[24:27], v[176:179], v[0:15]
	ds_read_b128 v[176:179], v192 offset:20480
	v_exp_f32_e32 v212, v108
	v_add_f32_e32 v211, 1.0, v211
	v_mfma_f32_32x32x16_f16 v[16:31], a[24:27], v[180:183], v[16:31]
	ds_read_b128 v[180:183], v192 offset:21504
	v_exp_f32_e32 v213, v109
	v_add_f32_e32 v212, 1.0, v212
	s_waitcnt lgkmcnt(6)
	v_mfma_f32_32x32x16_f16 v[0:15], a[28:31], v[184:187], v[0:15]
	ds_read_b128 v[184:187], v192 offset:22528
	v_exp_f32_e32 v214, v110
	v_add_f32_e32 v213, 1.0, v213
	v_mfma_f32_32x32x16_f16 v[16:31], a[28:31], v[188:191], v[16:31]
	ds_read_b128 v[188:191], v192 offset:23552
	s_add_u32 s44, s34, 0x11000
	s_addc_u32 s45, s35, 0
	s_mov_b32 m0, s57
	s_nop 0
	global_load_lds_dwordx4 v192, s[44:45] sc1
	v_exp_f32_e32 v215, v111
	v_add_f32_e32 v214, 1.0, v214
	s_waitcnt lgkmcnt(6)
	v_mfma_f32_32x32x16_f16 v[0:15], a[32:35], v[160:163], v[0:15]
	ds_read_b128 v[160:163], v192 offset:24576
	v_add_f32_e32 v215, 1.0, v215
	v_rcp_f32_e32 v200, v200
	v_mfma_f32_32x32x16_f16 v[16:31], a[32:35], v[164:167], v[16:31]
	ds_read_b128 v[164:167], v192 offset:25600
	v_rcp_f32_e32 v201, v201
	s_waitcnt lgkmcnt(6)
	v_mfma_f32_32x32x16_f16 v[0:15], a[36:39], v[168:171], v[0:15]
	ds_read_b128 v[168:171], v192 offset:26624
	v_rcp_f32_e32 v202, v202
	v_mfma_f32_32x32x16_f16 v[16:31], a[36:39], v[172:175], v[16:31]
	ds_read_b128 v[172:175], v192 offset:27648
	global_load_lds_dwordx4 v192, s[44:45] offset:1024 sc1
	v_rcp_f32_e32 v203, v203
	s_waitcnt lgkmcnt(6)
	v_mfma_f32_32x32x16_f16 v[0:15], a[40:43], v[176:179], v[0:15]
	ds_read_b128 v[176:179], v192 offset:28672
	v_rcp_f32_e32 v204, v204
	v_mfma_f32_32x32x16_f16 v[16:31], a[40:43], v[180:183], v[16:31]
	ds_read_b128 v[180:183], v192 offset:29696
	v_rcp_f32_e32 v205, v205
	v_mul_f32_e32 v204, v204, v152
	s_waitcnt lgkmcnt(6)
	v_mfma_f32_32x32x16_f16 v[0:15], a[44:47], v[184:187], v[0:15]
	ds_read_b128 v[184:187], v192 offset:30720
	v_rcp_f32_e32 v206, v206
	v_mul_f32_e32 v205, v205, v153
	v_mfma_f32_32x32x16_f16 v[16:31], a[44:47], v[188:191], v[16:31]
	ds_read_b128 v[188:191], v192 offset:31744
	global_load_lds_dwordx4 v192, s[44:45] offset:2048 sc1
	v_rcp_f32_e32 v207, v207
	v_mul_f32_e32 v206, v206, v154
	s_waitcnt vmcnt(9)
	s_barrier
	s_waitcnt lgkmcnt(6)
	v_mfma_f32_32x32x16_f16 v[0:15], a[48:51], v[160:163], v[0:15]
	ds_read_b128 v[160:163], v192 offset:32768
	v_rcp_f32_e32 v208, v208
	v_mul_f32_e32 v207, v207, v155
	ds_read_b128 v[236:239], v248 offset:0
	ds_read_b64 v[240:241], v248 offset:32
	ds_read_b128 v[242:245], v248 offset:16
	ds_read_b64 v[246:247], v248 offset:40
	v_mfma_f32_32x32x16_f16 v[16:31], a[48:51], v[164:167], v[16:31]
	ds_read_b128 v[164:167], v192 offset:33792
	v_rcp_f32_e32 v209, v209
	v_fmamk_f32 v208, v208, 0xc0b8aa3b, v198
	s_waitcnt lgkmcnt(3)
	s_waitcnt vmcnt(6)
	v_fma_f32 v64, v229, v237, v240
	v_mfma_f32_32x32x16_f16 v[0:15], a[52:55], v[168:171], v[0:15]
	ds_read_b128 v[168:171], v192 offset:34816
	v_rcp_f32_e32 v210, v210
	v_fmamk_f32 v209, v209, 0xc0b8aa3b, v198
	v_fma_f32 v152, v200, v208, v204
	v_fma_f32 v65, v229, v239, v241
	v_fmac_f32_e32 v64, v228, v236
	v_mfma_f32_32x32x16_f16 v[16:31], a[52:55], v[172:175], v[16:31]
	ds_read_b128 v[172:175], v192 offset:35840
	global_load_lds_dwordx4 v192, s[44:45] offset:3072 sc1
	v_rcp_f32_e32 v211, v211
	v_fmamk_f32 v210, v210, 0xc0b8aa3b, v198
	v_fma_f32 v153, v201, v209, v205
	v_fmac_f32_e32 v65, v228, v238
	v_fma_f32 v80, v231, v237, v240
	v_mfma_f32_32x32x16_f16 v[0:15], a[56:59], v[176:179], v[0:15]
	ds_read_b128 v[176:179], v192 offset:36864
	v_rcp_f32_e32 v212, v212
	v_fmamk_f32 v211, v211, 0xc0b8aa3b, v198
	v_fma_f32 v154, v202, v210, v206
	v_fma_f32 v81, v231, v239, v241
	v_fmac_f32_e32 v80, v230, v236
	v_mfma_f32_32x32x16_f16 v[16:31], a[56:59], v[180:183], v[16:31]
	ds_read_b128 v[180:183], v192 offset:37888
	v_rcp_f32_e32 v213, v213
	v_fma_f32 v155, v203, v211, v207
	v_fmac_f32_e32 v81, v230, v238
	ds_read_b128 v[236:239], v248 offset:48
	ds_read_b64 v[240:241], v248 offset:80
	v_mfma_f32_32x32x16_f16 v[0:15], a[60:63], v[184:187], v[0:15]
	ds_read_b128 v[184:187], v192 offset:38912
	v_rcp_f32_e32 v214, v214
	s_waitcnt lgkmcnt(8)
	v_fma_f32 v66, v229, v243, v246
	v_mfma_f32_32x32x16_f16 v[16:31], a[60:63], v[188:191], v[16:31]
	ds_read_b128 v[188:191], v192 offset:39936
	s_add_u32 s44, s34, 0x18000
	s_addc_u32 s45, s35, 0
	s_mov_b32 m0, s58
	s_nop 0
	global_load_lds_dwordx4 v192, s[44:45] sc1
	v_rcp_f32_e32 v215, v215
	v_fma_f32 v67, v229, v245, v247
	v_fmac_f32_e32 v66, v228, v242
	s_waitcnt lgkmcnt(8)
	v_mfma_f32_32x32x16_f16 v[0:15], a[64:67], v[160:163], v[0:15]
	ds_read_b128 v[160:163], v192 offset:40960
	v_exp_f32_e32 v200, v152
	v_fmac_f32_e32 v67, v228, v244
	v_fma_f32 v82, v231, v243, v246
	v_mfma_f32_32x32x16_f16 v[16:31], a[64:67], v[164:167], v[16:31]
	ds_read_b128 v[164:167], v192 offset:41984
	v_exp_f32_e32 v201, v153
	v_add_f32_e32 v200, 1.0, v200
	v_fma_f32 v83, v231, v245, v247
	v_fmac_f32_e32 v82, v230, v242
	s_waitcnt lgkmcnt(8)
	v_mfma_f32_32x32x16_f16 v[0:15], a[68:71], v[168:171], v[0:15]
	ds_read_b128 v[168:171], v192 offset:43008
	v_exp_f32_e32 v202, v154
	v_add_f32_e32 v201, 1.0, v201
	v_fmac_f32_e32 v83, v230, v244
	ds_read_b128 v[242:245], v248 offset:64
	ds_read_b64 v[246:247], v248 offset:88
	v_mfma_f32_32x32x16_f16 v[16:31], a[68:71], v[172:175], v[16:31]
	ds_read_b128 v[172:175], v192 offset:44032
	global_load_lds_dwordx4 v192, s[44:45] offset:1024 sc1
	v_exp_f32_e32 v203, v155
	v_add_f32_e32 v202, 1.0, v202
	s_waitcnt lgkmcnt(8)
	v_fma_f32 v68, v229, v237, v240
	v_mfma_f32_32x32x16_f16 v[0:15], a[72:75], v[176:179], v[0:15]
	ds_read_b128 v[176:179], v192 offset:45056
	v_add_f32_e32 v203, 1.0, v203
	v_rcp_f32_e32 v200, v200
	v_fma_f32 v69, v229, v239, v241
	v_fmac_f32_e32 v68, v228, v236
	v_mfma_f32_32x32x16_f16 v[16:31], a[72:75], v[180:183], v[16:31]
	ds_read_b128 v[180:183], v192 offset:46080
	v_rcp_f32_e32 v201, v201
	v_fma_f32 v200, v200, 2.0, -1.0
	v_fmac_f32_e32 v69, v228, v238
	v_fma_f32 v84, v231, v237, v240
	s_waitcnt lgkmcnt(8)
	v_mfma_f32_32x32x16_f16 v[0:15], a[76:79], v[184:187], v[0:15]
	ds_read_b128 v[184:187], v192 offset:47104
	v_rcp_f32_e32 v202, v202
	v_fma_f32 v201, v201, 2.0, -1.0
	v_mul_f32_e32 v216, v212, v200
	v_fma_f32 v85, v231, v239, v241
	v_fmac_f32_e32 v84, v230, v236
	v_mfma_f32_32x32x16_f16 v[16:31], a[76:79], v[188:191], v[16:31]
	ds_read_b128 v[188:191], v192 offset:48128
	global_load_lds_dwordx4 v192, s[44:45] offset:2048 sc1
	v_rcp_f32_e32 v203, v203
	v_fma_f32 v202, v202, 2.0, -1.0
	v_mul_f32_e32 v217, v213, v201
	v_fmac_f32_e32 v85, v230, v238
	ds_read_b128 v[236:239], v248 offset:96
	ds_read_b64 v[240:241], v248 offset:128
	s_waitcnt lgkmcnt(10)
	v_mfma_f32_32x32x16_f16 v[0:15], a[80:83], v[160:163], v[0:15]
	ds_read_b128 v[160:163], v192 offset:49152
	v_fma_f32 v203, v203, 2.0, -1.0
	v_mul_f32_e32 v218, v214, v202
	v_exp_f32_e32 v200, v112
	s_waitcnt lgkmcnt(8)
	v_fma_f32 v70, v229, v243, v246
	v_mfma_f32_32x32x16_f16 v[16:31], a[80:83], v[164:167], v[16:31]
	ds_read_b128 v[164:167], v192 offset:50176
	v_mul_f32_e32 v219, v215, v203
	v_cvt_pk_f16_f32 v220, v216, v217
	v_exp_f32_e32 v201, v113
	v_fma_f32 v71, v229, v245, v247
	v_fmac_f32_e32 v70, v228, v242
	s_waitcnt lgkmcnt(8)
	v_mfma_f32_32x32x16_f16 v[0:15], a[84:87], v[168:171], v[0:15]
	ds_read_b128 v[168:171], v192 offset:51200
	v_cvt_pk_f16_f32 v221, v218, v219
	v_exp_f32_e32 v202, v114
	v_add_f32_e32 v200, 1.0, v200
	v_fmac_f32_e32 v71, v228, v244
	v_fma_f32 v86, v231, v243, v246
	v_mfma_f32_32x32x16_f16 v[16:31], a[84:87], v[172:175], v[16:31]
	ds_read_b128 v[172:175], v192 offset:52224
	global_load_lds_dwordx4 v192, s[44:45] offset:3072 sc1
	v_exp_f32_e32 v203, v115
	v_add_f32_e32 v201, 1.0, v201
	v_add_f32_e32 v202, 1.0, v202
	v_fma_f32 v87, v231, v245, v247
	v_fmac_f32_e32 v86, v230, v242
	s_waitcnt lgkmcnt(8)
	v_mfma_f32_32x32x16_f16 v[0:15], a[88:91], v[176:179], v[0:15]
	ds_read_b128 v[176:179], v192 offset:53248
	v_exp_f32_e32 v204, v116
	v_add_f32_e32 v203, 1.0, v203
	v_fmac_f32_e32 v87, v230, v244
	ds_read_b128 v[242:245], v248 offset:112
	ds_read_b64 v[246:247], v248 offset:136
	v_mfma_f32_32x32x16_f16 v[16:31], a[88:91], v[180:183], v[16:31]
	ds_read_b128 v[180:183], v192 offset:54272
	v_exp_f32_e32 v205, v117
	v_add_f32_e32 v204, 1.0, v204
	s_waitcnt lgkmcnt(8)
	v_fma_f32 v72, v229, v237, v240
	v_mfma_f32_32x32x16_f16 v[0:15], a[92:95], v[184:187], v[0:15]
	ds_read_b128 v[184:187], v192 offset:55296
	v_exp_f32_e32 v206, v118
	v_add_f32_e32 v205, 1.0, v205
	v_fma_f32 v73, v229, v239, v241
	v_fmac_f32_e32 v72, v228, v236
	v_mfma_f32_32x32x16_f16 v[16:31], a[92:95], v[188:191], v[16:31]
	ds_read_b128 v[188:191], v192 offset:56320
	s_add_u32 s44, s34, 0x19000
	s_addc_u32 s45, s35, 0
	s_mov_b32 m0, s59
	s_nop 0
	global_load_lds_dwordx4 v192, s[44:45] sc1
	s_lshl_b32 s64, s71, 3
	s_add_u32 s64, s64, s29
	s_lshl_b32 s64, s64, 7
	s_add_u32 s38, s8, s64
	s_addc_u32 s39, s9, 0
	global_load_dword v251, v196, s[38:39] sc1
	v_exp_f32_e32 v207, v119
	v_add_f32_e32 v206, 1.0, v206
	v_fmac_f32_e32 v73, v228, v238
	v_fma_f32 v88, v231, v237, v240
	s_waitcnt lgkmcnt(8)
	v_mfma_f32_32x32x16_f16 v[0:15], a[96:99], v[160:163], v[0:15]
	ds_read_b128 v[160:163], v192 offset:57344
	v_exp_f32_e32 v208, v120
	v_add_f32_e32 v207, 1.0, v207
	v_fma_f32 v89, v231, v239, v241
	v_fmac_f32_e32 v88, v230, v236
	v_mfma_f32_32x32x16_f16 v[16:31], a[96:99], v[164:167], v[16:31]
	ds_read_b128 v[164:167], v192 offset:58368
	v_exp_f32_e32 v209, v121
	v_add_f32_e32 v208, 1.0, v208
	v_fmac_f32_e32 v89, v230, v238
	ds_read_b128 v[236:239], v248 offset:144
	ds_read_b64 v[240:241], v248 offset:176
	s_waitcnt lgkmcnt(10)
	v_mfma_f32_32x32x16_f16 v[0:15], a[100:103], v[168:171], v[0:15]
	ds_read_b128 v[168:171], v192 offset:59392
	v_exp_f32_e32 v210, v122
	v_add_f32_e32 v209, 1.0, v209
	s_waitcnt lgkmcnt(8)
	v_fma_f32 v74, v229, v243, v246
	v_mfma_f32_32x32x16_f16 v[16:31], a[100:103], v[172:175], v[16:31]
	ds_read_b128 v[172:175], v192 offset:60416
	global_load_lds_dwordx4 v192, s[44:45] offset:1024 sc1
	v_exp_f32_e32 v211, v123
	v_add_f32_e32 v210, 1.0, v210
	v_fma_f32 v75, v229, v245, v247
	v_fmac_f32_e32 v74, v228, v242
	s_waitcnt lgkmcnt(8)
	v_mfma_f32_32x32x16_f16 v[0:15], a[104:107], v[176:179], v[0:15]
	ds_read_b128 v[176:179], v192 offset:61440
	v_exp_f32_e32 v212, v124
	v_add_f32_e32 v211, 1.0, v211
	v_fmac_f32_e32 v75, v228, v244
	v_fma_f32 v90, v231, v243, v246
	v_mfma_f32_32x32x16_f16 v[16:31], a[104:107], v[180:183], v[16:31]
	ds_read_b128 v[180:183], v192 offset:62464
	v_exp_f32_e32 v213, v125
	v_add_f32_e32 v212, 1.0, v212
	v_fma_f32 v91, v231, v245, v247
	v_fmac_f32_e32 v90, v230, v242
	s_waitcnt lgkmcnt(8)
	v_mfma_f32_32x32x16_f16 v[0:15], a[108:111], v[184:187], v[0:15]
	ds_read_b128 v[184:187], v192 offset:63488
	v_exp_f32_e32 v214, v126
	v_add_f32_e32 v213, 1.0, v213
	v_fmac_f32_e32 v91, v230, v244
	ds_read_b128 v[242:245], v248 offset:160
	ds_read_b64 v[246:247], v248 offset:184
	v_mfma_f32_32x32x16_f16 v[16:31], a[108:111], v[188:191], v[16:31]
	ds_read_b128 v[188:191], v192 offset:64512
	global_load_lds_dwordx4 v192, s[44:45] offset:2048 sc1
	v_exp_f32_e32 v215, v127
	v_add_f32_e32 v214, 1.0, v214
	s_waitcnt lgkmcnt(8)
	v_fma_f32 v76, v229, v237, v240
	s_waitcnt vmcnt(8)
	s_barrier
	v_mfma_f32_32x32x16_f16 v[0:15], a[112:115], v[160:163], v[0:15]
	ds_read_b128 v[160:163], v193 offset:0
	v_add_f32_e32 v215, 1.0, v215
	v_rcp_f32_e32 v200, v200
	v_fma_f32 v77, v229, v239, v241
	v_fmac_f32_e32 v76, v228, v236
	v_mfma_f32_32x32x16_f16 v[16:31], a[112:115], v[164:167], v[16:31]
	ds_read_b128 v[164:167], v193 offset:1024
	v_rcp_f32_e32 v201, v201
	v_fmac_f32_e32 v77, v228, v238
	v_fma_f32 v92, v231, v237, v240
	s_waitcnt lgkmcnt(8)
	v_mfma_f32_32x32x16_f16 v[0:15], a[116:119], v[168:171], v[0:15]
	ds_read_b128 v[168:171], v193 offset:2048
	v_rcp_f32_e32 v202, v202
	v_fma_f32 v93, v231, v239, v241
	v_fmac_f32_e32 v92, v230, v236
	v_mfma_f32_32x32x16_f16 v[16:31], a[116:119], v[172:175], v[16:31]
	ds_read_b128 v[172:175], v193 offset:3072
	global_load_lds_dwordx4 v192, s[44:45] offset:3072 sc1
	v_rcp_f32_e32 v203, v203
	v_fmac_f32_e32 v93, v230, v238
	s_waitcnt lgkmcnt(5)
	v_mfma_f32_32x32x16_f16 v[0:15], a[120:123], v[176:179], v[0:15]
	ds_read_b128 v[176:179], v193 offset:4096
	v_rcp_f32_e32 v204, v204
	v_fma_f32 v78, v229, v243, v246
	v_fma_f32 v79, v229, v245, v247
	v_mfma_f32_32x32x16_f16 v[16:31], a[120:123], v[180:183], v[16:31]
	ds_read_b128 v[180:183], v193 offset:5120
	v_rcp_f32_e32 v205, v205
	v_mul_f32_e32 v204, v204, v156
	v_fmac_f32_e32 v78, v228, v242
	v_fmac_f32_e32 v79, v228, v244
	s_waitcnt lgkmcnt(6)
	v_mfma_f32_32x32x16_f16 v[0:15], a[124:127], v[184:187], v[0:15]
	ds_read_b128 v[184:187], v193 offset:6144
	v_rcp_f32_e32 v206, v206
	v_mul_f32_e32 v205, v205, v157
	v_fma_f32 v94, v231, v243, v246
	v_fma_f32 v95, v231, v245, v247
	v_mfma_f32_32x32x16_f16 v[16:31], a[124:127], v[188:191], v[16:31]
	ds_read_b128 v[188:191], v193 offset:7168
	s_waitcnt vmcnt(3)
	v_cmp_gt_u32_e32 vcc, 2, v251
	s_cbranch_vccz .LE_tok20

.LE_tok20:
	s_and_b32 s64, s71, 1
	s_lshl_b32 s64, s64, 22
	s_add_u32 s64, s64, s49
	s_add_u32 s64, s64, 0x20000
	s_add_u32 s34, s6, s64
	s_addc_u32 s35, s7, 0
	s_add_u32 s44, s34, 0x0
	s_addc_u32 s45, s35, 0
	s_mov_b32 m0, s52
	s_nop 0
	global_load_lds_dwordx4 v192, s[44:45] sc1
	v_rcp_f32_e32 v207, v207
	v_mul_f32_e32 v206, v206, v158
	v_fmac_f32_e32 v94, v230, v242
	v_fmac_f32_e32 v95, v230, v244
	s_waitcnt lgkmcnt(6)
	v_mfma_f32_32x32x16_f16 v[0:15], a[128:131], v[160:163], v[0:15]
	ds_read_b128 v[160:163], v193 offset:8192
	v_rcp_f32_e32 v208, v208
	v_mul_f32_e32 v207, v207, v159
	v_mfma_f32_32x32x16_f16 v[16:31], a[128:131], v[164:167], v[16:31]
	ds_read_b128 v[164:167], v193 offset:9216
	v_rcp_f32_e32 v209, v209
	v_fmamk_f32 v208, v208, 0xc0b8aa3b, v198
	s_waitcnt lgkmcnt(6)
	v_mfma_f32_32x32x16_f16 v[0:15], a[132:135], v[168:171], v[0:15]
	ds_read_b128 v[168:171], v193 offset:10240
	v_rcp_f32_e32 v210, v210
	v_fmamk_f32 v209, v209, 0xc0b8aa3b, v198
	v_fma_f32 v156, v200, v208, v204
	v_mfma_f32_32x32x16_f16 v[16:31], a[132:135], v[172:175], v[16:31]
	ds_read_b128 v[172:175], v193 offset:11264
	global_load_lds_dwordx4 v192, s[44:45] offset:1024 sc1
	v_rcp_f32_e32 v211, v211
	v_fmamk_f32 v210, v210, 0xc0b8aa3b, v198
	v_fma_f32 v157, v201, v209, v205
	s_waitcnt lgkmcnt(6)
	v_mfma_f32_32x32x16_f16 v[0:15], a[136:139], v[176:179], v[0:15]
	ds_read_b128 v[176:179], v193 offset:12288
	v_rcp_f32_e32 v212, v212
	v_fmamk_f32 v211, v211, 0xc0b8aa3b, v198
	v_fma_f32 v158, v202, v210, v206
	v_mfma_f32_32x32x16_f16 v[16:31], a[136:139], v[180:183], v[16:31]
	ds_read_b128 v[180:183], v193 offset:13312
	v_rcp_f32_e32 v213, v213
	v_fma_f32 v159, v203, v211, v207
	s_waitcnt lgkmcnt(6)
	v_mfma_f32_32x32x16_f16 v[0:15], a[140:143], v[184:187], v[0:15]
	ds_read_b128 v[184:187], v193 offset:14336
	v_rcp_f32_e32 v214, v214
	v_mfma_f32_32x32x16_f16 v[16:31], a[140:143], v[188:191], v[16:31]
	ds_read_b128 v[188:191], v193 offset:15360
	global_load_lds_dwordx4 v192, s[44:45] offset:2048 sc1
	v_rcp_f32_e32 v215, v215
	s_waitcnt lgkmcnt(6)
	v_mfma_f32_32x32x16_f16 v[0:15], a[144:147], v[160:163], v[0:15]
	ds_read_b128 v[160:163], v193 offset:16384
	v_exp_f32_e32 v200, v156
	v_mfma_f32_32x32x16_f16 v[16:31], a[144:147], v[164:167], v[16:31]
	ds_read_b128 v[164:167], v193 offset:17408
	v_exp_f32_e32 v201, v157
	v_add_f32_e32 v200, 1.0, v200
	s_waitcnt lgkmcnt(6)
	v_mfma_f32_32x32x16_f16 v[0:15], a[148:151], v[168:171], v[0:15]
	ds_read_b128 v[168:171], v193 offset:18432
	v_exp_f32_e32 v202, v158
	v_add_f32_e32 v201, 1.0, v201
	v_mfma_f32_32x32x16_f16 v[16:31], a[148:151], v[172:175], v[16:31]
	ds_read_b128 v[172:175], v193 offset:19456
	global_load_lds_dwordx4 v192, s[44:45] offset:3072 sc1
	v_exp_f32_e32 v203, v159
	v_add_f32_e32 v202, 1.0, v202
	s_waitcnt lgkmcnt(6)
	v_mfma_f32_32x32x16_f16 v[0:15], a[152:155], v[176:179], v[0:15]
	ds_read_b128 v[176:179], v193 offset:20480
	v_add_f32_e32 v203, 1.0, v203
	v_rcp_f32_e32 v200, v200
	v_mfma_f32_32x32x16_f16 v[16:31], a[152:155], v[180:183], v[16:31]
	ds_read_b128 v[180:183], v193 offset:21504
	v_rcp_f32_e32 v201, v201
	v_fma_f32 v200, v200, 2.0, -1.0
	s_waitcnt lgkmcnt(6)
	v_mfma_f32_32x32x16_f16 v[0:15], a[156:159], v[184:187], v[0:15]
	ds_read_b128 v[184:187], v193 offset:22528
	v_rcp_f32_e32 v202, v202
	v_fma_f32 v201, v201, 2.0, -1.0
	v_mul_f32_e32 v216, v212, v200
	v_mfma_f32_32x32x16_f16 v[16:31], a[156:159], v[188:191], v[16:31]
	ds_read_b128 v[188:191], v193 offset:23552
	s_add_u32 s44, s34, 0x1000
	s_addc_u32 s45, s35, 0
	s_mov_b32 m0, s53
	s_nop 0
	global_load_lds_dwordx4 v192, s[44:45] sc1
	v_rcp_f32_e32 v203, v203
	v_fma_f32 v202, v202, 2.0, -1.0
	v_mul_f32_e32 v217, v213, v201
	s_waitcnt lgkmcnt(6)
	v_mfma_f32_32x32x16_f16 v[0:15], a[160:163], v[160:163], v[0:15]
	ds_read_b128 v[160:163], v193 offset:24576
	v_fma_f32 v203, v203, 2.0, -1.0
	v_mul_f32_e32 v218, v214, v202
	v_mfma_f32_32x32x16_f16 v[16:31], a[160:163], v[164:167], v[16:31]
	ds_read_b128 v[164:167], v193 offset:25600
	v_mul_f32_e32 v219, v215, v203
	v_cvt_pk_f16_f32 v222, v216, v217
	s_waitcnt lgkmcnt(6)
	v_mfma_f32_32x32x16_f16 v[0:15], a[164:167], v[168:171], v[0:15]
	ds_read_b128 v[168:171], v193 offset:26624
	v_cvt_pk_f16_f32 v223, v218, v219
	v_mfma_f32_32x32x16_f16 v[16:31], a[164:167], v[172:175], v[16:31]
	ds_read_b128 v[172:175], v193 offset:27648
	global_load_lds_dwordx4 v192, s[44:45] offset:1024 sc1
	s_nop 1
	v_permlane32_swap_b32_e32 v220, v222
	v_permlane32_swap_b32_e32 v221, v223
	s_cmp_eq_u32 s31, 0
	s_cbranch_scc1 .LE_slow22
	global_store_dwordx4 v195, v[220:223], s[36:37] offset:0
	s_branch .LE_join23

.LE_join23:
	s_waitcnt lgkmcnt(6)
	v_mfma_f32_32x32x16_f16 v[0:15], a[168:171], v[176:179], v[0:15]
	ds_read_b128 v[176:179], v193 offset:28672
	v_mfma_f32_32x32x16_f16 v[16:31], a[168:171], v[180:183], v[16:31]
	ds_read_b128 v[180:183], v193 offset:29696
	s_waitcnt lgkmcnt(6)
	v_mfma_f32_32x32x16_f16 v[0:15], a[172:175], v[184:187], v[0:15]
	ds_read_b128 v[184:187], v193 offset:30720
	v_mfma_f32_32x32x16_f16 v[16:31], a[172:175], v[188:191], v[16:31]
	ds_read_b128 v[188:191], v193 offset:31744
	global_load_lds_dwordx4 v192, s[44:45] offset:2048 sc1
	s_waitcnt vmcnt(8)
	s_barrier
	s_waitcnt lgkmcnt(6)
	v_mfma_f32_32x32x16_f16 v[0:15], a[176:179], v[160:163], v[0:15]
	ds_read_b128 v[160:163], v193 offset:32768
	v_mfma_f32_32x32x16_f16 v[16:31], a[176:179], v[164:167], v[16:31]
	ds_read_b128 v[164:167], v193 offset:33792
	s_waitcnt lgkmcnt(6)
	v_mfma_f32_32x32x16_f16 v[0:15], a[180:183], v[168:171], v[0:15]
	ds_read_b128 v[168:171], v193 offset:34816
	v_mfma_f32_32x32x16_f16 v[16:31], a[180:183], v[172:175], v[16:31]
	ds_read_b128 v[172:175], v193 offset:35840
	global_load_lds_dwordx4 v192, s[44:45] offset:3072 sc1
	s_waitcnt lgkmcnt(6)
	v_mfma_f32_32x32x16_f16 v[0:15], a[184:187], v[176:179], v[0:15]
	ds_read_b128 v[176:179], v193 offset:36864
	v_mfma_f32_32x32x16_f16 v[16:31], a[184:187], v[180:183], v[16:31]
	ds_read_b128 v[180:183], v193 offset:37888
	s_waitcnt lgkmcnt(6)
	v_mfma_f32_32x32x16_f16 v[0:15], a[188:191], v[184:187], v[0:15]
	ds_read_b128 v[184:187], v193 offset:38912
	v_mfma_f32_32x32x16_f16 v[16:31], a[188:191], v[188:191], v[16:31]
	ds_read_b128 v[188:191], v193 offset:39936
	s_add_u32 s44, s34, 0x8000
	s_addc_u32 s45, s35, 0
	s_mov_b32 m0, s54
	s_nop 0
	global_load_lds_dwordx4 v192, s[44:45] sc1
	s_waitcnt lgkmcnt(6)
	v_mfma_f32_32x32x16_f16 v[0:15], a[192:195], v[160:163], v[0:15]
	ds_read_b128 v[160:163], v193 offset:40960
	s_waitcnt vmcnt(3)
	s_barrier
	v_mov_b32_e32 v199, 4
	s_cmp_eq_u32 s31, 0
	s_cbranch_scc1 .LE_slow24
	global_store_dword v197, v199, s[40:41]
	s_branch .LE_join25

.LE_join25:
	v_mfma_f32_32x32x16_f16 v[16:31], a[192:195], v[164:167], v[16:31]
	ds_read_b128 v[164:167], v193 offset:41984
	s_waitcnt lgkmcnt(6)
	v_mfma_f32_32x32x16_f16 v[0:15], a[196:199], v[168:171], v[0:15]
	ds_read_b128 v[168:171], v193 offset:43008
	v_mfma_f32_32x32x16_f16 v[16:31], a[196:199], v[172:175], v[16:31]
	ds_read_b128 v[172:175], v193 offset:44032
	global_load_lds_dwordx4 v192, s[44:45] offset:1024 sc1
	s_waitcnt lgkmcnt(6)
	v_mfma_f32_32x32x16_f16 v[0:15], a[200:203], v[176:179], v[0:15]
	ds_read_b128 v[176:179], v193 offset:45056
	v_mfma_f32_32x32x16_f16 v[16:31], a[200:203], v[180:183], v[16:31]
	ds_read_b128 v[180:183], v193 offset:46080
	s_waitcnt lgkmcnt(6)
	v_mfma_f32_32x32x16_f16 v[0:15], a[204:207], v[184:187], v[0:15]
	ds_read_b128 v[184:187], v193 offset:47104
	v_mfma_f32_32x32x16_f16 v[16:31], a[204:207], v[188:191], v[16:31]
	ds_read_b128 v[188:191], v193 offset:48128
	global_load_lds_dwordx4 v192, s[44:45] offset:2048 sc1
	s_waitcnt lgkmcnt(6)
	v_mfma_f32_32x32x16_f16 v[0:15], a[208:211], v[160:163], v[0:15]
	ds_read_b128 v[160:163], v193 offset:49152
	v_mfma_f32_32x32x16_f16 v[16:31], a[208:211], v[164:167], v[16:31]
	ds_read_b128 v[164:167], v193 offset:50176
	s_waitcnt lgkmcnt(6)
	v_mfma_f32_32x32x16_f16 v[0:15], a[212:215], v[168:171], v[0:15]
	ds_read_b128 v[168:171], v193 offset:51200
	v_mfma_f32_32x32x16_f16 v[16:31], a[212:215], v[172:175], v[16:31]
	ds_read_b128 v[172:175], v193 offset:52224
	global_load_lds_dwordx4 v192, s[44:45] offset:3072 sc1
	s_waitcnt lgkmcnt(6)
	v_mfma_f32_32x32x16_f16 v[0:15], a[216:219], v[176:179], v[0:15]
	ds_read_b128 v[176:179], v193 offset:53248
	v_mfma_f32_32x32x16_f16 v[16:31], a[216:219], v[180:183], v[16:31]
	ds_read_b128 v[180:183], v193 offset:54272
	s_waitcnt lgkmcnt(6)
	v_mfma_f32_32x32x16_f16 v[0:15], a[220:223], v[184:187], v[0:15]
	ds_read_b128 v[184:187], v193 offset:55296
	v_mfma_f32_32x32x16_f16 v[16:31], a[220:223], v[188:191], v[16:31]
	ds_read_b128 v[188:191], v193 offset:56320
	s_add_u32 s44, s34, 0x9000
	s_addc_u32 s45, s35, 0
	s_mov_b32 m0, s55
	s_nop 0
	global_load_lds_dwordx4 v192, s[44:45] sc1
	s_waitcnt lgkmcnt(6)
	v_mfma_f32_32x32x16_f16 v[0:15], a[224:227], v[160:163], v[0:15]
	ds_read_b128 v[160:163], v193 offset:57344
	v_mfma_f32_32x32x16_f16 v[16:31], a[224:227], v[164:167], v[16:31]
	ds_read_b128 v[164:167], v193 offset:58368
	s_waitcnt lgkmcnt(6)
	v_mfma_f32_32x32x16_f16 v[0:15], a[228:231], v[168:171], v[0:15]
	ds_read_b128 v[168:171], v193 offset:59392
	v_mfma_f32_32x32x16_f16 v[16:31], a[228:231], v[172:175], v[16:31]
	ds_read_b128 v[172:175], v193 offset:60416
	global_load_lds_dwordx4 v192, s[44:45] offset:1024 sc1
	s_waitcnt lgkmcnt(6)
	v_mfma_f32_32x32x16_f16 v[0:15], a[232:235], v[176:179], v[0:15]
	ds_read_b128 v[176:179], v193 offset:61440
	v_mfma_f32_32x32x16_f16 v[16:31], a[232:235], v[180:183], v[16:31]
	ds_read_b128 v[180:183], v193 offset:62464
	s_waitcnt lgkmcnt(6)
	v_mfma_f32_32x32x16_f16 v[0:15], a[236:239], v[184:187], v[0:15]
	ds_read_b128 v[184:187], v193 offset:63488
	v_mfma_f32_32x32x16_f16 v[16:31], a[236:239], v[188:191], v[16:31]
	ds_read_b128 v[188:191], v193 offset:64512
	global_load_lds_dwordx4 v192, s[44:45] offset:2048 sc1
	s_waitcnt vmcnt(8)
	s_barrier
	s_waitcnt lgkmcnt(6)
	v_mfma_f32_32x32x16_f16 v[0:15], a[240:243], v[160:163], v[0:15]
	ds_read_b128 v[160:163], v192 offset:0
	v_mfma_f32_32x32x16_f16 v[16:31], a[240:243], v[164:167], v[16:31]
	ds_read_b128 v[164:167], v192 offset:1024
	s_waitcnt lgkmcnt(6)
	v_mfma_f32_32x32x16_f16 v[0:15], a[244:247], v[168:171], v[0:15]
	ds_read_b128 v[168:171], v192 offset:2048
	v_mfma_f32_32x32x16_f16 v[16:31], a[244:247], v[172:175], v[16:31]
	ds_read_b128 v[172:175], v192 offset:3072
	global_load_lds_dwordx4 v192, s[44:45] offset:3072 sc1
	s_waitcnt lgkmcnt(6)
	v_mfma_f32_32x32x16_f16 v[0:15], a[248:251], v[176:179], v[0:15]
	ds_read_b128 v[176:179], v192 offset:4096
	v_mfma_f32_32x32x16_f16 v[16:31], a[248:251], v[180:183], v[16:31]
	ds_read_b128 v[180:183], v192 offset:5120
	s_waitcnt lgkmcnt(6)
	v_mfma_f32_32x32x16_f16 v[0:15], a[252:255], v[184:187], v[0:15]
	ds_read_b128 v[184:187], v192 offset:6144
	v_mfma_f32_32x32x16_f16 v[16:31], a[252:255], v[188:191], v[16:31]
	ds_read_b128 v[188:191], v192 offset:7168
	s_add_u32 s44, s34, 0x10000
	s_addc_u32 s45, s35, 0
	s_mov_b32 m0, s56
	s_nop 0
	global_load_lds_dwordx4 v192, s[44:45] sc1
	s_and_b32 s64, s33, 1
	s_lshl_b32 s64, s64, 22
	s_add_u32 s64, s64, s50
	s_add_u32 s36, s6, s64
	s_addc_u32 s37, s7, 0
	s_lshl_b32 s64, s33, 3
	s_add_u32 s64, s64, s29
	s_lshl_b32 s64, s64, 5
	s_add_u32 s64, s64, s30
	s_lshl_b32 s64, s64, 2
	s_add_u32 s40, s8, s64
	s_addc_u32 s41, s9, 0
	s_lshl_b32 s64, s33, 11
	s_lshl_b32 s65, s29, 8
	s_add_u32 s64, s64, s65
	s_add_u32 s64, s64, 192
	s_lshl_b32 s64, s64, 3
	s_add_u32 s42, s12, s64
	s_addc_u32 s43, s13, 0
	s_nop 11
	global_load_dwordx2 v[228:229], v249, s[42:43] offset:0
	global_load_dwordx2 v[230:231], v249, s[42:43] offset:256
	s_waitcnt lgkmcnt(6)
	v_mfma_f32_32x32x16_f16 v[32:47], a[0:3], v[160:163], v[32:47]
	ds_read_b128 v[160:163], v192 offset:8192
	v_exp_f32_e32 v200, v0
	v_mfma_f32_32x32x16_f16 v[48:63], a[0:3], v[164:167], v[48:63]
	ds_read_b128 v[164:167], v192 offset:9216
	v_exp_f32_e32 v201, v1
	v_add_f32_e32 v200, 1.0, v200
	s_waitcnt lgkmcnt(6)
	v_mfma_f32_32x32x16_f16 v[32:47], a[4:7], v[168:171], v[32:47]
	ds_read_b128 v[168:171], v192 offset:10240
	v_exp_f32_e32 v202, v2
	v_add_f32_e32 v201, 1.0, v201
	v_mfma_f32_32x32x16_f16 v[48:63], a[4:7], v[172:175], v[48:63]
	ds_read_b128 v[172:175], v192 offset:11264
	global_load_lds_dwordx4 v192, s[44:45] offset:1024 sc1
	v_exp_f32_e32 v203, v3
	v_add_f32_e32 v202, 1.0, v202
	s_waitcnt lgkmcnt(6)
	v_mfma_f32_32x32x16_f16 v[32:47], a[8:11], v[176:179], v[32:47]
	ds_read_b128 v[176:179], v192 offset:12288
	v_exp_f32_e32 v204, v4
	v_add_f32_e32 v203, 1.0, v203
	v_mfma_f32_32x32x16_f16 v[48:63], a[8:11], v[180:183], v[48:63]
	ds_read_b128 v[180:183], v192 offset:13312
	v_exp_f32_e32 v205, v5
	v_add_f32_e32 v204, 1.0, v204
	s_waitcnt lgkmcnt(6)
	v_mfma_f32_32x32x16_f16 v[32:47], a[12:15], v[184:187], v[32:47]
	ds_read_b128 v[184:187], v192 offset:14336
	v_exp_f32_e32 v206, v6
	v_add_f32_e32 v205, 1.0, v205
	v_mfma_f32_32x32x16_f16 v[48:63], a[12:15], v[188:191], v[48:63]
	ds_read_b128 v[188:191], v192 offset:15360
	global_load_lds_dwordx4 v192, s[44:45] offset:2048 sc1
	v_exp_f32_e32 v207, v7
	v_add_f32_e32 v206, 1.0, v206
	s_waitcnt lgkmcnt(6)
	v_mfma_f32_32x32x16_f16 v[32:47], a[16:19], v[160:163], v[32:47]
	ds_read_b128 v[160:163], v192 offset:16384
	v_exp_f32_e32 v208, v8
	v_add_f32_e32 v207, 1.0, v207
	v_mfma_f32_32x32x16_f16 v[48:63], a[16:19], v[164:167], v[48:63]
	ds_read_b128 v[164:167], v192 offset:17408
	v_exp_f32_e32 v209, v9
	v_add_f32_e32 v208, 1.0, v208
	s_waitcnt lgkmcnt(6)
	v_mfma_f32_32x32x16_f16 v[32:47], a[20:23], v[168:171], v[32:47]
	ds_read_b128 v[168:171], v192 offset:18432
	v_exp_f32_e32 v210, v10
	v_add_f32_e32 v209, 1.0, v209
	v_mfma_f32_32x32x16_f16 v[48:63], a[20:23], v[172:175], v[48:63]
	ds_read_b128 v[172:175], v192 offset:19456
	global_load_lds_dwordx4 v192, s[44:45] offset:3072 sc1
	v_exp_f32_e32 v211, v11
	v_add_f32_e32 v210, 1.0, v210
	s_waitcnt lgkmcnt(6)
	v_mfma_f32_32x32x16_f16 v[32:47], a[24:27], v[176:179], v[32:47]
	ds_read_b128 v[176:179], v192 offset:20480
	v_exp_f32_e32 v212, v12
	v_add_f32_e32 v211, 1.0, v211
	v_mfma_f32_32x32x16_f16 v[48:63], a[24:27], v[180:183], v[48:63]
	ds_read_b128 v[180:183], v192 offset:21504
	v_exp_f32_e32 v213, v13
	v_add_f32_e32 v212, 1.0, v212
	s_waitcnt lgkmcnt(6)
	v_mfma_f32_32x32x16_f16 v[32:47], a[28:31], v[184:187], v[32:47]
	ds_read_b128 v[184:187], v192 offset:22528
	v_exp_f32_e32 v214, v14
	v_add_f32_e32 v213, 1.0, v213
	v_mfma_f32_32x32x16_f16 v[48:63], a[28:31], v[188:191], v[48:63]
	ds_read_b128 v[188:191], v192 offset:23552
	s_add_u32 s44, s34, 0x11000
	s_addc_u32 s45, s35, 0
	s_mov_b32 m0, s57
	s_nop 0
	global_load_lds_dwordx4 v192, s[44:45] sc1
	v_exp_f32_e32 v215, v15
	v_add_f32_e32 v214, 1.0, v214
	s_waitcnt lgkmcnt(6)
	v_mfma_f32_32x32x16_f16 v[32:47], a[32:35], v[160:163], v[32:47]
	ds_read_b128 v[160:163], v192 offset:24576
	v_add_f32_e32 v215, 1.0, v215
	v_rcp_f32_e32 v200, v200
	v_mfma_f32_32x32x16_f16 v[48:63], a[32:35], v[164:167], v[48:63]
	ds_read_b128 v[164:167], v192 offset:25600
	v_rcp_f32_e32 v201, v201
	s_waitcnt lgkmcnt(6)
	v_mfma_f32_32x32x16_f16 v[32:47], a[36:39], v[168:171], v[32:47]
	ds_read_b128 v[168:171], v192 offset:26624
	v_rcp_f32_e32 v202, v202
	v_mfma_f32_32x32x16_f16 v[48:63], a[36:39], v[172:175], v[48:63]
	ds_read_b128 v[172:175], v192 offset:27648
	global_load_lds_dwordx4 v192, s[44:45] offset:1024 sc1
	v_rcp_f32_e32 v203, v203
	s_waitcnt lgkmcnt(6)
	v_mfma_f32_32x32x16_f16 v[32:47], a[40:43], v[176:179], v[32:47]
	ds_read_b128 v[176:179], v192 offset:28672
	v_rcp_f32_e32 v204, v204
	v_mfma_f32_32x32x16_f16 v[48:63], a[40:43], v[180:183], v[48:63]
	ds_read_b128 v[180:183], v192 offset:29696
	v_rcp_f32_e32 v205, v205
	v_mul_f32_e32 v204, v204, v128
	s_waitcnt lgkmcnt(6)
	v_mfma_f32_32x32x16_f16 v[32:47], a[44:47], v[184:187], v[32:47]
	ds_read_b128 v[184:187], v192 offset:30720
	v_rcp_f32_e32 v206, v206
	v_mul_f32_e32 v205, v205, v129
	v_mfma_f32_32x32x16_f16 v[48:63], a[44:47], v[188:191], v[48:63]
	ds_read_b128 v[188:191], v192 offset:31744
	global_load_lds_dwordx4 v192, s[44:45] offset:2048 sc1
	v_rcp_f32_e32 v207, v207
	v_mul_f32_e32 v206, v206, v130
	s_waitcnt vmcnt(9)
	s_barrier
	s_waitcnt lgkmcnt(6)
	v_mfma_f32_32x32x16_f16 v[32:47], a[48:51], v[160:163], v[32:47]
	ds_read_b128 v[160:163], v192 offset:32768
	v_rcp_f32_e32 v208, v208
	v_mul_f32_e32 v207, v207, v131
	ds_read_b128 v[236:239], v248 offset:0
	ds_read_b64 v[240:241], v248 offset:32
	ds_read_b128 v[242:245], v248 offset:16
	ds_read_b64 v[246:247], v248 offset:40
	v_mfma_f32_32x32x16_f16 v[48:63], a[48:51], v[164:167], v[48:63]
	ds_read_b128 v[164:167], v192 offset:33792
	v_rcp_f32_e32 v209, v209
	v_fmamk_f32 v208, v208, 0xc0b8aa3b, v198
	s_waitcnt lgkmcnt(3)
	s_waitcnt vmcnt(6)
	v_fma_f32 v96, v229, v237, v240
	v_mfma_f32_32x32x16_f16 v[32:47], a[52:55], v[168:171], v[32:47]
	ds_read_b128 v[168:171], v192 offset:34816
	v_rcp_f32_e32 v210, v210
	v_fmamk_f32 v209, v209, 0xc0b8aa3b, v198
	v_fma_f32 v128, v200, v208, v204
	v_fma_f32 v97, v229, v239, v241
	v_fmac_f32_e32 v96, v228, v236
	v_mfma_f32_32x32x16_f16 v[48:63], a[52:55], v[172:175], v[48:63]
	ds_read_b128 v[172:175], v192 offset:35840
	global_load_lds_dwordx4 v192, s[44:45] offset:3072 sc1
	v_rcp_f32_e32 v211, v211
	v_fmamk_f32 v210, v210, 0xc0b8aa3b, v198
	v_fma_f32 v129, v201, v209, v205
	v_fmac_f32_e32 v97, v228, v238
	v_fma_f32 v112, v231, v237, v240
	v_mfma_f32_32x32x16_f16 v[32:47], a[56:59], v[176:179], v[32:47]
	ds_read_b128 v[176:179], v192 offset:36864
	v_rcp_f32_e32 v212, v212
	v_fmamk_f32 v211, v211, 0xc0b8aa3b, v198
	v_fma_f32 v130, v202, v210, v206
	v_fma_f32 v113, v231, v239, v241
	v_fmac_f32_e32 v112, v230, v236
	v_mfma_f32_32x32x16_f16 v[48:63], a[56:59], v[180:183], v[48:63]
	ds_read_b128 v[180:183], v192 offset:37888
	v_rcp_f32_e32 v213, v213
	v_fma_f32 v131, v203, v211, v207
	v_fmac_f32_e32 v113, v230, v238
	ds_read_b128 v[236:239], v248 offset:48
	ds_read_b64 v[240:241], v248 offset:80
	v_mfma_f32_32x32x16_f16 v[32:47], a[60:63], v[184:187], v[32:47]
	ds_read_b128 v[184:187], v192 offset:38912
	v_rcp_f32_e32 v214, v214
	s_waitcnt lgkmcnt(8)
	v_fma_f32 v98, v229, v243, v246
	v_mfma_f32_32x32x16_f16 v[48:63], a[60:63], v[188:191], v[48:63]
	ds_read_b128 v[188:191], v192 offset:39936
	s_add_u32 s44, s34, 0x18000
	s_addc_u32 s45, s35, 0
	s_mov_b32 m0, s58
	s_nop 0
	global_load_lds_dwordx4 v192, s[44:45] sc1
	v_rcp_f32_e32 v215, v215
	v_fma_f32 v99, v229, v245, v247
	v_fmac_f32_e32 v98, v228, v242
	s_waitcnt lgkmcnt(8)
	v_mfma_f32_32x32x16_f16 v[32:47], a[64:67], v[160:163], v[32:47]
	ds_read_b128 v[160:163], v192 offset:40960
	v_exp_f32_e32 v200, v128
	v_fmac_f32_e32 v99, v228, v244
	v_fma_f32 v114, v231, v243, v246
	v_mfma_f32_32x32x16_f16 v[48:63], a[64:67], v[164:167], v[48:63]
	ds_read_b128 v[164:167], v192 offset:41984
	v_exp_f32_e32 v201, v129
	v_add_f32_e32 v200, 1.0, v200
	v_fma_f32 v115, v231, v245, v247
	v_fmac_f32_e32 v114, v230, v242
	s_waitcnt lgkmcnt(8)
	v_mfma_f32_32x32x16_f16 v[32:47], a[68:71], v[168:171], v[32:47]
	ds_read_b128 v[168:171], v192 offset:43008
	v_exp_f32_e32 v202, v130
	v_add_f32_e32 v201, 1.0, v201
	v_fmac_f32_e32 v115, v230, v244
	ds_read_b128 v[242:245], v248 offset:64
	ds_read_b64 v[246:247], v248 offset:88
	v_mfma_f32_32x32x16_f16 v[48:63], a[68:71], v[172:175], v[48:63]
	ds_read_b128 v[172:175], v192 offset:44032
	global_load_lds_dwordx4 v192, s[44:45] offset:1024 sc1
	v_exp_f32_e32 v203, v131
	v_add_f32_e32 v202, 1.0, v202
	s_waitcnt lgkmcnt(8)
	v_fma_f32 v100, v229, v237, v240
	v_mfma_f32_32x32x16_f16 v[32:47], a[72:75], v[176:179], v[32:47]
	ds_read_b128 v[176:179], v192 offset:45056
	v_add_f32_e32 v203, 1.0, v203
	v_rcp_f32_e32 v200, v200
	v_fma_f32 v101, v229, v239, v241
	v_fmac_f32_e32 v100, v228, v236
	v_mfma_f32_32x32x16_f16 v[48:63], a[72:75], v[180:183], v[48:63]
	ds_read_b128 v[180:183], v192 offset:46080
	v_rcp_f32_e32 v201, v201
	v_fma_f32 v200, v200, 2.0, -1.0
	v_fmac_f32_e32 v101, v228, v238
	v_fma_f32 v116, v231, v237, v240
	s_waitcnt lgkmcnt(8)
	v_mfma_f32_32x32x16_f16 v[32:47], a[76:79], v[184:187], v[32:47]
	ds_read_b128 v[184:187], v192 offset:47104
	v_rcp_f32_e32 v202, v202
	v_fma_f32 v201, v201, 2.0, -1.0
	v_mul_f32_e32 v216, v212, v200
	v_fma_f32 v117, v231, v239, v241
	v_fmac_f32_e32 v116, v230, v236
	v_mfma_f32_32x32x16_f16 v[48:63], a[76:79], v[188:191], v[48:63]
	ds_read_b128 v[188:191], v192 offset:48128
	global_load_lds_dwordx4 v192, s[44:45] offset:2048 sc1
	v_rcp_f32_e32 v203, v203
	v_fma_f32 v202, v202, 2.0, -1.0
	v_mul_f32_e32 v217, v213, v201
	v_fmac_f32_e32 v117, v230, v238
	ds_read_b128 v[236:239], v248 offset:96
	ds_read_b64 v[240:241], v248 offset:128
	s_waitcnt lgkmcnt(10)
	v_mfma_f32_32x32x16_f16 v[32:47], a[80:83], v[160:163], v[32:47]
	ds_read_b128 v[160:163], v192 offset:49152
	v_fma_f32 v203, v203, 2.0, -1.0
	v_mul_f32_e32 v218, v214, v202
	v_exp_f32_e32 v200, v16
	s_waitcnt lgkmcnt(8)
	v_fma_f32 v102, v229, v243, v246
	v_mfma_f32_32x32x16_f16 v[48:63], a[80:83], v[164:167], v[48:63]
	ds_read_b128 v[164:167], v192 offset:50176
	v_mul_f32_e32 v219, v215, v203
	v_cvt_pk_f16_f32 v220, v216, v217
	v_exp_f32_e32 v201, v17
	v_fma_f32 v103, v229, v245, v247
	v_fmac_f32_e32 v102, v228, v242
	s_waitcnt lgkmcnt(8)
	v_mfma_f32_32x32x16_f16 v[32:47], a[84:87], v[168:171], v[32:47]
	ds_read_b128 v[168:171], v192 offset:51200
	v_cvt_pk_f16_f32 v221, v218, v219
	v_exp_f32_e32 v202, v18
	v_add_f32_e32 v200, 1.0, v200
	v_fmac_f32_e32 v103, v228, v244
	v_fma_f32 v118, v231, v243, v246
	v_mfma_f32_32x32x16_f16 v[48:63], a[84:87], v[172:175], v[48:63]
	ds_read_b128 v[172:175], v192 offset:52224
	global_load_lds_dwordx4 v192, s[44:45] offset:3072 sc1
	s_cmp_lg_u32 s33, s60
	s_cbranch_scc1 .LE_nht26
	s_add_u32 s46, s62, 0x0
	s_addc_u32 s47, s63, 0
	global_store_dwordx4 v250, v[216:219], s[46:47]
	s_waitcnt vmcnt(0)
.LE_nht26:
	v_exp_f32_e32 v203, v19
	v_fma_f32 v119, v231, v245, v247
	v_fmac_f32_e32 v118, v230, v242
	s_waitcnt lgkmcnt(8)
	v_mfma_f32_32x32x16_f16 v[32:47], a[88:91], v[176:179], v[32:47]
	ds_read_b128 v[176:179], v192 offset:53248
	v_exp_f32_e32 v204, v20
	v_add_f32_e32 v201, 1.0, v201
	v_add_f32_e32 v202, 1.0, v202
	v_fmac_f32_e32 v119, v230, v244
	ds_read_b128 v[242:245], v248 offset:112
	ds_read_b64 v[246:247], v248 offset:136
	v_mfma_f32_32x32x16_f16 v[48:63], a[88:91], v[180:183], v[48:63]
	ds_read_b128 v[180:183], v192 offset:54272
	v_exp_f32_e32 v205, v21
	v_add_f32_e32 v203, 1.0, v203
	v_add_f32_e32 v204, 1.0, v204
	s_waitcnt lgkmcnt(8)
	v_fma_f32 v104, v229, v237, v240
	v_mfma_f32_32x32x16_f16 v[32:47], a[92:95], v[184:187], v[32:47]
	ds_read_b128 v[184:187], v192 offset:55296
	v_exp_f32_e32 v206, v22
	v_add_f32_e32 v205, 1.0, v205
	v_fma_f32 v105, v229, v239, v241
	v_fmac_f32_e32 v104, v228, v236
	v_mfma_f32_32x32x16_f16 v[48:63], a[92:95], v[188:191], v[48:63]
	ds_read_b128 v[188:191], v192 offset:56320
	s_add_u32 s44, s34, 0x19000
	s_addc_u32 s45, s35, 0
	s_mov_b32 m0, s59
	s_nop 0
	global_load_lds_dwordx4 v192, s[44:45] sc1
	s_lshl_b32 s64, s71, 3
	s_add_u32 s64, s64, s29
	s_lshl_b32 s64, s64, 7
	s_add_u32 s38, s8, s64
	s_addc_u32 s39, s9, 0
	global_load_dword v251, v196, s[38:39] sc1
	v_exp_f32_e32 v207, v23
	v_add_f32_e32 v206, 1.0, v206
	v_fmac_f32_e32 v105, v228, v238
	v_fma_f32 v120, v231, v237, v240
	s_waitcnt lgkmcnt(8)
	v_mfma_f32_32x32x16_f16 v[32:47], a[96:99], v[160:163], v[32:47]
	ds_read_b128 v[160:163], v192 offset:57344
	v_exp_f32_e32 v208, v24
	v_add_f32_e32 v207, 1.0, v207
	v_fma_f32 v121, v231, v239, v241
	v_fmac_f32_e32 v120, v230, v236
	v_mfma_f32_32x32x16_f16 v[48:63], a[96:99], v[164:167], v[48:63]
	ds_read_b128 v[164:167], v192 offset:58368
	v_exp_f32_e32 v209, v25
	v_add_f32_e32 v208, 1.0, v208
	v_fmac_f32_e32 v121, v230, v238
	ds_read_b128 v[236:239], v248 offset:144
	ds_read_b64 v[240:241], v248 offset:176
	s_waitcnt lgkmcnt(10)
	v_mfma_f32_32x32x16_f16 v[32:47], a[100:103], v[168:171], v[32:47]
	ds_read_b128 v[168:171], v192 offset:59392
	v_exp_f32_e32 v210, v26
	v_add_f32_e32 v209, 1.0, v209
	s_waitcnt lgkmcnt(8)
	v_fma_f32 v106, v229, v243, v246
	v_mfma_f32_32x32x16_f16 v[48:63], a[100:103], v[172:175], v[48:63]
	ds_read_b128 v[172:175], v192 offset:60416
	global_load_lds_dwordx4 v192, s[44:45] offset:1024 sc1
	v_exp_f32_e32 v211, v27
	v_add_f32_e32 v210, 1.0, v210
	v_fma_f32 v107, v229, v245, v247
	v_fmac_f32_e32 v106, v228, v242
	s_waitcnt lgkmcnt(8)
	v_mfma_f32_32x32x16_f16 v[32:47], a[104:107], v[176:179], v[32:47]
	ds_read_b128 v[176:179], v192 offset:61440
	v_exp_f32_e32 v212, v28
	v_add_f32_e32 v211, 1.0, v211
	v_fmac_f32_e32 v107, v228, v244
	v_fma_f32 v122, v231, v243, v246
	v_mfma_f32_32x32x16_f16 v[48:63], a[104:107], v[180:183], v[48:63]
	ds_read_b128 v[180:183], v192 offset:62464
	v_exp_f32_e32 v213, v29
	v_add_f32_e32 v212, 1.0, v212
	v_fma_f32 v123, v231, v245, v247
	v_fmac_f32_e32 v122, v230, v242
	s_waitcnt lgkmcnt(8)
	v_mfma_f32_32x32x16_f16 v[32:47], a[108:111], v[184:187], v[32:47]
	ds_read_b128 v[184:187], v192 offset:63488
	v_exp_f32_e32 v214, v30
	v_add_f32_e32 v213, 1.0, v213
	v_fmac_f32_e32 v123, v230, v244
	ds_read_b128 v[242:245], v248 offset:160
	ds_read_b64 v[246:247], v248 offset:184
	v_mfma_f32_32x32x16_f16 v[48:63], a[108:111], v[188:191], v[48:63]
	ds_read_b128 v[188:191], v192 offset:64512
	global_load_lds_dwordx4 v192, s[44:45] offset:2048 sc1
	v_exp_f32_e32 v215, v31
	v_add_f32_e32 v214, 1.0, v214
	s_waitcnt lgkmcnt(8)
	v_fma_f32 v108, v229, v237, v240
	s_waitcnt vmcnt(8)
	s_barrier
	v_mfma_f32_32x32x16_f16 v[32:47], a[112:115], v[160:163], v[32:47]
	ds_read_b128 v[160:163], v193 offset:0
	v_add_f32_e32 v215, 1.0, v215
	v_rcp_f32_e32 v200, v200
	v_fma_f32 v109, v229, v239, v241
	v_fmac_f32_e32 v108, v228, v236
	v_mfma_f32_32x32x16_f16 v[48:63], a[112:115], v[164:167], v[48:63]
	ds_read_b128 v[164:167], v193 offset:1024
	v_rcp_f32_e32 v201, v201
	v_fmac_f32_e32 v109, v228, v238
	v_fma_f32 v124, v231, v237, v240
	s_waitcnt lgkmcnt(8)
	v_mfma_f32_32x32x16_f16 v[32:47], a[116:119], v[168:171], v[32:47]
	ds_read_b128 v[168:171], v193 offset:2048
	v_rcp_f32_e32 v202, v202
	v_fma_f32 v125, v231, v239, v241
	v_fmac_f32_e32 v124, v230, v236
	v_mfma_f32_32x32x16_f16 v[48:63], a[116:119], v[172:175], v[48:63]
	ds_read_b128 v[172:175], v193 offset:3072
	global_load_lds_dwordx4 v192, s[44:45] offset:3072 sc1
	v_rcp_f32_e32 v203, v203
	v_fmac_f32_e32 v125, v230, v238
	s_waitcnt lgkmcnt(5)
	v_mfma_f32_32x32x16_f16 v[32:47], a[120:123], v[176:179], v[32:47]
	ds_read_b128 v[176:179], v193 offset:4096
	v_rcp_f32_e32 v204, v204
	v_fma_f32 v110, v229, v243, v246
	v_fma_f32 v111, v229, v245, v247
	v_mfma_f32_32x32x16_f16 v[48:63], a[120:123], v[180:183], v[48:63]
	ds_read_b128 v[180:183], v193 offset:5120
	v_rcp_f32_e32 v205, v205
	v_mul_f32_e32 v204, v204, v132
	v_fmac_f32_e32 v110, v228, v242
	v_fmac_f32_e32 v111, v228, v244
	s_waitcnt lgkmcnt(6)
	v_mfma_f32_32x32x16_f16 v[32:47], a[124:127], v[184:187], v[32:47]
	ds_read_b128 v[184:187], v193 offset:6144
	v_rcp_f32_e32 v206, v206
	v_mul_f32_e32 v205, v205, v133
	v_fma_f32 v126, v231, v243, v246
	v_fma_f32 v127, v231, v245, v247
	v_mfma_f32_32x32x16_f16 v[48:63], a[124:127], v[188:191], v[48:63]
	ds_read_b128 v[188:191], v193 offset:7168
	s_waitcnt vmcnt(3)
	v_cmp_gt_u32_e32 vcc, 3, v251
	s_cbranch_vccz .LE_tok27
.LE_tpoll28:
	s_cmp_eq_u32 s48, 0
	s_cbranch_scc1 .LE_tok27
	s_sub_u32 s48, s48, 1
	s_sleep 1
	global_load_dword v251, v196, s[38:39] sc1
	s_waitcnt vmcnt(0)
	v_cmp_gt_u32_e32 vcc, 3, v251
	s_cbranch_vccnz .LE_tpoll28
.LE_tok27:
	s_and_b32 s64, s71, 1
	s_lshl_b32 s64, s64, 22
	s_add_u32 s64, s64, s49
	s_add_u32 s64, s64, 0x40000
	s_add_u32 s34, s6, s64
	s_addc_u32 s35, s7, 0
	s_add_u32 s44, s34, 0x0
	s_addc_u32 s45, s35, 0
	s_mov_b32 m0, s52
	s_nop 0
	global_load_lds_dwordx4 v192, s[44:45] sc1
	v_rcp_f32_e32 v207, v207
	v_mul_f32_e32 v206, v206, v134
	v_fmac_f32_e32 v126, v230, v242
	v_fmac_f32_e32 v127, v230, v244
	s_waitcnt lgkmcnt(6)
	v_mfma_f32_32x32x16_f16 v[32:47], a[128:131], v[160:163], v[32:47]
	ds_read_b128 v[160:163], v193 offset:8192
	v_rcp_f32_e32 v208, v208
	v_mul_f32_e32 v207, v207, v135
	v_mfma_f32_32x32x16_f16 v[48:63], a[128:131], v[164:167], v[48:63]
	ds_read_b128 v[164:167], v193 offset:9216
	v_rcp_f32_e32 v209, v209
	v_fmamk_f32 v208, v208, 0xc0b8aa3b, v198
	s_waitcnt lgkmcnt(6)
	v_mfma_f32_32x32x16_f16 v[32:47], a[132:135], v[168:171], v[32:47]
	ds_read_b128 v[168:171], v193 offset:10240
	v_rcp_f32_e32 v210, v210
	v_fmamk_f32 v209, v209, 0xc0b8aa3b, v198
	v_fma_f32 v132, v200, v208, v204
	v_mfma_f32_32x32x16_f16 v[48:63], a[132:135], v[172:175], v[48:63]
	ds_read_b128 v[172:175], v193 offset:11264
	global_load_lds_dwordx4 v192, s[44:45] offset:1024 sc1
	v_rcp_f32_e32 v211, v211
	v_fmamk_f32 v210, v210, 0xc0b8aa3b, v198
	v_fma_f32 v133, v201, v209, v205
	s_waitcnt lgkmcnt(6)
	v_mfma_f32_32x32x16_f16 v[32:47], a[136:139], v[176:179], v[32:47]
	ds_read_b128 v[176:179], v193 offset:12288
	v_rcp_f32_e32 v212, v212
	v_fmamk_f32 v211, v211, 0xc0b8aa3b, v198
	v_fma_f32 v134, v202, v210, v206
	v_mfma_f32_32x32x16_f16 v[48:63], a[136:139], v[180:183], v[48:63]
	ds_read_b128 v[180:183], v193 offset:13312
	v_rcp_f32_e32 v213, v213
	v_fma_f32 v135, v203, v211, v207
	s_waitcnt lgkmcnt(6)
	v_mfma_f32_32x32x16_f16 v[32:47], a[140:143], v[184:187], v[32:47]
	ds_read_b128 v[184:187], v193 offset:14336
	v_rcp_f32_e32 v214, v214
	v_mfma_f32_32x32x16_f16 v[48:63], a[140:143], v[188:191], v[48:63]
	ds_read_b128 v[188:191], v193 offset:15360
	global_load_lds_dwordx4 v192, s[44:45] offset:2048 sc1
	v_rcp_f32_e32 v215, v215
	s_waitcnt lgkmcnt(6)
	v_mfma_f32_32x32x16_f16 v[32:47], a[144:147], v[160:163], v[32:47]
	ds_read_b128 v[160:163], v193 offset:16384
	v_exp_f32_e32 v200, v132
	v_mfma_f32_32x32x16_f16 v[48:63], a[144:147], v[164:167], v[48:63]
	ds_read_b128 v[164:167], v193 offset:17408
	v_exp_f32_e32 v201, v133
	v_add_f32_e32 v200, 1.0, v200
	s_waitcnt lgkmcnt(6)
	v_mfma_f32_32x32x16_f16 v[32:47], a[148:151], v[168:171], v[32:47]
	ds_read_b128 v[168:171], v193 offset:18432
	v_exp_f32_e32 v202, v134
	v_add_f32_e32 v201, 1.0, v201
	v_mfma_f32_32x32x16_f16 v[48:63], a[148:151], v[172:175], v[48:63]
	ds_read_b128 v[172:175], v193 offset:19456
	global_load_lds_dwordx4 v192, s[44:45] offset:3072 sc1
	v_exp_f32_e32 v203, v135
	v_add_f32_e32 v202, 1.0, v202
	s_waitcnt lgkmcnt(6)
	v_mfma_f32_32x32x16_f16 v[32:47], a[152:155], v[176:179], v[32:47]
	ds_read_b128 v[176:179], v193 offset:20480
	v_add_f32_e32 v203, 1.0, v203
	v_rcp_f32_e32 v200, v200
	v_mfma_f32_32x32x16_f16 v[48:63], a[152:155], v[180:183], v[48:63]
	ds_read_b128 v[180:183], v193 offset:21504
	v_rcp_f32_e32 v201, v201
	v_fma_f32 v200, v200, 2.0, -1.0
	s_waitcnt lgkmcnt(6)
	v_mfma_f32_32x32x16_f16 v[32:47], a[156:159], v[184:187], v[32:47]
	ds_read_b128 v[184:187], v193 offset:22528
	v_rcp_f32_e32 v202, v202
	v_fma_f32 v201, v201, 2.0, -1.0
	v_mul_f32_e32 v216, v212, v200
	v_mfma_f32_32x32x16_f16 v[48:63], a[156:159], v[188:191], v[48:63]
	ds_read_b128 v[188:191], v193 offset:23552
	s_add_u32 s44, s34, 0x1000
	s_addc_u32 s45, s35, 0
	s_mov_b32 m0, s53
	s_nop 0
	global_load_lds_dwordx4 v192, s[44:45] sc1
	v_rcp_f32_e32 v203, v203
	v_fma_f32 v202, v202, 2.0, -1.0
	v_mul_f32_e32 v217, v213, v201
	s_waitcnt lgkmcnt(6)
	v_mfma_f32_32x32x16_f16 v[32:47], a[160:163], v[160:163], v[32:47]
	ds_read_b128 v[160:163], v193 offset:24576
	v_fma_f32 v203, v203, 2.0, -1.0
	v_mul_f32_e32 v218, v214, v202
	v_mfma_f32_32x32x16_f16 v[48:63], a[160:163], v[164:167], v[48:63]
	ds_read_b128 v[164:167], v193 offset:25600
	v_mul_f32_e32 v219, v215, v203
	v_cvt_pk_f16_f32 v222, v216, v217
	s_waitcnt lgkmcnt(6)
	v_mfma_f32_32x32x16_f16 v[32:47], a[164:167], v[168:171], v[32:47]
	ds_read_b128 v[168:171], v193 offset:26624
	v_cvt_pk_f16_f32 v223, v218, v219
	v_mfma_f32_32x32x16_f16 v[48:63], a[164:167], v[172:175], v[48:63]
	ds_read_b128 v[172:175], v193 offset:27648
	global_load_lds_dwordx4 v192, s[44:45] offset:1024 sc1
	s_cmp_lg_u32 s33, s60
	s_cbranch_scc1 .LE_nht29
	s_add_u32 s46, s62, 0x20000
	s_addc_u32 s47, s63, 0
	global_store_dwordx4 v250, v[216:219], s[46:47]
	s_waitcnt vmcnt(0)
.LE_nht29:
	s_waitcnt lgkmcnt(6)
	v_mfma_f32_32x32x16_f16 v[32:47], a[168:171], v[176:179], v[32:47]
	ds_read_b128 v[176:179], v193 offset:28672
	s_nop 1
	v_permlane32_swap_b32_e32 v220, v222
	v_permlane32_swap_b32_e32 v221, v223
	s_cmp_eq_u32 s31, 0
	s_cbranch_scc1 .LE_slow30
	global_store_dwordx4 v195, v[220:223], s[36:37] offset:0
	s_branch .LE_join31

.LE_join31:
	v_mfma_f32_32x32x16_f16 v[48:63], a[168:171], v[180:183], v[48:63]
	ds_read_b128 v[180:183], v193 offset:29696
	s_waitcnt lgkmcnt(6)
	v_mfma_f32_32x32x16_f16 v[32:47], a[172:175], v[184:187], v[32:47]
	ds_read_b128 v[184:187], v193 offset:30720
	v_mfma_f32_32x32x16_f16 v[48:63], a[172:175], v[188:191], v[48:63]
	ds_read_b128 v[188:191], v193 offset:31744
	global_load_lds_dwordx4 v192, s[44:45] offset:2048 sc1
	s_waitcnt vmcnt(8)
	s_barrier
	s_waitcnt lgkmcnt(6)
	v_mfma_f32_32x32x16_f16 v[32:47], a[176:179], v[160:163], v[32:47]
	ds_read_b128 v[160:163], v193 offset:32768
	v_mfma_f32_32x32x16_f16 v[48:63], a[176:179], v[164:167], v[48:63]
	ds_read_b128 v[164:167], v193 offset:33792
	s_waitcnt lgkmcnt(6)
	v_mfma_f32_32x32x16_f16 v[32:47], a[180:183], v[168:171], v[32:47]
	ds_read_b128 v[168:171], v193 offset:34816
	v_mfma_f32_32x32x16_f16 v[48:63], a[180:183], v[172:175], v[48:63]
	ds_read_b128 v[172:175], v193 offset:35840
	global_load_lds_dwordx4 v192, s[44:45] offset:3072 sc1
	s_waitcnt lgkmcnt(6)
	v_mfma_f32_32x32x16_f16 v[32:47], a[184:187], v[176:179], v[32:47]
	ds_read_b128 v[176:179], v193 offset:36864
	v_mfma_f32_32x32x16_f16 v[48:63], a[184:187], v[180:183], v[48:63]
	ds_read_b128 v[180:183], v193 offset:37888
	s_waitcnt lgkmcnt(6)
	v_mfma_f32_32x32x16_f16 v[32:47], a[188:191], v[184:187], v[32:47]
	ds_read_b128 v[184:187], v193 offset:38912
	v_mfma_f32_32x32x16_f16 v[48:63], a[188:191], v[188:191], v[48:63]
	ds_read_b128 v[188:191], v193 offset:39936
	s_add_u32 s44, s34, 0x8000
	s_addc_u32 s45, s35, 0
	s_mov_b32 m0, s54
	s_nop 0
	global_load_lds_dwordx4 v192, s[44:45] sc1
	s_waitcnt lgkmcnt(6)
	v_mfma_f32_32x32x16_f16 v[32:47], a[192:195], v[160:163], v[32:47]
	ds_read_b128 v[160:163], v193 offset:40960
	v_mfma_f32_32x32x16_f16 v[48:63], a[192:195], v[164:167], v[48:63]
	ds_read_b128 v[164:167], v193 offset:41984
	s_waitcnt vmcnt(3)
	s_barrier
	v_mov_b32_e32 v199, 1
	s_cmp_eq_u32 s31, 0
	s_cbranch_scc1 .LE_slow32
	global_store_dword v197, v199, s[40:41]
	s_branch .LE_join33

.LE_join33:
	s_waitcnt lgkmcnt(6)
	v_mfma_f32_32x32x16_f16 v[32:47], a[196:199], v[168:171], v[32:47]
	ds_read_b128 v[168:171], v193 offset:43008
	v_mfma_f32_32x32x16_f16 v[48:63], a[196:199], v[172:175], v[48:63]
	ds_read_b128 v[172:175], v193 offset:44032
	global_load_lds_dwordx4 v192, s[44:45] offset:1024 sc1
	s_waitcnt lgkmcnt(6)
	v_mfma_f32_32x32x16_f16 v[32:47], a[200:203], v[176:179], v[32:47]
	ds_read_b128 v[176:179], v193 offset:45056
	v_mfma_f32_32x32x16_f16 v[48:63], a[200:203], v[180:183], v[48:63]
	ds_read_b128 v[180:183], v193 offset:46080
	s_waitcnt lgkmcnt(6)
	v_mfma_f32_32x32x16_f16 v[32:47], a[204:207], v[184:187], v[32:47]
	ds_read_b128 v[184:187], v193 offset:47104
	v_mfma_f32_32x32x16_f16 v[48:63], a[204:207], v[188:191], v[48:63]
	ds_read_b128 v[188:191], v193 offset:48128
	global_load_lds_dwordx4 v192, s[44:45] offset:2048 sc1
	s_waitcnt lgkmcnt(6)
	v_mfma_f32_32x32x16_f16 v[32:47], a[208:211], v[160:163], v[32:47]
	ds_read_b128 v[160:163], v193 offset:49152
	v_mfma_f32_32x32x16_f16 v[48:63], a[208:211], v[164:167], v[48:63]
	ds_read_b128 v[164:167], v193 offset:50176
	s_waitcnt lgkmcnt(6)
	v_mfma_f32_32x32x16_f16 v[32:47], a[212:215], v[168:171], v[32:47]
	ds_read_b128 v[168:171], v193 offset:51200
	v_mfma_f32_32x32x16_f16 v[48:63], a[212:215], v[172:175], v[48:63]
	ds_read_b128 v[172:175], v193 offset:52224
	global_load_lds_dwordx4 v192, s[44:45] offset:3072 sc1
	s_waitcnt lgkmcnt(6)
	v_mfma_f32_32x32x16_f16 v[32:47], a[216:219], v[176:179], v[32:47]
	ds_read_b128 v[176:179], v193 offset:53248
	v_mfma_f32_32x32x16_f16 v[48:63], a[216:219], v[180:183], v[48:63]
	ds_read_b128 v[180:183], v193 offset:54272
	s_waitcnt lgkmcnt(6)
	v_mfma_f32_32x32x16_f16 v[32:47], a[220:223], v[184:187], v[32:47]
	ds_read_b128 v[184:187], v193 offset:55296
	v_mfma_f32_32x32x16_f16 v[48:63], a[220:223], v[188:191], v[48:63]
	ds_read_b128 v[188:191], v193 offset:56320
	s_add_u32 s44, s34, 0x9000
	s_addc_u32 s45, s35, 0
	s_mov_b32 m0, s55
	s_nop 0
	global_load_lds_dwordx4 v192, s[44:45] sc1
	s_waitcnt lgkmcnt(6)
	v_mfma_f32_32x32x16_f16 v[32:47], a[224:227], v[160:163], v[32:47]
	ds_read_b128 v[160:163], v193 offset:57344
	v_mfma_f32_32x32x16_f16 v[48:63], a[224:227], v[164:167], v[48:63]
	ds_read_b128 v[164:167], v193 offset:58368
	s_waitcnt lgkmcnt(6)
	v_mfma_f32_32x32x16_f16 v[32:47], a[228:231], v[168:171], v[32:47]
	ds_read_b128 v[168:171], v193 offset:59392
	v_mfma_f32_32x32x16_f16 v[48:63], a[228:231], v[172:175], v[48:63]
	ds_read_b128 v[172:175], v193 offset:60416
	global_load_lds_dwordx4 v192, s[44:45] offset:1024 sc1
	s_waitcnt lgkmcnt(6)
	v_mfma_f32_32x32x16_f16 v[32:47], a[232:235], v[176:179], v[32:47]
	ds_read_b128 v[176:179], v193 offset:61440
	v_mfma_f32_32x32x16_f16 v[48:63], a[232:235], v[180:183], v[48:63]
	ds_read_b128 v[180:183], v193 offset:62464
	s_waitcnt lgkmcnt(6)
	v_mfma_f32_32x32x16_f16 v[32:47], a[236:239], v[184:187], v[32:47]
	ds_read_b128 v[184:187], v193 offset:63488
	v_mfma_f32_32x32x16_f16 v[48:63], a[236:239], v[188:191], v[48:63]
	ds_read_b128 v[188:191], v193 offset:64512
	global_load_lds_dwordx4 v192, s[44:45] offset:2048 sc1
	s_waitcnt vmcnt(8)
	s_barrier
	s_waitcnt lgkmcnt(6)
	v_mfma_f32_32x32x16_f16 v[32:47], a[240:243], v[160:163], v[32:47]
	ds_read_b128 v[160:163], v192 offset:0
	v_mfma_f32_32x32x16_f16 v[48:63], a[240:243], v[164:167], v[48:63]
	ds_read_b128 v[164:167], v192 offset:1024
	s_waitcnt lgkmcnt(6)
	v_mfma_f32_32x32x16_f16 v[32:47], a[244:247], v[168:171], v[32:47]
	ds_read_b128 v[168:171], v192 offset:2048
	v_mfma_f32_32x32x16_f16 v[48:63], a[244:247], v[172:175], v[48:63]
	ds_read_b128 v[172:175], v192 offset:3072
	global_load_lds_dwordx4 v192, s[44:45] offset:3072 sc1
	s_waitcnt lgkmcnt(6)
	v_mfma_f32_32x32x16_f16 v[32:47], a[248:251], v[176:179], v[32:47]
	ds_read_b128 v[176:179], v192 offset:4096
	v_mfma_f32_32x32x16_f16 v[48:63], a[248:251], v[180:183], v[48:63]
	ds_read_b128 v[180:183], v192 offset:5120
	s_waitcnt lgkmcnt(6)
	v_mfma_f32_32x32x16_f16 v[32:47], a[252:255], v[184:187], v[32:47]
	ds_read_b128 v[184:187], v192 offset:6144
	v_mfma_f32_32x32x16_f16 v[48:63], a[252:255], v[188:191], v[48:63]
	ds_read_b128 v[188:191], v192 offset:7168
	s_add_u32 s44, s34, 0x10000
	s_addc_u32 s45, s35, 0
	s_mov_b32 m0, s56
	s_nop 0
	global_load_lds_dwordx4 v192, s[44:45] sc1
	s_and_b32 s64, s33, 1
	s_lshl_b32 s64, s64, 22
	s_add_u32 s64, s64, s50
	s_add_u32 s64, s64, 0x20000
	s_add_u32 s36, s6, s64
	s_addc_u32 s37, s7, 0
	s_lshl_b32 s64, s33, 3
	s_add_u32 s64, s64, s29
	s_lshl_b32 s64, s64, 5
	s_add_u32 s64, s64, s30
	s_lshl_b32 s64, s64, 2
	s_add_u32 s40, s8, s64
	s_addc_u32 s41, s9, 0
	s_lshl_b32 s64, s61, 11
	s_lshl_b32 s65, s29, 8
	s_add_u32 s64, s64, s65
	s_lshl_b32 s64, s64, 3
	s_add_u32 s42, s12, s64
	s_addc_u32 s43, s13, 0
	s_nop 11
	global_load_dwordx2 v[228:229], v249, s[42:43] offset:0
	global_load_dwordx2 v[230:231], v249, s[42:43] offset:256
	s_waitcnt lgkmcnt(6)
	v_mfma_f32_32x32x16_f16 v[64:79], a[0:3], v[160:163], v[64:79]
	ds_read_b128 v[160:163], v192 offset:8192
	v_exp_f32_e32 v200, v32
	v_mfma_f32_32x32x16_f16 v[80:95], a[0:3], v[164:167], v[80:95]
	ds_read_b128 v[164:167], v192 offset:9216
	v_exp_f32_e32 v201, v33
	v_add_f32_e32 v200, 1.0, v200
	s_waitcnt lgkmcnt(6)
	v_mfma_f32_32x32x16_f16 v[64:79], a[4:7], v[168:171], v[64:79]
	ds_read_b128 v[168:171], v192 offset:10240
	v_exp_f32_e32 v202, v34
	v_add_f32_e32 v201, 1.0, v201
	v_mfma_f32_32x32x16_f16 v[80:95], a[4:7], v[172:175], v[80:95]
	ds_read_b128 v[172:175], v192 offset:11264
	global_load_lds_dwordx4 v192, s[44:45] offset:1024 sc1
	v_exp_f32_e32 v203, v35
	v_add_f32_e32 v202, 1.0, v202
	s_waitcnt lgkmcnt(6)
	v_mfma_f32_32x32x16_f16 v[64:79], a[8:11], v[176:179], v[64:79]
	ds_read_b128 v[176:179], v192 offset:12288
	v_exp_f32_e32 v204, v36
	v_add_f32_e32 v203, 1.0, v203
	v_mfma_f32_32x32x16_f16 v[80:95], a[8:11], v[180:183], v[80:95]
	ds_read_b128 v[180:183], v192 offset:13312
	v_exp_f32_e32 v205, v37
	v_add_f32_e32 v204, 1.0, v204
	s_waitcnt lgkmcnt(6)
	v_mfma_f32_32x32x16_f16 v[64:79], a[12:15], v[184:187], v[64:79]
	ds_read_b128 v[184:187], v192 offset:14336
	v_exp_f32_e32 v206, v38
	v_add_f32_e32 v205, 1.0, v205
	v_mfma_f32_32x32x16_f16 v[80:95], a[12:15], v[188:191], v[80:95]
	ds_read_b128 v[188:191], v192 offset:15360
	global_load_lds_dwordx4 v192, s[44:45] offset:2048 sc1
	v_exp_f32_e32 v207, v39
	v_add_f32_e32 v206, 1.0, v206
	s_waitcnt lgkmcnt(6)
	v_mfma_f32_32x32x16_f16 v[64:79], a[16:19], v[160:163], v[64:79]
	ds_read_b128 v[160:163], v192 offset:16384
	v_exp_f32_e32 v208, v40
	v_add_f32_e32 v207, 1.0, v207
	v_mfma_f32_32x32x16_f16 v[80:95], a[16:19], v[164:167], v[80:95]
	ds_read_b128 v[164:167], v192 offset:17408
	v_exp_f32_e32 v209, v41
	v_add_f32_e32 v208, 1.0, v208
	s_waitcnt lgkmcnt(6)
	v_mfma_f32_32x32x16_f16 v[64:79], a[20:23], v[168:171], v[64:79]
	ds_read_b128 v[168:171], v192 offset:18432
	v_exp_f32_e32 v210, v42
	v_add_f32_e32 v209, 1.0, v209
	v_mfma_f32_32x32x16_f16 v[80:95], a[20:23], v[172:175], v[80:95]
	ds_read_b128 v[172:175], v192 offset:19456
	global_load_lds_dwordx4 v192, s[44:45] offset:3072 sc1
	v_exp_f32_e32 v211, v43
	v_add_f32_e32 v210, 1.0, v210
	s_waitcnt lgkmcnt(6)
	v_mfma_f32_32x32x16_f16 v[64:79], a[24:27], v[176:179], v[64:79]
	ds_read_b128 v[176:179], v192 offset:20480
	v_exp_f32_e32 v212, v44
	v_add_f32_e32 v211, 1.0, v211
	v_mfma_f32_32x32x16_f16 v[80:95], a[24:27], v[180:183], v[80:95]
	ds_read_b128 v[180:183], v192 offset:21504
	v_exp_f32_e32 v213, v45
	v_add_f32_e32 v212, 1.0, v212
	s_waitcnt lgkmcnt(6)
	v_mfma_f32_32x32x16_f16 v[64:79], a[28:31], v[184:187], v[64:79]
	ds_read_b128 v[184:187], v192 offset:22528
	v_exp_f32_e32 v214, v46
	v_add_f32_e32 v213, 1.0, v213
	v_mfma_f32_32x32x16_f16 v[80:95], a[28:31], v[188:191], v[80:95]
	ds_read_b128 v[188:191], v192 offset:23552
	s_add_u32 s44, s34, 0x11000
	s_addc_u32 s45, s35, 0
	s_mov_b32 m0, s57
	s_nop 0
	global_load_lds_dwordx4 v192, s[44:45] sc1
	v_exp_f32_e32 v215, v47
	v_add_f32_e32 v214, 1.0, v214
	s_waitcnt lgkmcnt(6)
	v_mfma_f32_32x32x16_f16 v[64:79], a[32:35], v[160:163], v[64:79]
	ds_read_b128 v[160:163], v192 offset:24576
	v_add_f32_e32 v215, 1.0, v215
	v_rcp_f32_e32 v200, v200
	v_mfma_f32_32x32x16_f16 v[80:95], a[32:35], v[164:167], v[80:95]
	ds_read_b128 v[164:167], v192 offset:25600
	v_rcp_f32_e32 v201, v201
	s_waitcnt lgkmcnt(6)
	v_mfma_f32_32x32x16_f16 v[64:79], a[36:39], v[168:171], v[64:79]
	ds_read_b128 v[168:171], v192 offset:26624
	v_rcp_f32_e32 v202, v202
	v_mfma_f32_32x32x16_f16 v[80:95], a[36:39], v[172:175], v[80:95]
	ds_read_b128 v[172:175], v192 offset:27648
	global_load_lds_dwordx4 v192, s[44:45] offset:1024 sc1
	v_rcp_f32_e32 v203, v203
	s_waitcnt lgkmcnt(6)
	v_mfma_f32_32x32x16_f16 v[64:79], a[40:43], v[176:179], v[64:79]
	ds_read_b128 v[176:179], v192 offset:28672
	v_rcp_f32_e32 v204, v204
	v_mfma_f32_32x32x16_f16 v[80:95], a[40:43], v[180:183], v[80:95]
	ds_read_b128 v[180:183], v192 offset:29696
	v_rcp_f32_e32 v205, v205
	v_mul_f32_e32 v204, v204, v136
	s_waitcnt lgkmcnt(6)
	v_mfma_f32_32x32x16_f16 v[64:79], a[44:47], v[184:187], v[64:79]
	ds_read_b128 v[184:187], v192 offset:30720
	v_rcp_f32_e32 v206, v206
	v_mul_f32_e32 v205, v205, v137
	v_mfma_f32_32x32x16_f16 v[80:95], a[44:47], v[188:191], v[80:95]
	ds_read_b128 v[188:191], v192 offset:31744
	global_load_lds_dwordx4 v192, s[44:45] offset:2048 sc1
	v_rcp_f32_e32 v207, v207
	v_mul_f32_e32 v206, v206, v138
	s_waitcnt vmcnt(9)
	s_barrier
	s_waitcnt lgkmcnt(6)
	v_mfma_f32_32x32x16_f16 v[64:79], a[48:51], v[160:163], v[64:79]
	ds_read_b128 v[160:163], v192 offset:32768
	v_rcp_f32_e32 v208, v208
	v_mul_f32_e32 v207, v207, v139
	ds_read_b128 v[236:239], v248 offset:0
	ds_read_b64 v[240:241], v248 offset:32
	ds_read_b128 v[242:245], v248 offset:16
	ds_read_b64 v[246:247], v248 offset:40
	v_mfma_f32_32x32x16_f16 v[80:95], a[48:51], v[164:167], v[80:95]
	ds_read_b128 v[164:167], v192 offset:33792
	v_rcp_f32_e32 v209, v209
	v_fmamk_f32 v208, v208, 0xc0b8aa3b, v198
	s_waitcnt lgkmcnt(3)
	s_waitcnt vmcnt(6)
	v_fma_f32 v0, v229, v237, v240
	v_mfma_f32_32x32x16_f16 v[64:79], a[52:55], v[168:171], v[64:79]
	ds_read_b128 v[168:171], v192 offset:34816
	v_rcp_f32_e32 v210, v210
	v_fmamk_f32 v209, v209, 0xc0b8aa3b, v198
	v_fma_f32 v136, v200, v208, v204
	v_fma_f32 v1, v229, v239, v241
	v_fmac_f32_e32 v0, v228, v236
	v_mfma_f32_32x32x16_f16 v[80:95], a[52:55], v[172:175], v[80:95]
	ds_read_b128 v[172:175], v192 offset:35840
	global_load_lds_dwordx4 v192, s[44:45] offset:3072 sc1
	v_rcp_f32_e32 v211, v211
	v_fmamk_f32 v210, v210, 0xc0b8aa3b, v198
	v_fma_f32 v137, v201, v209, v205
	v_fmac_f32_e32 v1, v228, v238
	v_fma_f32 v16, v231, v237, v240
	v_mfma_f32_32x32x16_f16 v[64:79], a[56:59], v[176:179], v[64:79]
	ds_read_b128 v[176:179], v192 offset:36864
	v_rcp_f32_e32 v212, v212
	v_fmamk_f32 v211, v211, 0xc0b8aa3b, v198
	v_fma_f32 v138, v202, v210, v206
	v_fma_f32 v17, v231, v239, v241
	v_fmac_f32_e32 v16, v230, v236
	v_mfma_f32_32x32x16_f16 v[80:95], a[56:59], v[180:183], v[80:95]
	ds_read_b128 v[180:183], v192 offset:37888
	v_rcp_f32_e32 v213, v213
	v_fma_f32 v139, v203, v211, v207
	v_fmac_f32_e32 v17, v230, v238
	ds_read_b128 v[236:239], v248 offset:48
	ds_read_b64 v[240:241], v248 offset:80
	v_mfma_f32_32x32x16_f16 v[64:79], a[60:63], v[184:187], v[64:79]
	ds_read_b128 v[184:187], v192 offset:38912
	v_rcp_f32_e32 v214, v214
	s_waitcnt lgkmcnt(8)
	v_fma_f32 v2, v229, v243, v246
	v_mfma_f32_32x32x16_f16 v[80:95], a[60:63], v[188:191], v[80:95]
	ds_read_b128 v[188:191], v192 offset:39936
	s_add_u32 s44, s34, 0x18000
	s_addc_u32 s45, s35, 0
	s_mov_b32 m0, s58
	s_nop 0
	global_load_lds_dwordx4 v192, s[44:45] sc1
	v_rcp_f32_e32 v215, v215
	v_fma_f32 v3, v229, v245, v247
	v_fmac_f32_e32 v2, v228, v242
	s_waitcnt lgkmcnt(8)
	v_mfma_f32_32x32x16_f16 v[64:79], a[64:67], v[160:163], v[64:79]
	ds_read_b128 v[160:163], v192 offset:40960
	v_exp_f32_e32 v200, v136
	v_fmac_f32_e32 v3, v228, v244
	v_fma_f32 v18, v231, v243, v246
	v_mfma_f32_32x32x16_f16 v[80:95], a[64:67], v[164:167], v[80:95]
	ds_read_b128 v[164:167], v192 offset:41984
	v_exp_f32_e32 v201, v137
	v_add_f32_e32 v200, 1.0, v200
	v_fma_f32 v19, v231, v245, v247
	v_fmac_f32_e32 v18, v230, v242
	s_waitcnt lgkmcnt(8)
	v_mfma_f32_32x32x16_f16 v[64:79], a[68:71], v[168:171], v[64:79]
	ds_read_b128 v[168:171], v192 offset:43008
	v_exp_f32_e32 v202, v138
	v_add_f32_e32 v201, 1.0, v201
	v_fmac_f32_e32 v19, v230, v244
	ds_read_b128 v[242:245], v248 offset:64
	ds_read_b64 v[246:247], v248 offset:88
	v_mfma_f32_32x32x16_f16 v[80:95], a[68:71], v[172:175], v[80:95]
	ds_read_b128 v[172:175], v192 offset:44032
	global_load_lds_dwordx4 v192, s[44:45] offset:1024 sc1
	v_exp_f32_e32 v203, v139
	v_add_f32_e32 v202, 1.0, v202
	s_waitcnt lgkmcnt(8)
	v_fma_f32 v4, v229, v237, v240
	v_mfma_f32_32x32x16_f16 v[64:79], a[72:75], v[176:179], v[64:79]
	ds_read_b128 v[176:179], v192 offset:45056
	v_add_f32_e32 v203, 1.0, v203
	v_rcp_f32_e32 v200, v200
	v_fma_f32 v5, v229, v239, v241
	v_fmac_f32_e32 v4, v228, v236
	v_mfma_f32_32x32x16_f16 v[80:95], a[72:75], v[180:183], v[80:95]
	ds_read_b128 v[180:183], v192 offset:46080
	v_rcp_f32_e32 v201, v201
	v_fma_f32 v200, v200, 2.0, -1.0
	v_fmac_f32_e32 v5, v228, v238
	v_fma_f32 v20, v231, v237, v240
	s_waitcnt lgkmcnt(8)
	v_mfma_f32_32x32x16_f16 v[64:79], a[76:79], v[184:187], v[64:79]
	ds_read_b128 v[184:187], v192 offset:47104
	v_rcp_f32_e32 v202, v202
	v_fma_f32 v201, v201, 2.0, -1.0
	v_mul_f32_e32 v216, v212, v200
	v_fma_f32 v21, v231, v239, v241
	v_fmac_f32_e32 v20, v230, v236
	v_mfma_f32_32x32x16_f16 v[80:95], a[76:79], v[188:191], v[80:95]
	ds_read_b128 v[188:191], v192 offset:48128
	global_load_lds_dwordx4 v192, s[44:45] offset:2048 sc1
	v_rcp_f32_e32 v203, v203
	v_fma_f32 v202, v202, 2.0, -1.0
	v_mul_f32_e32 v217, v213, v201
	v_fmac_f32_e32 v21, v230, v238
	ds_read_b128 v[236:239], v248 offset:96
	ds_read_b64 v[240:241], v248 offset:128
	s_waitcnt lgkmcnt(10)
	v_mfma_f32_32x32x16_f16 v[64:79], a[80:83], v[160:163], v[64:79]
	ds_read_b128 v[160:163], v192 offset:49152
	v_fma_f32 v203, v203, 2.0, -1.0
	v_mul_f32_e32 v218, v214, v202
	v_exp_f32_e32 v200, v48
	s_waitcnt lgkmcnt(8)
	v_fma_f32 v6, v229, v243, v246
	v_mfma_f32_32x32x16_f16 v[80:95], a[80:83], v[164:167], v[80:95]
	ds_read_b128 v[164:167], v192 offset:50176
	v_mul_f32_e32 v219, v215, v203
	v_cvt_pk_f16_f32 v220, v216, v217
	v_exp_f32_e32 v201, v49
	v_fma_f32 v7, v229, v245, v247
	v_fmac_f32_e32 v6, v228, v242
	s_waitcnt lgkmcnt(8)
	v_mfma_f32_32x32x16_f16 v[64:79], a[84:87], v[168:171], v[64:79]
	ds_read_b128 v[168:171], v192 offset:51200
	v_cvt_pk_f16_f32 v221, v218, v219
	v_exp_f32_e32 v202, v50
	v_add_f32_e32 v200, 1.0, v200
	v_fmac_f32_e32 v7, v228, v244
	v_fma_f32 v22, v231, v243, v246
	v_mfma_f32_32x32x16_f16 v[80:95], a[84:87], v[172:175], v[80:95]
	ds_read_b128 v[172:175], v192 offset:52224
	global_load_lds_dwordx4 v192, s[44:45] offset:3072 sc1
	s_cmp_lg_u32 s33, s60
	s_cbranch_scc1 .LE_nht34
	s_add_u32 s46, s62, 0x40000
	s_addc_u32 s47, s63, 0
	global_store_dwordx4 v250, v[216:219], s[46:47]
	s_waitcnt vmcnt(0)
.LE_nht34:
	v_exp_f32_e32 v203, v51
	v_fma_f32 v23, v231, v245, v247
	v_fmac_f32_e32 v22, v230, v242
	s_waitcnt lgkmcnt(8)
	v_mfma_f32_32x32x16_f16 v[64:79], a[88:91], v[176:179], v[64:79]
	ds_read_b128 v[176:179], v192 offset:53248
	v_exp_f32_e32 v204, v52
	v_add_f32_e32 v201, 1.0, v201
	v_add_f32_e32 v202, 1.0, v202
	v_fmac_f32_e32 v23, v230, v244
	ds_read_b128 v[242:245], v248 offset:112
	ds_read_b64 v[246:247], v248 offset:136
	v_mfma_f32_32x32x16_f16 v[80:95], a[88:91], v[180:183], v[80:95]
	ds_read_b128 v[180:183], v192 offset:54272
	v_exp_f32_e32 v205, v53
	v_add_f32_e32 v203, 1.0, v203
	v_add_f32_e32 v204, 1.0, v204
	s_waitcnt lgkmcnt(8)
	v_fma_f32 v8, v229, v237, v240
	v_mfma_f32_32x32x16_f16 v[64:79], a[92:95], v[184:187], v[64:79]
	ds_read_b128 v[184:187], v192 offset:55296
	v_exp_f32_e32 v206, v54
	v_add_f32_e32 v205, 1.0, v205
	v_fma_f32 v9, v229, v239, v241
	v_fmac_f32_e32 v8, v228, v236
	v_mfma_f32_32x32x16_f16 v[80:95], a[92:95], v[188:191], v[80:95]
	ds_read_b128 v[188:191], v192 offset:56320
	s_add_u32 s44, s34, 0x19000
	s_addc_u32 s45, s35, 0
	s_mov_b32 m0, s59
	s_nop 0
	global_load_lds_dwordx4 v192, s[44:45] sc1
	s_lshl_b32 s64, s71, 3
	s_add_u32 s64, s64, s29
	s_lshl_b32 s64, s64, 7
	s_add_u32 s38, s8, s64
	s_addc_u32 s39, s9, 0
	global_load_dword v251, v196, s[38:39] sc1
	v_exp_f32_e32 v207, v55
	v_add_f32_e32 v206, 1.0, v206
	v_fmac_f32_e32 v9, v228, v238
	v_fma_f32 v24, v231, v237, v240
	s_waitcnt lgkmcnt(8)
	v_mfma_f32_32x32x16_f16 v[64:79], a[96:99], v[160:163], v[64:79]
	ds_read_b128 v[160:163], v192 offset:57344
	v_exp_f32_e32 v208, v56
	v_add_f32_e32 v207, 1.0, v207
	v_fma_f32 v25, v231, v239, v241
	v_fmac_f32_e32 v24, v230, v236
	v_mfma_f32_32x32x16_f16 v[80:95], a[96:99], v[164:167], v[80:95]
	ds_read_b128 v[164:167], v192 offset:58368
	v_exp_f32_e32 v209, v57
	v_add_f32_e32 v208, 1.0, v208
	v_fmac_f32_e32 v25, v230, v238
	ds_read_b128 v[236:239], v248 offset:144
	ds_read_b64 v[240:241], v248 offset:176
	s_waitcnt lgkmcnt(10)
	v_mfma_f32_32x32x16_f16 v[64:79], a[100:103], v[168:171], v[64:79]
	ds_read_b128 v[168:171], v192 offset:59392
	v_exp_f32_e32 v210, v58
	v_add_f32_e32 v209, 1.0, v209
	s_waitcnt lgkmcnt(8)
	v_fma_f32 v10, v229, v243, v246
	v_mfma_f32_32x32x16_f16 v[80:95], a[100:103], v[172:175], v[80:95]
	ds_read_b128 v[172:175], v192 offset:60416
	global_load_lds_dwordx4 v192, s[44:45] offset:1024 sc1
	v_exp_f32_e32 v211, v59
	v_add_f32_e32 v210, 1.0, v210
	v_fma_f32 v11, v229, v245, v247
	v_fmac_f32_e32 v10, v228, v242
	s_waitcnt lgkmcnt(8)
	v_mfma_f32_32x32x16_f16 v[64:79], a[104:107], v[176:179], v[64:79]
	ds_read_b128 v[176:179], v192 offset:61440
	v_exp_f32_e32 v212, v60
	v_add_f32_e32 v211, 1.0, v211
	v_fmac_f32_e32 v11, v228, v244
	v_fma_f32 v26, v231, v243, v246
	v_mfma_f32_32x32x16_f16 v[80:95], a[104:107], v[180:183], v[80:95]
	ds_read_b128 v[180:183], v192 offset:62464
	v_exp_f32_e32 v213, v61
	v_add_f32_e32 v212, 1.0, v212
	v_fma_f32 v27, v231, v245, v247
	v_fmac_f32_e32 v26, v230, v242
	s_waitcnt lgkmcnt(8)
	v_mfma_f32_32x32x16_f16 v[64:79], a[108:111], v[184:187], v[64:79]
	ds_read_b128 v[184:187], v192 offset:63488
	v_exp_f32_e32 v214, v62
	v_add_f32_e32 v213, 1.0, v213
	v_fmac_f32_e32 v27, v230, v244
	ds_read_b128 v[242:245], v248 offset:160
	ds_read_b64 v[246:247], v248 offset:184
	v_mfma_f32_32x32x16_f16 v[80:95], a[108:111], v[188:191], v[80:95]
	ds_read_b128 v[188:191], v192 offset:64512
	global_load_lds_dwordx4 v192, s[44:45] offset:2048 sc1
	v_exp_f32_e32 v215, v63
	v_add_f32_e32 v214, 1.0, v214
	s_waitcnt lgkmcnt(8)
	v_fma_f32 v12, v229, v237, v240
	s_waitcnt vmcnt(8)
	s_barrier
	v_mfma_f32_32x32x16_f16 v[64:79], a[112:115], v[160:163], v[64:79]
	ds_read_b128 v[160:163], v193 offset:0
	v_add_f32_e32 v215, 1.0, v215
	v_rcp_f32_e32 v200, v200
	v_fma_f32 v13, v229, v239, v241
	v_fmac_f32_e32 v12, v228, v236
	v_mfma_f32_32x32x16_f16 v[80:95], a[112:115], v[164:167], v[80:95]
	ds_read_b128 v[164:167], v193 offset:1024
	v_rcp_f32_e32 v201, v201
	v_fmac_f32_e32 v13, v228, v238
	v_fma_f32 v28, v231, v237, v240
	s_waitcnt lgkmcnt(8)
	v_mfma_f32_32x32x16_f16 v[64:79], a[116:119], v[168:171], v[64:79]
	ds_read_b128 v[168:171], v193 offset:2048
	v_rcp_f32_e32 v202, v202
	v_fma_f32 v29, v231, v239, v241
	v_fmac_f32_e32 v28, v230, v236
	v_mfma_f32_32x32x16_f16 v[80:95], a[116:119], v[172:175], v[80:95]
	ds_read_b128 v[172:175], v193 offset:3072
	global_load_lds_dwordx4 v192, s[44:45] offset:3072 sc1
	v_rcp_f32_e32 v203, v203
	v_fmac_f32_e32 v29, v230, v238
	s_waitcnt lgkmcnt(5)
	v_mfma_f32_32x32x16_f16 v[64:79], a[120:123], v[176:179], v[64:79]
	ds_read_b128 v[176:179], v193 offset:4096
	v_rcp_f32_e32 v204, v204
	v_fma_f32 v14, v229, v243, v246
	v_fma_f32 v15, v229, v245, v247
	v_mfma_f32_32x32x16_f16 v[80:95], a[120:123], v[180:183], v[80:95]
	ds_read_b128 v[180:183], v193 offset:5120
	v_rcp_f32_e32 v205, v205
	v_mul_f32_e32 v204, v204, v140
	v_fmac_f32_e32 v14, v228, v242
	v_fmac_f32_e32 v15, v228, v244
	s_waitcnt lgkmcnt(6)
	v_mfma_f32_32x32x16_f16 v[64:79], a[124:127], v[184:187], v[64:79]
	ds_read_b128 v[184:187], v193 offset:6144
	v_rcp_f32_e32 v206, v206
	v_mul_f32_e32 v205, v205, v141
	v_fma_f32 v30, v231, v243, v246
	v_fma_f32 v31, v231, v245, v247
	v_mfma_f32_32x32x16_f16 v[80:95], a[124:127], v[188:191], v[80:95]
	ds_read_b128 v[188:191], v193 offset:7168
	s_waitcnt vmcnt(3)
	v_cmp_gt_u32_e32 vcc, 4, v251
	s_cbranch_vccz .LE_tok35
.LE_tpoll36:
	s_cmp_eq_u32 s48, 0
	s_cbranch_scc1 .LE_tok35
	s_sub_u32 s48, s48, 1
	s_sleep 1
	global_load_dword v251, v196, s[38:39] sc1
	s_waitcnt vmcnt(0)
	v_cmp_gt_u32_e32 vcc, 4, v251
	s_cbranch_vccnz .LE_tpoll36
.LE_tok35:
	s_and_b32 s64, s71, 1
	s_lshl_b32 s64, s64, 22
	s_add_u32 s64, s64, s49
	s_add_u32 s64, s64, 0x60000
	s_add_u32 s34, s6, s64
	s_addc_u32 s35, s7, 0
	s_add_u32 s44, s34, 0x0
	s_addc_u32 s45, s35, 0
	s_mov_b32 m0, s52
	s_nop 0
	global_load_lds_dwordx4 v192, s[44:45] sc1
	v_rcp_f32_e32 v207, v207
	v_mul_f32_e32 v206, v206, v142
	v_fmac_f32_e32 v30, v230, v242
	v_fmac_f32_e32 v31, v230, v244
	s_waitcnt lgkmcnt(6)
	v_mfma_f32_32x32x16_f16 v[64:79], a[128:131], v[160:163], v[64:79]
	ds_read_b128 v[160:163], v193 offset:8192
	v_rcp_f32_e32 v208, v208
	v_mul_f32_e32 v207, v207, v143
	v_mfma_f32_32x32x16_f16 v[80:95], a[128:131], v[164:167], v[80:95]
	ds_read_b128 v[164:167], v193 offset:9216
	v_rcp_f32_e32 v209, v209
	v_fmamk_f32 v208, v208, 0xc0b8aa3b, v198
	s_waitcnt lgkmcnt(6)
	v_mfma_f32_32x32x16_f16 v[64:79], a[132:135], v[168:171], v[64:79]
	ds_read_b128 v[168:171], v193 offset:10240
	v_rcp_f32_e32 v210, v210
	v_fmamk_f32 v209, v209, 0xc0b8aa3b, v198
	v_fma_f32 v140, v200, v208, v204
	v_mfma_f32_32x32x16_f16 v[80:95], a[132:135], v[172:175], v[80:95]
	ds_read_b128 v[172:175], v193 offset:11264
	global_load_lds_dwordx4 v192, s[44:45] offset:1024 sc1
	v_rcp_f32_e32 v211, v211
	v_fmamk_f32 v210, v210, 0xc0b8aa3b, v198
	v_fma_f32 v141, v201, v209, v205
	s_waitcnt lgkmcnt(6)
	v_mfma_f32_32x32x16_f16 v[64:79], a[136:139], v[176:179], v[64:79]
	ds_read_b128 v[176:179], v193 offset:12288
	v_rcp_f32_e32 v212, v212
	v_fmamk_f32 v211, v211, 0xc0b8aa3b, v198
	v_fma_f32 v142, v202, v210, v206
	v_mfma_f32_32x32x16_f16 v[80:95], a[136:139], v[180:183], v[80:95]
	ds_read_b128 v[180:183], v193 offset:13312
	v_rcp_f32_e32 v213, v213
	v_fma_f32 v143, v203, v211, v207
	s_waitcnt lgkmcnt(6)
	v_mfma_f32_32x32x16_f16 v[64:79], a[140:143], v[184:187], v[64:79]
	ds_read_b128 v[184:187], v193 offset:14336
	v_rcp_f32_e32 v214, v214
	v_mfma_f32_32x32x16_f16 v[80:95], a[140:143], v[188:191], v[80:95]
	ds_read_b128 v[188:191], v193 offset:15360
	global_load_lds_dwordx4 v192, s[44:45] offset:2048 sc1
	v_rcp_f32_e32 v215, v215
	s_waitcnt lgkmcnt(6)
	v_mfma_f32_32x32x16_f16 v[64:79], a[144:147], v[160:163], v[64:79]
	ds_read_b128 v[160:163], v193 offset:16384
	v_exp_f32_e32 v200, v140
	v_mfma_f32_32x32x16_f16 v[80:95], a[144:147], v[164:167], v[80:95]
	ds_read_b128 v[164:167], v193 offset:17408
	v_exp_f32_e32 v201, v141
	v_add_f32_e32 v200, 1.0, v200
	s_waitcnt lgkmcnt(6)
	v_mfma_f32_32x32x16_f16 v[64:79], a[148:151], v[168:171], v[64:79]
	ds_read_b128 v[168:171], v193 offset:18432
	v_exp_f32_e32 v202, v142
	v_add_f32_e32 v201, 1.0, v201
	v_mfma_f32_32x32x16_f16 v[80:95], a[148:151], v[172:175], v[80:95]
	ds_read_b128 v[172:175], v193 offset:19456
	global_load_lds_dwordx4 v192, s[44:45] offset:3072 sc1
	v_exp_f32_e32 v203, v143
	v_add_f32_e32 v202, 1.0, v202
	s_waitcnt lgkmcnt(6)
	v_mfma_f32_32x32x16_f16 v[64:79], a[152:155], v[176:179], v[64:79]
	ds_read_b128 v[176:179], v193 offset:20480
	v_add_f32_e32 v203, 1.0, v203
	v_rcp_f32_e32 v200, v200
	v_mfma_f32_32x32x16_f16 v[80:95], a[152:155], v[180:183], v[80:95]
	ds_read_b128 v[180:183], v193 offset:21504
	v_rcp_f32_e32 v201, v201
	v_fma_f32 v200, v200, 2.0, -1.0
	s_waitcnt lgkmcnt(6)
	v_mfma_f32_32x32x16_f16 v[64:79], a[156:159], v[184:187], v[64:79]
	ds_read_b128 v[184:187], v193 offset:22528
	v_rcp_f32_e32 v202, v202
	v_fma_f32 v201, v201, 2.0, -1.0
	v_mul_f32_e32 v216, v212, v200
	v_mfma_f32_32x32x16_f16 v[80:95], a[156:159], v[188:191], v[80:95]
	ds_read_b128 v[188:191], v193 offset:23552
	s_add_u32 s44, s34, 0x1000
	s_addc_u32 s45, s35, 0
	s_mov_b32 m0, s53
	s_nop 0
	global_load_lds_dwordx4 v192, s[44:45] sc1
	v_rcp_f32_e32 v203, v203
	v_fma_f32 v202, v202, 2.0, -1.0
	v_mul_f32_e32 v217, v213, v201
	s_waitcnt lgkmcnt(6)
	v_mfma_f32_32x32x16_f16 v[64:79], a[160:163], v[160:163], v[64:79]
	ds_read_b128 v[160:163], v193 offset:24576
	v_fma_f32 v203, v203, 2.0, -1.0
	v_mul_f32_e32 v218, v214, v202
	v_mfma_f32_32x32x16_f16 v[80:95], a[160:163], v[164:167], v[80:95]
	ds_read_b128 v[164:167], v193 offset:25600
	v_mul_f32_e32 v219, v215, v203
	v_cvt_pk_f16_f32 v222, v216, v217
	s_waitcnt lgkmcnt(6)
	v_mfma_f32_32x32x16_f16 v[64:79], a[164:167], v[168:171], v[64:79]
	ds_read_b128 v[168:171], v193 offset:26624
	v_cvt_pk_f16_f32 v223, v218, v219
	v_mfma_f32_32x32x16_f16 v[80:95], a[164:167], v[172:175], v[80:95]
	ds_read_b128 v[172:175], v193 offset:27648
	global_load_lds_dwordx4 v192, s[44:45] offset:1024 sc1
	s_cmp_lg_u32 s33, s60
	s_cbranch_scc1 .LE_nht37
	s_add_u32 s46, s62, 0x60000
	s_addc_u32 s47, s63, 0
	global_store_dwordx4 v250, v[216:219], s[46:47]
	s_waitcnt vmcnt(0)
.LE_nht37:
	s_waitcnt lgkmcnt(6)
	v_mfma_f32_32x32x16_f16 v[64:79], a[168:171], v[176:179], v[64:79]
	ds_read_b128 v[176:179], v193 offset:28672
	s_nop 1
	v_permlane32_swap_b32_e32 v220, v222
	v_permlane32_swap_b32_e32 v221, v223
	s_cmp_eq_u32 s31, 0
	s_cbranch_scc1 .LE_slow38
	global_store_dwordx4 v195, v[220:223], s[36:37] offset:0
	s_branch .LE_join39

.LE_join39:
	v_mfma_f32_32x32x16_f16 v[80:95], a[168:171], v[180:183], v[80:95]
	ds_read_b128 v[180:183], v193 offset:29696
	s_waitcnt lgkmcnt(6)
	v_mfma_f32_32x32x16_f16 v[64:79], a[172:175], v[184:187], v[64:79]
	ds_read_b128 v[184:187], v193 offset:30720
	v_mfma_f32_32x32x16_f16 v[80:95], a[172:175], v[188:191], v[80:95]
	ds_read_b128 v[188:191], v193 offset:31744
	global_load_lds_dwordx4 v192, s[44:45] offset:2048 sc1
	s_waitcnt vmcnt(8)
	s_barrier
	s_waitcnt lgkmcnt(6)
	v_mfma_f32_32x32x16_f16 v[64:79], a[176:179], v[160:163], v[64:79]
	ds_read_b128 v[160:163], v193 offset:32768
	v_mfma_f32_32x32x16_f16 v[80:95], a[176:179], v[164:167], v[80:95]
	ds_read_b128 v[164:167], v193 offset:33792
	s_waitcnt lgkmcnt(6)
	v_mfma_f32_32x32x16_f16 v[64:79], a[180:183], v[168:171], v[64:79]
	ds_read_b128 v[168:171], v193 offset:34816
	v_mfma_f32_32x32x16_f16 v[80:95], a[180:183], v[172:175], v[80:95]
	ds_read_b128 v[172:175], v193 offset:35840
	global_load_lds_dwordx4 v192, s[44:45] offset:3072 sc1
	s_waitcnt lgkmcnt(6)
	v_mfma_f32_32x32x16_f16 v[64:79], a[184:187], v[176:179], v[64:79]
	ds_read_b128 v[176:179], v193 offset:36864
	v_mfma_f32_32x32x16_f16 v[80:95], a[184:187], v[180:183], v[80:95]
	ds_read_b128 v[180:183], v193 offset:37888
	s_waitcnt lgkmcnt(6)
	v_mfma_f32_32x32x16_f16 v[64:79], a[188:191], v[184:187], v[64:79]
	ds_read_b128 v[184:187], v193 offset:38912
	v_mfma_f32_32x32x16_f16 v[80:95], a[188:191], v[188:191], v[80:95]
	ds_read_b128 v[188:191], v193 offset:39936
	s_add_u32 s44, s34, 0x8000
	s_addc_u32 s45, s35, 0
	s_mov_b32 m0, s54
	s_nop 0
	global_load_lds_dwordx4 v192, s[44:45] sc1
	s_waitcnt lgkmcnt(6)
	v_mfma_f32_32x32x16_f16 v[64:79], a[192:195], v[160:163], v[64:79]
	ds_read_b128 v[160:163], v193 offset:40960
	v_mfma_f32_32x32x16_f16 v[80:95], a[192:195], v[164:167], v[80:95]
	ds_read_b128 v[164:167], v193 offset:41984
	s_waitcnt vmcnt(3)
	s_barrier
	v_mov_b32_e32 v199, 2
	s_cmp_eq_u32 s31, 0
	s_cbranch_scc1 .LE_slow40
	global_store_dword v197, v199, s[40:41]
	s_branch .LE_join41

.LE_join41:
	s_waitcnt lgkmcnt(6)
	v_mfma_f32_32x32x16_f16 v[64:79], a[196:199], v[168:171], v[64:79]
	ds_read_b128 v[168:171], v193 offset:43008
	v_mfma_f32_32x32x16_f16 v[80:95], a[196:199], v[172:175], v[80:95]
	ds_read_b128 v[172:175], v193 offset:44032
	global_load_lds_dwordx4 v192, s[44:45] offset:1024 sc1
	s_waitcnt lgkmcnt(6)
	v_mfma_f32_32x32x16_f16 v[64:79], a[200:203], v[176:179], v[64:79]
	ds_read_b128 v[176:179], v193 offset:45056
	v_mfma_f32_32x32x16_f16 v[80:95], a[200:203], v[180:183], v[80:95]
	ds_read_b128 v[180:183], v193 offset:46080
	s_waitcnt lgkmcnt(6)
	v_mfma_f32_32x32x16_f16 v[64:79], a[204:207], v[184:187], v[64:79]
	ds_read_b128 v[184:187], v193 offset:47104
	v_mfma_f32_32x32x16_f16 v[80:95], a[204:207], v[188:191], v[80:95]
	ds_read_b128 v[188:191], v193 offset:48128
	global_load_lds_dwordx4 v192, s[44:45] offset:2048 sc1
	s_waitcnt lgkmcnt(6)
	v_mfma_f32_32x32x16_f16 v[64:79], a[208:211], v[160:163], v[64:79]
	ds_read_b128 v[160:163], v193 offset:49152
	v_mfma_f32_32x32x16_f16 v[80:95], a[208:211], v[164:167], v[80:95]
	ds_read_b128 v[164:167], v193 offset:50176
	s_waitcnt lgkmcnt(6)
	v_mfma_f32_32x32x16_f16 v[64:79], a[212:215], v[168:171], v[64:79]
	ds_read_b128 v[168:171], v193 offset:51200
	v_mfma_f32_32x32x16_f16 v[80:95], a[212:215], v[172:175], v[80:95]
	ds_read_b128 v[172:175], v193 offset:52224
	global_load_lds_dwordx4 v192, s[44:45] offset:3072 sc1
	s_waitcnt lgkmcnt(6)
	v_mfma_f32_32x32x16_f16 v[64:79], a[216:219], v[176:179], v[64:79]
	ds_read_b128 v[176:179], v193 offset:53248
	v_mfma_f32_32x32x16_f16 v[80:95], a[216:219], v[180:183], v[80:95]
	ds_read_b128 v[180:183], v193 offset:54272
	s_waitcnt lgkmcnt(6)
	v_mfma_f32_32x32x16_f16 v[64:79], a[220:223], v[184:187], v[64:79]
	ds_read_b128 v[184:187], v193 offset:55296
	v_mfma_f32_32x32x16_f16 v[80:95], a[220:223], v[188:191], v[80:95]
	ds_read_b128 v[188:191], v193 offset:56320
	s_add_u32 s44, s34, 0x9000
	s_addc_u32 s45, s35, 0
	s_mov_b32 m0, s55
	s_nop 0
	global_load_lds_dwordx4 v192, s[44:45] sc1
	s_waitcnt lgkmcnt(6)
	v_mfma_f32_32x32x16_f16 v[64:79], a[224:227], v[160:163], v[64:79]
	ds_read_b128 v[160:163], v193 offset:57344
	v_mfma_f32_32x32x16_f16 v[80:95], a[224:227], v[164:167], v[80:95]
	ds_read_b128 v[164:167], v193 offset:58368
	s_waitcnt lgkmcnt(6)
	v_mfma_f32_32x32x16_f16 v[64:79], a[228:231], v[168:171], v[64:79]
	ds_read_b128 v[168:171], v193 offset:59392
	v_mfma_f32_32x32x16_f16 v[80:95], a[228:231], v[172:175], v[80:95]
	ds_read_b128 v[172:175], v193 offset:60416
	global_load_lds_dwordx4 v192, s[44:45] offset:1024 sc1
	s_waitcnt lgkmcnt(6)
	v_mfma_f32_32x32x16_f16 v[64:79], a[232:235], v[176:179], v[64:79]
	ds_read_b128 v[176:179], v193 offset:61440
	v_mfma_f32_32x32x16_f16 v[80:95], a[232:235], v[180:183], v[80:95]
	ds_read_b128 v[180:183], v193 offset:62464
	s_waitcnt lgkmcnt(6)
	v_mfma_f32_32x32x16_f16 v[64:79], a[236:239], v[184:187], v[64:79]
	ds_read_b128 v[184:187], v193 offset:63488
	v_mfma_f32_32x32x16_f16 v[80:95], a[236:239], v[188:191], v[80:95]
	ds_read_b128 v[188:191], v193 offset:64512
	global_load_lds_dwordx4 v192, s[44:45] offset:2048 sc1
	s_waitcnt vmcnt(8)
	s_barrier
	s_waitcnt lgkmcnt(6)
	v_mfma_f32_32x32x16_f16 v[64:79], a[240:243], v[160:163], v[64:79]
	ds_read_b128 v[160:163], v192 offset:0
	v_mfma_f32_32x32x16_f16 v[80:95], a[240:243], v[164:167], v[80:95]
	ds_read_b128 v[164:167], v192 offset:1024
	s_waitcnt lgkmcnt(6)
	v_mfma_f32_32x32x16_f16 v[64:79], a[244:247], v[168:171], v[64:79]
	ds_read_b128 v[168:171], v192 offset:2048
	v_mfma_f32_32x32x16_f16 v[80:95], a[244:247], v[172:175], v[80:95]
	ds_read_b128 v[172:175], v192 offset:3072
	global_load_lds_dwordx4 v192, s[44:45] offset:3072 sc1
	s_waitcnt lgkmcnt(6)
	v_mfma_f32_32x32x16_f16 v[64:79], a[248:251], v[176:179], v[64:79]
	ds_read_b128 v[176:179], v192 offset:4096
	v_mfma_f32_32x32x16_f16 v[80:95], a[248:251], v[180:183], v[80:95]
	ds_read_b128 v[180:183], v192 offset:5120
	s_waitcnt lgkmcnt(6)
	v_mfma_f32_32x32x16_f16 v[64:79], a[252:255], v[184:187], v[64:79]
	ds_read_b128 v[184:187], v192 offset:6144
	v_mfma_f32_32x32x16_f16 v[80:95], a[252:255], v[188:191], v[80:95]
	ds_read_b128 v[188:191], v192 offset:7168
	s_add_u32 s44, s34, 0x10000
	s_addc_u32 s45, s35, 0
	s_mov_b32 m0, s56
	s_nop 0
	global_load_lds_dwordx4 v192, s[44:45] sc1
	s_and_b32 s64, s33, 1
	s_lshl_b32 s64, s64, 22
	s_add_u32 s64, s64, s50
	s_add_u32 s64, s64, 0x40000
	s_add_u32 s36, s6, s64
	s_addc_u32 s37, s7, 0
	s_lshl_b32 s64, s33, 3
	s_add_u32 s64, s64, s29
	s_lshl_b32 s64, s64, 5
	s_add_u32 s64, s64, s30
	s_lshl_b32 s64, s64, 2
	s_add_u32 s40, s8, s64
	s_addc_u32 s41, s9, 0
	s_lshl_b32 s64, s61, 11
	s_lshl_b32 s65, s29, 8
	s_add_u32 s64, s64, s65
	s_add_u32 s64, s64, 64
	s_lshl_b32 s64, s64, 3
	s_add_u32 s42, s12, s64
	s_addc_u32 s43, s13, 0
	s_nop 11
	global_load_dwordx2 v[228:229], v249, s[42:43] offset:0
	global_load_dwordx2 v[230:231], v249, s[42:43] offset:256
	s_waitcnt lgkmcnt(6)
	v_mfma_f32_32x32x16_f16 v[96:111], a[0:3], v[160:163], v[96:111]
	ds_read_b128 v[160:163], v192 offset:8192
	v_exp_f32_e32 v200, v64
	v_mfma_f32_32x32x16_f16 v[112:127], a[0:3], v[164:167], v[112:127]
	ds_read_b128 v[164:167], v192 offset:9216
	v_exp_f32_e32 v201, v65
	v_add_f32_e32 v200, 1.0, v200
	s_waitcnt lgkmcnt(6)
	v_mfma_f32_32x32x16_f16 v[96:111], a[4:7], v[168:171], v[96:111]
	ds_read_b128 v[168:171], v192 offset:10240
	v_exp_f32_e32 v202, v66
	v_add_f32_e32 v201, 1.0, v201
	v_mfma_f32_32x32x16_f16 v[112:127], a[4:7], v[172:175], v[112:127]
	ds_read_b128 v[172:175], v192 offset:11264
	global_load_lds_dwordx4 v192, s[44:45] offset:1024 sc1
	v_exp_f32_e32 v203, v67
	v_add_f32_e32 v202, 1.0, v202
	s_waitcnt lgkmcnt(6)
	v_mfma_f32_32x32x16_f16 v[96:111], a[8:11], v[176:179], v[96:111]
	ds_read_b128 v[176:179], v192 offset:12288
	v_exp_f32_e32 v204, v68
	v_add_f32_e32 v203, 1.0, v203
	v_mfma_f32_32x32x16_f16 v[112:127], a[8:11], v[180:183], v[112:127]
	ds_read_b128 v[180:183], v192 offset:13312
	v_exp_f32_e32 v205, v69
	v_add_f32_e32 v204, 1.0, v204
	s_waitcnt lgkmcnt(6)
	v_mfma_f32_32x32x16_f16 v[96:111], a[12:15], v[184:187], v[96:111]
	ds_read_b128 v[184:187], v192 offset:14336
	v_exp_f32_e32 v206, v70
	v_add_f32_e32 v205, 1.0, v205
	v_mfma_f32_32x32x16_f16 v[112:127], a[12:15], v[188:191], v[112:127]
	ds_read_b128 v[188:191], v192 offset:15360
	global_load_lds_dwordx4 v192, s[44:45] offset:2048 sc1
	v_exp_f32_e32 v207, v71
	v_add_f32_e32 v206, 1.0, v206
	s_waitcnt lgkmcnt(6)
	v_mfma_f32_32x32x16_f16 v[96:111], a[16:19], v[160:163], v[96:111]
	ds_read_b128 v[160:163], v192 offset:16384
	v_exp_f32_e32 v208, v72
	v_add_f32_e32 v207, 1.0, v207
	v_mfma_f32_32x32x16_f16 v[112:127], a[16:19], v[164:167], v[112:127]
	ds_read_b128 v[164:167], v192 offset:17408
	v_exp_f32_e32 v209, v73
	v_add_f32_e32 v208, 1.0, v208
	s_waitcnt lgkmcnt(6)
	v_mfma_f32_32x32x16_f16 v[96:111], a[20:23], v[168:171], v[96:111]
	ds_read_b128 v[168:171], v192 offset:18432
	v_exp_f32_e32 v210, v74
	v_add_f32_e32 v209, 1.0, v209
	v_mfma_f32_32x32x16_f16 v[112:127], a[20:23], v[172:175], v[112:127]
	ds_read_b128 v[172:175], v192 offset:19456
	global_load_lds_dwordx4 v192, s[44:45] offset:3072 sc1
	v_exp_f32_e32 v211, v75
	v_add_f32_e32 v210, 1.0, v210
	s_waitcnt lgkmcnt(6)
	v_mfma_f32_32x32x16_f16 v[96:111], a[24:27], v[176:179], v[96:111]
	ds_read_b128 v[176:179], v192 offset:20480
	v_exp_f32_e32 v212, v76
	v_add_f32_e32 v211, 1.0, v211
	v_mfma_f32_32x32x16_f16 v[112:127], a[24:27], v[180:183], v[112:127]
	ds_read_b128 v[180:183], v192 offset:21504
	v_exp_f32_e32 v213, v77
	v_add_f32_e32 v212, 1.0, v212
	s_waitcnt lgkmcnt(6)
	v_mfma_f32_32x32x16_f16 v[96:111], a[28:31], v[184:187], v[96:111]
	ds_read_b128 v[184:187], v192 offset:22528
	v_exp_f32_e32 v214, v78
	v_add_f32_e32 v213, 1.0, v213
	v_mfma_f32_32x32x16_f16 v[112:127], a[28:31], v[188:191], v[112:127]
	ds_read_b128 v[188:191], v192 offset:23552
	s_add_u32 s44, s34, 0x11000
	s_addc_u32 s45, s35, 0
	s_mov_b32 m0, s57
	s_nop 0
	global_load_lds_dwordx4 v192, s[44:45] sc1
	v_exp_f32_e32 v215, v79
	v_add_f32_e32 v214, 1.0, v214
	s_waitcnt lgkmcnt(6)
	v_mfma_f32_32x32x16_f16 v[96:111], a[32:35], v[160:163], v[96:111]
	ds_read_b128 v[160:163], v192 offset:24576
	v_add_f32_e32 v215, 1.0, v215
	v_rcp_f32_e32 v200, v200
	v_mfma_f32_32x32x16_f16 v[112:127], a[32:35], v[164:167], v[112:127]
	ds_read_b128 v[164:167], v192 offset:25600
	v_rcp_f32_e32 v201, v201
	s_waitcnt lgkmcnt(6)
	v_mfma_f32_32x32x16_f16 v[96:111], a[36:39], v[168:171], v[96:111]
	ds_read_b128 v[168:171], v192 offset:26624
	v_rcp_f32_e32 v202, v202
	v_mfma_f32_32x32x16_f16 v[112:127], a[36:39], v[172:175], v[112:127]
	ds_read_b128 v[172:175], v192 offset:27648
	global_load_lds_dwordx4 v192, s[44:45] offset:1024 sc1
	v_rcp_f32_e32 v203, v203
	s_waitcnt lgkmcnt(6)
	v_mfma_f32_32x32x16_f16 v[96:111], a[40:43], v[176:179], v[96:111]
	ds_read_b128 v[176:179], v192 offset:28672
	v_rcp_f32_e32 v204, v204
	v_mfma_f32_32x32x16_f16 v[112:127], a[40:43], v[180:183], v[112:127]
	ds_read_b128 v[180:183], v192 offset:29696
	v_rcp_f32_e32 v205, v205
	v_mul_f32_e32 v204, v204, v144
	s_waitcnt lgkmcnt(6)
	v_mfma_f32_32x32x16_f16 v[96:111], a[44:47], v[184:187], v[96:111]
	ds_read_b128 v[184:187], v192 offset:30720
	v_rcp_f32_e32 v206, v206
	v_mul_f32_e32 v205, v205, v145
	v_mfma_f32_32x32x16_f16 v[112:127], a[44:47], v[188:191], v[112:127]
	ds_read_b128 v[188:191], v192 offset:31744
	global_load_lds_dwordx4 v192, s[44:45] offset:2048 sc1
	v_rcp_f32_e32 v207, v207
	v_mul_f32_e32 v206, v206, v146
	s_waitcnt vmcnt(9)
	s_barrier
	s_waitcnt lgkmcnt(6)
	v_mfma_f32_32x32x16_f16 v[96:111], a[48:51], v[160:163], v[96:111]
	ds_read_b128 v[160:163], v192 offset:32768
	v_rcp_f32_e32 v208, v208
	v_mul_f32_e32 v207, v207, v147
	ds_read_b128 v[236:239], v248 offset:0
	ds_read_b64 v[240:241], v248 offset:32
	ds_read_b128 v[242:245], v248 offset:16
	ds_read_b64 v[246:247], v248 offset:40
	v_mfma_f32_32x32x16_f16 v[112:127], a[48:51], v[164:167], v[112:127]
	ds_read_b128 v[164:167], v192 offset:33792
	v_rcp_f32_e32 v209, v209
	v_fmamk_f32 v208, v208, 0xc0b8aa3b, v198
	s_waitcnt lgkmcnt(3)
	s_waitcnt vmcnt(6)
	v_fma_f32 v32, v229, v237, v240
	v_mfma_f32_32x32x16_f16 v[96:111], a[52:55], v[168:171], v[96:111]
	ds_read_b128 v[168:171], v192 offset:34816
	v_rcp_f32_e32 v210, v210
	v_fmamk_f32 v209, v209, 0xc0b8aa3b, v198
	v_fma_f32 v144, v200, v208, v204
	v_fma_f32 v33, v229, v239, v241
	v_fmac_f32_e32 v32, v228, v236
	v_mfma_f32_32x32x16_f16 v[112:127], a[52:55], v[172:175], v[112:127]
	ds_read_b128 v[172:175], v192 offset:35840
	global_load_lds_dwordx4 v192, s[44:45] offset:3072 sc1
	v_rcp_f32_e32 v211, v211
	v_fmamk_f32 v210, v210, 0xc0b8aa3b, v198
	v_fma_f32 v145, v201, v209, v205
	v_fmac_f32_e32 v33, v228, v238
	v_fma_f32 v48, v231, v237, v240
	v_mfma_f32_32x32x16_f16 v[96:111], a[56:59], v[176:179], v[96:111]
	ds_read_b128 v[176:179], v192 offset:36864
	v_rcp_f32_e32 v212, v212
	v_fmamk_f32 v211, v211, 0xc0b8aa3b, v198
	v_fma_f32 v146, v202, v210, v206
	v_fma_f32 v49, v231, v239, v241
	v_fmac_f32_e32 v48, v230, v236
	v_mfma_f32_32x32x16_f16 v[112:127], a[56:59], v[180:183], v[112:127]
	ds_read_b128 v[180:183], v192 offset:37888
	v_rcp_f32_e32 v213, v213
	v_fma_f32 v147, v203, v211, v207
	v_fmac_f32_e32 v49, v230, v238
	ds_read_b128 v[236:239], v248 offset:48
	ds_read_b64 v[240:241], v248 offset:80
	v_mfma_f32_32x32x16_f16 v[96:111], a[60:63], v[184:187], v[96:111]
	ds_read_b128 v[184:187], v192 offset:38912
	v_rcp_f32_e32 v214, v214
	s_waitcnt lgkmcnt(8)
	v_fma_f32 v34, v229, v243, v246
	v_mfma_f32_32x32x16_f16 v[112:127], a[60:63], v[188:191], v[112:127]
	ds_read_b128 v[188:191], v192 offset:39936
	s_add_u32 s44, s34, 0x18000
	s_addc_u32 s45, s35, 0
	s_mov_b32 m0, s58
	s_nop 0
	global_load_lds_dwordx4 v192, s[44:45] sc1
	v_rcp_f32_e32 v215, v215
	v_fma_f32 v35, v229, v245, v247
	v_fmac_f32_e32 v34, v228, v242
	s_waitcnt lgkmcnt(8)
	v_mfma_f32_32x32x16_f16 v[96:111], a[64:67], v[160:163], v[96:111]
	ds_read_b128 v[160:163], v192 offset:40960
	v_exp_f32_e32 v200, v144
	v_fmac_f32_e32 v35, v228, v244
	v_fma_f32 v50, v231, v243, v246
	v_mfma_f32_32x32x16_f16 v[112:127], a[64:67], v[164:167], v[112:127]
	ds_read_b128 v[164:167], v192 offset:41984
	v_exp_f32_e32 v201, v145
	v_add_f32_e32 v200, 1.0, v200
	v_fma_f32 v51, v231, v245, v247
	v_fmac_f32_e32 v50, v230, v242
	s_waitcnt lgkmcnt(8)
	v_mfma_f32_32x32x16_f16 v[96:111], a[68:71], v[168:171], v[96:111]
	ds_read_b128 v[168:171], v192 offset:43008
	v_exp_f32_e32 v202, v146
	v_add_f32_e32 v201, 1.0, v201
	v_fmac_f32_e32 v51, v230, v244
	ds_read_b128 v[242:245], v248 offset:64
	ds_read_b64 v[246:247], v248 offset:88
	v_mfma_f32_32x32x16_f16 v[112:127], a[68:71], v[172:175], v[112:127]
	ds_read_b128 v[172:175], v192 offset:44032
	global_load_lds_dwordx4 v192, s[44:45] offset:1024 sc1
	v_exp_f32_e32 v203, v147
	v_add_f32_e32 v202, 1.0, v202
	s_waitcnt lgkmcnt(8)
	v_fma_f32 v36, v229, v237, v240
	v_mfma_f32_32x32x16_f16 v[96:111], a[72:75], v[176:179], v[96:111]
	ds_read_b128 v[176:179], v192 offset:45056
	v_add_f32_e32 v203, 1.0, v203
	v_rcp_f32_e32 v200, v200
	v_fma_f32 v37, v229, v239, v241
	v_fmac_f32_e32 v36, v228, v236
	v_mfma_f32_32x32x16_f16 v[112:127], a[72:75], v[180:183], v[112:127]
	ds_read_b128 v[180:183], v192 offset:46080
	v_rcp_f32_e32 v201, v201
	v_fma_f32 v200, v200, 2.0, -1.0
	v_fmac_f32_e32 v37, v228, v238
	v_fma_f32 v52, v231, v237, v240
	s_waitcnt lgkmcnt(8)
	v_mfma_f32_32x32x16_f16 v[96:111], a[76:79], v[184:187], v[96:111]
	ds_read_b128 v[184:187], v192 offset:47104
	v_rcp_f32_e32 v202, v202
	v_fma_f32 v201, v201, 2.0, -1.0
	v_mul_f32_e32 v216, v212, v200
	v_fma_f32 v53, v231, v239, v241
	v_fmac_f32_e32 v52, v230, v236
	v_mfma_f32_32x32x16_f16 v[112:127], a[76:79], v[188:191], v[112:127]
	ds_read_b128 v[188:191], v192 offset:48128
	global_load_lds_dwordx4 v192, s[44:45] offset:2048 sc1
	v_rcp_f32_e32 v203, v203
	v_fma_f32 v202, v202, 2.0, -1.0
	v_mul_f32_e32 v217, v213, v201
	v_fmac_f32_e32 v53, v230, v238
	ds_read_b128 v[236:239], v248 offset:96
	ds_read_b64 v[240:241], v248 offset:128
	s_waitcnt lgkmcnt(10)
	v_mfma_f32_32x32x16_f16 v[96:111], a[80:83], v[160:163], v[96:111]
	ds_read_b128 v[160:163], v192 offset:49152
	v_fma_f32 v203, v203, 2.0, -1.0
	v_mul_f32_e32 v218, v214, v202
	v_exp_f32_e32 v200, v80
	s_waitcnt lgkmcnt(8)
	v_fma_f32 v38, v229, v243, v246
	v_mfma_f32_32x32x16_f16 v[112:127], a[80:83], v[164:167], v[112:127]
	ds_read_b128 v[164:167], v192 offset:50176
	v_mul_f32_e32 v219, v215, v203
	v_cvt_pk_f16_f32 v220, v216, v217
	v_exp_f32_e32 v201, v81
	v_fma_f32 v39, v229, v245, v247
	v_fmac_f32_e32 v38, v228, v242
	s_waitcnt lgkmcnt(8)
	v_mfma_f32_32x32x16_f16 v[96:111], a[84:87], v[168:171], v[96:111]
	ds_read_b128 v[168:171], v192 offset:51200
	v_cvt_pk_f16_f32 v221, v218, v219
	v_exp_f32_e32 v202, v82
	v_add_f32_e32 v200, 1.0, v200
	v_fmac_f32_e32 v39, v228, v244
	v_fma_f32 v54, v231, v243, v246
	v_mfma_f32_32x32x16_f16 v[112:127], a[84:87], v[172:175], v[112:127]
	ds_read_b128 v[172:175], v192 offset:52224
	global_load_lds_dwordx4 v192, s[44:45] offset:3072 sc1
	s_cmp_lg_u32 s33, s60
	s_cbranch_scc1 .LE_nht42
	s_add_u32 s46, s62, 0x80000
	s_addc_u32 s47, s63, 0
	global_store_dwordx4 v250, v[216:219], s[46:47]
	s_waitcnt vmcnt(0)
.LE_nht42:
	v_exp_f32_e32 v203, v83
	v_fma_f32 v55, v231, v245, v247
	v_fmac_f32_e32 v54, v230, v242
	s_waitcnt lgkmcnt(8)
	v_mfma_f32_32x32x16_f16 v[96:111], a[88:91], v[176:179], v[96:111]
	ds_read_b128 v[176:179], v192 offset:53248
	v_exp_f32_e32 v204, v84
	v_add_f32_e32 v201, 1.0, v201
	v_add_f32_e32 v202, 1.0, v202
	v_fmac_f32_e32 v55, v230, v244
	ds_read_b128 v[242:245], v248 offset:112
	ds_read_b64 v[246:247], v248 offset:136
	v_mfma_f32_32x32x16_f16 v[112:127], a[88:91], v[180:183], v[112:127]
	ds_read_b128 v[180:183], v192 offset:54272
	v_exp_f32_e32 v205, v85
	v_add_f32_e32 v203, 1.0, v203
	v_add_f32_e32 v204, 1.0, v204
	s_waitcnt lgkmcnt(8)
	v_fma_f32 v40, v229, v237, v240
	v_mfma_f32_32x32x16_f16 v[96:111], a[92:95], v[184:187], v[96:111]
	ds_read_b128 v[184:187], v192 offset:55296
	v_exp_f32_e32 v206, v86
	v_add_f32_e32 v205, 1.0, v205
	v_fma_f32 v41, v229, v239, v241
	v_fmac_f32_e32 v40, v228, v236
	v_mfma_f32_32x32x16_f16 v[112:127], a[92:95], v[188:191], v[112:127]
	ds_read_b128 v[188:191], v192 offset:56320
	s_add_u32 s44, s34, 0x19000
	s_addc_u32 s45, s35, 0
	s_mov_b32 m0, s59
	s_nop 0
	global_load_lds_dwordx4 v192, s[44:45] sc1
	s_lshl_b32 s64, s33, 3
	s_add_u32 s64, s64, s29
	s_lshl_b32 s64, s64, 7
	s_add_u32 s38, s8, s64
	s_addc_u32 s39, s9, 0
	global_load_dword v251, v196, s[38:39] sc1
	v_exp_f32_e32 v207, v87
	v_add_f32_e32 v206, 1.0, v206
	v_fmac_f32_e32 v41, v228, v238
	v_fma_f32 v56, v231, v237, v240
	s_waitcnt lgkmcnt(8)
	v_mfma_f32_32x32x16_f16 v[96:111], a[96:99], v[160:163], v[96:111]
	ds_read_b128 v[160:163], v192 offset:57344
	v_exp_f32_e32 v208, v88
	v_add_f32_e32 v207, 1.0, v207
	v_fma_f32 v57, v231, v239, v241
	v_fmac_f32_e32 v56, v230, v236
	v_mfma_f32_32x32x16_f16 v[112:127], a[96:99], v[164:167], v[112:127]
	ds_read_b128 v[164:167], v192 offset:58368
	v_exp_f32_e32 v209, v89
	v_add_f32_e32 v208, 1.0, v208
	v_fmac_f32_e32 v57, v230, v238
	ds_read_b128 v[236:239], v248 offset:144
	ds_read_b64 v[240:241], v248 offset:176
	s_waitcnt lgkmcnt(10)
	v_mfma_f32_32x32x16_f16 v[96:111], a[100:103], v[168:171], v[96:111]
	ds_read_b128 v[168:171], v192 offset:59392
	v_exp_f32_e32 v210, v90
	v_add_f32_e32 v209, 1.0, v209
	s_waitcnt lgkmcnt(8)
	v_fma_f32 v42, v229, v243, v246
	v_mfma_f32_32x32x16_f16 v[112:127], a[100:103], v[172:175], v[112:127]
	ds_read_b128 v[172:175], v192 offset:60416
	global_load_lds_dwordx4 v192, s[44:45] offset:1024 sc1
	v_exp_f32_e32 v211, v91
	v_add_f32_e32 v210, 1.0, v210
	v_fma_f32 v43, v229, v245, v247
	v_fmac_f32_e32 v42, v228, v242
	s_waitcnt lgkmcnt(8)
	v_mfma_f32_32x32x16_f16 v[96:111], a[104:107], v[176:179], v[96:111]
	ds_read_b128 v[176:179], v192 offset:61440
	v_exp_f32_e32 v212, v92
	v_add_f32_e32 v211, 1.0, v211
	v_fmac_f32_e32 v43, v228, v244
	v_fma_f32 v58, v231, v243, v246
	v_mfma_f32_32x32x16_f16 v[112:127], a[104:107], v[180:183], v[112:127]
	ds_read_b128 v[180:183], v192 offset:62464
	v_exp_f32_e32 v213, v93
	v_add_f32_e32 v212, 1.0, v212
	v_fma_f32 v59, v231, v245, v247
	v_fmac_f32_e32 v58, v230, v242
	s_waitcnt lgkmcnt(8)
	v_mfma_f32_32x32x16_f16 v[96:111], a[108:111], v[184:187], v[96:111]
	ds_read_b128 v[184:187], v192 offset:63488
	v_exp_f32_e32 v214, v94
	v_add_f32_e32 v213, 1.0, v213
	v_fmac_f32_e32 v59, v230, v244
	ds_read_b128 v[242:245], v248 offset:160
	ds_read_b64 v[246:247], v248 offset:184
	v_mfma_f32_32x32x16_f16 v[112:127], a[108:111], v[188:191], v[112:127]
	ds_read_b128 v[188:191], v192 offset:64512
	global_load_lds_dwordx4 v192, s[44:45] offset:2048 sc1
	v_exp_f32_e32 v215, v95
	v_add_f32_e32 v214, 1.0, v214
	s_waitcnt lgkmcnt(8)
	v_fma_f32 v44, v229, v237, v240
	s_waitcnt vmcnt(8)
	s_barrier
	v_mfma_f32_32x32x16_f16 v[96:111], a[112:115], v[160:163], v[96:111]
	ds_read_b128 v[160:163], v193 offset:0
	v_add_f32_e32 v215, 1.0, v215
	v_rcp_f32_e32 v200, v200
	v_fma_f32 v45, v229, v239, v241
	v_fmac_f32_e32 v44, v228, v236
	v_mfma_f32_32x32x16_f16 v[112:127], a[112:115], v[164:167], v[112:127]
	ds_read_b128 v[164:167], v193 offset:1024
	v_rcp_f32_e32 v201, v201
	v_fmac_f32_e32 v45, v228, v238
	v_fma_f32 v60, v231, v237, v240
	s_waitcnt lgkmcnt(8)
	v_mfma_f32_32x32x16_f16 v[96:111], a[116:119], v[168:171], v[96:111]
	ds_read_b128 v[168:171], v193 offset:2048
	v_rcp_f32_e32 v202, v202
	v_fma_f32 v61, v231, v239, v241
	v_fmac_f32_e32 v60, v230, v236
	v_mfma_f32_32x32x16_f16 v[112:127], a[116:119], v[172:175], v[112:127]
	ds_read_b128 v[172:175], v193 offset:3072
	global_load_lds_dwordx4 v192, s[44:45] offset:3072 sc1
	v_rcp_f32_e32 v203, v203
	v_fmac_f32_e32 v61, v230, v238
	s_waitcnt lgkmcnt(5)
	v_mfma_f32_32x32x16_f16 v[96:111], a[120:123], v[176:179], v[96:111]
	ds_read_b128 v[176:179], v193 offset:4096
	v_rcp_f32_e32 v204, v204
	v_fma_f32 v46, v229, v243, v246
	v_fma_f32 v47, v229, v245, v247
	v_mfma_f32_32x32x16_f16 v[112:127], a[120:123], v[180:183], v[112:127]
	ds_read_b128 v[180:183], v193 offset:5120
	v_rcp_f32_e32 v205, v205
	v_mul_f32_e32 v204, v204, v148
	v_fmac_f32_e32 v46, v228, v242
	v_fmac_f32_e32 v47, v228, v244
	s_waitcnt lgkmcnt(6)
	v_mfma_f32_32x32x16_f16 v[96:111], a[124:127], v[184:187], v[96:111]
	ds_read_b128 v[184:187], v193 offset:6144
	v_rcp_f32_e32 v206, v206
	v_mul_f32_e32 v205, v205, v149
	v_fma_f32 v62, v231, v243, v246
	v_fma_f32 v63, v231, v245, v247
	v_mfma_f32_32x32x16_f16 v[112:127], a[124:127], v[188:191], v[112:127]
	ds_read_b128 v[188:191], v193 offset:7168
	s_waitcnt vmcnt(3)
	v_cmp_gt_u32_e32 vcc, 1, v251
	s_cbranch_vccz .LE_tok43

.LE_tok43:
	s_and_b32 s64, s33, 1
	s_lshl_b32 s64, s64, 22
	s_add_u32 s64, s64, s49
	s_add_u32 s34, s6, s64
	s_addc_u32 s35, s7, 0
	s_add_u32 s44, s34, 0x0
	s_addc_u32 s45, s35, 0
	s_mov_b32 m0, s52
	s_nop 0
	global_load_lds_dwordx4 v192, s[44:45] sc1
	v_rcp_f32_e32 v207, v207
	v_mul_f32_e32 v206, v206, v150
	v_fmac_f32_e32 v62, v230, v242
	v_fmac_f32_e32 v63, v230, v244
	s_waitcnt lgkmcnt(6)
	v_mfma_f32_32x32x16_f16 v[96:111], a[128:131], v[160:163], v[96:111]
	ds_read_b128 v[160:163], v193 offset:8192
	v_rcp_f32_e32 v208, v208
	v_mul_f32_e32 v207, v207, v151
	v_mfma_f32_32x32x16_f16 v[112:127], a[128:131], v[164:167], v[112:127]
	ds_read_b128 v[164:167], v193 offset:9216
	v_rcp_f32_e32 v209, v209
	v_fmamk_f32 v208, v208, 0xc0b8aa3b, v198
	s_waitcnt lgkmcnt(6)
	v_mfma_f32_32x32x16_f16 v[96:111], a[132:135], v[168:171], v[96:111]
	ds_read_b128 v[168:171], v193 offset:10240
	v_rcp_f32_e32 v210, v210
	v_fmamk_f32 v209, v209, 0xc0b8aa3b, v198
	v_fma_f32 v148, v200, v208, v204
	v_mfma_f32_32x32x16_f16 v[112:127], a[132:135], v[172:175], v[112:127]
	ds_read_b128 v[172:175], v193 offset:11264
	global_load_lds_dwordx4 v192, s[44:45] offset:1024 sc1
	v_rcp_f32_e32 v211, v211
	v_fmamk_f32 v210, v210, 0xc0b8aa3b, v198
	v_fma_f32 v149, v201, v209, v205
	s_waitcnt lgkmcnt(6)
	v_mfma_f32_32x32x16_f16 v[96:111], a[136:139], v[176:179], v[96:111]
	ds_read_b128 v[176:179], v193 offset:12288
	v_rcp_f32_e32 v212, v212
	v_fmamk_f32 v211, v211, 0xc0b8aa3b, v198
	v_fma_f32 v150, v202, v210, v206
	v_mfma_f32_32x32x16_f16 v[112:127], a[136:139], v[180:183], v[112:127]
	ds_read_b128 v[180:183], v193 offset:13312
	v_rcp_f32_e32 v213, v213
	v_fma_f32 v151, v203, v211, v207
	s_waitcnt lgkmcnt(6)
	v_mfma_f32_32x32x16_f16 v[96:111], a[140:143], v[184:187], v[96:111]
	ds_read_b128 v[184:187], v193 offset:14336
	v_rcp_f32_e32 v214, v214
	v_mfma_f32_32x32x16_f16 v[112:127], a[140:143], v[188:191], v[112:127]
	ds_read_b128 v[188:191], v193 offset:15360
	global_load_lds_dwordx4 v192, s[44:45] offset:2048 sc1
	v_rcp_f32_e32 v215, v215
	s_waitcnt lgkmcnt(6)
	v_mfma_f32_32x32x16_f16 v[96:111], a[144:147], v[160:163], v[96:111]
	ds_read_b128 v[160:163], v193 offset:16384
	v_exp_f32_e32 v200, v148
	v_mfma_f32_32x32x16_f16 v[112:127], a[144:147], v[164:167], v[112:127]
	ds_read_b128 v[164:167], v193 offset:17408
	v_exp_f32_e32 v201, v149
	v_add_f32_e32 v200, 1.0, v200
	s_waitcnt lgkmcnt(6)
	v_mfma_f32_32x32x16_f16 v[96:111], a[148:151], v[168:171], v[96:111]
	ds_read_b128 v[168:171], v193 offset:18432
	v_exp_f32_e32 v202, v150
	v_add_f32_e32 v201, 1.0, v201
	v_mfma_f32_32x32x16_f16 v[112:127], a[148:151], v[172:175], v[112:127]
	ds_read_b128 v[172:175], v193 offset:19456
	global_load_lds_dwordx4 v192, s[44:45] offset:3072 sc1
	v_exp_f32_e32 v203, v151
	v_add_f32_e32 v202, 1.0, v202
	s_waitcnt lgkmcnt(6)
	v_mfma_f32_32x32x16_f16 v[96:111], a[152:155], v[176:179], v[96:111]
	ds_read_b128 v[176:179], v193 offset:20480
	v_add_f32_e32 v203, 1.0, v203
	v_rcp_f32_e32 v200, v200
	v_mfma_f32_32x32x16_f16 v[112:127], a[152:155], v[180:183], v[112:127]
	ds_read_b128 v[180:183], v193 offset:21504
	v_rcp_f32_e32 v201, v201
	v_fma_f32 v200, v200, 2.0, -1.0
	s_waitcnt lgkmcnt(6)
	v_mfma_f32_32x32x16_f16 v[96:111], a[156:159], v[184:187], v[96:111]
	ds_read_b128 v[184:187], v193 offset:22528
	v_rcp_f32_e32 v202, v202
	v_fma_f32 v201, v201, 2.0, -1.0
	v_mul_f32_e32 v216, v212, v200
	v_mfma_f32_32x32x16_f16 v[112:127], a[156:159], v[188:191], v[112:127]
	ds_read_b128 v[188:191], v193 offset:23552
	s_add_u32 s44, s34, 0x1000
	s_addc_u32 s45, s35, 0
	s_mov_b32 m0, s53
	s_nop 0
	global_load_lds_dwordx4 v192, s[44:45] sc1
	v_rcp_f32_e32 v203, v203
	v_fma_f32 v202, v202, 2.0, -1.0
	v_mul_f32_e32 v217, v213, v201
	s_waitcnt lgkmcnt(6)
	v_mfma_f32_32x32x16_f16 v[96:111], a[160:163], v[160:163], v[96:111]
	ds_read_b128 v[160:163], v193 offset:24576
	v_fma_f32 v203, v203, 2.0, -1.0
	v_mul_f32_e32 v218, v214, v202
	v_mfma_f32_32x32x16_f16 v[112:127], a[160:163], v[164:167], v[112:127]
	ds_read_b128 v[164:167], v193 offset:25600
	v_mul_f32_e32 v219, v215, v203
	v_cvt_pk_f16_f32 v222, v216, v217
	s_waitcnt lgkmcnt(6)
	v_mfma_f32_32x32x16_f16 v[96:111], a[164:167], v[168:171], v[96:111]
	ds_read_b128 v[168:171], v193 offset:26624
	v_cvt_pk_f16_f32 v223, v218, v219
	v_mfma_f32_32x32x16_f16 v[112:127], a[164:167], v[172:175], v[112:127]
	ds_read_b128 v[172:175], v193 offset:27648
	global_load_lds_dwordx4 v192, s[44:45] offset:1024 sc1
	s_cmp_lg_u32 s33, s60
	s_cbranch_scc1 .LE_nht45
	s_add_u32 s46, s62, 0xa0000
	s_addc_u32 s47, s63, 0
	global_store_dwordx4 v250, v[216:219], s[46:47]
	s_waitcnt vmcnt(0)
.LE_nht45:
	s_waitcnt lgkmcnt(6)
	v_mfma_f32_32x32x16_f16 v[96:111], a[168:171], v[176:179], v[96:111]
	ds_read_b128 v[176:179], v193 offset:28672
	s_nop 1
	v_permlane32_swap_b32_e32 v220, v222
	v_permlane32_swap_b32_e32 v221, v223
	s_cmp_eq_u32 s31, 0
	s_cbranch_scc1 .LE_slow46
	global_store_dwordx4 v195, v[220:223], s[36:37] offset:0
	s_branch .LE_join47

.LE_join47:
	v_mfma_f32_32x32x16_f16 v[112:127], a[168:171], v[180:183], v[112:127]
	ds_read_b128 v[180:183], v193 offset:29696
	s_waitcnt lgkmcnt(6)
	v_mfma_f32_32x32x16_f16 v[96:111], a[172:175], v[184:187], v[96:111]
	ds_read_b128 v[184:187], v193 offset:30720
	v_mfma_f32_32x32x16_f16 v[112:127], a[172:175], v[188:191], v[112:127]
	ds_read_b128 v[188:191], v193 offset:31744
	global_load_lds_dwordx4 v192, s[44:45] offset:2048 sc1
	s_waitcnt vmcnt(8)
	s_barrier
	s_waitcnt lgkmcnt(6)
	v_mfma_f32_32x32x16_f16 v[96:111], a[176:179], v[160:163], v[96:111]
	ds_read_b128 v[160:163], v193 offset:32768
	v_mfma_f32_32x32x16_f16 v[112:127], a[176:179], v[164:167], v[112:127]
	ds_read_b128 v[164:167], v193 offset:33792
	s_waitcnt lgkmcnt(6)
	v_mfma_f32_32x32x16_f16 v[96:111], a[180:183], v[168:171], v[96:111]
	ds_read_b128 v[168:171], v193 offset:34816
	v_mfma_f32_32x32x16_f16 v[112:127], a[180:183], v[172:175], v[112:127]
	ds_read_b128 v[172:175], v193 offset:35840
	global_load_lds_dwordx4 v192, s[44:45] offset:3072 sc1
	s_waitcnt lgkmcnt(6)
	v_mfma_f32_32x32x16_f16 v[96:111], a[184:187], v[176:179], v[96:111]
	ds_read_b128 v[176:179], v193 offset:36864
	v_mfma_f32_32x32x16_f16 v[112:127], a[184:187], v[180:183], v[112:127]
	ds_read_b128 v[180:183], v193 offset:37888
	s_waitcnt lgkmcnt(6)
	v_mfma_f32_32x32x16_f16 v[96:111], a[188:191], v[184:187], v[96:111]
	ds_read_b128 v[184:187], v193 offset:38912
	v_mfma_f32_32x32x16_f16 v[112:127], a[188:191], v[188:191], v[112:127]
	ds_read_b128 v[188:191], v193 offset:39936
	s_add_u32 s44, s34, 0x8000
	s_addc_u32 s45, s35, 0
	s_mov_b32 m0, s54
	s_nop 0
	global_load_lds_dwordx4 v192, s[44:45] sc1
	s_waitcnt lgkmcnt(6)
	v_mfma_f32_32x32x16_f16 v[96:111], a[192:195], v[160:163], v[96:111]
	ds_read_b128 v[160:163], v193 offset:40960
	v_mfma_f32_32x32x16_f16 v[112:127], a[192:195], v[164:167], v[112:127]
	ds_read_b128 v[164:167], v193 offset:41984
	s_waitcnt vmcnt(3)
	s_barrier
	v_mov_b32_e32 v199, 3
	s_cmp_eq_u32 s31, 0
	s_cbranch_scc1 .LE_slow48
	global_store_dword v197, v199, s[40:41]
	s_branch .LE_join49

.LE_join49:
	s_waitcnt lgkmcnt(6)
	v_mfma_f32_32x32x16_f16 v[96:111], a[196:199], v[168:171], v[96:111]
	ds_read_b128 v[168:171], v193 offset:43008
	v_mfma_f32_32x32x16_f16 v[112:127], a[196:199], v[172:175], v[112:127]
	ds_read_b128 v[172:175], v193 offset:44032
	global_load_lds_dwordx4 v192, s[44:45] offset:1024 sc1
	s_waitcnt lgkmcnt(6)
	v_mfma_f32_32x32x16_f16 v[96:111], a[200:203], v[176:179], v[96:111]
	ds_read_b128 v[176:179], v193 offset:45056
	v_mfma_f32_32x32x16_f16 v[112:127], a[200:203], v[180:183], v[112:127]
	ds_read_b128 v[180:183], v193 offset:46080
	s_waitcnt lgkmcnt(6)
	v_mfma_f32_32x32x16_f16 v[96:111], a[204:207], v[184:187], v[96:111]
	ds_read_b128 v[184:187], v193 offset:47104
	v_mfma_f32_32x32x16_f16 v[112:127], a[204:207], v[188:191], v[112:127]
	ds_read_b128 v[188:191], v193 offset:48128
	global_load_lds_dwordx4 v192, s[44:45] offset:2048 sc1
	s_waitcnt lgkmcnt(6)
	v_mfma_f32_32x32x16_f16 v[96:111], a[208:211], v[160:163], v[96:111]
	ds_read_b128 v[160:163], v193 offset:49152
	v_mfma_f32_32x32x16_f16 v[112:127], a[208:211], v[164:167], v[112:127]
	ds_read_b128 v[164:167], v193 offset:50176
	s_waitcnt lgkmcnt(6)
	v_mfma_f32_32x32x16_f16 v[96:111], a[212:215], v[168:171], v[96:111]
	ds_read_b128 v[168:171], v193 offset:51200
	v_mfma_f32_32x32x16_f16 v[112:127], a[212:215], v[172:175], v[112:127]
	ds_read_b128 v[172:175], v193 offset:52224
	global_load_lds_dwordx4 v192, s[44:45] offset:3072 sc1
	s_waitcnt lgkmcnt(6)
	v_mfma_f32_32x32x16_f16 v[96:111], a[216:219], v[176:179], v[96:111]
	ds_read_b128 v[176:179], v193 offset:53248
	v_mfma_f32_32x32x16_f16 v[112:127], a[216:219], v[180:183], v[112:127]
	ds_read_b128 v[180:183], v193 offset:54272
	s_waitcnt lgkmcnt(6)
	v_mfma_f32_32x32x16_f16 v[96:111], a[220:223], v[184:187], v[96:111]
	ds_read_b128 v[184:187], v193 offset:55296
	v_mfma_f32_32x32x16_f16 v[112:127], a[220:223], v[188:191], v[112:127]
	ds_read_b128 v[188:191], v193 offset:56320
	s_add_u32 s44, s34, 0x9000
	s_addc_u32 s45, s35, 0
	s_mov_b32 m0, s55
	s_nop 0
	global_load_lds_dwordx4 v192, s[44:45] sc1
	s_waitcnt lgkmcnt(6)
	v_mfma_f32_32x32x16_f16 v[96:111], a[224:227], v[160:163], v[96:111]
	ds_read_b128 v[160:163], v193 offset:57344
	v_mfma_f32_32x32x16_f16 v[112:127], a[224:227], v[164:167], v[112:127]
	ds_read_b128 v[164:167], v193 offset:58368
	s_waitcnt lgkmcnt(6)
	v_mfma_f32_32x32x16_f16 v[96:111], a[228:231], v[168:171], v[96:111]
	ds_read_b128 v[168:171], v193 offset:59392
	v_mfma_f32_32x32x16_f16 v[112:127], a[228:231], v[172:175], v[112:127]
	ds_read_b128 v[172:175], v193 offset:60416
	global_load_lds_dwordx4 v192, s[44:45] offset:1024 sc1
	s_waitcnt lgkmcnt(6)
	v_mfma_f32_32x32x16_f16 v[96:111], a[232:235], v[176:179], v[96:111]
	ds_read_b128 v[176:179], v193 offset:61440
	v_mfma_f32_32x32x16_f16 v[112:127], a[232:235], v[180:183], v[112:127]
	ds_read_b128 v[180:183], v193 offset:62464
	s_waitcnt lgkmcnt(6)
	v_mfma_f32_32x32x16_f16 v[96:111], a[236:239], v[184:187], v[96:111]
	ds_read_b128 v[184:187], v193 offset:63488
	v_mfma_f32_32x32x16_f16 v[112:127], a[236:239], v[188:191], v[112:127]
	ds_read_b128 v[188:191], v193 offset:64512
	global_load_lds_dwordx4 v192, s[44:45] offset:2048 sc1
	s_waitcnt vmcnt(8)
	s_barrier
	s_waitcnt lgkmcnt(6)
	v_mfma_f32_32x32x16_f16 v[96:111], a[240:243], v[160:163], v[96:111]
	ds_read_b128 v[160:163], v192 offset:0
	v_mfma_f32_32x32x16_f16 v[112:127], a[240:243], v[164:167], v[112:127]
	ds_read_b128 v[164:167], v192 offset:1024
	s_waitcnt lgkmcnt(6)
	v_mfma_f32_32x32x16_f16 v[96:111], a[244:247], v[168:171], v[96:111]
	ds_read_b128 v[168:171], v192 offset:2048
	v_mfma_f32_32x32x16_f16 v[112:127], a[244:247], v[172:175], v[112:127]
	ds_read_b128 v[172:175], v192 offset:3072
	global_load_lds_dwordx4 v192, s[44:45] offset:3072 sc1
	s_waitcnt lgkmcnt(6)
	v_mfma_f32_32x32x16_f16 v[96:111], a[248:251], v[176:179], v[96:111]
	ds_read_b128 v[176:179], v192 offset:4096
	v_mfma_f32_32x32x16_f16 v[112:127], a[248:251], v[180:183], v[112:127]
	ds_read_b128 v[180:183], v192 offset:5120
	s_waitcnt lgkmcnt(6)
	v_mfma_f32_32x32x16_f16 v[96:111], a[252:255], v[184:187], v[96:111]
	ds_read_b128 v[184:187], v192 offset:6144
	v_mfma_f32_32x32x16_f16 v[112:127], a[252:255], v[188:191], v[112:127]
	ds_read_b128 v[188:191], v192 offset:7168
	s_add_u32 s44, s34, 0x10000
	s_addc_u32 s45, s35, 0
	s_mov_b32 m0, s56
	s_nop 0
	global_load_lds_dwordx4 v192, s[44:45] sc1
	s_add_u32 s33, s33, 1
	s_cmp_lt_u32 s33, s28
	s_cbranch_scc1 .LE_loop16
.LE_end17:
	s_nop 15
	s_nop 3
	v_exp_f32_e32 v200, v96
	v_exp_f32_e32 v201, v97
	v_exp_f32_e32 v202, v98
	v_exp_f32_e32 v203, v99
	v_exp_f32_e32 v204, v100
	v_exp_f32_e32 v205, v101
	v_exp_f32_e32 v206, v102
	v_exp_f32_e32 v207, v103
	v_exp_f32_e32 v208, v104
	v_exp_f32_e32 v209, v105
	v_exp_f32_e32 v210, v106
	v_exp_f32_e32 v211, v107
	v_exp_f32_e32 v212, v108
	v_exp_f32_e32 v213, v109
	v_exp_f32_e32 v214, v110
	v_exp_f32_e32 v215, v111
	v_add_f32_e32 v200, 1.0, v200
	v_add_f32_e32 v201, 1.0, v201
	v_add_f32_e32 v202, 1.0, v202
	v_add_f32_e32 v203, 1.0, v203
	v_add_f32_e32 v204, 1.0, v204
	v_add_f32_e32 v205, 1.0, v205
	v_add_f32_e32 v206, 1.0, v206
	v_add_f32_e32 v207, 1.0, v207
	v_add_f32_e32 v208, 1.0, v208
	v_add_f32_e32 v209, 1.0, v209
	v_add_f32_e32 v210, 1.0, v210
	v_add_f32_e32 v211, 1.0, v211
	v_add_f32_e32 v212, 1.0, v212
	v_add_f32_e32 v213, 1.0, v213
	v_add_f32_e32 v214, 1.0, v214
	v_add_f32_e32 v215, 1.0, v215
	v_rcp_f32_e32 v200, v200
	v_rcp_f32_e32 v201, v201
	v_rcp_f32_e32 v202, v202
	v_rcp_f32_e32 v203, v203
	v_rcp_f32_e32 v204, v204
	v_rcp_f32_e32 v205, v205
	v_rcp_f32_e32 v206, v206
	v_rcp_f32_e32 v207, v207
	v_rcp_f32_e32 v208, v208
	v_rcp_f32_e32 v209, v209
	v_rcp_f32_e32 v210, v210
	v_rcp_f32_e32 v211, v211
	v_rcp_f32_e32 v212, v212
	v_rcp_f32_e32 v213, v213
	v_rcp_f32_e32 v214, v214
	v_rcp_f32_e32 v215, v215
	v_fmamk_f32 v208, v208, 0xc0b8aa3b, v198
	v_fmamk_f32 v209, v209, 0xc0b8aa3b, v198
	v_fmamk_f32 v210, v210, 0xc0b8aa3b, v198
	v_fmamk_f32 v211, v211, 0xc0b8aa3b, v198
	v_mul_f32_e32 v204, v204, v152
	v_mul_f32_e32 v205, v205, v153
	v_mul_f32_e32 v206, v206, v154
	v_mul_f32_e32 v207, v207, v155
	v_fma_f32 v152, v200, v208, v204
	v_fma_f32 v153, v201, v209, v205
	v_fma_f32 v154, v202, v210, v206
	v_fma_f32 v155, v203, v211, v207
	v_exp_f32_e32 v200, v152
	v_exp_f32_e32 v201, v153
	v_exp_f32_e32 v202, v154
	v_exp_f32_e32 v203, v155
	v_add_f32_e32 v200, 1.0, v200
	v_add_f32_e32 v201, 1.0, v201
	v_add_f32_e32 v202, 1.0, v202
	v_add_f32_e32 v203, 1.0, v203
	v_rcp_f32_e32 v200, v200
	v_rcp_f32_e32 v201, v201
	v_rcp_f32_e32 v202, v202
	v_rcp_f32_e32 v203, v203
	v_fma_f32 v200, v200, 2.0, -1.0
	v_fma_f32 v201, v201, 2.0, -1.0
	v_fma_f32 v202, v202, 2.0, -1.0
	v_fma_f32 v203, v203, 2.0, -1.0
	v_mul_f32_e32 v216, v212, v200
	v_mul_f32_e32 v217, v213, v201
	v_mul_f32_e32 v218, v214, v202
	v_mul_f32_e32 v219, v215, v203
	v_cvt_pk_f16_f32 v220, v216, v217
	v_cvt_pk_f16_f32 v221, v218, v219
	s_add_u32 s46, s62, 0xc0000
	s_addc_u32 s47, s63, 0
	global_store_dwordx4 v250, v[216:219], s[46:47]
	s_waitcnt vmcnt(0)
	v_exp_f32_e32 v200, v112
	v_exp_f32_e32 v201, v113
	v_exp_f32_e32 v202, v114
	v_exp_f32_e32 v203, v115
	v_exp_f32_e32 v204, v116
	v_exp_f32_e32 v205, v117
	v_exp_f32_e32 v206, v118
	v_exp_f32_e32 v207, v119
	v_exp_f32_e32 v208, v120
	v_exp_f32_e32 v209, v121
	v_exp_f32_e32 v210, v122
	v_exp_f32_e32 v211, v123
	v_exp_f32_e32 v212, v124
	v_exp_f32_e32 v213, v125
	v_exp_f32_e32 v214, v126
	v_exp_f32_e32 v215, v127
	v_add_f32_e32 v200, 1.0, v200
	v_add_f32_e32 v201, 1.0, v201
	v_add_f32_e32 v202, 1.0, v202
	v_add_f32_e32 v203, 1.0, v203
	v_add_f32_e32 v204, 1.0, v204
	v_add_f32_e32 v205, 1.0, v205
	v_add_f32_e32 v206, 1.0, v206
	v_add_f32_e32 v207, 1.0, v207
	v_add_f32_e32 v208, 1.0, v208
	v_add_f32_e32 v209, 1.0, v209
	v_add_f32_e32 v210, 1.0, v210
	v_add_f32_e32 v211, 1.0, v211
	v_add_f32_e32 v212, 1.0, v212
	v_add_f32_e32 v213, 1.0, v213
	v_add_f32_e32 v214, 1.0, v214
	v_add_f32_e32 v215, 1.0, v215
	v_rcp_f32_e32 v200, v200
	v_rcp_f32_e32 v201, v201
	v_rcp_f32_e32 v202, v202
	v_rcp_f32_e32 v203, v203
	v_rcp_f32_e32 v204, v204
	v_rcp_f32_e32 v205, v205
	v_rcp_f32_e32 v206, v206
	v_rcp_f32_e32 v207, v207
	v_rcp_f32_e32 v208, v208
	v_rcp_f32_e32 v209, v209
	v_rcp_f32_e32 v210, v210
	v_rcp_f32_e32 v211, v211
	v_rcp_f32_e32 v212, v212
	v_rcp_f32_e32 v213, v213
	v_rcp_f32_e32 v214, v214
	v_rcp_f32_e32 v215, v215
	v_fmamk_f32 v208, v208, 0xc0b8aa3b, v198
	v_fmamk_f32 v209, v209, 0xc0b8aa3b, v198
	v_fmamk_f32 v210, v210, 0xc0b8aa3b, v198
	v_fmamk_f32 v211, v211, 0xc0b8aa3b, v198
	v_mul_f32_e32 v204, v204, v156
	v_mul_f32_e32 v205, v205, v157
	v_mul_f32_e32 v206, v206, v158
	v_mul_f32_e32 v207, v207, v159
	v_fma_f32 v156, v200, v208, v204
	v_fma_f32 v157, v201, v209, v205
	v_fma_f32 v158, v202, v210, v206
	v_fma_f32 v159, v203, v211, v207
	v_exp_f32_e32 v200, v156
	v_exp_f32_e32 v201, v157
	v_exp_f32_e32 v202, v158
	v_exp_f32_e32 v203, v159
	v_add_f32_e32 v200, 1.0, v200
	v_add_f32_e32 v201, 1.0, v201
	v_add_f32_e32 v202, 1.0, v202
	v_add_f32_e32 v203, 1.0, v203
	v_rcp_f32_e32 v200, v200
	v_rcp_f32_e32 v201, v201
	v_rcp_f32_e32 v202, v202
	v_rcp_f32_e32 v203, v203
	v_fma_f32 v200, v200, 2.0, -1.0
	v_fma_f32 v201, v201, 2.0, -1.0
	v_fma_f32 v202, v202, 2.0, -1.0
	v_fma_f32 v203, v203, 2.0, -1.0
	v_mul_f32_e32 v216, v212, v200
	v_mul_f32_e32 v217, v213, v201
	v_mul_f32_e32 v218, v214, v202
	v_mul_f32_e32 v219, v215, v203
	v_cvt_pk_f16_f32 v222, v216, v217
	v_cvt_pk_f16_f32 v223, v218, v219
	s_add_u32 s46, s62, 0xe0000
	s_addc_u32 s47, s63, 0
	global_store_dwordx4 v250, v[216:219], s[46:47]
	s_waitcnt vmcnt(0)
	s_waitcnt vmcnt(0) lgkmcnt(0)
	s_endpgm
	.p2align 8

.LD_cdone1:
	s_waitcnt lgkmcnt(0)
	s_barrier
	v_mov_b32_e32 v252, 0x22000
	ds_read_b32 v200, v252
	ds_read_b32 v201, v252 offset:4
	ds_read_b32 v202, v252 offset:8
	s_waitcnt lgkmcnt(0)
	s_nop 1
	v_readfirstlane_b32 s31, v200
	v_readfirstlane_b32 s29, v201
	v_readfirstlane_b32 s30, v202
	s_nop 3
	s_barrier
	s_lshl_b32 s49, s29, 19
	s_lshl_b32 s64, s32, 13
	s_add_u32 s49, s49, s64
	s_mov_b32 s51, s64
	s_add_u32 s52, s51, 0x0
	s_add_u32 s53, s51, 0x1000
	s_add_u32 s54, s51, 0x8000
	s_add_u32 s55, s51, 0x9000
	s_add_u32 s56, s51, 0x10000
	s_add_u32 s57, s51, 0x11000
	s_add_u32 s58, s51, 0x18000
	s_add_u32 s59, s51, 0x19000
	s_lshl_b32 s64, s29, 8
	s_lshl_b32 s65, s30, 1
	s_add_u32 s64, s64, s65
	s_lshr_b32 s65, s32, 1
	s_add_u32 s64, s64, s65
	s_lshl_b32 s64, s64, 11
	s_and_b32 s65, s32, 1
	s_lshl_b32 s65, s65, 9
	s_add_u32 s50, s64, s65
	s_sub_u32 s60, s28, 1
	s_lshl_b32 s64, s30, 2
	s_add_u32 s64, s64, s32
	s_lshl_b32 s64, s64, 16
	s_add_u32 s44, s4, s64
	s_addc_u32 s45, s5, 0
	global_load_dwordx4 a[0:3], v192, s[44:45] offset:0
	global_load_dwordx4 a[4:7], v192, s[44:45] offset:1024
	global_load_dwordx4 a[8:11], v192, s[44:45] offset:2048
	global_load_dwordx4 a[12:15], v192, s[44:45] offset:3072
	s_add_u32 s44, s44, 0x1000
	s_addc_u32 s45, s45, 0
	global_load_dwordx4 a[16:19], v192, s[44:45] offset:0
	global_load_dwordx4 a[20:23], v192, s[44:45] offset:1024
	global_load_dwordx4 a[24:27], v192, s[44:45] offset:2048
	global_load_dwordx4 a[28:31], v192, s[44:45] offset:3072
	s_add_u32 s44, s44, 0x1000
	s_addc_u32 s45, s45, 0
	global_load_dwordx4 a[32:35], v192, s[44:45] offset:0
	global_load_dwordx4 a[36:39], v192, s[44:45] offset:1024
	global_load_dwordx4 a[40:43], v192, s[44:45] offset:2048
	global_load_dwordx4 a[44:47], v192, s[44:45] offset:3072
	s_add_u32 s44, s44, 0x1000
	s_addc_u32 s45, s45, 0
	global_load_dwordx4 a[48:51], v192, s[44:45] offset:0
	global_load_dwordx4 a[52:55], v192, s[44:45] offset:1024
	global_load_dwordx4 a[56:59], v192, s[44:45] offset:2048
	global_load_dwordx4 a[60:63], v192, s[44:45] offset:3072
	s_add_u32 s44, s44, 0x1000
	s_addc_u32 s45, s45, 0
	global_load_dwordx4 a[64:67], v192, s[44:45] offset:0
	global_load_dwordx4 a[68:71], v192, s[44:45] offset:1024
	global_load_dwordx4 a[72:75], v192, s[44:45] offset:2048
	global_load_dwordx4 a[76:79], v192, s[44:45] offset:3072
	s_add_u32 s44, s44, 0x1000
	s_addc_u32 s45, s45, 0
	global_load_dwordx4 a[80:83], v192, s[44:45] offset:0
	global_load_dwordx4 a[84:87], v192, s[44:45] offset:1024
	global_load_dwordx4 a[88:91], v192, s[44:45] offset:2048
	global_load_dwordx4 a[92:95], v192, s[44:45] offset:3072
	s_add_u32 s44, s44, 0x1000
	s_addc_u32 s45, s45, 0
	global_load_dwordx4 a[96:99], v192, s[44:45] offset:0
	global_load_dwordx4 a[100:103], v192, s[44:45] offset:1024
	global_load_dwordx4 a[104:107], v192, s[44:45] offset:2048
	global_load_dwordx4 a[108:111], v192, s[44:45] offset:3072
	s_add_u32 s44, s44, 0x1000
	s_addc_u32 s45, s45, 0
	global_load_dwordx4 a[112:115], v192, s[44:45] offset:0
	global_load_dwordx4 a[116:119], v192, s[44:45] offset:1024
	global_load_dwordx4 a[120:123], v192, s[44:45] offset:2048
	global_load_dwordx4 a[124:127], v192, s[44:45] offset:3072
	s_add_u32 s44, s44, 0x1000
	s_addc_u32 s45, s45, 0
	s_waitcnt vmcnt(16)
	global_load_dwordx4 a[128:131], v192, s[44:45] offset:0
	global_load_dwordx4 a[132:135], v192, s[44:45] offset:1024
	global_load_dwordx4 a[136:139], v192, s[44:45] offset:2048
	global_load_dwordx4 a[140:143], v192, s[44:45] offset:3072
	s_add_u32 s44, s44, 0x1000
	s_addc_u32 s45, s45, 0
	global_load_dwordx4 a[144:147], v192, s[44:45] offset:0
	global_load_dwordx4 a[148:151], v192, s[44:45] offset:1024
	global_load_dwordx4 a[152:155], v192, s[44:45] offset:2048
	global_load_dwordx4 a[156:159], v192, s[44:45] offset:3072
	s_add_u32 s44, s44, 0x1000
	s_addc_u32 s45, s45, 0
	global_load_dwordx4 a[160:163], v192, s[44:45] offset:0
	global_load_dwordx4 a[164:167], v192, s[44:45] offset:1024
	global_load_dwordx4 a[168:171], v192, s[44:45] offset:2048
	global_load_dwordx4 a[172:175], v192, s[44:45] offset:3072
	s_add_u32 s44, s44, 0x1000
	s_addc_u32 s45, s45, 0
	global_load_dwordx4 a[176:179], v192, s[44:45] offset:0
	global_load_dwordx4 a[180:183], v192, s[44:45] offset:1024
	global_load_dwordx4 a[184:187], v192, s[44:45] offset:2048
	global_load_dwordx4 a[188:191], v192, s[44:45] offset:3072
	s_add_u32 s44, s44, 0x1000
	s_addc_u32 s45, s45, 0
	global_load_dwordx4 a[192:195], v192, s[44:45] offset:0
	global_load_dwordx4 a[196:199], v192, s[44:45] offset:1024
	global_load_dwordx4 a[200:203], v192, s[44:45] offset:2048
	global_load_dwordx4 a[204:207], v192, s[44:45] offset:3072
	s_add_u32 s44, s44, 0x1000
	s_addc_u32 s45, s45, 0
	global_load_dwordx4 a[208:211], v192, s[44:45] offset:0
	global_load_dwordx4 a[212:215], v192, s[44:45] offset:1024
	global_load_dwordx4 a[216:219], v192, s[44:45] offset:2048
	global_load_dwordx4 a[220:223], v192, s[44:45] offset:3072
	s_add_u32 s44, s44, 0x1000
	s_addc_u32 s45, s45, 0
	global_load_dwordx4 a[224:227], v192, s[44:45] offset:0
	global_load_dwordx4 a[228:231], v192, s[44:45] offset:1024
	global_load_dwordx4 a[232:235], v192, s[44:45] offset:2048
	global_load_dwordx4 a[236:239], v192, s[44:45] offset:3072
	s_add_u32 s44, s44, 0x1000
	s_addc_u32 s45, s45, 0
	global_load_dwordx4 a[240:243], v192, s[44:45] offset:0
	global_load_dwordx4 a[244:247], v192, s[44:45] offset:1024
	global_load_dwordx4 a[248:251], v192, s[44:45] offset:2048
	global_load_dwordx4 a[252:255], v192, s[44:45] offset:3072
	s_add_u32 s44, s44, 0x1000
	s_addc_u32 s45, s45, 0
	v_mov_b32_e32 v128, 0
	v_mov_b32_e32 v129, 0
	v_mov_b32_e32 v130, 0
	v_mov_b32_e32 v131, 0
	v_mov_b32_e32 v132, 0
	v_mov_b32_e32 v133, 0
	v_mov_b32_e32 v134, 0
	v_mov_b32_e32 v135, 0
	v_mov_b32_e32 v136, 0
	v_mov_b32_e32 v137, 0
	v_mov_b32_e32 v138, 0
	v_mov_b32_e32 v139, 0
	v_mov_b32_e32 v140, 0
	v_mov_b32_e32 v141, 0
	v_mov_b32_e32 v142, 0
	v_mov_b32_e32 v143, 0
	v_mov_b32_e32 v144, 0
	v_mov_b32_e32 v145, 0
	v_mov_b32_e32 v146, 0
	v_mov_b32_e32 v147, 0
	v_mov_b32_e32 v148, 0
	v_mov_b32_e32 v149, 0
	v_mov_b32_e32 v150, 0
	v_mov_b32_e32 v151, 0
	v_mov_b32_e32 v152, 0
	v_mov_b32_e32 v153, 0
	v_mov_b32_e32 v154, 0
	v_mov_b32_e32 v155, 0
	v_mov_b32_e32 v156, 0
	v_mov_b32_e32 v157, 0
	v_mov_b32_e32 v158, 0
	v_mov_b32_e32 v159, 0
	s_lshl_b32 s64, s30, 5
	s_lshl_b32 s65, s32, 3
	s_add_u32 s64, s64, s65
	v_lshlrev_b32_e32 v255, 2, v254
	v_add_u32_e32 v255, s64, v255
	v_lshlrev_b32_e32 v200, 2, v255
	global_load_dwordx4 v[228:231], v200, s[22:23]
	v_add_u32_e32 v201, 0x1000, v200
	global_load_dwordx4 v[232:235], v201, s[22:23]
	s_lshl_b32 s65, s32, 11
	v_lshl_add_u32 v248, v253, 3, s65
	v_add_u32_e32 v248, 0x20000, v248
	v_and_b32_e32 v250, 15, v194
	s_mul_i32 s65, s32, 128
	v_lshl_add_u32 v249, v250, 3, s65
	v_add_u32_e32 v249, 0x20000, v249
	v_lshlrev_b32_e32 v250, 3, v250
	s_lshl_b32 s65, s30, 11
	s_lshl_b32 s66, s29, 8
	s_add_u32 s65, s65, s66
	s_mul_i32 s66, s32, 16
	s_add_u32 s65, s65, s66
	s_lshl_b32 s65, s65, 3
	s_add_u32 s62, s24, s65
	s_addc_u32 s63, s25, 0
	s_lshl_b32 s65, s29, 5
	s_add_u32 s65, s65, s30
	s_lshl_b32 s65, s65, 2
	s_add_u32 s65, s65, s32
	s_lshl_b32 s65, s65, 15
	s_add_u32 s42, s18, s65
	s_addc_u32 s43, s19, 0
	s_waitcnt vmcnt(0)
	s_waitcnt vmcnt(0)
	s_mov_b32 s33, 0
	s_add_u32 s46, s42, 0x0
	s_addc_u32 s47, s43, 0
	global_load_dwordx4 v[0:3], v192, s[46:47] offset:0
	global_load_dwordx4 v[4:7], v192, s[46:47] offset:1024
	global_load_dwordx4 v[8:11], v192, s[46:47] offset:2048
	global_load_dwordx4 v[12:15], v192, s[46:47] offset:3072
	s_add_u32 s46, s42, 0x1000
	s_addc_u32 s47, s43, 0
	global_load_dwordx4 v[16:19], v192, s[46:47] offset:0
	global_load_dwordx4 v[20:23], v192, s[46:47] offset:1024
	global_load_dwordx4 v[24:27], v192, s[46:47] offset:2048
	global_load_dwordx4 v[28:31], v192, s[46:47] offset:3072
	s_add_u32 s46, s42, 0x2000
	s_addc_u32 s47, s43, 0
	global_load_dwordx4 v[32:35], v192, s[46:47] offset:0
	global_load_dwordx4 v[36:39], v192, s[46:47] offset:1024
	global_load_dwordx4 v[40:43], v192, s[46:47] offset:2048
	global_load_dwordx4 v[44:47], v192, s[46:47] offset:3072
	s_add_u32 s46, s42, 0x3000
	s_addc_u32 s47, s43, 0
	global_load_dwordx4 v[48:51], v192, s[46:47] offset:0
	global_load_dwordx4 v[52:55], v192, s[46:47] offset:1024
	global_load_dwordx4 v[56:59], v192, s[46:47] offset:2048
	global_load_dwordx4 v[60:63], v192, s[46:47] offset:3072
	s_add_u32 s46, s42, 0x4000
	s_addc_u32 s47, s43, 0
	global_load_dwordx4 v[64:67], v192, s[46:47] offset:0
	global_load_dwordx4 v[68:71], v192, s[46:47] offset:1024
	global_load_dwordx4 v[72:75], v192, s[46:47] offset:2048
	global_load_dwordx4 v[76:79], v192, s[46:47] offset:3072
	s_add_u32 s46, s42, 0x5000
	s_addc_u32 s47, s43, 0
	global_load_dwordx4 v[80:83], v192, s[46:47] offset:0
	global_load_dwordx4 v[84:87], v192, s[46:47] offset:1024
	global_load_dwordx4 v[88:91], v192, s[46:47] offset:2048
	global_load_dwordx4 v[92:95], v192, s[46:47] offset:3072
	s_add_u32 s46, s42, 0x6000
	s_addc_u32 s47, s43, 0
	global_load_dwordx4 v[96:99], v192, s[46:47] offset:0
	global_load_dwordx4 v[100:103], v192, s[46:47] offset:1024
	global_load_dwordx4 v[104:107], v192, s[46:47] offset:2048
	global_load_dwordx4 v[108:111], v192, s[46:47] offset:3072
	s_add_u32 s46, s42, 0x7000
	s_addc_u32 s47, s43, 0
	global_load_dwordx4 v[112:115], v192, s[46:47] offset:0
	global_load_dwordx4 v[116:119], v192, s[46:47] offset:1024
	global_load_dwordx4 v[120:123], v192, s[46:47] offset:2048
	global_load_dwordx4 v[124:127], v192, s[46:47] offset:3072
	s_waitcnt vmcnt(0)
	s_waitcnt lgkmcnt(0)
	s_lshl_b32 s64, s33, 3
	s_add_u32 s64, s64, s29
	s_lshl_b32 s64, s64, 5
	s_add_u32 s64, s64, s30
	s_lshl_b32 s64, s64, 2
	s_add_u32 s40, s8, s64
	s_addc_u32 s41, s9, 0
	s_and_b32 s64, s33, 1
	s_lshl_b32 s64, s64, 22
	s_add_u32 s64, s64, s50
	s_add_u32 s36, s6, s64
	s_addc_u32 s37, s7, 0
	s_lshl_b32 s64, s33, 19
	s_add_u32 s72, s62, s64
	s_addc_u32 s73, s63, 0
	v_exp_f32_e32 v200, v0
	v_exp_f32_e32 v201, v1
	v_exp_f32_e32 v202, v2
	v_exp_f32_e32 v203, v3
	v_exp_f32_e32 v204, v4
	v_exp_f32_e32 v205, v5
	v_exp_f32_e32 v206, v6
	v_exp_f32_e32 v207, v7
	v_exp_f32_e32 v208, v8
	v_exp_f32_e32 v209, v9
	v_exp_f32_e32 v210, v10
	v_exp_f32_e32 v211, v11
	v_exp_f32_e32 v212, v12
	v_exp_f32_e32 v213, v13
	v_exp_f32_e32 v214, v14
	v_exp_f32_e32 v215, v15
	v_add_f32_e32 v200, 1.0, v200
	v_add_f32_e32 v201, 1.0, v201
	v_add_f32_e32 v202, 1.0, v202
	v_add_f32_e32 v203, 1.0, v203
	v_add_f32_e32 v204, 1.0, v204
	v_add_f32_e32 v205, 1.0, v205
	v_add_f32_e32 v206, 1.0, v206
	v_add_f32_e32 v207, 1.0, v207
	v_add_f32_e32 v208, 1.0, v208
	v_add_f32_e32 v209, 1.0, v209
	v_add_f32_e32 v210, 1.0, v210
	v_add_f32_e32 v211, 1.0, v211
	v_add_f32_e32 v212, 1.0, v212
	v_add_f32_e32 v213, 1.0, v213
	v_add_f32_e32 v214, 1.0, v214
	v_add_f32_e32 v215, 1.0, v215
	v_rcp_f32_e32 v200, v200
	v_rcp_f32_e32 v201, v201
	v_rcp_f32_e32 v202, v202
	v_rcp_f32_e32 v203, v203
	v_rcp_f32_e32 v204, v204
	v_rcp_f32_e32 v205, v205
	v_rcp_f32_e32 v206, v206
	v_rcp_f32_e32 v207, v207
	v_rcp_f32_e32 v208, v208
	v_rcp_f32_e32 v209, v209
	v_rcp_f32_e32 v210, v210
	v_rcp_f32_e32 v211, v211
	v_rcp_f32_e32 v212, v212
	v_rcp_f32_e32 v213, v213
	v_rcp_f32_e32 v214, v214
	v_rcp_f32_e32 v215, v215
	v_fmamk_f32 v208, v208, 0xc0b8aa3b, v198
	v_fmamk_f32 v209, v209, 0xc0b8aa3b, v198
	v_fmamk_f32 v210, v210, 0xc0b8aa3b, v198
	v_fmamk_f32 v211, v211, 0xc0b8aa3b, v198
	v_mul_f32_e32 v204, v204, v128
	v_mul_f32_e32 v205, v205, v129
	v_mul_f32_e32 v206, v206, v130
	v_mul_f32_e32 v207, v207, v131
	v_fma_f32 v128, v200, v208, v204
	v_fma_f32 v129, v201, v209, v205
	v_fma_f32 v130, v202, v210, v206
	v_fma_f32 v131, v203, v211, v207
	v_exp_f32_e32 v200, v128
	v_exp_f32_e32 v201, v129
	v_exp_f32_e32 v202, v130
	v_exp_f32_e32 v203, v131
	v_add_f32_e32 v200, 1.0, v200
	v_add_f32_e32 v201, 1.0, v201
	v_add_f32_e32 v202, 1.0, v202
	v_add_f32_e32 v203, 1.0, v203
	v_rcp_f32_e32 v200, v200
	v_rcp_f32_e32 v201, v201
	v_rcp_f32_e32 v202, v202
	v_rcp_f32_e32 v203, v203
	v_fma_f32 v200, v200, 2.0, -1.0
	v_fma_f32 v201, v201, 2.0, -1.0
	v_fma_f32 v202, v202, 2.0, -1.0
	v_fma_f32 v203, v203, 2.0, -1.0
	v_mul_f32_e32 v216, v212, v200
	v_mul_f32_e32 v217, v213, v201
	v_mul_f32_e32 v218, v214, v202
	v_mul_f32_e32 v219, v215, v203
	v_mul_f32_e32 v236, v216, v228
	v_mul_f32_e32 v237, v216, v232
	v_fmac_f32_e32 v236, v217, v229
	v_fmac_f32_e32 v237, v217, v233
	v_fmac_f32_e32 v236, v218, v230
	v_fmac_f32_e32 v237, v218, v234
	v_fmac_f32_e32 v236, v219, v231
	v_fmac_f32_e32 v237, v219, v235
	v_mov_b32_e32 v238, v236
	v_mov_b32_e32 v239, v236
	v_mov_b32_e32 v240, v237
	v_mov_b32_e32 v241, v237
	s_nop 1
	v_permlane32_swap_b32_e32 v238, v239
	v_permlane32_swap_b32_e32 v240, v241
	v_add_f32_e32 v238, v238, v239
	v_add_f32_e32 v239, v240, v241
	ds_write_b64 v248, v[238:239] offset:0
	v_cvt_pk_f16_f32 v220, v216, v217
	v_cvt_pk_f16_f32 v221, v218, v219
	v_exp_f32_e32 v200, v16
	v_exp_f32_e32 v201, v17
	v_exp_f32_e32 v202, v18
	v_exp_f32_e32 v203, v19
	v_exp_f32_e32 v204, v20
	v_exp_f32_e32 v205, v21
	v_exp_f32_e32 v206, v22
	v_exp_f32_e32 v207, v23
	v_exp_f32_e32 v208, v24
	v_exp_f32_e32 v209, v25
	v_exp_f32_e32 v210, v26
	v_exp_f32_e32 v211, v27
	v_exp_f32_e32 v212, v28
	v_exp_f32_e32 v213, v29
	v_exp_f32_e32 v214, v30
	v_exp_f32_e32 v215, v31
	v_add_f32_e32 v200, 1.0, v200
	v_add_f32_e32 v201, 1.0, v201
	v_add_f32_e32 v202, 1.0, v202
	v_add_f32_e32 v203, 1.0, v203
	v_add_f32_e32 v204, 1.0, v204
	v_add_f32_e32 v205, 1.0, v205
	v_add_f32_e32 v206, 1.0, v206
	v_add_f32_e32 v207, 1.0, v207
	v_add_f32_e32 v208, 1.0, v208
	v_add_f32_e32 v209, 1.0, v209
	v_add_f32_e32 v210, 1.0, v210
	v_add_f32_e32 v211, 1.0, v211
	v_add_f32_e32 v212, 1.0, v212
	v_add_f32_e32 v213, 1.0, v213
	v_add_f32_e32 v214, 1.0, v214
	v_add_f32_e32 v215, 1.0, v215
	v_rcp_f32_e32 v200, v200
	v_rcp_f32_e32 v201, v201
	v_rcp_f32_e32 v202, v202
	v_rcp_f32_e32 v203, v203
	v_rcp_f32_e32 v204, v204
	v_rcp_f32_e32 v205, v205
	v_rcp_f32_e32 v206, v206
	v_rcp_f32_e32 v207, v207
	v_rcp_f32_e32 v208, v208
	v_rcp_f32_e32 v209, v209
	v_rcp_f32_e32 v210, v210
	v_rcp_f32_e32 v211, v211
	v_rcp_f32_e32 v212, v212
	v_rcp_f32_e32 v213, v213
	v_rcp_f32_e32 v214, v214
	v_rcp_f32_e32 v215, v215
	v_fmamk_f32 v208, v208, 0xc0b8aa3b, v198
	v_fmamk_f32 v209, v209, 0xc0b8aa3b, v198
	v_fmamk_f32 v210, v210, 0xc0b8aa3b, v198
	v_fmamk_f32 v211, v211, 0xc0b8aa3b, v198
	v_mul_f32_e32 v204, v204, v132
	v_mul_f32_e32 v205, v205, v133
	v_mul_f32_e32 v206, v206, v134
	v_mul_f32_e32 v207, v207, v135
	v_fma_f32 v132, v200, v208, v204
	v_fma_f32 v133, v201, v209, v205
	v_fma_f32 v134, v202, v210, v206
	v_fma_f32 v135, v203, v211, v207
	v_exp_f32_e32 v200, v132
	v_exp_f32_e32 v201, v133
	v_exp_f32_e32 v202, v134
	v_exp_f32_e32 v203, v135
	v_add_f32_e32 v200, 1.0, v200
	v_add_f32_e32 v201, 1.0, v201
	v_add_f32_e32 v202, 1.0, v202
	v_add_f32_e32 v203, 1.0, v203
	v_rcp_f32_e32 v200, v200
	v_rcp_f32_e32 v201, v201
	v_rcp_f32_e32 v202, v202
	v_rcp_f32_e32 v203, v203
	v_fma_f32 v200, v200, 2.0, -1.0
	v_fma_f32 v201, v201, 2.0, -1.0
	v_fma_f32 v202, v202, 2.0, -1.0
	v_fma_f32 v203, v203, 2.0, -1.0
	v_mul_f32_e32 v216, v212, v200
	v_mul_f32_e32 v217, v213, v201
	v_mul_f32_e32 v218, v214, v202
	v_mul_f32_e32 v219, v215, v203
	v_mul_f32_e32 v236, v216, v228
	v_mul_f32_e32 v237, v216, v232
	v_fmac_f32_e32 v236, v217, v229
	v_fmac_f32_e32 v237, v217, v233
	v_fmac_f32_e32 v236, v218, v230
	v_fmac_f32_e32 v237, v218, v234
	v_fmac_f32_e32 v236, v219, v231
	v_fmac_f32_e32 v237, v219, v235
	v_mov_b32_e32 v238, v236
	v_mov_b32_e32 v239, v236
	v_mov_b32_e32 v240, v237
	v_mov_b32_e32 v241, v237
	s_nop 1
	v_permlane32_swap_b32_e32 v238, v239
	v_permlane32_swap_b32_e32 v240, v241
	v_add_f32_e32 v238, v238, v239
	v_add_f32_e32 v239, v240, v241
	ds_write_b64 v248, v[238:239] offset:256
	v_cvt_pk_f16_f32 v222, v216, v217
	v_cvt_pk_f16_f32 v223, v218, v219
	s_nop 1
	v_permlane32_swap_b32_e32 v220, v222
	v_permlane32_swap_b32_e32 v221, v223
	s_cmp_eq_u32 s31, 0
	s_cbranch_scc1 .LD_slow4
	global_store_dwordx4 v195, v[220:223], s[36:37] offset:0
	s_branch .LD_join5

.LD_join5:
	s_waitcnt vmcnt(0)
	s_waitcnt lgkmcnt(0)
	s_barrier
	v_mov_b32_e32 v199, 1
	s_cmp_eq_u32 s31, 0
	s_cbranch_scc1 .LD_slow6
	global_store_dword v197, v199, s[40:41]
	s_branch .LD_join7

.LD_join7:
	ds_read_b64 v[200:201], v249 offset:0
	ds_read_b64 v[202:203], v249 offset:2048
	ds_read_b64 v[204:205], v249 offset:4096
	ds_read_b64 v[206:207], v249 offset:6144
	s_waitcnt lgkmcnt(0)
	v_add_f32_e32 v200, v200, v202
	v_add_f32_e32 v201, v201, v203
	v_add_f32_e32 v200, v200, v204
	v_add_f32_e32 v201, v201, v205
	v_add_f32_e32 v200, v200, v206
	v_add_f32_e32 v201, v201, v207
	global_store_dwordx2 v250, v[200:201], s[72:73]
	s_and_b32 s64, s33, 1
	s_lshl_b32 s64, s64, 22
	s_add_u32 s64, s64, s50
	s_add_u32 s64, s64, 0x20000
	s_add_u32 s36, s6, s64
	s_addc_u32 s37, s7, 0
	s_lshl_b32 s64, s33, 19
	s_add_u32 s64, s64, 0x200
	s_add_u32 s72, s62, s64
	s_addc_u32 s73, s63, 0
	v_exp_f32_e32 v200, v32
	v_exp_f32_e32 v201, v33
	v_exp_f32_e32 v202, v34
	v_exp_f32_e32 v203, v35
	v_exp_f32_e32 v204, v36
	v_exp_f32_e32 v205, v37
	v_exp_f32_e32 v206, v38
	v_exp_f32_e32 v207, v39
	v_exp_f32_e32 v208, v40
	v_exp_f32_e32 v209, v41
	v_exp_f32_e32 v210, v42
	v_exp_f32_e32 v211, v43
	v_exp_f32_e32 v212, v44
	v_exp_f32_e32 v213, v45
	v_exp_f32_e32 v214, v46
	v_exp_f32_e32 v215, v47
	v_add_f32_e32 v200, 1.0, v200
	v_add_f32_e32 v201, 1.0, v201
	v_add_f32_e32 v202, 1.0, v202
	v_add_f32_e32 v203, 1.0, v203
	v_add_f32_e32 v204, 1.0, v204
	v_add_f32_e32 v205, 1.0, v205
	v_add_f32_e32 v206, 1.0, v206
	v_add_f32_e32 v207, 1.0, v207
	v_add_f32_e32 v208, 1.0, v208
	v_add_f32_e32 v209, 1.0, v209
	v_add_f32_e32 v210, 1.0, v210
	v_add_f32_e32 v211, 1.0, v211
	v_add_f32_e32 v212, 1.0, v212
	v_add_f32_e32 v213, 1.0, v213
	v_add_f32_e32 v214, 1.0, v214
	v_add_f32_e32 v215, 1.0, v215
	v_rcp_f32_e32 v200, v200
	v_rcp_f32_e32 v201, v201
	v_rcp_f32_e32 v202, v202
	v_rcp_f32_e32 v203, v203
	v_rcp_f32_e32 v204, v204
	v_rcp_f32_e32 v205, v205
	v_rcp_f32_e32 v206, v206
	v_rcp_f32_e32 v207, v207
	v_rcp_f32_e32 v208, v208
	v_rcp_f32_e32 v209, v209
	v_rcp_f32_e32 v210, v210
	v_rcp_f32_e32 v211, v211
	v_rcp_f32_e32 v212, v212
	v_rcp_f32_e32 v213, v213
	v_rcp_f32_e32 v214, v214
	v_rcp_f32_e32 v215, v215
	v_fmamk_f32 v208, v208, 0xc0b8aa3b, v198
	v_fmamk_f32 v209, v209, 0xc0b8aa3b, v198
	v_fmamk_f32 v210, v210, 0xc0b8aa3b, v198
	v_fmamk_f32 v211, v211, 0xc0b8aa3b, v198
	v_mul_f32_e32 v204, v204, v136
	v_mul_f32_e32 v205, v205, v137
	v_mul_f32_e32 v206, v206, v138
	v_mul_f32_e32 v207, v207, v139
	v_fma_f32 v136, v200, v208, v204
	v_fma_f32 v137, v201, v209, v205
	v_fma_f32 v138, v202, v210, v206
	v_fma_f32 v139, v203, v211, v207
	v_exp_f32_e32 v200, v136
	v_exp_f32_e32 v201, v137
	v_exp_f32_e32 v202, v138
	v_exp_f32_e32 v203, v139
	v_add_f32_e32 v200, 1.0, v200
	v_add_f32_e32 v201, 1.0, v201
	v_add_f32_e32 v202, 1.0, v202
	v_add_f32_e32 v203, 1.0, v203
	v_rcp_f32_e32 v200, v200
	v_rcp_f32_e32 v201, v201
	v_rcp_f32_e32 v202, v202
	v_rcp_f32_e32 v203, v203
	v_fma_f32 v200, v200, 2.0, -1.0
	v_fma_f32 v201, v201, 2.0, -1.0
	v_fma_f32 v202, v202, 2.0, -1.0
	v_fma_f32 v203, v203, 2.0, -1.0
	v_mul_f32_e32 v216, v212, v200
	v_mul_f32_e32 v217, v213, v201
	v_mul_f32_e32 v218, v214, v202
	v_mul_f32_e32 v219, v215, v203
	v_mul_f32_e32 v236, v216, v228
	v_mul_f32_e32 v237, v216, v232
	v_fmac_f32_e32 v236, v217, v229
	v_fmac_f32_e32 v237, v217, v233
	v_fmac_f32_e32 v236, v218, v230
	v_fmac_f32_e32 v237, v218, v234
	v_fmac_f32_e32 v236, v219, v231
	v_fmac_f32_e32 v237, v219, v235
	v_mov_b32_e32 v238, v236
	v_mov_b32_e32 v239, v236
	v_mov_b32_e32 v240, v237
	v_mov_b32_e32 v241, v237
	s_nop 1
	v_permlane32_swap_b32_e32 v238, v239
	v_permlane32_swap_b32_e32 v240, v241
	v_add_f32_e32 v238, v238, v239
	v_add_f32_e32 v239, v240, v241
	ds_write_b64 v248, v[238:239] offset:512
	v_cvt_pk_f16_f32 v220, v216, v217
	v_cvt_pk_f16_f32 v221, v218, v219
	v_exp_f32_e32 v200, v48
	v_exp_f32_e32 v201, v49
	v_exp_f32_e32 v202, v50
	v_exp_f32_e32 v203, v51
	v_exp_f32_e32 v204, v52
	v_exp_f32_e32 v205, v53
	v_exp_f32_e32 v206, v54
	v_exp_f32_e32 v207, v55
	v_exp_f32_e32 v208, v56
	v_exp_f32_e32 v209, v57
	v_exp_f32_e32 v210, v58
	v_exp_f32_e32 v211, v59
	v_exp_f32_e32 v212, v60
	v_exp_f32_e32 v213, v61
	v_exp_f32_e32 v214, v62
	v_exp_f32_e32 v215, v63
	v_add_f32_e32 v200, 1.0, v200
	v_add_f32_e32 v201, 1.0, v201
	v_add_f32_e32 v202, 1.0, v202
	v_add_f32_e32 v203, 1.0, v203
	v_add_f32_e32 v204, 1.0, v204
	v_add_f32_e32 v205, 1.0, v205
	v_add_f32_e32 v206, 1.0, v206
	v_add_f32_e32 v207, 1.0, v207
	v_add_f32_e32 v208, 1.0, v208
	v_add_f32_e32 v209, 1.0, v209
	v_add_f32_e32 v210, 1.0, v210
	v_add_f32_e32 v211, 1.0, v211
	v_add_f32_e32 v212, 1.0, v212
	v_add_f32_e32 v213, 1.0, v213
	v_add_f32_e32 v214, 1.0, v214
	v_add_f32_e32 v215, 1.0, v215
	v_rcp_f32_e32 v200, v200
	v_rcp_f32_e32 v201, v201
	v_rcp_f32_e32 v202, v202
	v_rcp_f32_e32 v203, v203
	v_rcp_f32_e32 v204, v204
	v_rcp_f32_e32 v205, v205
	v_rcp_f32_e32 v206, v206
	v_rcp_f32_e32 v207, v207
	v_rcp_f32_e32 v208, v208
	v_rcp_f32_e32 v209, v209
	v_rcp_f32_e32 v210, v210
	v_rcp_f32_e32 v211, v211
	v_rcp_f32_e32 v212, v212
	v_rcp_f32_e32 v213, v213
	v_rcp_f32_e32 v214, v214
	v_rcp_f32_e32 v215, v215
	v_fmamk_f32 v208, v208, 0xc0b8aa3b, v198
	v_fmamk_f32 v209, v209, 0xc0b8aa3b, v198
	v_fmamk_f32 v210, v210, 0xc0b8aa3b, v198
	v_fmamk_f32 v211, v211, 0xc0b8aa3b, v198
	v_mul_f32_e32 v204, v204, v140
	v_mul_f32_e32 v205, v205, v141
	v_mul_f32_e32 v206, v206, v142
	v_mul_f32_e32 v207, v207, v143
	v_fma_f32 v140, v200, v208, v204
	v_fma_f32 v141, v201, v209, v205
	v_fma_f32 v142, v202, v210, v206
	v_fma_f32 v143, v203, v211, v207
	v_exp_f32_e32 v200, v140
	v_exp_f32_e32 v201, v141
	v_exp_f32_e32 v202, v142
	v_exp_f32_e32 v203, v143
	v_add_f32_e32 v200, 1.0, v200
	v_add_f32_e32 v201, 1.0, v201
	v_add_f32_e32 v202, 1.0, v202
	v_add_f32_e32 v203, 1.0, v203
	v_rcp_f32_e32 v200, v200
	v_rcp_f32_e32 v201, v201
	v_rcp_f32_e32 v202, v202
	v_rcp_f32_e32 v203, v203
	v_fma_f32 v200, v200, 2.0, -1.0
	v_fma_f32 v201, v201, 2.0, -1.0
	v_fma_f32 v202, v202, 2.0, -1.0
	v_fma_f32 v203, v203, 2.0, -1.0
	v_mul_f32_e32 v216, v212, v200
	v_mul_f32_e32 v217, v213, v201
	v_mul_f32_e32 v218, v214, v202
	v_mul_f32_e32 v219, v215, v203
	v_mul_f32_e32 v236, v216, v228
	v_mul_f32_e32 v237, v216, v232
	v_fmac_f32_e32 v236, v217, v229
	v_fmac_f32_e32 v237, v217, v233
	v_fmac_f32_e32 v236, v218, v230
	v_fmac_f32_e32 v237, v218, v234
	v_fmac_f32_e32 v236, v219, v231
	v_fmac_f32_e32 v237, v219, v235
	v_mov_b32_e32 v238, v236
	v_mov_b32_e32 v239, v236
	v_mov_b32_e32 v240, v237
	v_mov_b32_e32 v241, v237
	s_nop 1
	v_permlane32_swap_b32_e32 v238, v239
	v_permlane32_swap_b32_e32 v240, v241
	v_add_f32_e32 v238, v238, v239
	v_add_f32_e32 v239, v240, v241
	ds_write_b64 v248, v[238:239] offset:768
	v_cvt_pk_f16_f32 v222, v216, v217
	v_cvt_pk_f16_f32 v223, v218, v219
	s_nop 1
	v_permlane32_swap_b32_e32 v220, v222
	v_permlane32_swap_b32_e32 v221, v223
	s_cmp_eq_u32 s31, 0
	s_cbranch_scc1 .LD_slow8
	global_store_dwordx4 v195, v[220:223], s[36:37] offset:0
	s_branch .LD_join9

.LD_join9:
	s_waitcnt vmcnt(0)
	s_waitcnt lgkmcnt(0)
	s_barrier
	v_mov_b32_e32 v199, 2
	s_cmp_eq_u32 s31, 0
	s_cbranch_scc1 .LD_slow10
	global_store_dword v197, v199, s[40:41]
	s_branch .LD_join11

.LD_join11:
	ds_read_b64 v[200:201], v249 offset:512
	ds_read_b64 v[202:203], v249 offset:2560
	ds_read_b64 v[204:205], v249 offset:4608
	ds_read_b64 v[206:207], v249 offset:6656
	s_waitcnt lgkmcnt(0)
	v_add_f32_e32 v200, v200, v202
	v_add_f32_e32 v201, v201, v203
	v_add_f32_e32 v200, v200, v204
	v_add_f32_e32 v201, v201, v205
	v_add_f32_e32 v200, v200, v206
	v_add_f32_e32 v201, v201, v207
	global_store_dwordx2 v250, v[200:201], s[72:73]
	s_and_b32 s64, s33, 1
	s_lshl_b32 s64, s64, 22
	s_add_u32 s64, s64, s50
	s_add_u32 s64, s64, 0x40000
	s_add_u32 s36, s6, s64
	s_addc_u32 s37, s7, 0
	s_lshl_b32 s64, s33, 19
	s_add_u32 s64, s64, 0x400
	s_add_u32 s72, s62, s64
	s_addc_u32 s73, s63, 0
	v_exp_f32_e32 v200, v64
	v_exp_f32_e32 v201, v65
	v_exp_f32_e32 v202, v66
	v_exp_f32_e32 v203, v67
	v_exp_f32_e32 v204, v68
	v_exp_f32_e32 v205, v69
	v_exp_f32_e32 v206, v70
	v_exp_f32_e32 v207, v71
	v_exp_f32_e32 v208, v72
	v_exp_f32_e32 v209, v73
	v_exp_f32_e32 v210, v74
	v_exp_f32_e32 v211, v75
	v_exp_f32_e32 v212, v76
	v_exp_f32_e32 v213, v77
	v_exp_f32_e32 v214, v78
	v_exp_f32_e32 v215, v79
	v_add_f32_e32 v200, 1.0, v200
	v_add_f32_e32 v201, 1.0, v201
	v_add_f32_e32 v202, 1.0, v202
	v_add_f32_e32 v203, 1.0, v203
	v_add_f32_e32 v204, 1.0, v204
	v_add_f32_e32 v205, 1.0, v205
	v_add_f32_e32 v206, 1.0, v206
	v_add_f32_e32 v207, 1.0, v207
	v_add_f32_e32 v208, 1.0, v208
	v_add_f32_e32 v209, 1.0, v209
	v_add_f32_e32 v210, 1.0, v210
	v_add_f32_e32 v211, 1.0, v211
	v_add_f32_e32 v212, 1.0, v212
	v_add_f32_e32 v213, 1.0, v213
	v_add_f32_e32 v214, 1.0, v214
	v_add_f32_e32 v215, 1.0, v215
	v_rcp_f32_e32 v200, v200
	v_rcp_f32_e32 v201, v201
	v_rcp_f32_e32 v202, v202
	v_rcp_f32_e32 v203, v203
	v_rcp_f32_e32 v204, v204
	v_rcp_f32_e32 v205, v205
	v_rcp_f32_e32 v206, v206
	v_rcp_f32_e32 v207, v207
	v_rcp_f32_e32 v208, v208
	v_rcp_f32_e32 v209, v209
	v_rcp_f32_e32 v210, v210
	v_rcp_f32_e32 v211, v211
	v_rcp_f32_e32 v212, v212
	v_rcp_f32_e32 v213, v213
	v_rcp_f32_e32 v214, v214
	v_rcp_f32_e32 v215, v215
	v_fmamk_f32 v208, v208, 0xc0b8aa3b, v198
	v_fmamk_f32 v209, v209, 0xc0b8aa3b, v198
	v_fmamk_f32 v210, v210, 0xc0b8aa3b, v198
	v_fmamk_f32 v211, v211, 0xc0b8aa3b, v198
	v_mul_f32_e32 v204, v204, v144
	v_mul_f32_e32 v205, v205, v145
	v_mul_f32_e32 v206, v206, v146
	v_mul_f32_e32 v207, v207, v147
	v_fma_f32 v144, v200, v208, v204
	v_fma_f32 v145, v201, v209, v205
	v_fma_f32 v146, v202, v210, v206
	v_fma_f32 v147, v203, v211, v207
	v_exp_f32_e32 v200, v144
	v_exp_f32_e32 v201, v145
	v_exp_f32_e32 v202, v146
	v_exp_f32_e32 v203, v147
	v_add_f32_e32 v200, 1.0, v200
	v_add_f32_e32 v201, 1.0, v201
	v_add_f32_e32 v202, 1.0, v202
	v_add_f32_e32 v203, 1.0, v203
	v_rcp_f32_e32 v200, v200
	v_rcp_f32_e32 v201, v201
	v_rcp_f32_e32 v202, v202
	v_rcp_f32_e32 v203, v203
	v_fma_f32 v200, v200, 2.0, -1.0
	v_fma_f32 v201, v201, 2.0, -1.0
	v_fma_f32 v202, v202, 2.0, -1.0
	v_fma_f32 v203, v203, 2.0, -1.0
	v_mul_f32_e32 v216, v212, v200
	v_mul_f32_e32 v217, v213, v201
	v_mul_f32_e32 v218, v214, v202
	v_mul_f32_e32 v219, v215, v203
	v_mul_f32_e32 v236, v216, v228
	v_mul_f32_e32 v237, v216, v232
	v_fmac_f32_e32 v236, v217, v229
	v_fmac_f32_e32 v237, v217, v233
	v_fmac_f32_e32 v236, v218, v230
	v_fmac_f32_e32 v237, v218, v234
	v_fmac_f32_e32 v236, v219, v231
	v_fmac_f32_e32 v237, v219, v235
	v_mov_b32_e32 v238, v236
	v_mov_b32_e32 v239, v236
	v_mov_b32_e32 v240, v237
	v_mov_b32_e32 v241, v237
	s_nop 1
	v_permlane32_swap_b32_e32 v238, v239
	v_permlane32_swap_b32_e32 v240, v241
	v_add_f32_e32 v238, v238, v239
	v_add_f32_e32 v239, v240, v241
	ds_write_b64 v248, v[238:239] offset:1024
	v_cvt_pk_f16_f32 v220, v216, v217
	v_cvt_pk_f16_f32 v221, v218, v219
	v_exp_f32_e32 v200, v80
	v_exp_f32_e32 v201, v81
	v_exp_f32_e32 v202, v82
	v_exp_f32_e32 v203, v83
	v_exp_f32_e32 v204, v84
	v_exp_f32_e32 v205, v85
	v_exp_f32_e32 v206, v86
	v_exp_f32_e32 v207, v87
	v_exp_f32_e32 v208, v88
	v_exp_f32_e32 v209, v89
	v_exp_f32_e32 v210, v90
	v_exp_f32_e32 v211, v91
	v_exp_f32_e32 v212, v92
	v_exp_f32_e32 v213, v93
	v_exp_f32_e32 v214, v94
	v_exp_f32_e32 v215, v95
	v_add_f32_e32 v200, 1.0, v200
	v_add_f32_e32 v201, 1.0, v201
	v_add_f32_e32 v202, 1.0, v202
	v_add_f32_e32 v203, 1.0, v203
	v_add_f32_e32 v204, 1.0, v204
	v_add_f32_e32 v205, 1.0, v205
	v_add_f32_e32 v206, 1.0, v206
	v_add_f32_e32 v207, 1.0, v207
	v_add_f32_e32 v208, 1.0, v208
	v_add_f32_e32 v209, 1.0, v209
	v_add_f32_e32 v210, 1.0, v210
	v_add_f32_e32 v211, 1.0, v211
	v_add_f32_e32 v212, 1.0, v212
	v_add_f32_e32 v213, 1.0, v213
	v_add_f32_e32 v214, 1.0, v214
	v_add_f32_e32 v215, 1.0, v215
	v_rcp_f32_e32 v200, v200
	v_rcp_f32_e32 v201, v201
	v_rcp_f32_e32 v202, v202
	v_rcp_f32_e32 v203, v203
	v_rcp_f32_e32 v204, v204
	v_rcp_f32_e32 v205, v205
	v_rcp_f32_e32 v206, v206
	v_rcp_f32_e32 v207, v207
	v_rcp_f32_e32 v208, v208
	v_rcp_f32_e32 v209, v209
	v_rcp_f32_e32 v210, v210
	v_rcp_f32_e32 v211, v211
	v_rcp_f32_e32 v212, v212
	v_rcp_f32_e32 v213, v213
	v_rcp_f32_e32 v214, v214
	v_rcp_f32_e32 v215, v215
	v_fmamk_f32 v208, v208, 0xc0b8aa3b, v198
	v_fmamk_f32 v209, v209, 0xc0b8aa3b, v198
	v_fmamk_f32 v210, v210, 0xc0b8aa3b, v198
	v_fmamk_f32 v211, v211, 0xc0b8aa3b, v198
	v_mul_f32_e32 v204, v204, v148
	v_mul_f32_e32 v205, v205, v149
	v_mul_f32_e32 v206, v206, v150
	v_mul_f32_e32 v207, v207, v151
	v_fma_f32 v148, v200, v208, v204
	v_fma_f32 v149, v201, v209, v205
	v_fma_f32 v150, v202, v210, v206
	v_fma_f32 v151, v203, v211, v207
	v_exp_f32_e32 v200, v148
	v_exp_f32_e32 v201, v149
	v_exp_f32_e32 v202, v150
	v_exp_f32_e32 v203, v151
	v_add_f32_e32 v200, 1.0, v200
	v_add_f32_e32 v201, 1.0, v201
	v_add_f32_e32 v202, 1.0, v202
	v_add_f32_e32 v203, 1.0, v203
	v_rcp_f32_e32 v200, v200
	v_rcp_f32_e32 v201, v201
	v_rcp_f32_e32 v202, v202
	v_rcp_f32_e32 v203, v203
	v_fma_f32 v200, v200, 2.0, -1.0
	v_fma_f32 v201, v201, 2.0, -1.0
	v_fma_f32 v202, v202, 2.0, -1.0
	v_fma_f32 v203, v203, 2.0, -1.0
	v_mul_f32_e32 v216, v212, v200
	v_mul_f32_e32 v217, v213, v201
	v_mul_f32_e32 v218, v214, v202
	v_mul_f32_e32 v219, v215, v203
	v_mul_f32_e32 v236, v216, v228
	v_mul_f32_e32 v237, v216, v232
	v_fmac_f32_e32 v236, v217, v229
	v_fmac_f32_e32 v237, v217, v233
	v_fmac_f32_e32 v236, v218, v230
	v_fmac_f32_e32 v237, v218, v234
	v_fmac_f32_e32 v236, v219, v231
	v_fmac_f32_e32 v237, v219, v235
	v_mov_b32_e32 v238, v236
	v_mov_b32_e32 v239, v236
	v_mov_b32_e32 v240, v237
	v_mov_b32_e32 v241, v237
	s_nop 1
	v_permlane32_swap_b32_e32 v238, v239
	v_permlane32_swap_b32_e32 v240, v241
	v_add_f32_e32 v238, v238, v239
	v_add_f32_e32 v239, v240, v241
	ds_write_b64 v248, v[238:239] offset:1280
	v_cvt_pk_f16_f32 v222, v216, v217
	v_cvt_pk_f16_f32 v223, v218, v219
	s_nop 1
	v_permlane32_swap_b32_e32 v220, v222
	v_permlane32_swap_b32_e32 v221, v223
	s_cmp_eq_u32 s31, 0
	s_cbranch_scc1 .LD_slow12
	global_store_dwordx4 v195, v[220:223], s[36:37] offset:0
	s_branch .LD_join13

.LD_join13:
	s_waitcnt vmcnt(0)
	s_waitcnt lgkmcnt(0)
	s_barrier
	v_mov_b32_e32 v199, 3
	s_cmp_eq_u32 s31, 0
	s_cbranch_scc1 .LD_slow14
	global_store_dword v197, v199, s[40:41]
	s_branch .LD_join15

.LD_join15:
	ds_read_b64 v[200:201], v249 offset:1024
	ds_read_b64 v[202:203], v249 offset:3072
	ds_read_b64 v[204:205], v249 offset:5120
	ds_read_b64 v[206:207], v249 offset:7168
	s_waitcnt lgkmcnt(0)
	v_add_f32_e32 v200, v200, v202
	v_add_f32_e32 v201, v201, v203
	v_add_f32_e32 v200, v200, v204
	v_add_f32_e32 v201, v201, v205
	v_add_f32_e32 v200, v200, v206
	v_add_f32_e32 v201, v201, v207
	global_store_dwordx2 v250, v[200:201], s[72:73]
	s_mov_b32 s33, 1
	s_add_u32 s46, s42, 0x0
	s_addc_u32 s47, s43, 0
	global_load_dwordx4 v[0:3], v192, s[46:47] offset:0
	global_load_dwordx4 v[4:7], v192, s[46:47] offset:1024
	global_load_dwordx4 v[8:11], v192, s[46:47] offset:2048
	global_load_dwordx4 v[12:15], v192, s[46:47] offset:3072
	s_add_u32 s46, s42, 0x1000
	s_addc_u32 s47, s43, 0
	global_load_dwordx4 v[16:19], v192, s[46:47] offset:0
	global_load_dwordx4 v[20:23], v192, s[46:47] offset:1024
	global_load_dwordx4 v[24:27], v192, s[46:47] offset:2048
	global_load_dwordx4 v[28:31], v192, s[46:47] offset:3072
	s_add_u32 s46, s42, 0x2000
	s_addc_u32 s47, s43, 0
	global_load_dwordx4 v[32:35], v192, s[46:47] offset:0
	global_load_dwordx4 v[36:39], v192, s[46:47] offset:1024
	global_load_dwordx4 v[40:43], v192, s[46:47] offset:2048
	global_load_dwordx4 v[44:47], v192, s[46:47] offset:3072
	s_add_u32 s46, s42, 0x3000
	s_addc_u32 s47, s43, 0
	global_load_dwordx4 v[48:51], v192, s[46:47] offset:0
	global_load_dwordx4 v[52:55], v192, s[46:47] offset:1024
	global_load_dwordx4 v[56:59], v192, s[46:47] offset:2048
	global_load_dwordx4 v[60:63], v192, s[46:47] offset:3072
	s_waitcnt vmcnt(0)
	s_waitcnt lgkmcnt(0)
	s_cmp_ge_u32 s33, s28
	s_cbranch_scc1 .LD_end17
	s_sub_u32 s71, s33, 1
	s_and_b32 s64, s71, 1
	s_lshl_b32 s64, s64, 22
	s_add_u32 s64, s64, s49
	s_add_u32 s34, s6, s64
	s_addc_u32 s35, s7, 0
	s_lshl_b32 s64, s71, 3
	s_add_u32 s64, s64, s29
	s_lshl_b32 s64, s64, 7
	s_add_u32 s38, s8, s64
	s_addc_u32 s39, s9, 0

.LD_loop16:
	s_sub_u32 s71, s33, 1
	s_add_u32 s61, s33, 1
	s_min_u32 s61, s61, s60
	s_and_b32 s64, s71, 1
	s_lshl_b32 s64, s64, 22
	s_add_u32 s64, s64, s50
	s_add_u32 s64, s64, 0x60000
	s_add_u32 s36, s6, s64
	s_addc_u32 s37, s7, 0
	s_lshl_b32 s64, s71, 3
	s_add_u32 s64, s64, s29
	s_lshl_b32 s64, s64, 5
	s_add_u32 s64, s64, s30
	s_lshl_b32 s64, s64, 2
	s_add_u32 s40, s8, s64
	s_addc_u32 s41, s9, 0
	s_lshl_b32 s64, s71, 19
	s_add_u32 s64, s64, 0x600
	s_add_u32 s72, s62, s64
	s_addc_u32 s73, s63, 0
	s_nop 11
	s_waitcnt lgkmcnt(6)
	v_mfma_f32_32x32x16_f16 v[0:15], a[0:3], v[160:163], v[0:15]
	ds_read_b128 v[160:163], v192 offset:8192
	v_exp_f32_e32 v200, v96
	v_mfma_f32_32x32x16_f16 v[16:31], a[0:3], v[164:167], v[16:31]
	ds_read_b128 v[164:167], v192 offset:9216
	v_exp_f32_e32 v201, v97
	v_add_f32_e32 v200, 1.0, v200
	s_waitcnt lgkmcnt(6)
	v_mfma_f32_32x32x16_f16 v[0:15], a[4:7], v[168:171], v[0:15]
	ds_read_b128 v[168:171], v192 offset:10240
	v_exp_f32_e32 v202, v98
	v_add_f32_e32 v201, 1.0, v201
	v_mfma_f32_32x32x16_f16 v[16:31], a[4:7], v[172:175], v[16:31]
	ds_read_b128 v[172:175], v192 offset:11264
	global_load_lds_dwordx4 v192, s[44:45] offset:1024 sc1
	v_exp_f32_e32 v203, v99
	v_add_f32_e32 v202, 1.0, v202
	s_waitcnt lgkmcnt(6)
	v_mfma_f32_32x32x16_f16 v[0:15], a[8:11], v[176:179], v[0:15]
	ds_read_b128 v[176:179], v192 offset:12288
	v_exp_f32_e32 v204, v100
	v_add_f32_e32 v203, 1.0, v203
	v_mfma_f32_32x32x16_f16 v[16:31], a[8:11], v[180:183], v[16:31]
	ds_read_b128 v[180:183], v192 offset:13312
	v_exp_f32_e32 v205, v101
	v_add_f32_e32 v204, 1.0, v204
	s_waitcnt lgkmcnt(6)
	v_mfma_f32_32x32x16_f16 v[0:15], a[12:15], v[184:187], v[0:15]
	ds_read_b128 v[184:187], v192 offset:14336
	v_exp_f32_e32 v206, v102
	v_add_f32_e32 v205, 1.0, v205
	v_mfma_f32_32x32x16_f16 v[16:31], a[12:15], v[188:191], v[16:31]
	ds_read_b128 v[188:191], v192 offset:15360
	global_load_lds_dwordx4 v192, s[44:45] offset:2048 sc1
	v_exp_f32_e32 v207, v103
	v_add_f32_e32 v206, 1.0, v206
	s_waitcnt lgkmcnt(6)
	v_mfma_f32_32x32x16_f16 v[0:15], a[16:19], v[160:163], v[0:15]
	ds_read_b128 v[160:163], v192 offset:16384
	v_exp_f32_e32 v208, v104
	v_add_f32_e32 v207, 1.0, v207
	v_mfma_f32_32x32x16_f16 v[16:31], a[16:19], v[164:167], v[16:31]
	ds_read_b128 v[164:167], v192 offset:17408
	v_exp_f32_e32 v209, v105
	v_add_f32_e32 v208, 1.0, v208
	s_waitcnt lgkmcnt(6)
	v_mfma_f32_32x32x16_f16 v[0:15], a[20:23], v[168:171], v[0:15]
	ds_read_b128 v[168:171], v192 offset:18432
	v_exp_f32_e32 v210, v106
	v_add_f32_e32 v209, 1.0, v209
	v_mfma_f32_32x32x16_f16 v[16:31], a[20:23], v[172:175], v[16:31]
	ds_read_b128 v[172:175], v192 offset:19456
	global_load_lds_dwordx4 v192, s[44:45] offset:3072 sc1
	v_exp_f32_e32 v211, v107
	v_add_f32_e32 v210, 1.0, v210
	s_waitcnt lgkmcnt(6)
	v_mfma_f32_32x32x16_f16 v[0:15], a[24:27], v[176:179], v[0:15]
	ds_read_b128 v[176:179], v192 offset:20480
	v_exp_f32_e32 v212, v108
	v_add_f32_e32 v211, 1.0, v211
	v_mfma_f32_32x32x16_f16 v[16:31], a[24:27], v[180:183], v[16:31]
	ds_read_b128 v[180:183], v192 offset:21504
	v_exp_f32_e32 v213, v109
	v_add_f32_e32 v212, 1.0, v212
	s_waitcnt lgkmcnt(6)
	v_mfma_f32_32x32x16_f16 v[0:15], a[28:31], v[184:187], v[0:15]
	ds_read_b128 v[184:187], v192 offset:22528
	v_exp_f32_e32 v214, v110
	v_add_f32_e32 v213, 1.0, v213
	v_mfma_f32_32x32x16_f16 v[16:31], a[28:31], v[188:191], v[16:31]
	ds_read_b128 v[188:191], v192 offset:23552
	s_add_u32 s44, s34, 0x11000
	s_addc_u32 s45, s35, 0
	s_mov_b32 m0, s57
	s_nop 0
	global_load_lds_dwordx4 v192, s[44:45] sc1
	v_exp_f32_e32 v215, v111
	v_add_f32_e32 v214, 1.0, v214
	s_waitcnt lgkmcnt(6)
	v_mfma_f32_32x32x16_f16 v[0:15], a[32:35], v[160:163], v[0:15]
	ds_read_b128 v[160:163], v192 offset:24576
	v_add_f32_e32 v215, 1.0, v215
	v_rcp_f32_e32 v200, v200
	v_mfma_f32_32x32x16_f16 v[16:31], a[32:35], v[164:167], v[16:31]
	ds_read_b128 v[164:167], v192 offset:25600
	v_rcp_f32_e32 v201, v201
	s_waitcnt lgkmcnt(6)
	v_mfma_f32_32x32x16_f16 v[0:15], a[36:39], v[168:171], v[0:15]
	ds_read_b128 v[168:171], v192 offset:26624
	v_rcp_f32_e32 v202, v202
	v_mfma_f32_32x32x16_f16 v[16:31], a[36:39], v[172:175], v[16:31]
	ds_read_b128 v[172:175], v192 offset:27648
	global_load_lds_dwordx4 v192, s[44:45] offset:1024 sc1
	v_rcp_f32_e32 v203, v203
	s_waitcnt lgkmcnt(6)
	v_mfma_f32_32x32x16_f16 v[0:15], a[40:43], v[176:179], v[0:15]
	ds_read_b128 v[176:179], v192 offset:28672
	v_rcp_f32_e32 v204, v204
	v_mfma_f32_32x32x16_f16 v[16:31], a[40:43], v[180:183], v[16:31]
	ds_read_b128 v[180:183], v192 offset:29696
	v_rcp_f32_e32 v205, v205
	v_mul_f32_e32 v204, v204, v152
	s_waitcnt lgkmcnt(6)
	v_mfma_f32_32x32x16_f16 v[0:15], a[44:47], v[184:187], v[0:15]
	ds_read_b128 v[184:187], v192 offset:30720
	v_rcp_f32_e32 v206, v206
	v_mul_f32_e32 v205, v205, v153
	v_mfma_f32_32x32x16_f16 v[16:31], a[44:47], v[188:191], v[16:31]
	ds_read_b128 v[188:191], v192 offset:31744
	global_load_lds_dwordx4 v192, s[44:45] offset:2048 sc1
	v_rcp_f32_e32 v207, v207
	v_mul_f32_e32 v206, v206, v154
	s_waitcnt vmcnt(7)
	s_barrier
	s_waitcnt lgkmcnt(6)
	v_mfma_f32_32x32x16_f16 v[0:15], a[48:51], v[160:163], v[0:15]
	ds_read_b128 v[160:163], v192 offset:32768
	v_rcp_f32_e32 v208, v208
	v_mul_f32_e32 v207, v207, v155
	s_add_u32 s46, s42, 0x4000
	s_addc_u32 s47, s43, 0
	global_load_dwordx4 v[64:67], v192, s[46:47] offset:0
	v_mfma_f32_32x32x16_f16 v[16:31], a[48:51], v[164:167], v[16:31]
	ds_read_b128 v[164:167], v192 offset:33792
	v_rcp_f32_e32 v209, v209
	v_fmamk_f32 v208, v208, 0xc0b8aa3b, v198
	global_load_dwordx4 v[68:71], v192, s[46:47] offset:1024
	global_load_dwordx4 v[72:75], v192, s[46:47] offset:2048
	s_waitcnt lgkmcnt(6)
	v_mfma_f32_32x32x16_f16 v[0:15], a[52:55], v[168:171], v[0:15]
	ds_read_b128 v[168:171], v192 offset:34816
	v_rcp_f32_e32 v210, v210
	v_fmamk_f32 v209, v209, 0xc0b8aa3b, v198
	v_fma_f32 v152, v200, v208, v204
	global_load_dwordx4 v[76:79], v192, s[46:47] offset:3072
	s_add_u32 s46, s42, 0x5000
	s_addc_u32 s47, s43, 0
	v_mfma_f32_32x32x16_f16 v[16:31], a[52:55], v[172:175], v[16:31]
	ds_read_b128 v[172:175], v192 offset:35840
	global_load_lds_dwordx4 v192, s[44:45] offset:3072 sc1
	v_rcp_f32_e32 v211, v211
	v_fmamk_f32 v210, v210, 0xc0b8aa3b, v198
	v_fma_f32 v153, v201, v209, v205
	global_load_dwordx4 v[80:83], v192, s[46:47] offset:0
	global_load_dwordx4 v[84:87], v192, s[46:47] offset:1024
	s_waitcnt lgkmcnt(6)
	v_mfma_f32_32x32x16_f16 v[0:15], a[56:59], v[176:179], v[0:15]
	ds_read_b128 v[176:179], v192 offset:36864
	v_rcp_f32_e32 v212, v212
	v_fmamk_f32 v211, v211, 0xc0b8aa3b, v198
	v_fma_f32 v154, v202, v210, v206
	global_load_dwordx4 v[88:91], v192, s[46:47] offset:2048
	global_load_dwordx4 v[92:95], v192, s[46:47] offset:3072
	v_mfma_f32_32x32x16_f16 v[16:31], a[56:59], v[180:183], v[16:31]
	ds_read_b128 v[180:183], v192 offset:37888
	v_rcp_f32_e32 v213, v213
	v_fma_f32 v155, v203, v211, v207
	s_waitcnt lgkmcnt(6)
	v_mfma_f32_32x32x16_f16 v[0:15], a[60:63], v[184:187], v[0:15]
	ds_read_b128 v[184:187], v192 offset:38912
	v_rcp_f32_e32 v214, v214
	v_mfma_f32_32x32x16_f16 v[16:31], a[60:63], v[188:191], v[16:31]
	ds_read_b128 v[188:191], v192 offset:39936
	s_add_u32 s44, s34, 0x18000
	s_addc_u32 s45, s35, 0
	s_mov_b32 m0, s58
	s_nop 0
	global_load_lds_dwordx4 v192, s[44:45] sc1
	v_rcp_f32_e32 v215, v215
	s_waitcnt lgkmcnt(6)
	v_mfma_f32_32x32x16_f16 v[0:15], a[64:67], v[160:163], v[0:15]
	ds_read_b128 v[160:163], v192 offset:40960
	v_exp_f32_e32 v200, v152
	v_mfma_f32_32x32x16_f16 v[16:31], a[64:67], v[164:167], v[16:31]
	ds_read_b128 v[164:167], v192 offset:41984
	v_exp_f32_e32 v201, v153
	v_add_f32_e32 v200, 1.0, v200
	s_waitcnt lgkmcnt(6)
	v_mfma_f32_32x32x16_f16 v[0:15], a[68:71], v[168:171], v[0:15]
	ds_read_b128 v[168:171], v192 offset:43008
	v_exp_f32_e32 v202, v154
	v_add_f32_e32 v201, 1.0, v201
	v_mfma_f32_32x32x16_f16 v[16:31], a[68:71], v[172:175], v[16:31]
	ds_read_b128 v[172:175], v192 offset:44032
	global_load_lds_dwordx4 v192, s[44:45] offset:1024 sc1
	v_exp_f32_e32 v203, v155
	v_add_f32_e32 v202, 1.0, v202
	s_waitcnt lgkmcnt(6)
	v_mfma_f32_32x32x16_f16 v[0:15], a[72:75], v[176:179], v[0:15]
	ds_read_b128 v[176:179], v192 offset:45056
	v_add_f32_e32 v203, 1.0, v203
	v_rcp_f32_e32 v200, v200
	v_mfma_f32_32x32x16_f16 v[16:31], a[72:75], v[180:183], v[16:31]
	ds_read_b128 v[180:183], v192 offset:46080
	v_rcp_f32_e32 v201, v201
	v_fma_f32 v200, v200, 2.0, -1.0
	s_waitcnt lgkmcnt(6)
	v_mfma_f32_32x32x16_f16 v[0:15], a[76:79], v[184:187], v[0:15]
	ds_read_b128 v[184:187], v192 offset:47104
	v_rcp_f32_e32 v202, v202
	v_fma_f32 v201, v201, 2.0, -1.0
	v_mul_f32_e32 v216, v212, v200
	v_mfma_f32_32x32x16_f16 v[16:31], a[76:79], v[188:191], v[16:31]
	ds_read_b128 v[188:191], v192 offset:48128
	global_load_lds_dwordx4 v192, s[44:45] offset:2048 sc1
	v_rcp_f32_e32 v203, v203
	v_fma_f32 v202, v202, 2.0, -1.0
	v_mul_f32_e32 v217, v213, v201
	s_waitcnt lgkmcnt(6)
	v_mfma_f32_32x32x16_f16 v[0:15], a[80:83], v[160:163], v[0:15]
	ds_read_b128 v[160:163], v192 offset:49152
	v_fma_f32 v203, v203, 2.0, -1.0
	v_mul_f32_e32 v218, v214, v202
	v_exp_f32_e32 v200, v112
	v_mfma_f32_32x32x16_f16 v[16:31], a[80:83], v[164:167], v[16:31]
	ds_read_b128 v[164:167], v192 offset:50176
	v_mul_f32_e32 v219, v215, v203
	v_mul_f32_e32 v236, v216, v228
	v_exp_f32_e32 v201, v113
	s_waitcnt lgkmcnt(6)
	v_mfma_f32_32x32x16_f16 v[0:15], a[84:87], v[168:171], v[0:15]
	ds_read_b128 v[168:171], v192 offset:51200
	v_mul_f32_e32 v237, v216, v232
	v_fmac_f32_e32 v236, v217, v229
	v_exp_f32_e32 v202, v114
	v_mfma_f32_32x32x16_f16 v[16:31], a[84:87], v[172:175], v[16:31]
	ds_read_b128 v[172:175], v192 offset:52224
	global_load_lds_dwordx4 v192, s[44:45] offset:3072 sc1
	v_fmac_f32_e32 v237, v217, v233
	v_fmac_f32_e32 v236, v218, v230
	v_exp_f32_e32 v203, v115
	s_waitcnt lgkmcnt(6)
	v_mfma_f32_32x32x16_f16 v[0:15], a[88:91], v[176:179], v[0:15]
	ds_read_b128 v[176:179], v192 offset:53248
	v_fmac_f32_e32 v237, v218, v234
	v_fmac_f32_e32 v236, v219, v231
	v_exp_f32_e32 v204, v116
	v_mfma_f32_32x32x16_f16 v[16:31], a[88:91], v[180:183], v[16:31]
	ds_read_b128 v[180:183], v192 offset:54272
	v_fmac_f32_e32 v237, v219, v235
	v_mov_b32_e32 v238, v236
	v_exp_f32_e32 v205, v117
	s_waitcnt lgkmcnt(6)
	v_mfma_f32_32x32x16_f16 v[0:15], a[92:95], v[184:187], v[0:15]
	ds_read_b128 v[184:187], v192 offset:55296
	v_mov_b32_e32 v239, v236
	v_mov_b32_e32 v240, v237
	v_exp_f32_e32 v206, v118
	v_mfma_f32_32x32x16_f16 v[16:31], a[92:95], v[188:191], v[16:31]
	ds_read_b128 v[188:191], v192 offset:56320
	s_add_u32 s44, s34, 0x19000
	s_addc_u32 s45, s35, 0
	s_mov_b32 m0, s59
	s_nop 0
	global_load_lds_dwordx4 v192, s[44:45] sc1
	s_lshl_b32 s64, s71, 3
	s_add_u32 s64, s64, s29
	s_lshl_b32 s64, s64, 7
	s_add_u32 s38, s8, s64
	s_addc_u32 s39, s9, 0
	global_load_dword v251, v196, s[38:39] sc1
	v_mov_b32_e32 v241, v237
	v_cvt_pk_f16_f32 v220, v216, v217
	v_exp_f32_e32 v207, v119
	s_waitcnt lgkmcnt(6)
	v_mfma_f32_32x32x16_f16 v[0:15], a[96:99], v[160:163], v[0:15]
	ds_read_b128 v[160:163], v192 offset:57344
	s_nop 1
	v_permlane32_swap_b32_e32 v238, v239
	v_permlane32_swap_b32_e32 v240, v241
	v_add_f32_e32 v238, v238, v239
	v_add_f32_e32 v239, v240, v241
	ds_write_b64 v248, v[238:239] offset:1536
	v_exp_f32_e32 v208, v120
	v_mfma_f32_32x32x16_f16 v[16:31], a[96:99], v[164:167], v[16:31]
	ds_read_b128 v[164:167], v192 offset:58368
	v_cvt_pk_f16_f32 v221, v218, v219
	v_exp_f32_e32 v209, v121
	v_add_f32_e32 v200, 1.0, v200
	s_waitcnt lgkmcnt(7)
	v_mfma_f32_32x32x16_f16 v[0:15], a[100:103], v[168:171], v[0:15]
	ds_read_b128 v[168:171], v192 offset:59392
	v_exp_f32_e32 v210, v122
	v_add_f32_e32 v201, 1.0, v201
	v_add_f32_e32 v202, 1.0, v202
	v_mfma_f32_32x32x16_f16 v[16:31], a[100:103], v[172:175], v[16:31]
	ds_read_b128 v[172:175], v192 offset:60416
	global_load_lds_dwordx4 v192, s[44:45] offset:1024 sc1
	v_exp_f32_e32 v211, v123
	v_add_f32_e32 v203, 1.0, v203
	v_add_f32_e32 v204, 1.0, v204
	s_waitcnt lgkmcnt(7)
	v_mfma_f32_32x32x16_f16 v[0:15], a[104:107], v[176:179], v[0:15]
	ds_read_b128 v[176:179], v192 offset:61440
	v_exp_f32_e32 v212, v124
	v_add_f32_e32 v205, 1.0, v205
	v_add_f32_e32 v206, 1.0, v206
	v_mfma_f32_32x32x16_f16 v[16:31], a[104:107], v[180:183], v[16:31]
	ds_read_b128 v[180:183], v192 offset:62464
	v_exp_f32_e32 v213, v125
	v_add_f32_e32 v207, 1.0, v207
	v_add_f32_e32 v208, 1.0, v208
	s_waitcnt lgkmcnt(7)
	v_mfma_f32_32x32x16_f16 v[0:15], a[108:111], v[184:187], v[0:15]
	ds_read_b128 v[184:187], v192 offset:63488
	v_exp_f32_e32 v214, v126
	v_add_f32_e32 v209, 1.0, v209
	v_add_f32_e32 v210, 1.0, v210
	v_mfma_f32_32x32x16_f16 v[16:31], a[108:111], v[188:191], v[16:31]
	ds_read_b128 v[188:191], v192 offset:64512
	global_load_lds_dwordx4 v192, s[44:45] offset:2048 sc1
	v_exp_f32_e32 v215, v127
	v_add_f32_e32 v211, 1.0, v211
	v_add_f32_e32 v212, 1.0, v212
	s_waitcnt vmcnt(12)
	s_barrier
	s_waitcnt lgkmcnt(6)
	v_mfma_f32_32x32x16_f16 v[0:15], a[112:115], v[160:163], v[0:15]
	ds_read_b128 v[160:163], v193 offset:0
	v_add_f32_e32 v213, 1.0, v213
	v_add_f32_e32 v214, 1.0, v214
	v_rcp_f32_e32 v200, v200
	v_mfma_f32_32x32x16_f16 v[16:31], a[112:115], v[164:167], v[16:31]
	ds_read_b128 v[164:167], v193 offset:1024
	v_add_f32_e32 v215, 1.0, v215
	v_rcp_f32_e32 v201, v201
	s_waitcnt lgkmcnt(6)
	v_mfma_f32_32x32x16_f16 v[0:15], a[116:119], v[168:171], v[0:15]
	ds_read_b128 v[168:171], v193 offset:2048
	v_rcp_f32_e32 v202, v202
	v_mfma_f32_32x32x16_f16 v[16:31], a[116:119], v[172:175], v[16:31]
	ds_read_b128 v[172:175], v193 offset:3072
	global_load_lds_dwordx4 v192, s[44:45] offset:3072 sc1
	v_rcp_f32_e32 v203, v203
	s_waitcnt lgkmcnt(6)
	v_mfma_f32_32x32x16_f16 v[0:15], a[120:123], v[176:179], v[0:15]
	ds_read_b128 v[176:179], v193 offset:4096
	v_rcp_f32_e32 v204, v204
	v_mfma_f32_32x32x16_f16 v[16:31], a[120:123], v[180:183], v[16:31]
	ds_read_b128 v[180:183], v193 offset:5120
	v_rcp_f32_e32 v205, v205
	v_mul_f32_e32 v204, v204, v156
	s_waitcnt lgkmcnt(6)
	v_mfma_f32_32x32x16_f16 v[0:15], a[124:127], v[184:187], v[0:15]
	ds_read_b128 v[184:187], v193 offset:6144
	v_rcp_f32_e32 v206, v206
	v_mul_f32_e32 v205, v205, v157
	v_mfma_f32_32x32x16_f16 v[16:31], a[124:127], v[188:191], v[16:31]
	ds_read_b128 v[188:191], v193 offset:7168
	s_waitcnt vmcnt(3)
	v_cmp_gt_u32_e32 vcc, 2, v251
	s_cbranch_vccz .LD_tok20

.LD_tok20:
	s_and_b32 s64, s71, 1
	s_lshl_b32 s64, s64, 22
	s_add_u32 s64, s64, s49
	s_add_u32 s64, s64, 0x20000
	s_add_u32 s34, s6, s64
	s_addc_u32 s35, s7, 0
	s_add_u32 s44, s34, 0x0
	s_addc_u32 s45, s35, 0
	s_mov_b32 m0, s52
	s_nop 0
	global_load_lds_dwordx4 v192, s[44:45] sc1
	v_rcp_f32_e32 v207, v207
	v_mul_f32_e32 v206, v206, v158
	s_waitcnt lgkmcnt(6)
	v_mfma_f32_32x32x16_f16 v[0:15], a[128:131], v[160:163], v[0:15]
	ds_read_b128 v[160:163], v193 offset:8192
	v_rcp_f32_e32 v208, v208
	v_mul_f32_e32 v207, v207, v159
	v_mfma_f32_32x32x16_f16 v[16:31], a[128:131], v[164:167], v[16:31]
	ds_read_b128 v[164:167], v193 offset:9216
	v_rcp_f32_e32 v209, v209
	v_fmamk_f32 v208, v208, 0xc0b8aa3b, v198
	s_waitcnt lgkmcnt(6)
	v_mfma_f32_32x32x16_f16 v[0:15], a[132:135], v[168:171], v[0:15]
	ds_read_b128 v[168:171], v193 offset:10240
	v_rcp_f32_e32 v210, v210
	v_fmamk_f32 v209, v209, 0xc0b8aa3b, v198
	v_fma_f32 v156, v200, v208, v204
	v_mfma_f32_32x32x16_f16 v[16:31], a[132:135], v[172:175], v[16:31]
	ds_read_b128 v[172:175], v193 offset:11264
	global_load_lds_dwordx4 v192, s[44:45] offset:1024 sc1
	v_rcp_f32_e32 v211, v211
	v_fmamk_f32 v210, v210, 0xc0b8aa3b, v198
	v_fma_f32 v157, v201, v209, v205
	s_waitcnt lgkmcnt(6)
	v_mfma_f32_32x32x16_f16 v[0:15], a[136:139], v[176:179], v[0:15]
	ds_read_b128 v[176:179], v193 offset:12288
	v_rcp_f32_e32 v212, v212
	v_fmamk_f32 v211, v211, 0xc0b8aa3b, v198
	v_fma_f32 v158, v202, v210, v206
	v_mfma_f32_32x32x16_f16 v[16:31], a[136:139], v[180:183], v[16:31]
	ds_read_b128 v[180:183], v193 offset:13312
	v_rcp_f32_e32 v213, v213
	v_fma_f32 v159, v203, v211, v207
	s_waitcnt lgkmcnt(6)
	v_mfma_f32_32x32x16_f16 v[0:15], a[140:143], v[184:187], v[0:15]
	ds_read_b128 v[184:187], v193 offset:14336
	v_rcp_f32_e32 v214, v214
	v_mfma_f32_32x32x16_f16 v[16:31], a[140:143], v[188:191], v[16:31]
	ds_read_b128 v[188:191], v193 offset:15360
	global_load_lds_dwordx4 v192, s[44:45] offset:2048 sc1
	v_rcp_f32_e32 v215, v215
	s_waitcnt lgkmcnt(6)
	v_mfma_f32_32x32x16_f16 v[0:15], a[144:147], v[160:163], v[0:15]
	ds_read_b128 v[160:163], v193 offset:16384
	v_exp_f32_e32 v200, v156
	v_mfma_f32_32x32x16_f16 v[16:31], a[144:147], v[164:167], v[16:31]
	ds_read_b128 v[164:167], v193 offset:17408
	v_exp_f32_e32 v201, v157
	v_add_f32_e32 v200, 1.0, v200
	s_waitcnt lgkmcnt(6)
	v_mfma_f32_32x32x16_f16 v[0:15], a[148:151], v[168:171], v[0:15]
	ds_read_b128 v[168:171], v193 offset:18432
	v_exp_f32_e32 v202, v158
	v_add_f32_e32 v201, 1.0, v201
	v_mfma_f32_32x32x16_f16 v[16:31], a[148:151], v[172:175], v[16:31]
	ds_read_b128 v[172:175], v193 offset:19456
	global_load_lds_dwordx4 v192, s[44:45] offset:3072 sc1
	v_exp_f32_e32 v203, v159
	v_add_f32_e32 v202, 1.0, v202
	s_waitcnt lgkmcnt(6)
	v_mfma_f32_32x32x16_f16 v[0:15], a[152:155], v[176:179], v[0:15]
	ds_read_b128 v[176:179], v193 offset:20480
	v_add_f32_e32 v203, 1.0, v203
	v_rcp_f32_e32 v200, v200
	v_mfma_f32_32x32x16_f16 v[16:31], a[152:155], v[180:183], v[16:31]
	ds_read_b128 v[180:183], v193 offset:21504
	v_rcp_f32_e32 v201, v201
	v_fma_f32 v200, v200, 2.0, -1.0
	s_waitcnt lgkmcnt(6)
	v_mfma_f32_32x32x16_f16 v[0:15], a[156:159], v[184:187], v[0:15]
	ds_read_b128 v[184:187], v193 offset:22528
	v_rcp_f32_e32 v202, v202
	v_fma_f32 v201, v201, 2.0, -1.0
	v_mul_f32_e32 v216, v212, v200
	v_mfma_f32_32x32x16_f16 v[16:31], a[156:159], v[188:191], v[16:31]
	ds_read_b128 v[188:191], v193 offset:23552
	s_add_u32 s44, s34, 0x1000
	s_addc_u32 s45, s35, 0
	s_mov_b32 m0, s53
	s_nop 0
	global_load_lds_dwordx4 v192, s[44:45] sc1
	v_rcp_f32_e32 v203, v203
	v_fma_f32 v202, v202, 2.0, -1.0
	v_mul_f32_e32 v217, v213, v201
	s_waitcnt lgkmcnt(6)
	v_mfma_f32_32x32x16_f16 v[0:15], a[160:163], v[160:163], v[0:15]
	ds_read_b128 v[160:163], v193 offset:24576
	v_fma_f32 v203, v203, 2.0, -1.0
	v_mul_f32_e32 v218, v214, v202
	v_mfma_f32_32x32x16_f16 v[16:31], a[160:163], v[164:167], v[16:31]
	ds_read_b128 v[164:167], v193 offset:25600
	v_mul_f32_e32 v219, v215, v203
	v_mul_f32_e32 v236, v216, v228
	s_waitcnt lgkmcnt(6)
	v_mfma_f32_32x32x16_f16 v[0:15], a[164:167], v[168:171], v[0:15]
	ds_read_b128 v[168:171], v193 offset:26624
	v_mul_f32_e32 v237, v216, v232
	v_fmac_f32_e32 v236, v217, v229
	v_mfma_f32_32x32x16_f16 v[16:31], a[164:167], v[172:175], v[16:31]
	ds_read_b128 v[172:175], v193 offset:27648
	global_load_lds_dwordx4 v192, s[44:45] offset:1024 sc1
	v_fmac_f32_e32 v237, v217, v233
	v_fmac_f32_e32 v236, v218, v230
	s_waitcnt lgkmcnt(6)
	v_mfma_f32_32x32x16_f16 v[0:15], a[168:171], v[176:179], v[0:15]
	ds_read_b128 v[176:179], v193 offset:28672
	v_fmac_f32_e32 v237, v218, v234
	v_fmac_f32_e32 v236, v219, v231
	v_mfma_f32_32x32x16_f16 v[16:31], a[168:171], v[180:183], v[16:31]
	ds_read_b128 v[180:183], v193 offset:29696
	v_fmac_f32_e32 v237, v219, v235
	v_mov_b32_e32 v238, v236
	s_waitcnt lgkmcnt(6)
	v_mfma_f32_32x32x16_f16 v[0:15], a[172:175], v[184:187], v[0:15]
	ds_read_b128 v[184:187], v193 offset:30720
	v_mov_b32_e32 v239, v236
	v_mov_b32_e32 v240, v237
	v_mfma_f32_32x32x16_f16 v[16:31], a[172:175], v[188:191], v[16:31]
	ds_read_b128 v[188:191], v193 offset:31744
	global_load_lds_dwordx4 v192, s[44:45] offset:2048 sc1
	v_mov_b32_e32 v241, v237
	v_cvt_pk_f16_f32 v222, v216, v217
	s_waitcnt vmcnt(7)
	s_barrier
	s_waitcnt lgkmcnt(6)
	v_mfma_f32_32x32x16_f16 v[0:15], a[176:179], v[160:163], v[0:15]
	ds_read_b128 v[160:163], v193 offset:32768
	s_nop 1
	v_permlane32_swap_b32_e32 v238, v239
	v_permlane32_swap_b32_e32 v240, v241
	v_add_f32_e32 v238, v238, v239
	v_add_f32_e32 v239, v240, v241
	ds_write_b64 v248, v[238:239] offset:1792
	v_mfma_f32_32x32x16_f16 v[16:31], a[176:179], v[164:167], v[16:31]
	ds_read_b128 v[164:167], v193 offset:33792
	v_cvt_pk_f16_f32 v223, v218, v219
	s_waitcnt lgkmcnt(7)
	v_mfma_f32_32x32x16_f16 v[0:15], a[180:183], v[168:171], v[0:15]
	ds_read_b128 v[168:171], v193 offset:34816
	s_nop 1
	v_permlane32_swap_b32_e32 v220, v222
	v_permlane32_swap_b32_e32 v221, v223
	s_cmp_eq_u32 s31, 0
	s_cbranch_scc1 .LD_slow22
	global_store_dwordx4 v195, v[220:223], s[36:37] offset:0
	s_branch .LD_join23

.LD_join23:
	v_mfma_f32_32x32x16_f16 v[16:31], a[180:183], v[172:175], v[16:31]
	ds_read_b128 v[172:175], v193 offset:35840
	global_load_lds_dwordx4 v192, s[44:45] offset:3072 sc1
	s_waitcnt lgkmcnt(7)
	v_mfma_f32_32x32x16_f16 v[0:15], a[184:187], v[176:179], v[0:15]
	ds_read_b128 v[176:179], v193 offset:36864
	v_mfma_f32_32x32x16_f16 v[16:31], a[184:187], v[180:183], v[16:31]
	ds_read_b128 v[180:183], v193 offset:37888
	s_waitcnt lgkmcnt(7)
	v_mfma_f32_32x32x16_f16 v[0:15], a[188:191], v[184:187], v[0:15]
	ds_read_b128 v[184:187], v193 offset:38912
	v_mfma_f32_32x32x16_f16 v[16:31], a[188:191], v[188:191], v[16:31]
	ds_read_b128 v[188:191], v193 offset:39936
	s_add_u32 s44, s34, 0x8000
	s_addc_u32 s45, s35, 0
	s_mov_b32 m0, s54
	s_nop 0
	global_load_lds_dwordx4 v192, s[44:45] sc1
	s_waitcnt lgkmcnt(6)
	v_mfma_f32_32x32x16_f16 v[0:15], a[192:195], v[160:163], v[0:15]
	ds_read_b128 v[160:163], v193 offset:40960
	v_mfma_f32_32x32x16_f16 v[16:31], a[192:195], v[164:167], v[16:31]
	ds_read_b128 v[164:167], v193 offset:41984
	s_waitcnt lgkmcnt(6)
	v_mfma_f32_32x32x16_f16 v[0:15], a[196:199], v[168:171], v[0:15]
	ds_read_b128 v[168:171], v193 offset:43008
	v_mfma_f32_32x32x16_f16 v[16:31], a[196:199], v[172:175], v[16:31]
	ds_read_b128 v[172:175], v193 offset:44032
	global_load_lds_dwordx4 v192, s[44:45] offset:1024 sc1
	s_waitcnt lgkmcnt(6)
	v_mfma_f32_32x32x16_f16 v[0:15], a[200:203], v[176:179], v[0:15]
	ds_read_b128 v[176:179], v193 offset:45056
	v_mfma_f32_32x32x16_f16 v[16:31], a[200:203], v[180:183], v[16:31]
	ds_read_b128 v[180:183], v193 offset:46080
	s_waitcnt lgkmcnt(6)
	v_mfma_f32_32x32x16_f16 v[0:15], a[204:207], v[184:187], v[0:15]
	ds_read_b128 v[184:187], v193 offset:47104
	v_mfma_f32_32x32x16_f16 v[16:31], a[204:207], v[188:191], v[16:31]
	ds_read_b128 v[188:191], v193 offset:48128
	global_load_lds_dwordx4 v192, s[44:45] offset:2048 sc1
	s_waitcnt vmcnt(4)
	s_barrier
	v_mov_b32_e32 v199, 4
	s_cmp_eq_u32 s31, 0
	s_cbranch_scc1 .LD_slow24
	global_store_dword v197, v199, s[40:41]
	s_branch .LD_join25

.LD_join25:
	ds_read_b64 v[200:201], v249 offset:1536
	ds_read_b64 v[202:203], v249 offset:3584
	ds_read_b64 v[204:205], v249 offset:5632
	ds_read_b64 v[206:207], v249 offset:7680
	s_waitcnt lgkmcnt(10)
	v_mfma_f32_32x32x16_f16 v[0:15], a[208:211], v[160:163], v[0:15]
	ds_read_b128 v[160:163], v193 offset:49152
	v_mfma_f32_32x32x16_f16 v[16:31], a[208:211], v[164:167], v[16:31]
	ds_read_b128 v[164:167], v193 offset:50176
	s_waitcnt lgkmcnt(10)
	v_mfma_f32_32x32x16_f16 v[0:15], a[212:215], v[168:171], v[0:15]
	ds_read_b128 v[168:171], v193 offset:51200
	v_mfma_f32_32x32x16_f16 v[16:31], a[212:215], v[172:175], v[16:31]
	ds_read_b128 v[172:175], v193 offset:52224
	global_load_lds_dwordx4 v192, s[44:45] offset:3072 sc1
	s_waitcnt lgkmcnt(10)
	v_mfma_f32_32x32x16_f16 v[0:15], a[216:219], v[176:179], v[0:15]
	ds_read_b128 v[176:179], v193 offset:53248
	v_mfma_f32_32x32x16_f16 v[16:31], a[216:219], v[180:183], v[16:31]
	ds_read_b128 v[180:183], v193 offset:54272
	s_waitcnt lgkmcnt(10)
	v_mfma_f32_32x32x16_f16 v[0:15], a[220:223], v[184:187], v[0:15]
	ds_read_b128 v[184:187], v193 offset:55296
	v_mfma_f32_32x32x16_f16 v[16:31], a[220:223], v[188:191], v[16:31]
	ds_read_b128 v[188:191], v193 offset:56320
	s_add_u32 s44, s34, 0x9000
	s_addc_u32 s45, s35, 0
	s_mov_b32 m0, s55
	s_nop 0
	global_load_lds_dwordx4 v192, s[44:45] sc1
	s_waitcnt lgkmcnt(6)
	v_mfma_f32_32x32x16_f16 v[0:15], a[224:227], v[160:163], v[0:15]
	ds_read_b128 v[160:163], v193 offset:57344
	v_mfma_f32_32x32x16_f16 v[16:31], a[224:227], v[164:167], v[16:31]
	ds_read_b128 v[164:167], v193 offset:58368
	s_waitcnt lgkmcnt(6)
	v_mfma_f32_32x32x16_f16 v[0:15], a[228:231], v[168:171], v[0:15]
	ds_read_b128 v[168:171], v193 offset:59392
	v_mfma_f32_32x32x16_f16 v[16:31], a[228:231], v[172:175], v[16:31]
	ds_read_b128 v[172:175], v193 offset:60416
	global_load_lds_dwordx4 v192, s[44:45] offset:1024 sc1
	v_add_f32_e32 v200, v200, v202
	v_add_f32_e32 v201, v201, v203
	v_add_f32_e32 v200, v200, v204
	v_add_f32_e32 v201, v201, v205
	v_add_f32_e32 v200, v200, v206
	v_add_f32_e32 v201, v201, v207
	global_store_dwordx2 v250, v[200:201], s[72:73]
	s_waitcnt lgkmcnt(6)
	v_mfma_f32_32x32x16_f16 v[0:15], a[232:235], v[176:179], v[0:15]
	ds_read_b128 v[176:179], v193 offset:61440
	v_mfma_f32_32x32x16_f16 v[16:31], a[232:235], v[180:183], v[16:31]
	ds_read_b128 v[180:183], v193 offset:62464
	s_waitcnt lgkmcnt(6)
	v_mfma_f32_32x32x16_f16 v[0:15], a[236:239], v[184:187], v[0:15]
	ds_read_b128 v[184:187], v193 offset:63488
	v_mfma_f32_32x32x16_f16 v[16:31], a[236:239], v[188:191], v[16:31]
	ds_read_b128 v[188:191], v193 offset:64512
	global_load_lds_dwordx4 v192, s[44:45] offset:2048 sc1
	s_waitcnt vmcnt(9)
	s_barrier
	s_waitcnt lgkmcnt(6)
	v_mfma_f32_32x32x16_f16 v[0:15], a[240:243], v[160:163], v[0:15]
	ds_read_b128 v[160:163], v192 offset:0
	v_mfma_f32_32x32x16_f16 v[16:31], a[240:243], v[164:167], v[16:31]
	ds_read_b128 v[164:167], v192 offset:1024
	s_waitcnt lgkmcnt(6)
	v_mfma_f32_32x32x16_f16 v[0:15], a[244:247], v[168:171], v[0:15]
	ds_read_b128 v[168:171], v192 offset:2048
	v_mfma_f32_32x32x16_f16 v[16:31], a[244:247], v[172:175], v[16:31]
	ds_read_b128 v[172:175], v192 offset:3072
	global_load_lds_dwordx4 v192, s[44:45] offset:3072 sc1
	s_waitcnt lgkmcnt(6)
	v_mfma_f32_32x32x16_f16 v[0:15], a[248:251], v[176:179], v[0:15]
	ds_read_b128 v[176:179], v192 offset:4096
	v_mfma_f32_32x32x16_f16 v[16:31], a[248:251], v[180:183], v[16:31]
	ds_read_b128 v[180:183], v192 offset:5120
	s_waitcnt lgkmcnt(6)
	v_mfma_f32_32x32x16_f16 v[0:15], a[252:255], v[184:187], v[0:15]
	ds_read_b128 v[184:187], v192 offset:6144
	v_mfma_f32_32x32x16_f16 v[16:31], a[252:255], v[188:191], v[16:31]
	ds_read_b128 v[188:191], v192 offset:7168
	s_add_u32 s44, s34, 0x10000
	s_addc_u32 s45, s35, 0
	s_mov_b32 m0, s56
	s_nop 0
	global_load_lds_dwordx4 v192, s[44:45] sc1
	s_and_b32 s64, s33, 1
	s_lshl_b32 s64, s64, 22
	s_add_u32 s64, s64, s50
	s_add_u32 s36, s6, s64
	s_addc_u32 s37, s7, 0
	s_lshl_b32 s64, s33, 3
	s_add_u32 s64, s64, s29
	s_lshl_b32 s64, s64, 5
	s_add_u32 s64, s64, s30
	s_lshl_b32 s64, s64, 2
	s_add_u32 s40, s8, s64
	s_addc_u32 s41, s9, 0
	s_lshl_b32 s64, s33, 19
	s_add_u32 s72, s62, s64
	s_addc_u32 s73, s63, 0
	s_nop 11
	s_waitcnt lgkmcnt(6)
	v_mfma_f32_32x32x16_f16 v[32:47], a[0:3], v[160:163], v[32:47]
	ds_read_b128 v[160:163], v192 offset:8192
	v_exp_f32_e32 v200, v0
	v_mfma_f32_32x32x16_f16 v[48:63], a[0:3], v[164:167], v[48:63]
	ds_read_b128 v[164:167], v192 offset:9216
	v_exp_f32_e32 v201, v1
	v_add_f32_e32 v200, 1.0, v200
	s_waitcnt lgkmcnt(6)
	v_mfma_f32_32x32x16_f16 v[32:47], a[4:7], v[168:171], v[32:47]
	ds_read_b128 v[168:171], v192 offset:10240
	v_exp_f32_e32 v202, v2
	v_add_f32_e32 v201, 1.0, v201
	v_mfma_f32_32x32x16_f16 v[48:63], a[4:7], v[172:175], v[48:63]
	ds_read_b128 v[172:175], v192 offset:11264
	global_load_lds_dwordx4 v192, s[44:45] offset:1024 sc1
	v_exp_f32_e32 v203, v3
	v_add_f32_e32 v202, 1.0, v202
	s_waitcnt lgkmcnt(6)
	v_mfma_f32_32x32x16_f16 v[32:47], a[8:11], v[176:179], v[32:47]
	ds_read_b128 v[176:179], v192 offset:12288
	v_exp_f32_e32 v204, v4
	v_add_f32_e32 v203, 1.0, v203
	v_mfma_f32_32x32x16_f16 v[48:63], a[8:11], v[180:183], v[48:63]
	ds_read_b128 v[180:183], v192 offset:13312
	v_exp_f32_e32 v205, v5
	v_add_f32_e32 v204, 1.0, v204
	s_waitcnt lgkmcnt(6)
	v_mfma_f32_32x32x16_f16 v[32:47], a[12:15], v[184:187], v[32:47]
	ds_read_b128 v[184:187], v192 offset:14336
	v_exp_f32_e32 v206, v6
	v_add_f32_e32 v205, 1.0, v205
	v_mfma_f32_32x32x16_f16 v[48:63], a[12:15], v[188:191], v[48:63]
	ds_read_b128 v[188:191], v192 offset:15360
	global_load_lds_dwordx4 v192, s[44:45] offset:2048 sc1
	v_exp_f32_e32 v207, v7
	v_add_f32_e32 v206, 1.0, v206
	s_waitcnt lgkmcnt(6)
	v_mfma_f32_32x32x16_f16 v[32:47], a[16:19], v[160:163], v[32:47]
	ds_read_b128 v[160:163], v192 offset:16384
	v_exp_f32_e32 v208, v8
	v_add_f32_e32 v207, 1.0, v207
	v_mfma_f32_32x32x16_f16 v[48:63], a[16:19], v[164:167], v[48:63]
	ds_read_b128 v[164:167], v192 offset:17408
	v_exp_f32_e32 v209, v9
	v_add_f32_e32 v208, 1.0, v208
	s_waitcnt lgkmcnt(6)
	v_mfma_f32_32x32x16_f16 v[32:47], a[20:23], v[168:171], v[32:47]
	ds_read_b128 v[168:171], v192 offset:18432
	v_exp_f32_e32 v210, v10
	v_add_f32_e32 v209, 1.0, v209
	v_mfma_f32_32x32x16_f16 v[48:63], a[20:23], v[172:175], v[48:63]
	ds_read_b128 v[172:175], v192 offset:19456
	global_load_lds_dwordx4 v192, s[44:45] offset:3072 sc1
	v_exp_f32_e32 v211, v11
	v_add_f32_e32 v210, 1.0, v210
	s_waitcnt lgkmcnt(6)
	v_mfma_f32_32x32x16_f16 v[32:47], a[24:27], v[176:179], v[32:47]
	ds_read_b128 v[176:179], v192 offset:20480
	v_exp_f32_e32 v212, v12
	v_add_f32_e32 v211, 1.0, v211
	v_mfma_f32_32x32x16_f16 v[48:63], a[24:27], v[180:183], v[48:63]
	ds_read_b128 v[180:183], v192 offset:21504
	v_exp_f32_e32 v213, v13
	v_add_f32_e32 v212, 1.0, v212
	s_waitcnt lgkmcnt(6)
	v_mfma_f32_32x32x16_f16 v[32:47], a[28:31], v[184:187], v[32:47]
	ds_read_b128 v[184:187], v192 offset:22528
	v_exp_f32_e32 v214, v14
	v_add_f32_e32 v213, 1.0, v213
	v_mfma_f32_32x32x16_f16 v[48:63], a[28:31], v[188:191], v[48:63]
	ds_read_b128 v[188:191], v192 offset:23552
	s_add_u32 s44, s34, 0x11000
	s_addc_u32 s45, s35, 0
	s_mov_b32 m0, s57
	s_nop 0
	global_load_lds_dwordx4 v192, s[44:45] sc1
	v_exp_f32_e32 v215, v15
	v_add_f32_e32 v214, 1.0, v214
	s_waitcnt lgkmcnt(6)
	v_mfma_f32_32x32x16_f16 v[32:47], a[32:35], v[160:163], v[32:47]
	ds_read_b128 v[160:163], v192 offset:24576
	v_add_f32_e32 v215, 1.0, v215
	v_rcp_f32_e32 v200, v200
	v_mfma_f32_32x32x16_f16 v[48:63], a[32:35], v[164:167], v[48:63]
	ds_read_b128 v[164:167], v192 offset:25600
	v_rcp_f32_e32 v201, v201
	s_waitcnt lgkmcnt(6)
	v_mfma_f32_32x32x16_f16 v[32:47], a[36:39], v[168:171], v[32:47]
	ds_read_b128 v[168:171], v192 offset:26624
	v_rcp_f32_e32 v202, v202
	v_mfma_f32_32x32x16_f16 v[48:63], a[36:39], v[172:175], v[48:63]
	ds_read_b128 v[172:175], v192 offset:27648
	global_load_lds_dwordx4 v192, s[44:45] offset:1024 sc1
	v_rcp_f32_e32 v203, v203
	s_waitcnt lgkmcnt(6)
	v_mfma_f32_32x32x16_f16 v[32:47], a[40:43], v[176:179], v[32:47]
	ds_read_b128 v[176:179], v192 offset:28672
	v_rcp_f32_e32 v204, v204
	v_mfma_f32_32x32x16_f16 v[48:63], a[40:43], v[180:183], v[48:63]
	ds_read_b128 v[180:183], v192 offset:29696
	v_rcp_f32_e32 v205, v205
	v_mul_f32_e32 v204, v204, v128
	s_waitcnt lgkmcnt(6)
	v_mfma_f32_32x32x16_f16 v[32:47], a[44:47], v[184:187], v[32:47]
	ds_read_b128 v[184:187], v192 offset:30720
	v_rcp_f32_e32 v206, v206
	v_mul_f32_e32 v205, v205, v129
	v_mfma_f32_32x32x16_f16 v[48:63], a[44:47], v[188:191], v[48:63]
	ds_read_b128 v[188:191], v192 offset:31744
	global_load_lds_dwordx4 v192, s[44:45] offset:2048 sc1
	v_rcp_f32_e32 v207, v207
	v_mul_f32_e32 v206, v206, v130
	s_waitcnt vmcnt(7)
	s_barrier
	s_waitcnt lgkmcnt(6)
	v_mfma_f32_32x32x16_f16 v[32:47], a[48:51], v[160:163], v[32:47]
	ds_read_b128 v[160:163], v192 offset:32768
	v_rcp_f32_e32 v208, v208
	v_mul_f32_e32 v207, v207, v131
	s_add_u32 s46, s42, 0x6000
	s_addc_u32 s47, s43, 0
	global_load_dwordx4 v[96:99], v192, s[46:47] offset:0
	v_mfma_f32_32x32x16_f16 v[48:63], a[48:51], v[164:167], v[48:63]
	ds_read_b128 v[164:167], v192 offset:33792
	v_rcp_f32_e32 v209, v209
	v_fmamk_f32 v208, v208, 0xc0b8aa3b, v198
	global_load_dwordx4 v[100:103], v192, s[46:47] offset:1024
	global_load_dwordx4 v[104:107], v192, s[46:47] offset:2048
	s_waitcnt lgkmcnt(6)
	v_mfma_f32_32x32x16_f16 v[32:47], a[52:55], v[168:171], v[32:47]
	ds_read_b128 v[168:171], v192 offset:34816
	v_rcp_f32_e32 v210, v210
	v_fmamk_f32 v209, v209, 0xc0b8aa3b, v198
	v_fma_f32 v128, v200, v208, v204
	global_load_dwordx4 v[108:111], v192, s[46:47] offset:3072
	s_add_u32 s46, s42, 0x7000
	s_addc_u32 s47, s43, 0
	v_mfma_f32_32x32x16_f16 v[48:63], a[52:55], v[172:175], v[48:63]
	ds_read_b128 v[172:175], v192 offset:35840
	global_load_lds_dwordx4 v192, s[44:45] offset:3072 sc1
	v_rcp_f32_e32 v211, v211
	v_fmamk_f32 v210, v210, 0xc0b8aa3b, v198
	v_fma_f32 v129, v201, v209, v205
	global_load_dwordx4 v[112:115], v192, s[46:47] offset:0
	global_load_dwordx4 v[116:119], v192, s[46:47] offset:1024
	s_waitcnt lgkmcnt(6)
	v_mfma_f32_32x32x16_f16 v[32:47], a[56:59], v[176:179], v[32:47]
	ds_read_b128 v[176:179], v192 offset:36864
	v_rcp_f32_e32 v212, v212
	v_fmamk_f32 v211, v211, 0xc0b8aa3b, v198
	v_fma_f32 v130, v202, v210, v206
	global_load_dwordx4 v[120:123], v192, s[46:47] offset:2048
	global_load_dwordx4 v[124:127], v192, s[46:47] offset:3072
	v_mfma_f32_32x32x16_f16 v[48:63], a[56:59], v[180:183], v[48:63]
	ds_read_b128 v[180:183], v192 offset:37888
	v_rcp_f32_e32 v213, v213
	v_fma_f32 v131, v203, v211, v207
	s_waitcnt lgkmcnt(6)
	v_mfma_f32_32x32x16_f16 v[32:47], a[60:63], v[184:187], v[32:47]
	ds_read_b128 v[184:187], v192 offset:38912
	v_rcp_f32_e32 v214, v214
	v_mfma_f32_32x32x16_f16 v[48:63], a[60:63], v[188:191], v[48:63]
	ds_read_b128 v[188:191], v192 offset:39936
	s_add_u32 s44, s34, 0x18000
	s_addc_u32 s45, s35, 0
	s_mov_b32 m0, s58
	s_nop 0
	global_load_lds_dwordx4 v192, s[44:45] sc1
	v_rcp_f32_e32 v215, v215
	s_waitcnt lgkmcnt(6)
	v_mfma_f32_32x32x16_f16 v[32:47], a[64:67], v[160:163], v[32:47]
	ds_read_b128 v[160:163], v192 offset:40960
	v_exp_f32_e32 v200, v128
	v_mfma_f32_32x32x16_f16 v[48:63], a[64:67], v[164:167], v[48:63]
	ds_read_b128 v[164:167], v192 offset:41984
	v_exp_f32_e32 v201, v129
	v_add_f32_e32 v200, 1.0, v200
	s_waitcnt lgkmcnt(6)
	v_mfma_f32_32x32x16_f16 v[32:47], a[68:71], v[168:171], v[32:47]
	ds_read_b128 v[168:171], v192 offset:43008
	v_exp_f32_e32 v202, v130
	v_add_f32_e32 v201, 1.0, v201
	v_mfma_f32_32x32x16_f16 v[48:63], a[68:71], v[172:175], v[48:63]
	ds_read_b128 v[172:175], v192 offset:44032
	global_load_lds_dwordx4 v192, s[44:45] offset:1024 sc1
	v_exp_f32_e32 v203, v131
	v_add_f32_e32 v202, 1.0, v202
	s_waitcnt lgkmcnt(6)
	v_mfma_f32_32x32x16_f16 v[32:47], a[72:75], v[176:179], v[32:47]
	ds_read_b128 v[176:179], v192 offset:45056
	v_add_f32_e32 v203, 1.0, v203
	v_rcp_f32_e32 v200, v200
	v_mfma_f32_32x32x16_f16 v[48:63], a[72:75], v[180:183], v[48:63]
	ds_read_b128 v[180:183], v192 offset:46080
	v_rcp_f32_e32 v201, v201
	v_fma_f32 v200, v200, 2.0, -1.0
	s_waitcnt lgkmcnt(6)
	v_mfma_f32_32x32x16_f16 v[32:47], a[76:79], v[184:187], v[32:47]
	ds_read_b128 v[184:187], v192 offset:47104
	v_rcp_f32_e32 v202, v202
	v_fma_f32 v201, v201, 2.0, -1.0
	v_mul_f32_e32 v216, v212, v200
	v_mfma_f32_32x32x16_f16 v[48:63], a[76:79], v[188:191], v[48:63]
	ds_read_b128 v[188:191], v192 offset:48128
	global_load_lds_dwordx4 v192, s[44:45] offset:2048 sc1
	v_rcp_f32_e32 v203, v203
	v_fma_f32 v202, v202, 2.0, -1.0
	v_mul_f32_e32 v217, v213, v201
	s_waitcnt lgkmcnt(6)
	v_mfma_f32_32x32x16_f16 v[32:47], a[80:83], v[160:163], v[32:47]
	ds_read_b128 v[160:163], v192 offset:49152
	v_fma_f32 v203, v203, 2.0, -1.0
	v_mul_f32_e32 v218, v214, v202
	v_exp_f32_e32 v200, v16
	v_mfma_f32_32x32x16_f16 v[48:63], a[80:83], v[164:167], v[48:63]
	ds_read_b128 v[164:167], v192 offset:50176
	v_mul_f32_e32 v219, v215, v203
	v_mul_f32_e32 v236, v216, v228
	v_exp_f32_e32 v201, v17
	s_waitcnt lgkmcnt(6)
	v_mfma_f32_32x32x16_f16 v[32:47], a[84:87], v[168:171], v[32:47]
	ds_read_b128 v[168:171], v192 offset:51200
	v_mul_f32_e32 v237, v216, v232
	v_fmac_f32_e32 v236, v217, v229
	v_exp_f32_e32 v202, v18
	v_mfma_f32_32x32x16_f16 v[48:63], a[84:87], v[172:175], v[48:63]
	ds_read_b128 v[172:175], v192 offset:52224
	global_load_lds_dwordx4 v192, s[44:45] offset:3072 sc1
	v_fmac_f32_e32 v237, v217, v233
	v_fmac_f32_e32 v236, v218, v230
	v_exp_f32_e32 v203, v19
	s_waitcnt lgkmcnt(6)
	v_mfma_f32_32x32x16_f16 v[32:47], a[88:91], v[176:179], v[32:47]
	ds_read_b128 v[176:179], v192 offset:53248
	v_fmac_f32_e32 v237, v218, v234
	v_fmac_f32_e32 v236, v219, v231
	v_exp_f32_e32 v204, v20
	v_mfma_f32_32x32x16_f16 v[48:63], a[88:91], v[180:183], v[48:63]
	ds_read_b128 v[180:183], v192 offset:54272
	v_fmac_f32_e32 v237, v219, v235
	v_mov_b32_e32 v238, v236
	v_exp_f32_e32 v205, v21
	s_waitcnt lgkmcnt(6)
	v_mfma_f32_32x32x16_f16 v[32:47], a[92:95], v[184:187], v[32:47]
	ds_read_b128 v[184:187], v192 offset:55296
	v_mov_b32_e32 v239, v236
	v_mov_b32_e32 v240, v237
	v_exp_f32_e32 v206, v22
	v_mfma_f32_32x32x16_f16 v[48:63], a[92:95], v[188:191], v[48:63]
	ds_read_b128 v[188:191], v192 offset:56320
	s_add_u32 s44, s34, 0x19000
	s_addc_u32 s45, s35, 0
	s_mov_b32 m0, s59
	s_nop 0
	global_load_lds_dwordx4 v192, s[44:45] sc1
	s_lshl_b32 s64, s71, 3
	s_add_u32 s64, s64, s29
	s_lshl_b32 s64, s64, 7
	s_add_u32 s38, s8, s64
	s_addc_u32 s39, s9, 0
	global_load_dword v251, v196, s[38:39] sc1
	v_mov_b32_e32 v241, v237
	v_cvt_pk_f16_f32 v220, v216, v217
	v_exp_f32_e32 v207, v23
	s_waitcnt lgkmcnt(6)
	v_mfma_f32_32x32x16_f16 v[32:47], a[96:99], v[160:163], v[32:47]
	ds_read_b128 v[160:163], v192 offset:57344
	s_nop 1
	v_permlane32_swap_b32_e32 v238, v239
	v_permlane32_swap_b32_e32 v240, v241
	v_add_f32_e32 v238, v238, v239
	v_add_f32_e32 v239, v240, v241
	ds_write_b64 v248, v[238:239] offset:0
	v_exp_f32_e32 v208, v24
	v_mfma_f32_32x32x16_f16 v[48:63], a[96:99], v[164:167], v[48:63]
	ds_read_b128 v[164:167], v192 offset:58368
	v_cvt_pk_f16_f32 v221, v218, v219
	v_exp_f32_e32 v209, v25
	v_add_f32_e32 v200, 1.0, v200
	s_waitcnt lgkmcnt(7)
	v_mfma_f32_32x32x16_f16 v[32:47], a[100:103], v[168:171], v[32:47]
	ds_read_b128 v[168:171], v192 offset:59392
	v_exp_f32_e32 v210, v26
	v_add_f32_e32 v201, 1.0, v201
	v_add_f32_e32 v202, 1.0, v202
	v_mfma_f32_32x32x16_f16 v[48:63], a[100:103], v[172:175], v[48:63]
	ds_read_b128 v[172:175], v192 offset:60416
	global_load_lds_dwordx4 v192, s[44:45] offset:1024 sc1
	v_exp_f32_e32 v211, v27
	v_add_f32_e32 v203, 1.0, v203
	v_add_f32_e32 v204, 1.0, v204
	s_waitcnt lgkmcnt(7)
	v_mfma_f32_32x32x16_f16 v[32:47], a[104:107], v[176:179], v[32:47]
	ds_read_b128 v[176:179], v192 offset:61440
	v_exp_f32_e32 v212, v28
	v_add_f32_e32 v205, 1.0, v205
	v_add_f32_e32 v206, 1.0, v206
	v_mfma_f32_32x32x16_f16 v[48:63], a[104:107], v[180:183], v[48:63]
	ds_read_b128 v[180:183], v192 offset:62464
	v_exp_f32_e32 v213, v29
	v_add_f32_e32 v207, 1.0, v207
	v_add_f32_e32 v208, 1.0, v208
	s_waitcnt lgkmcnt(7)
	v_mfma_f32_32x32x16_f16 v[32:47], a[108:111], v[184:187], v[32:47]
	ds_read_b128 v[184:187], v192 offset:63488
	v_exp_f32_e32 v214, v30
	v_add_f32_e32 v209, 1.0, v209
	v_add_f32_e32 v210, 1.0, v210
	v_mfma_f32_32x32x16_f16 v[48:63], a[108:111], v[188:191], v[48:63]
	ds_read_b128 v[188:191], v192 offset:64512
	global_load_lds_dwordx4 v192, s[44:45] offset:2048 sc1
	v_exp_f32_e32 v215, v31
	v_add_f32_e32 v211, 1.0, v211
	v_add_f32_e32 v212, 1.0, v212
	s_waitcnt vmcnt(12)
	s_barrier
	s_waitcnt lgkmcnt(6)
	v_mfma_f32_32x32x16_f16 v[32:47], a[112:115], v[160:163], v[32:47]
	ds_read_b128 v[160:163], v193 offset:0
	v_add_f32_e32 v213, 1.0, v213
	v_add_f32_e32 v214, 1.0, v214
	v_rcp_f32_e32 v200, v200
	v_mfma_f32_32x32x16_f16 v[48:63], a[112:115], v[164:167], v[48:63]
	ds_read_b128 v[164:167], v193 offset:1024
	v_add_f32_e32 v215, 1.0, v215
	v_rcp_f32_e32 v201, v201
	s_waitcnt lgkmcnt(6)
	v_mfma_f32_32x32x16_f16 v[32:47], a[116:119], v[168:171], v[32:47]
	ds_read_b128 v[168:171], v193 offset:2048
	v_rcp_f32_e32 v202, v202
	v_mfma_f32_32x32x16_f16 v[48:63], a[116:119], v[172:175], v[48:63]
	ds_read_b128 v[172:175], v193 offset:3072
	global_load_lds_dwordx4 v192, s[44:45] offset:3072 sc1
	v_rcp_f32_e32 v203, v203
	s_waitcnt lgkmcnt(6)
	v_mfma_f32_32x32x16_f16 v[32:47], a[120:123], v[176:179], v[32:47]
	ds_read_b128 v[176:179], v193 offset:4096
	v_rcp_f32_e32 v204, v204
	v_mfma_f32_32x32x16_f16 v[48:63], a[120:123], v[180:183], v[48:63]
	ds_read_b128 v[180:183], v193 offset:5120
	v_rcp_f32_e32 v205, v205
	v_mul_f32_e32 v204, v204, v132
	s_waitcnt lgkmcnt(6)
	v_mfma_f32_32x32x16_f16 v[32:47], a[124:127], v[184:187], v[32:47]
	ds_read_b128 v[184:187], v193 offset:6144
	v_rcp_f32_e32 v206, v206
	v_mul_f32_e32 v205, v205, v133
	v_mfma_f32_32x32x16_f16 v[48:63], a[124:127], v[188:191], v[48:63]
	ds_read_b128 v[188:191], v193 offset:7168
	s_waitcnt vmcnt(3)
	v_cmp_gt_u32_e32 vcc, 3, v251
	s_cbranch_vccz .LD_tok26

.LD_tok26:
	s_and_b32 s64, s71, 1
	s_lshl_b32 s64, s64, 22
	s_add_u32 s64, s64, s49
	s_add_u32 s64, s64, 0x40000
	s_add_u32 s34, s6, s64
	s_addc_u32 s35, s7, 0
	s_add_u32 s44, s34, 0x0
	s_addc_u32 s45, s35, 0
	s_mov_b32 m0, s52
	s_nop 0
	global_load_lds_dwordx4 v192, s[44:45] sc1
	v_rcp_f32_e32 v207, v207
	v_mul_f32_e32 v206, v206, v134
	s_waitcnt lgkmcnt(6)
	v_mfma_f32_32x32x16_f16 v[32:47], a[128:131], v[160:163], v[32:47]
	ds_read_b128 v[160:163], v193 offset:8192
	v_rcp_f32_e32 v208, v208
	v_mul_f32_e32 v207, v207, v135
	v_mfma_f32_32x32x16_f16 v[48:63], a[128:131], v[164:167], v[48:63]
	ds_read_b128 v[164:167], v193 offset:9216
	v_rcp_f32_e32 v209, v209
	v_fmamk_f32 v208, v208, 0xc0b8aa3b, v198
	s_waitcnt lgkmcnt(6)
	v_mfma_f32_32x32x16_f16 v[32:47], a[132:135], v[168:171], v[32:47]
	ds_read_b128 v[168:171], v193 offset:10240
	v_rcp_f32_e32 v210, v210
	v_fmamk_f32 v209, v209, 0xc0b8aa3b, v198
	v_fma_f32 v132, v200, v208, v204
	v_mfma_f32_32x32x16_f16 v[48:63], a[132:135], v[172:175], v[48:63]
	ds_read_b128 v[172:175], v193 offset:11264
	global_load_lds_dwordx4 v192, s[44:45] offset:1024 sc1
	v_rcp_f32_e32 v211, v211
	v_fmamk_f32 v210, v210, 0xc0b8aa3b, v198
	v_fma_f32 v133, v201, v209, v205
	s_waitcnt lgkmcnt(6)
	v_mfma_f32_32x32x16_f16 v[32:47], a[136:139], v[176:179], v[32:47]
	ds_read_b128 v[176:179], v193 offset:12288
	v_rcp_f32_e32 v212, v212
	v_fmamk_f32 v211, v211, 0xc0b8aa3b, v198
	v_fma_f32 v134, v202, v210, v206
	v_mfma_f32_32x32x16_f16 v[48:63], a[136:139], v[180:183], v[48:63]
	ds_read_b128 v[180:183], v193 offset:13312
	v_rcp_f32_e32 v213, v213
	v_fma_f32 v135, v203, v211, v207
	s_waitcnt lgkmcnt(6)
	v_mfma_f32_32x32x16_f16 v[32:47], a[140:143], v[184:187], v[32:47]
	ds_read_b128 v[184:187], v193 offset:14336
	v_rcp_f32_e32 v214, v214
	v_mfma_f32_32x32x16_f16 v[48:63], a[140:143], v[188:191], v[48:63]
	ds_read_b128 v[188:191], v193 offset:15360
	global_load_lds_dwordx4 v192, s[44:45] offset:2048 sc1
	v_rcp_f32_e32 v215, v215
	s_waitcnt lgkmcnt(6)
	v_mfma_f32_32x32x16_f16 v[32:47], a[144:147], v[160:163], v[32:47]
	ds_read_b128 v[160:163], v193 offset:16384
	v_exp_f32_e32 v200, v132
	v_mfma_f32_32x32x16_f16 v[48:63], a[144:147], v[164:167], v[48:63]
	ds_read_b128 v[164:167], v193 offset:17408
	v_exp_f32_e32 v201, v133
	v_add_f32_e32 v200, 1.0, v200
	s_waitcnt lgkmcnt(6)
	v_mfma_f32_32x32x16_f16 v[32:47], a[148:151], v[168:171], v[32:47]
	ds_read_b128 v[168:171], v193 offset:18432
	v_exp_f32_e32 v202, v134
	v_add_f32_e32 v201, 1.0, v201
	v_mfma_f32_32x32x16_f16 v[48:63], a[148:151], v[172:175], v[48:63]
	ds_read_b128 v[172:175], v193 offset:19456
	global_load_lds_dwordx4 v192, s[44:45] offset:3072 sc1
	v_exp_f32_e32 v203, v135
	v_add_f32_e32 v202, 1.0, v202
	s_waitcnt lgkmcnt(6)
	v_mfma_f32_32x32x16_f16 v[32:47], a[152:155], v[176:179], v[32:47]
	ds_read_b128 v[176:179], v193 offset:20480
	v_add_f32_e32 v203, 1.0, v203
	v_rcp_f32_e32 v200, v200
	v_mfma_f32_32x32x16_f16 v[48:63], a[152:155], v[180:183], v[48:63]
	ds_read_b128 v[180:183], v193 offset:21504
	v_rcp_f32_e32 v201, v201
	v_fma_f32 v200, v200, 2.0, -1.0
	s_waitcnt lgkmcnt(6)
	v_mfma_f32_32x32x16_f16 v[32:47], a[156:159], v[184:187], v[32:47]
	ds_read_b128 v[184:187], v193 offset:22528
	v_rcp_f32_e32 v202, v202
	v_fma_f32 v201, v201, 2.0, -1.0
	v_mul_f32_e32 v216, v212, v200
	v_mfma_f32_32x32x16_f16 v[48:63], a[156:159], v[188:191], v[48:63]
	ds_read_b128 v[188:191], v193 offset:23552
	s_add_u32 s44, s34, 0x1000
	s_addc_u32 s45, s35, 0
	s_mov_b32 m0, s53
	s_nop 0
	global_load_lds_dwordx4 v192, s[44:45] sc1
	v_rcp_f32_e32 v203, v203
	v_fma_f32 v202, v202, 2.0, -1.0
	v_mul_f32_e32 v217, v213, v201
	s_waitcnt lgkmcnt(6)
	v_mfma_f32_32x32x16_f16 v[32:47], a[160:163], v[160:163], v[32:47]
	ds_read_b128 v[160:163], v193 offset:24576
	v_fma_f32 v203, v203, 2.0, -1.0
	v_mul_f32_e32 v218, v214, v202
	v_mfma_f32_32x32x16_f16 v[48:63], a[160:163], v[164:167], v[48:63]
	ds_read_b128 v[164:167], v193 offset:25600
	v_mul_f32_e32 v219, v215, v203
	v_mul_f32_e32 v236, v216, v228
	s_waitcnt lgkmcnt(6)
	v_mfma_f32_32x32x16_f16 v[32:47], a[164:167], v[168:171], v[32:47]
	ds_read_b128 v[168:171], v193 offset:26624
	v_mul_f32_e32 v237, v216, v232
	v_fmac_f32_e32 v236, v217, v229
	v_mfma_f32_32x32x16_f16 v[48:63], a[164:167], v[172:175], v[48:63]
	ds_read_b128 v[172:175], v193 offset:27648
	global_load_lds_dwordx4 v192, s[44:45] offset:1024 sc1
	v_fmac_f32_e32 v237, v217, v233
	v_fmac_f32_e32 v236, v218, v230
	s_waitcnt lgkmcnt(6)
	v_mfma_f32_32x32x16_f16 v[32:47], a[168:171], v[176:179], v[32:47]
	ds_read_b128 v[176:179], v193 offset:28672
	v_fmac_f32_e32 v237, v218, v234
	v_fmac_f32_e32 v236, v219, v231
	v_mfma_f32_32x32x16_f16 v[48:63], a[168:171], v[180:183], v[48:63]
	ds_read_b128 v[180:183], v193 offset:29696
	v_fmac_f32_e32 v237, v219, v235
	v_mov_b32_e32 v238, v236
	s_waitcnt lgkmcnt(6)
	v_mfma_f32_32x32x16_f16 v[32:47], a[172:175], v[184:187], v[32:47]
	ds_read_b128 v[184:187], v193 offset:30720
	v_mov_b32_e32 v239, v236
	v_mov_b32_e32 v240, v237
	v_mfma_f32_32x32x16_f16 v[48:63], a[172:175], v[188:191], v[48:63]
	ds_read_b128 v[188:191], v193 offset:31744
	global_load_lds_dwordx4 v192, s[44:45] offset:2048 sc1
	v_mov_b32_e32 v241, v237
	v_cvt_pk_f16_f32 v222, v216, v217
	s_waitcnt vmcnt(7)
	s_barrier
	s_waitcnt lgkmcnt(6)
	v_mfma_f32_32x32x16_f16 v[32:47], a[176:179], v[160:163], v[32:47]
	ds_read_b128 v[160:163], v193 offset:32768
	s_nop 1
	v_permlane32_swap_b32_e32 v238, v239
	v_permlane32_swap_b32_e32 v240, v241
	v_add_f32_e32 v238, v238, v239
	v_add_f32_e32 v239, v240, v241
	ds_write_b64 v248, v[238:239] offset:256
	v_mfma_f32_32x32x16_f16 v[48:63], a[176:179], v[164:167], v[48:63]
	ds_read_b128 v[164:167], v193 offset:33792
	v_cvt_pk_f16_f32 v223, v218, v219
	s_waitcnt lgkmcnt(7)
	v_mfma_f32_32x32x16_f16 v[32:47], a[180:183], v[168:171], v[32:47]
	ds_read_b128 v[168:171], v193 offset:34816
	s_nop 1
	v_permlane32_swap_b32_e32 v220, v222
	v_permlane32_swap_b32_e32 v221, v223
	s_cmp_eq_u32 s31, 0
	s_cbranch_scc1 .LD_slow28
	global_store_dwordx4 v195, v[220:223], s[36:37] offset:0
	s_branch .LD_join29

.LD_join29:
	v_mfma_f32_32x32x16_f16 v[48:63], a[180:183], v[172:175], v[48:63]
	ds_read_b128 v[172:175], v193 offset:35840
	global_load_lds_dwordx4 v192, s[44:45] offset:3072 sc1
	s_waitcnt lgkmcnt(7)
	v_mfma_f32_32x32x16_f16 v[32:47], a[184:187], v[176:179], v[32:47]
	ds_read_b128 v[176:179], v193 offset:36864
	v_mfma_f32_32x32x16_f16 v[48:63], a[184:187], v[180:183], v[48:63]
	ds_read_b128 v[180:183], v193 offset:37888
	s_waitcnt lgkmcnt(7)
	v_mfma_f32_32x32x16_f16 v[32:47], a[188:191], v[184:187], v[32:47]
	ds_read_b128 v[184:187], v193 offset:38912
	v_mfma_f32_32x32x16_f16 v[48:63], a[188:191], v[188:191], v[48:63]
	ds_read_b128 v[188:191], v193 offset:39936
	s_add_u32 s44, s34, 0x8000
	s_addc_u32 s45, s35, 0
	s_mov_b32 m0, s54
	s_nop 0
	global_load_lds_dwordx4 v192, s[44:45] sc1
	s_waitcnt lgkmcnt(6)
	v_mfma_f32_32x32x16_f16 v[32:47], a[192:195], v[160:163], v[32:47]
	ds_read_b128 v[160:163], v193 offset:40960
	v_mfma_f32_32x32x16_f16 v[48:63], a[192:195], v[164:167], v[48:63]
	ds_read_b128 v[164:167], v193 offset:41984
	s_waitcnt lgkmcnt(6)
	v_mfma_f32_32x32x16_f16 v[32:47], a[196:199], v[168:171], v[32:47]
	ds_read_b128 v[168:171], v193 offset:43008
	v_mfma_f32_32x32x16_f16 v[48:63], a[196:199], v[172:175], v[48:63]
	ds_read_b128 v[172:175], v193 offset:44032
	global_load_lds_dwordx4 v192, s[44:45] offset:1024 sc1
	s_waitcnt lgkmcnt(6)
	v_mfma_f32_32x32x16_f16 v[32:47], a[200:203], v[176:179], v[32:47]
	ds_read_b128 v[176:179], v193 offset:45056
	v_mfma_f32_32x32x16_f16 v[48:63], a[200:203], v[180:183], v[48:63]
	ds_read_b128 v[180:183], v193 offset:46080
	s_waitcnt lgkmcnt(6)
	v_mfma_f32_32x32x16_f16 v[32:47], a[204:207], v[184:187], v[32:47]
	ds_read_b128 v[184:187], v193 offset:47104
	v_mfma_f32_32x32x16_f16 v[48:63], a[204:207], v[188:191], v[48:63]
	ds_read_b128 v[188:191], v193 offset:48128
	global_load_lds_dwordx4 v192, s[44:45] offset:2048 sc1
	s_waitcnt vmcnt(4)
	s_barrier
	v_mov_b32_e32 v199, 1
	s_cmp_eq_u32 s31, 0
	s_cbranch_scc1 .LD_slow30
	global_store_dword v197, v199, s[40:41]
	s_branch .LD_join31

.LD_join31:
	ds_read_b64 v[200:201], v249 offset:0
	ds_read_b64 v[202:203], v249 offset:2048
	ds_read_b64 v[204:205], v249 offset:4096
	ds_read_b64 v[206:207], v249 offset:6144
	s_waitcnt lgkmcnt(10)
	v_mfma_f32_32x32x16_f16 v[32:47], a[208:211], v[160:163], v[32:47]
	ds_read_b128 v[160:163], v193 offset:49152
	v_mfma_f32_32x32x16_f16 v[48:63], a[208:211], v[164:167], v[48:63]
	ds_read_b128 v[164:167], v193 offset:50176
	s_waitcnt lgkmcnt(10)
	v_mfma_f32_32x32x16_f16 v[32:47], a[212:215], v[168:171], v[32:47]
	ds_read_b128 v[168:171], v193 offset:51200
	v_mfma_f32_32x32x16_f16 v[48:63], a[212:215], v[172:175], v[48:63]
	ds_read_b128 v[172:175], v193 offset:52224
	global_load_lds_dwordx4 v192, s[44:45] offset:3072 sc1
	s_waitcnt lgkmcnt(10)
	v_mfma_f32_32x32x16_f16 v[32:47], a[216:219], v[176:179], v[32:47]
	ds_read_b128 v[176:179], v193 offset:53248
	v_mfma_f32_32x32x16_f16 v[48:63], a[216:219], v[180:183], v[48:63]
	ds_read_b128 v[180:183], v193 offset:54272
	s_waitcnt lgkmcnt(10)
	v_mfma_f32_32x32x16_f16 v[32:47], a[220:223], v[184:187], v[32:47]
	ds_read_b128 v[184:187], v193 offset:55296
	v_mfma_f32_32x32x16_f16 v[48:63], a[220:223], v[188:191], v[48:63]
	ds_read_b128 v[188:191], v193 offset:56320
	s_add_u32 s44, s34, 0x9000
	s_addc_u32 s45, s35, 0
	s_mov_b32 m0, s55
	s_nop 0
	global_load_lds_dwordx4 v192, s[44:45] sc1
	s_waitcnt lgkmcnt(6)
	v_mfma_f32_32x32x16_f16 v[32:47], a[224:227], v[160:163], v[32:47]
	ds_read_b128 v[160:163], v193 offset:57344
	v_mfma_f32_32x32x16_f16 v[48:63], a[224:227], v[164:167], v[48:63]
	ds_read_b128 v[164:167], v193 offset:58368
	s_waitcnt lgkmcnt(6)
	v_mfma_f32_32x32x16_f16 v[32:47], a[228:231], v[168:171], v[32:47]
	ds_read_b128 v[168:171], v193 offset:59392
	v_mfma_f32_32x32x16_f16 v[48:63], a[228:231], v[172:175], v[48:63]
	ds_read_b128 v[172:175], v193 offset:60416
	global_load_lds_dwordx4 v192, s[44:45] offset:1024 sc1
	v_add_f32_e32 v200, v200, v202
	v_add_f32_e32 v201, v201, v203
	v_add_f32_e32 v200, v200, v204
	v_add_f32_e32 v201, v201, v205
	v_add_f32_e32 v200, v200, v206
	v_add_f32_e32 v201, v201, v207
	global_store_dwordx2 v250, v[200:201], s[72:73]
	s_waitcnt lgkmcnt(6)
	v_mfma_f32_32x32x16_f16 v[32:47], a[232:235], v[176:179], v[32:47]
	ds_read_b128 v[176:179], v193 offset:61440
	v_mfma_f32_32x32x16_f16 v[48:63], a[232:235], v[180:183], v[48:63]
	ds_read_b128 v[180:183], v193 offset:62464
	s_waitcnt lgkmcnt(6)
	v_mfma_f32_32x32x16_f16 v[32:47], a[236:239], v[184:187], v[32:47]
	ds_read_b128 v[184:187], v193 offset:63488
	v_mfma_f32_32x32x16_f16 v[48:63], a[236:239], v[188:191], v[48:63]
	ds_read_b128 v[188:191], v193 offset:64512
	global_load_lds_dwordx4 v192, s[44:45] offset:2048 sc1
	s_waitcnt vmcnt(9)
	s_barrier
	s_waitcnt lgkmcnt(6)
	v_mfma_f32_32x32x16_f16 v[32:47], a[240:243], v[160:163], v[32:47]
	ds_read_b128 v[160:163], v192 offset:0
	v_mfma_f32_32x32x16_f16 v[48:63], a[240:243], v[164:167], v[48:63]
	ds_read_b128 v[164:167], v192 offset:1024
	s_waitcnt lgkmcnt(6)
	v_mfma_f32_32x32x16_f16 v[32:47], a[244:247], v[168:171], v[32:47]
	ds_read_b128 v[168:171], v192 offset:2048
	v_mfma_f32_32x32x16_f16 v[48:63], a[244:247], v[172:175], v[48:63]
	ds_read_b128 v[172:175], v192 offset:3072
	global_load_lds_dwordx4 v192, s[44:45] offset:3072 sc1
	s_waitcnt lgkmcnt(6)
	v_mfma_f32_32x32x16_f16 v[32:47], a[248:251], v[176:179], v[32:47]
	ds_read_b128 v[176:179], v192 offset:4096
	v_mfma_f32_32x32x16_f16 v[48:63], a[248:251], v[180:183], v[48:63]
	ds_read_b128 v[180:183], v192 offset:5120
	s_waitcnt lgkmcnt(6)
	v_mfma_f32_32x32x16_f16 v[32:47], a[252:255], v[184:187], v[32:47]
	ds_read_b128 v[184:187], v192 offset:6144
	v_mfma_f32_32x32x16_f16 v[48:63], a[252:255], v[188:191], v[48:63]
	ds_read_b128 v[188:191], v192 offset:7168
	s_add_u32 s44, s34, 0x10000
	s_addc_u32 s45, s35, 0
	s_mov_b32 m0, s56
	s_nop 0
	global_load_lds_dwordx4 v192, s[44:45] sc1
	s_and_b32 s64, s33, 1
	s_lshl_b32 s64, s64, 22
	s_add_u32 s64, s64, s50
	s_add_u32 s64, s64, 0x20000
	s_add_u32 s36, s6, s64
	s_addc_u32 s37, s7, 0
	s_lshl_b32 s64, s33, 3
	s_add_u32 s64, s64, s29
	s_lshl_b32 s64, s64, 5
	s_add_u32 s64, s64, s30
	s_lshl_b32 s64, s64, 2
	s_add_u32 s40, s8, s64
	s_addc_u32 s41, s9, 0
	s_lshl_b32 s64, s33, 19
	s_add_u32 s64, s64, 0x200
	s_add_u32 s72, s62, s64
	s_addc_u32 s73, s63, 0
	s_nop 11
	s_waitcnt lgkmcnt(6)
	v_mfma_f32_32x32x16_f16 v[64:79], a[0:3], v[160:163], v[64:79]
	ds_read_b128 v[160:163], v192 offset:8192
	v_exp_f32_e32 v200, v32
	v_mfma_f32_32x32x16_f16 v[80:95], a[0:3], v[164:167], v[80:95]
	ds_read_b128 v[164:167], v192 offset:9216
	v_exp_f32_e32 v201, v33
	v_add_f32_e32 v200, 1.0, v200
	s_waitcnt lgkmcnt(6)
	v_mfma_f32_32x32x16_f16 v[64:79], a[4:7], v[168:171], v[64:79]
	ds_read_b128 v[168:171], v192 offset:10240
	v_exp_f32_e32 v202, v34
	v_add_f32_e32 v201, 1.0, v201
	v_mfma_f32_32x32x16_f16 v[80:95], a[4:7], v[172:175], v[80:95]
	ds_read_b128 v[172:175], v192 offset:11264
	global_load_lds_dwordx4 v192, s[44:45] offset:1024 sc1
	v_exp_f32_e32 v203, v35
	v_add_f32_e32 v202, 1.0, v202
	s_waitcnt lgkmcnt(6)
	v_mfma_f32_32x32x16_f16 v[64:79], a[8:11], v[176:179], v[64:79]
	ds_read_b128 v[176:179], v192 offset:12288
	v_exp_f32_e32 v204, v36
	v_add_f32_e32 v203, 1.0, v203
	v_mfma_f32_32x32x16_f16 v[80:95], a[8:11], v[180:183], v[80:95]
	ds_read_b128 v[180:183], v192 offset:13312
	v_exp_f32_e32 v205, v37
	v_add_f32_e32 v204, 1.0, v204
	s_waitcnt lgkmcnt(6)
	v_mfma_f32_32x32x16_f16 v[64:79], a[12:15], v[184:187], v[64:79]
	ds_read_b128 v[184:187], v192 offset:14336
	v_exp_f32_e32 v206, v38
	v_add_f32_e32 v205, 1.0, v205
	v_mfma_f32_32x32x16_f16 v[80:95], a[12:15], v[188:191], v[80:95]
	ds_read_b128 v[188:191], v192 offset:15360
	global_load_lds_dwordx4 v192, s[44:45] offset:2048 sc1
	v_exp_f32_e32 v207, v39
	v_add_f32_e32 v206, 1.0, v206
	s_waitcnt lgkmcnt(6)
	v_mfma_f32_32x32x16_f16 v[64:79], a[16:19], v[160:163], v[64:79]
	ds_read_b128 v[160:163], v192 offset:16384
	v_exp_f32_e32 v208, v40
	v_add_f32_e32 v207, 1.0, v207
	v_mfma_f32_32x32x16_f16 v[80:95], a[16:19], v[164:167], v[80:95]
	ds_read_b128 v[164:167], v192 offset:17408
	v_exp_f32_e32 v209, v41
	v_add_f32_e32 v208, 1.0, v208
	s_waitcnt lgkmcnt(6)
	v_mfma_f32_32x32x16_f16 v[64:79], a[20:23], v[168:171], v[64:79]
	ds_read_b128 v[168:171], v192 offset:18432
	v_exp_f32_e32 v210, v42
	v_add_f32_e32 v209, 1.0, v209
	v_mfma_f32_32x32x16_f16 v[80:95], a[20:23], v[172:175], v[80:95]
	ds_read_b128 v[172:175], v192 offset:19456
	global_load_lds_dwordx4 v192, s[44:45] offset:3072 sc1
	v_exp_f32_e32 v211, v43
	v_add_f32_e32 v210, 1.0, v210
	s_waitcnt lgkmcnt(6)
	v_mfma_f32_32x32x16_f16 v[64:79], a[24:27], v[176:179], v[64:79]
	ds_read_b128 v[176:179], v192 offset:20480
	v_exp_f32_e32 v212, v44
	v_add_f32_e32 v211, 1.0, v211
	v_mfma_f32_32x32x16_f16 v[80:95], a[24:27], v[180:183], v[80:95]
	ds_read_b128 v[180:183], v192 offset:21504
	v_exp_f32_e32 v213, v45
	v_add_f32_e32 v212, 1.0, v212
	s_waitcnt lgkmcnt(6)
	v_mfma_f32_32x32x16_f16 v[64:79], a[28:31], v[184:187], v[64:79]
	ds_read_b128 v[184:187], v192 offset:22528
	v_exp_f32_e32 v214, v46
	v_add_f32_e32 v213, 1.0, v213
	v_mfma_f32_32x32x16_f16 v[80:95], a[28:31], v[188:191], v[80:95]
	ds_read_b128 v[188:191], v192 offset:23552
	s_add_u32 s44, s34, 0x11000
	s_addc_u32 s45, s35, 0
	s_mov_b32 m0, s57
	s_nop 0
	global_load_lds_dwordx4 v192, s[44:45] sc1
	v_exp_f32_e32 v215, v47
	v_add_f32_e32 v214, 1.0, v214
	s_waitcnt lgkmcnt(6)
	v_mfma_f32_32x32x16_f16 v[64:79], a[32:35], v[160:163], v[64:79]
	ds_read_b128 v[160:163], v192 offset:24576
	v_add_f32_e32 v215, 1.0, v215
	v_rcp_f32_e32 v200, v200
	v_mfma_f32_32x32x16_f16 v[80:95], a[32:35], v[164:167], v[80:95]
	ds_read_b128 v[164:167], v192 offset:25600
	v_rcp_f32_e32 v201, v201
	s_waitcnt lgkmcnt(6)
	v_mfma_f32_32x32x16_f16 v[64:79], a[36:39], v[168:171], v[64:79]
	ds_read_b128 v[168:171], v192 offset:26624
	v_rcp_f32_e32 v202, v202
	v_mfma_f32_32x32x16_f16 v[80:95], a[36:39], v[172:175], v[80:95]
	ds_read_b128 v[172:175], v192 offset:27648
	global_load_lds_dwordx4 v192, s[44:45] offset:1024 sc1
	v_rcp_f32_e32 v203, v203
	s_waitcnt lgkmcnt(6)
	v_mfma_f32_32x32x16_f16 v[64:79], a[40:43], v[176:179], v[64:79]
	ds_read_b128 v[176:179], v192 offset:28672
	v_rcp_f32_e32 v204, v204
	v_mfma_f32_32x32x16_f16 v[80:95], a[40:43], v[180:183], v[80:95]
	ds_read_b128 v[180:183], v192 offset:29696
	v_rcp_f32_e32 v205, v205
	v_mul_f32_e32 v204, v204, v136
	s_waitcnt lgkmcnt(6)
	v_mfma_f32_32x32x16_f16 v[64:79], a[44:47], v[184:187], v[64:79]
	ds_read_b128 v[184:187], v192 offset:30720
	v_rcp_f32_e32 v206, v206
	v_mul_f32_e32 v205, v205, v137
	v_mfma_f32_32x32x16_f16 v[80:95], a[44:47], v[188:191], v[80:95]
	ds_read_b128 v[188:191], v192 offset:31744
	global_load_lds_dwordx4 v192, s[44:45] offset:2048 sc1
	v_rcp_f32_e32 v207, v207
	v_mul_f32_e32 v206, v206, v138
	s_waitcnt vmcnt(7)
	s_barrier
	s_waitcnt lgkmcnt(6)
	v_mfma_f32_32x32x16_f16 v[64:79], a[48:51], v[160:163], v[64:79]
	ds_read_b128 v[160:163], v192 offset:32768
	v_rcp_f32_e32 v208, v208
	v_mul_f32_e32 v207, v207, v139
	s_add_u32 s46, s42, 0x0
	s_addc_u32 s47, s43, 0
	global_load_dwordx4 v[0:3], v192, s[46:47] offset:0
	v_mfma_f32_32x32x16_f16 v[80:95], a[48:51], v[164:167], v[80:95]
	ds_read_b128 v[164:167], v192 offset:33792
	v_rcp_f32_e32 v209, v209
	v_fmamk_f32 v208, v208, 0xc0b8aa3b, v198
	global_load_dwordx4 v[4:7], v192, s[46:47] offset:1024
	global_load_dwordx4 v[8:11], v192, s[46:47] offset:2048
	s_waitcnt lgkmcnt(6)
	v_mfma_f32_32x32x16_f16 v[64:79], a[52:55], v[168:171], v[64:79]
	ds_read_b128 v[168:171], v192 offset:34816
	v_rcp_f32_e32 v210, v210
	v_fmamk_f32 v209, v209, 0xc0b8aa3b, v198
	v_fma_f32 v136, v200, v208, v204
	global_load_dwordx4 v[12:15], v192, s[46:47] offset:3072
	s_add_u32 s46, s42, 0x1000
	s_addc_u32 s47, s43, 0
	v_mfma_f32_32x32x16_f16 v[80:95], a[52:55], v[172:175], v[80:95]
	ds_read_b128 v[172:175], v192 offset:35840
	global_load_lds_dwordx4 v192, s[44:45] offset:3072 sc1
	v_rcp_f32_e32 v211, v211
	v_fmamk_f32 v210, v210, 0xc0b8aa3b, v198
	v_fma_f32 v137, v201, v209, v205
	global_load_dwordx4 v[16:19], v192, s[46:47] offset:0
	global_load_dwordx4 v[20:23], v192, s[46:47] offset:1024
	s_waitcnt lgkmcnt(6)
	v_mfma_f32_32x32x16_f16 v[64:79], a[56:59], v[176:179], v[64:79]
	ds_read_b128 v[176:179], v192 offset:36864
	v_rcp_f32_e32 v212, v212
	v_fmamk_f32 v211, v211, 0xc0b8aa3b, v198
	v_fma_f32 v138, v202, v210, v206
	global_load_dwordx4 v[24:27], v192, s[46:47] offset:2048
	global_load_dwordx4 v[28:31], v192, s[46:47] offset:3072
	v_mfma_f32_32x32x16_f16 v[80:95], a[56:59], v[180:183], v[80:95]
	ds_read_b128 v[180:183], v192 offset:37888
	v_rcp_f32_e32 v213, v213
	v_fma_f32 v139, v203, v211, v207
	s_waitcnt lgkmcnt(6)
	v_mfma_f32_32x32x16_f16 v[64:79], a[60:63], v[184:187], v[64:79]
	ds_read_b128 v[184:187], v192 offset:38912
	v_rcp_f32_e32 v214, v214
	v_mfma_f32_32x32x16_f16 v[80:95], a[60:63], v[188:191], v[80:95]
	ds_read_b128 v[188:191], v192 offset:39936
	s_add_u32 s44, s34, 0x18000
	s_addc_u32 s45, s35, 0
	s_mov_b32 m0, s58
	s_nop 0
	global_load_lds_dwordx4 v192, s[44:45] sc1
	v_rcp_f32_e32 v215, v215
	s_waitcnt lgkmcnt(6)
	v_mfma_f32_32x32x16_f16 v[64:79], a[64:67], v[160:163], v[64:79]
	ds_read_b128 v[160:163], v192 offset:40960
	v_exp_f32_e32 v200, v136
	v_mfma_f32_32x32x16_f16 v[80:95], a[64:67], v[164:167], v[80:95]
	ds_read_b128 v[164:167], v192 offset:41984
	v_exp_f32_e32 v201, v137
	v_add_f32_e32 v200, 1.0, v200
	s_waitcnt lgkmcnt(6)
	v_mfma_f32_32x32x16_f16 v[64:79], a[68:71], v[168:171], v[64:79]
	ds_read_b128 v[168:171], v192 offset:43008
	v_exp_f32_e32 v202, v138
	v_add_f32_e32 v201, 1.0, v201
	v_mfma_f32_32x32x16_f16 v[80:95], a[68:71], v[172:175], v[80:95]
	ds_read_b128 v[172:175], v192 offset:44032
	global_load_lds_dwordx4 v192, s[44:45] offset:1024 sc1
	v_exp_f32_e32 v203, v139
	v_add_f32_e32 v202, 1.0, v202
	s_waitcnt lgkmcnt(6)
	v_mfma_f32_32x32x16_f16 v[64:79], a[72:75], v[176:179], v[64:79]
	ds_read_b128 v[176:179], v192 offset:45056
	v_add_f32_e32 v203, 1.0, v203
	v_rcp_f32_e32 v200, v200
	v_mfma_f32_32x32x16_f16 v[80:95], a[72:75], v[180:183], v[80:95]
	ds_read_b128 v[180:183], v192 offset:46080
	v_rcp_f32_e32 v201, v201
	v_fma_f32 v200, v200, 2.0, -1.0
	s_waitcnt lgkmcnt(6)
	v_mfma_f32_32x32x16_f16 v[64:79], a[76:79], v[184:187], v[64:79]
	ds_read_b128 v[184:187], v192 offset:47104
	v_rcp_f32_e32 v202, v202
	v_fma_f32 v201, v201, 2.0, -1.0
	v_mul_f32_e32 v216, v212, v200
	v_mfma_f32_32x32x16_f16 v[80:95], a[76:79], v[188:191], v[80:95]
	ds_read_b128 v[188:191], v192 offset:48128
	global_load_lds_dwordx4 v192, s[44:45] offset:2048 sc1
	v_rcp_f32_e32 v203, v203
	v_fma_f32 v202, v202, 2.0, -1.0
	v_mul_f32_e32 v217, v213, v201
	s_waitcnt lgkmcnt(6)
	v_mfma_f32_32x32x16_f16 v[64:79], a[80:83], v[160:163], v[64:79]
	ds_read_b128 v[160:163], v192 offset:49152
	v_fma_f32 v203, v203, 2.0, -1.0
	v_mul_f32_e32 v218, v214, v202
	v_exp_f32_e32 v200, v48
	v_mfma_f32_32x32x16_f16 v[80:95], a[80:83], v[164:167], v[80:95]
	ds_read_b128 v[164:167], v192 offset:50176
	v_mul_f32_e32 v219, v215, v203
	v_mul_f32_e32 v236, v216, v228
	v_exp_f32_e32 v201, v49
	s_waitcnt lgkmcnt(6)
	v_mfma_f32_32x32x16_f16 v[64:79], a[84:87], v[168:171], v[64:79]
	ds_read_b128 v[168:171], v192 offset:51200
	v_mul_f32_e32 v237, v216, v232
	v_fmac_f32_e32 v236, v217, v229
	v_exp_f32_e32 v202, v50
	v_mfma_f32_32x32x16_f16 v[80:95], a[84:87], v[172:175], v[80:95]
	ds_read_b128 v[172:175], v192 offset:52224
	global_load_lds_dwordx4 v192, s[44:45] offset:3072 sc1
	v_fmac_f32_e32 v237, v217, v233
	v_fmac_f32_e32 v236, v218, v230
	v_exp_f32_e32 v203, v51
	s_waitcnt lgkmcnt(6)
	v_mfma_f32_32x32x16_f16 v[64:79], a[88:91], v[176:179], v[64:79]
	ds_read_b128 v[176:179], v192 offset:53248
	v_fmac_f32_e32 v237, v218, v234
	v_fmac_f32_e32 v236, v219, v231
	v_exp_f32_e32 v204, v52
	v_mfma_f32_32x32x16_f16 v[80:95], a[88:91], v[180:183], v[80:95]
	ds_read_b128 v[180:183], v192 offset:54272
	v_fmac_f32_e32 v237, v219, v235
	v_mov_b32_e32 v238, v236
	v_exp_f32_e32 v205, v53
	s_waitcnt lgkmcnt(6)
	v_mfma_f32_32x32x16_f16 v[64:79], a[92:95], v[184:187], v[64:79]
	ds_read_b128 v[184:187], v192 offset:55296
	v_mov_b32_e32 v239, v236
	v_mov_b32_e32 v240, v237
	v_exp_f32_e32 v206, v54
	v_mfma_f32_32x32x16_f16 v[80:95], a[92:95], v[188:191], v[80:95]
	ds_read_b128 v[188:191], v192 offset:56320
	s_add_u32 s44, s34, 0x19000
	s_addc_u32 s45, s35, 0
	s_mov_b32 m0, s59
	s_nop 0
	global_load_lds_dwordx4 v192, s[44:45] sc1
	s_lshl_b32 s64, s71, 3
	s_add_u32 s64, s64, s29
	s_lshl_b32 s64, s64, 7
	s_add_u32 s38, s8, s64
	s_addc_u32 s39, s9, 0
	global_load_dword v251, v196, s[38:39] sc1
	v_mov_b32_e32 v241, v237
	v_cvt_pk_f16_f32 v220, v216, v217
	v_exp_f32_e32 v207, v55
	s_waitcnt lgkmcnt(6)
	v_mfma_f32_32x32x16_f16 v[64:79], a[96:99], v[160:163], v[64:79]
	ds_read_b128 v[160:163], v192 offset:57344
	s_nop 1
	v_permlane32_swap_b32_e32 v238, v239
	v_permlane32_swap_b32_e32 v240, v241
	v_add_f32_e32 v238, v238, v239
	v_add_f32_e32 v239, v240, v241
	ds_write_b64 v248, v[238:239] offset:512
	v_exp_f32_e32 v208, v56
	v_mfma_f32_32x32x16_f16 v[80:95], a[96:99], v[164:167], v[80:95]
	ds_read_b128 v[164:167], v192 offset:58368
	v_cvt_pk_f16_f32 v221, v218, v219
	v_exp_f32_e32 v209, v57
	v_add_f32_e32 v200, 1.0, v200
	s_waitcnt lgkmcnt(7)
	v_mfma_f32_32x32x16_f16 v[64:79], a[100:103], v[168:171], v[64:79]
	ds_read_b128 v[168:171], v192 offset:59392
	v_exp_f32_e32 v210, v58
	v_add_f32_e32 v201, 1.0, v201
	v_add_f32_e32 v202, 1.0, v202
	v_mfma_f32_32x32x16_f16 v[80:95], a[100:103], v[172:175], v[80:95]
	ds_read_b128 v[172:175], v192 offset:60416
	global_load_lds_dwordx4 v192, s[44:45] offset:1024 sc1
	v_exp_f32_e32 v211, v59
	v_add_f32_e32 v203, 1.0, v203
	v_add_f32_e32 v204, 1.0, v204
	s_waitcnt lgkmcnt(7)
	v_mfma_f32_32x32x16_f16 v[64:79], a[104:107], v[176:179], v[64:79]
	ds_read_b128 v[176:179], v192 offset:61440
	v_exp_f32_e32 v212, v60
	v_add_f32_e32 v205, 1.0, v205
	v_add_f32_e32 v206, 1.0, v206
	v_mfma_f32_32x32x16_f16 v[80:95], a[104:107], v[180:183], v[80:95]
	ds_read_b128 v[180:183], v192 offset:62464
	v_exp_f32_e32 v213, v61
	v_add_f32_e32 v207, 1.0, v207
	v_add_f32_e32 v208, 1.0, v208
	s_waitcnt lgkmcnt(7)
	v_mfma_f32_32x32x16_f16 v[64:79], a[108:111], v[184:187], v[64:79]
	ds_read_b128 v[184:187], v192 offset:63488
	v_exp_f32_e32 v214, v62
	v_add_f32_e32 v209, 1.0, v209
	v_add_f32_e32 v210, 1.0, v210
	v_mfma_f32_32x32x16_f16 v[80:95], a[108:111], v[188:191], v[80:95]
	ds_read_b128 v[188:191], v192 offset:64512
	global_load_lds_dwordx4 v192, s[44:45] offset:2048 sc1
	v_exp_f32_e32 v215, v63
	v_add_f32_e32 v211, 1.0, v211
	v_add_f32_e32 v212, 1.0, v212
	s_waitcnt vmcnt(12)
	s_barrier
	s_waitcnt lgkmcnt(6)
	v_mfma_f32_32x32x16_f16 v[64:79], a[112:115], v[160:163], v[64:79]
	ds_read_b128 v[160:163], v193 offset:0
	v_add_f32_e32 v213, 1.0, v213
	v_add_f32_e32 v214, 1.0, v214
	v_rcp_f32_e32 v200, v200
	v_mfma_f32_32x32x16_f16 v[80:95], a[112:115], v[164:167], v[80:95]
	ds_read_b128 v[164:167], v193 offset:1024
	v_add_f32_e32 v215, 1.0, v215
	v_rcp_f32_e32 v201, v201
	s_waitcnt lgkmcnt(6)
	v_mfma_f32_32x32x16_f16 v[64:79], a[116:119], v[168:171], v[64:79]
	ds_read_b128 v[168:171], v193 offset:2048
	v_rcp_f32_e32 v202, v202
	v_mfma_f32_32x32x16_f16 v[80:95], a[116:119], v[172:175], v[80:95]
	ds_read_b128 v[172:175], v193 offset:3072
	global_load_lds_dwordx4 v192, s[44:45] offset:3072 sc1
	v_rcp_f32_e32 v203, v203
	s_waitcnt lgkmcnt(6)
	v_mfma_f32_32x32x16_f16 v[64:79], a[120:123], v[176:179], v[64:79]
	ds_read_b128 v[176:179], v193 offset:4096
	v_rcp_f32_e32 v204, v204
	v_mfma_f32_32x32x16_f16 v[80:95], a[120:123], v[180:183], v[80:95]
	ds_read_b128 v[180:183], v193 offset:5120
	v_rcp_f32_e32 v205, v205
	v_mul_f32_e32 v204, v204, v140
	s_waitcnt lgkmcnt(6)
	v_mfma_f32_32x32x16_f16 v[64:79], a[124:127], v[184:187], v[64:79]
	ds_read_b128 v[184:187], v193 offset:6144
	v_rcp_f32_e32 v206, v206
	v_mul_f32_e32 v205, v205, v141
	v_mfma_f32_32x32x16_f16 v[80:95], a[124:127], v[188:191], v[80:95]
	ds_read_b128 v[188:191], v193 offset:7168
	s_waitcnt vmcnt(3)
	v_cmp_gt_u32_e32 vcc, 4, v251
	s_cbranch_vccz .LD_tok32

.LD_tok32:
	s_and_b32 s64, s71, 1
	s_lshl_b32 s64, s64, 22
	s_add_u32 s64, s64, s49
	s_add_u32 s64, s64, 0x60000
	s_add_u32 s34, s6, s64
	s_addc_u32 s35, s7, 0
	s_add_u32 s44, s34, 0x0
	s_addc_u32 s45, s35, 0
	s_mov_b32 m0, s52
	s_nop 0
	global_load_lds_dwordx4 v192, s[44:45] sc1
	v_rcp_f32_e32 v207, v207
	v_mul_f32_e32 v206, v206, v142
	s_waitcnt lgkmcnt(6)
	v_mfma_f32_32x32x16_f16 v[64:79], a[128:131], v[160:163], v[64:79]
	ds_read_b128 v[160:163], v193 offset:8192
	v_rcp_f32_e32 v208, v208
	v_mul_f32_e32 v207, v207, v143
	v_mfma_f32_32x32x16_f16 v[80:95], a[128:131], v[164:167], v[80:95]
	ds_read_b128 v[164:167], v193 offset:9216
	v_rcp_f32_e32 v209, v209
	v_fmamk_f32 v208, v208, 0xc0b8aa3b, v198
	s_waitcnt lgkmcnt(6)
	v_mfma_f32_32x32x16_f16 v[64:79], a[132:135], v[168:171], v[64:79]
	ds_read_b128 v[168:171], v193 offset:10240
	v_rcp_f32_e32 v210, v210
	v_fmamk_f32 v209, v209, 0xc0b8aa3b, v198
	v_fma_f32 v140, v200, v208, v204
	v_mfma_f32_32x32x16_f16 v[80:95], a[132:135], v[172:175], v[80:95]
	ds_read_b128 v[172:175], v193 offset:11264
	global_load_lds_dwordx4 v192, s[44:45] offset:1024 sc1
	v_rcp_f32_e32 v211, v211
	v_fmamk_f32 v210, v210, 0xc0b8aa3b, v198
	v_fma_f32 v141, v201, v209, v205
	s_waitcnt lgkmcnt(6)
	v_mfma_f32_32x32x16_f16 v[64:79], a[136:139], v[176:179], v[64:79]
	ds_read_b128 v[176:179], v193 offset:12288
	v_rcp_f32_e32 v212, v212
	v_fmamk_f32 v211, v211, 0xc0b8aa3b, v198
	v_fma_f32 v142, v202, v210, v206
	v_mfma_f32_32x32x16_f16 v[80:95], a[136:139], v[180:183], v[80:95]
	ds_read_b128 v[180:183], v193 offset:13312
	v_rcp_f32_e32 v213, v213
	v_fma_f32 v143, v203, v211, v207
	s_waitcnt lgkmcnt(6)
	v_mfma_f32_32x32x16_f16 v[64:79], a[140:143], v[184:187], v[64:79]
	ds_read_b128 v[184:187], v193 offset:14336
	v_rcp_f32_e32 v214, v214
	v_mfma_f32_32x32x16_f16 v[80:95], a[140:143], v[188:191], v[80:95]
	ds_read_b128 v[188:191], v193 offset:15360
	global_load_lds_dwordx4 v192, s[44:45] offset:2048 sc1
	v_rcp_f32_e32 v215, v215
	s_waitcnt lgkmcnt(6)
	v_mfma_f32_32x32x16_f16 v[64:79], a[144:147], v[160:163], v[64:79]
	ds_read_b128 v[160:163], v193 offset:16384
	v_exp_f32_e32 v200, v140
	v_mfma_f32_32x32x16_f16 v[80:95], a[144:147], v[164:167], v[80:95]
	ds_read_b128 v[164:167], v193 offset:17408
	v_exp_f32_e32 v201, v141
	v_add_f32_e32 v200, 1.0, v200
	s_waitcnt lgkmcnt(6)
	v_mfma_f32_32x32x16_f16 v[64:79], a[148:151], v[168:171], v[64:79]
	ds_read_b128 v[168:171], v193 offset:18432
	v_exp_f32_e32 v202, v142
	v_add_f32_e32 v201, 1.0, v201
	v_mfma_f32_32x32x16_f16 v[80:95], a[148:151], v[172:175], v[80:95]
	ds_read_b128 v[172:175], v193 offset:19456
	global_load_lds_dwordx4 v192, s[44:45] offset:3072 sc1
	v_exp_f32_e32 v203, v143
	v_add_f32_e32 v202, 1.0, v202
	s_waitcnt lgkmcnt(6)
	v_mfma_f32_32x32x16_f16 v[64:79], a[152:155], v[176:179], v[64:79]
	ds_read_b128 v[176:179], v193 offset:20480
	v_add_f32_e32 v203, 1.0, v203
	v_rcp_f32_e32 v200, v200
	v_mfma_f32_32x32x16_f16 v[80:95], a[152:155], v[180:183], v[80:95]
	ds_read_b128 v[180:183], v193 offset:21504
	v_rcp_f32_e32 v201, v201
	v_fma_f32 v200, v200, 2.0, -1.0
	s_waitcnt lgkmcnt(6)
	v_mfma_f32_32x32x16_f16 v[64:79], a[156:159], v[184:187], v[64:79]
	ds_read_b128 v[184:187], v193 offset:22528
	v_rcp_f32_e32 v202, v202
	v_fma_f32 v201, v201, 2.0, -1.0
	v_mul_f32_e32 v216, v212, v200
	v_mfma_f32_32x32x16_f16 v[80:95], a[156:159], v[188:191], v[80:95]
	ds_read_b128 v[188:191], v193 offset:23552
	s_add_u32 s44, s34, 0x1000
	s_addc_u32 s45, s35, 0
	s_mov_b32 m0, s53
	s_nop 0
	global_load_lds_dwordx4 v192, s[44:45] sc1
	v_rcp_f32_e32 v203, v203
	v_fma_f32 v202, v202, 2.0, -1.0
	v_mul_f32_e32 v217, v213, v201
	s_waitcnt lgkmcnt(6)
	v_mfma_f32_32x32x16_f16 v[64:79], a[160:163], v[160:163], v[64:79]
	ds_read_b128 v[160:163], v193 offset:24576
	v_fma_f32 v203, v203, 2.0, -1.0
	v_mul_f32_e32 v218, v214, v202
	v_mfma_f32_32x32x16_f16 v[80:95], a[160:163], v[164:167], v[80:95]
	ds_read_b128 v[164:167], v193 offset:25600
	v_mul_f32_e32 v219, v215, v203
	v_mul_f32_e32 v236, v216, v228
	s_waitcnt lgkmcnt(6)
	v_mfma_f32_32x32x16_f16 v[64:79], a[164:167], v[168:171], v[64:79]
	ds_read_b128 v[168:171], v193 offset:26624
	v_mul_f32_e32 v237, v216, v232
	v_fmac_f32_e32 v236, v217, v229
	v_mfma_f32_32x32x16_f16 v[80:95], a[164:167], v[172:175], v[80:95]
	ds_read_b128 v[172:175], v193 offset:27648
	global_load_lds_dwordx4 v192, s[44:45] offset:1024 sc1
	v_fmac_f32_e32 v237, v217, v233
	v_fmac_f32_e32 v236, v218, v230
	s_waitcnt lgkmcnt(6)
	v_mfma_f32_32x32x16_f16 v[64:79], a[168:171], v[176:179], v[64:79]
	ds_read_b128 v[176:179], v193 offset:28672
	v_fmac_f32_e32 v237, v218, v234
	v_fmac_f32_e32 v236, v219, v231
	v_mfma_f32_32x32x16_f16 v[80:95], a[168:171], v[180:183], v[80:95]
	ds_read_b128 v[180:183], v193 offset:29696
	v_fmac_f32_e32 v237, v219, v235
	v_mov_b32_e32 v238, v236
	s_waitcnt lgkmcnt(6)
	v_mfma_f32_32x32x16_f16 v[64:79], a[172:175], v[184:187], v[64:79]
	ds_read_b128 v[184:187], v193 offset:30720
	v_mov_b32_e32 v239, v236
	v_mov_b32_e32 v240, v237
	v_mfma_f32_32x32x16_f16 v[80:95], a[172:175], v[188:191], v[80:95]
	ds_read_b128 v[188:191], v193 offset:31744
	global_load_lds_dwordx4 v192, s[44:45] offset:2048 sc1
	v_mov_b32_e32 v241, v237
	v_cvt_pk_f16_f32 v222, v216, v217
	s_waitcnt vmcnt(7)
	s_barrier
	s_waitcnt lgkmcnt(6)
	v_mfma_f32_32x32x16_f16 v[64:79], a[176:179], v[160:163], v[64:79]
	ds_read_b128 v[160:163], v193 offset:32768
	s_nop 1
	v_permlane32_swap_b32_e32 v238, v239
	v_permlane32_swap_b32_e32 v240, v241
	v_add_f32_e32 v238, v238, v239
	v_add_f32_e32 v239, v240, v241
	ds_write_b64 v248, v[238:239] offset:768
	v_mfma_f32_32x32x16_f16 v[80:95], a[176:179], v[164:167], v[80:95]
	ds_read_b128 v[164:167], v193 offset:33792
	v_cvt_pk_f16_f32 v223, v218, v219
	s_waitcnt lgkmcnt(7)
	v_mfma_f32_32x32x16_f16 v[64:79], a[180:183], v[168:171], v[64:79]
	ds_read_b128 v[168:171], v193 offset:34816
	s_nop 1
	v_permlane32_swap_b32_e32 v220, v222
	v_permlane32_swap_b32_e32 v221, v223
	s_cmp_eq_u32 s31, 0
	s_cbranch_scc1 .LD_slow34
	global_store_dwordx4 v195, v[220:223], s[36:37] offset:0
	s_branch .LD_join35

.LD_join35:
	v_mfma_f32_32x32x16_f16 v[80:95], a[180:183], v[172:175], v[80:95]
	ds_read_b128 v[172:175], v193 offset:35840
	global_load_lds_dwordx4 v192, s[44:45] offset:3072 sc1
	s_waitcnt lgkmcnt(7)
	v_mfma_f32_32x32x16_f16 v[64:79], a[184:187], v[176:179], v[64:79]
	ds_read_b128 v[176:179], v193 offset:36864
	v_mfma_f32_32x32x16_f16 v[80:95], a[184:187], v[180:183], v[80:95]
	ds_read_b128 v[180:183], v193 offset:37888
	s_waitcnt lgkmcnt(7)
	v_mfma_f32_32x32x16_f16 v[64:79], a[188:191], v[184:187], v[64:79]
	ds_read_b128 v[184:187], v193 offset:38912
	v_mfma_f32_32x32x16_f16 v[80:95], a[188:191], v[188:191], v[80:95]
	ds_read_b128 v[188:191], v193 offset:39936
	s_add_u32 s44, s34, 0x8000
	s_addc_u32 s45, s35, 0
	s_mov_b32 m0, s54
	s_nop 0
	global_load_lds_dwordx4 v192, s[44:45] sc1
	s_waitcnt lgkmcnt(6)
	v_mfma_f32_32x32x16_f16 v[64:79], a[192:195], v[160:163], v[64:79]
	ds_read_b128 v[160:163], v193 offset:40960
	v_mfma_f32_32x32x16_f16 v[80:95], a[192:195], v[164:167], v[80:95]
	ds_read_b128 v[164:167], v193 offset:41984
	s_waitcnt lgkmcnt(6)
	v_mfma_f32_32x32x16_f16 v[64:79], a[196:199], v[168:171], v[64:79]
	ds_read_b128 v[168:171], v193 offset:43008
	v_mfma_f32_32x32x16_f16 v[80:95], a[196:199], v[172:175], v[80:95]
	ds_read_b128 v[172:175], v193 offset:44032
	global_load_lds_dwordx4 v192, s[44:45] offset:1024 sc1
	s_waitcnt lgkmcnt(6)
	v_mfma_f32_32x32x16_f16 v[64:79], a[200:203], v[176:179], v[64:79]
	ds_read_b128 v[176:179], v193 offset:45056
	v_mfma_f32_32x32x16_f16 v[80:95], a[200:203], v[180:183], v[80:95]
	ds_read_b128 v[180:183], v193 offset:46080
	s_waitcnt lgkmcnt(6)
	v_mfma_f32_32x32x16_f16 v[64:79], a[204:207], v[184:187], v[64:79]
	ds_read_b128 v[184:187], v193 offset:47104
	v_mfma_f32_32x32x16_f16 v[80:95], a[204:207], v[188:191], v[80:95]
	ds_read_b128 v[188:191], v193 offset:48128
	global_load_lds_dwordx4 v192, s[44:45] offset:2048 sc1
	s_waitcnt vmcnt(4)
	s_barrier
	v_mov_b32_e32 v199, 2
	s_cmp_eq_u32 s31, 0
	s_cbranch_scc1 .LD_slow36
	global_store_dword v197, v199, s[40:41]
	s_branch .LD_join37

.LD_join37:
	ds_read_b64 v[200:201], v249 offset:512
	ds_read_b64 v[202:203], v249 offset:2560
	ds_read_b64 v[204:205], v249 offset:4608
	ds_read_b64 v[206:207], v249 offset:6656
	s_waitcnt lgkmcnt(10)
	v_mfma_f32_32x32x16_f16 v[64:79], a[208:211], v[160:163], v[64:79]
	ds_read_b128 v[160:163], v193 offset:49152
	v_mfma_f32_32x32x16_f16 v[80:95], a[208:211], v[164:167], v[80:95]
	ds_read_b128 v[164:167], v193 offset:50176
	s_waitcnt lgkmcnt(10)
	v_mfma_f32_32x32x16_f16 v[64:79], a[212:215], v[168:171], v[64:79]
	ds_read_b128 v[168:171], v193 offset:51200
	v_mfma_f32_32x32x16_f16 v[80:95], a[212:215], v[172:175], v[80:95]
	ds_read_b128 v[172:175], v193 offset:52224
	global_load_lds_dwordx4 v192, s[44:45] offset:3072 sc1
	s_waitcnt lgkmcnt(10)
	v_mfma_f32_32x32x16_f16 v[64:79], a[216:219], v[176:179], v[64:79]
	ds_read_b128 v[176:179], v193 offset:53248
	v_mfma_f32_32x32x16_f16 v[80:95], a[216:219], v[180:183], v[80:95]
	ds_read_b128 v[180:183], v193 offset:54272
	s_waitcnt lgkmcnt(10)
	v_mfma_f32_32x32x16_f16 v[64:79], a[220:223], v[184:187], v[64:79]
	ds_read_b128 v[184:187], v193 offset:55296
	v_mfma_f32_32x32x16_f16 v[80:95], a[220:223], v[188:191], v[80:95]
	ds_read_b128 v[188:191], v193 offset:56320
	s_add_u32 s44, s34, 0x9000
	s_addc_u32 s45, s35, 0
	s_mov_b32 m0, s55
	s_nop 0
	global_load_lds_dwordx4 v192, s[44:45] sc1
	s_waitcnt lgkmcnt(6)
	v_mfma_f32_32x32x16_f16 v[64:79], a[224:227], v[160:163], v[64:79]
	ds_read_b128 v[160:163], v193 offset:57344
	v_mfma_f32_32x32x16_f16 v[80:95], a[224:227], v[164:167], v[80:95]
	ds_read_b128 v[164:167], v193 offset:58368
	s_waitcnt lgkmcnt(6)
	v_mfma_f32_32x32x16_f16 v[64:79], a[228:231], v[168:171], v[64:79]
	ds_read_b128 v[168:171], v193 offset:59392
	v_mfma_f32_32x32x16_f16 v[80:95], a[228:231], v[172:175], v[80:95]
	ds_read_b128 v[172:175], v193 offset:60416
	global_load_lds_dwordx4 v192, s[44:45] offset:1024 sc1
	v_add_f32_e32 v200, v200, v202
	v_add_f32_e32 v201, v201, v203
	v_add_f32_e32 v200, v200, v204
	v_add_f32_e32 v201, v201, v205
	v_add_f32_e32 v200, v200, v206
	v_add_f32_e32 v201, v201, v207
	global_store_dwordx2 v250, v[200:201], s[72:73]
	s_waitcnt lgkmcnt(6)
	v_mfma_f32_32x32x16_f16 v[64:79], a[232:235], v[176:179], v[64:79]
	ds_read_b128 v[176:179], v193 offset:61440
	v_mfma_f32_32x32x16_f16 v[80:95], a[232:235], v[180:183], v[80:95]
	ds_read_b128 v[180:183], v193 offset:62464
	s_waitcnt lgkmcnt(6)
	v_mfma_f32_32x32x16_f16 v[64:79], a[236:239], v[184:187], v[64:79]
	ds_read_b128 v[184:187], v193 offset:63488
	v_mfma_f32_32x32x16_f16 v[80:95], a[236:239], v[188:191], v[80:95]
	ds_read_b128 v[188:191], v193 offset:64512
	global_load_lds_dwordx4 v192, s[44:45] offset:2048 sc1
	s_waitcnt vmcnt(9)
	s_barrier
	s_waitcnt lgkmcnt(6)
	v_mfma_f32_32x32x16_f16 v[64:79], a[240:243], v[160:163], v[64:79]
	ds_read_b128 v[160:163], v192 offset:0
	v_mfma_f32_32x32x16_f16 v[80:95], a[240:243], v[164:167], v[80:95]
	ds_read_b128 v[164:167], v192 offset:1024
	s_waitcnt lgkmcnt(6)
	v_mfma_f32_32x32x16_f16 v[64:79], a[244:247], v[168:171], v[64:79]
	ds_read_b128 v[168:171], v192 offset:2048
	v_mfma_f32_32x32x16_f16 v[80:95], a[244:247], v[172:175], v[80:95]
	ds_read_b128 v[172:175], v192 offset:3072
	global_load_lds_dwordx4 v192, s[44:45] offset:3072 sc1
	s_waitcnt lgkmcnt(6)
	v_mfma_f32_32x32x16_f16 v[64:79], a[248:251], v[176:179], v[64:79]
	ds_read_b128 v[176:179], v192 offset:4096
	v_mfma_f32_32x32x16_f16 v[80:95], a[248:251], v[180:183], v[80:95]
	ds_read_b128 v[180:183], v192 offset:5120
	s_waitcnt lgkmcnt(6)
	v_mfma_f32_32x32x16_f16 v[64:79], a[252:255], v[184:187], v[64:79]
	ds_read_b128 v[184:187], v192 offset:6144
	v_mfma_f32_32x32x16_f16 v[80:95], a[252:255], v[188:191], v[80:95]
	ds_read_b128 v[188:191], v192 offset:7168
	s_add_u32 s44, s34, 0x10000
	s_addc_u32 s45, s35, 0
	s_mov_b32 m0, s56
	s_nop 0
	global_load_lds_dwordx4 v192, s[44:45] sc1
	s_and_b32 s64, s33, 1
	s_lshl_b32 s64, s64, 22
	s_add_u32 s64, s64, s50
	s_add_u32 s64, s64, 0x40000
	s_add_u32 s36, s6, s64
	s_addc_u32 s37, s7, 0
	s_lshl_b32 s64, s33, 3
	s_add_u32 s64, s64, s29
	s_lshl_b32 s64, s64, 5
	s_add_u32 s64, s64, s30
	s_lshl_b32 s64, s64, 2
	s_add_u32 s40, s8, s64
	s_addc_u32 s41, s9, 0
	s_lshl_b32 s64, s33, 19
	s_add_u32 s64, s64, 0x400
	s_add_u32 s72, s62, s64
	s_addc_u32 s73, s63, 0
	s_nop 11
	s_waitcnt lgkmcnt(6)
	v_mfma_f32_32x32x16_f16 v[96:111], a[0:3], v[160:163], v[96:111]
	ds_read_b128 v[160:163], v192 offset:8192
	v_exp_f32_e32 v200, v64
	v_mfma_f32_32x32x16_f16 v[112:127], a[0:3], v[164:167], v[112:127]
	ds_read_b128 v[164:167], v192 offset:9216
	v_exp_f32_e32 v201, v65
	v_add_f32_e32 v200, 1.0, v200
	s_waitcnt lgkmcnt(6)
	v_mfma_f32_32x32x16_f16 v[96:111], a[4:7], v[168:171], v[96:111]
	ds_read_b128 v[168:171], v192 offset:10240
	v_exp_f32_e32 v202, v66
	v_add_f32_e32 v201, 1.0, v201
	v_mfma_f32_32x32x16_f16 v[112:127], a[4:7], v[172:175], v[112:127]
	ds_read_b128 v[172:175], v192 offset:11264
	global_load_lds_dwordx4 v192, s[44:45] offset:1024 sc1
	v_exp_f32_e32 v203, v67
	v_add_f32_e32 v202, 1.0, v202
	s_waitcnt lgkmcnt(6)
	v_mfma_f32_32x32x16_f16 v[96:111], a[8:11], v[176:179], v[96:111]
	ds_read_b128 v[176:179], v192 offset:12288
	v_exp_f32_e32 v204, v68
	v_add_f32_e32 v203, 1.0, v203
	v_mfma_f32_32x32x16_f16 v[112:127], a[8:11], v[180:183], v[112:127]
	ds_read_b128 v[180:183], v192 offset:13312
	v_exp_f32_e32 v205, v69
	v_add_f32_e32 v204, 1.0, v204
	s_waitcnt lgkmcnt(6)
	v_mfma_f32_32x32x16_f16 v[96:111], a[12:15], v[184:187], v[96:111]
	ds_read_b128 v[184:187], v192 offset:14336
	v_exp_f32_e32 v206, v70
	v_add_f32_e32 v205, 1.0, v205
	v_mfma_f32_32x32x16_f16 v[112:127], a[12:15], v[188:191], v[112:127]
	ds_read_b128 v[188:191], v192 offset:15360
	global_load_lds_dwordx4 v192, s[44:45] offset:2048 sc1
	v_exp_f32_e32 v207, v71
	v_add_f32_e32 v206, 1.0, v206
	s_waitcnt lgkmcnt(6)
	v_mfma_f32_32x32x16_f16 v[96:111], a[16:19], v[160:163], v[96:111]
	ds_read_b128 v[160:163], v192 offset:16384
	v_exp_f32_e32 v208, v72
	v_add_f32_e32 v207, 1.0, v207
	v_mfma_f32_32x32x16_f16 v[112:127], a[16:19], v[164:167], v[112:127]
	ds_read_b128 v[164:167], v192 offset:17408
	v_exp_f32_e32 v209, v73
	v_add_f32_e32 v208, 1.0, v208
	s_waitcnt lgkmcnt(6)
	v_mfma_f32_32x32x16_f16 v[96:111], a[20:23], v[168:171], v[96:111]
	ds_read_b128 v[168:171], v192 offset:18432
	v_exp_f32_e32 v210, v74
	v_add_f32_e32 v209, 1.0, v209
	v_mfma_f32_32x32x16_f16 v[112:127], a[20:23], v[172:175], v[112:127]
	ds_read_b128 v[172:175], v192 offset:19456
	global_load_lds_dwordx4 v192, s[44:45] offset:3072 sc1
	v_exp_f32_e32 v211, v75
	v_add_f32_e32 v210, 1.0, v210
	s_waitcnt lgkmcnt(6)
	v_mfma_f32_32x32x16_f16 v[96:111], a[24:27], v[176:179], v[96:111]
	ds_read_b128 v[176:179], v192 offset:20480
	v_exp_f32_e32 v212, v76
	v_add_f32_e32 v211, 1.0, v211
	v_mfma_f32_32x32x16_f16 v[112:127], a[24:27], v[180:183], v[112:127]
	ds_read_b128 v[180:183], v192 offset:21504
	v_exp_f32_e32 v213, v77
	v_add_f32_e32 v212, 1.0, v212
	s_waitcnt lgkmcnt(6)
	v_mfma_f32_32x32x16_f16 v[96:111], a[28:31], v[184:187], v[96:111]
	ds_read_b128 v[184:187], v192 offset:22528
	v_exp_f32_e32 v214, v78
	v_add_f32_e32 v213, 1.0, v213
	v_mfma_f32_32x32x16_f16 v[112:127], a[28:31], v[188:191], v[112:127]
	ds_read_b128 v[188:191], v192 offset:23552
	s_add_u32 s44, s34, 0x11000
	s_addc_u32 s45, s35, 0
	s_mov_b32 m0, s57
	s_nop 0
	global_load_lds_dwordx4 v192, s[44:45] sc1
	v_exp_f32_e32 v215, v79
	v_add_f32_e32 v214, 1.0, v214
	s_waitcnt lgkmcnt(6)
	v_mfma_f32_32x32x16_f16 v[96:111], a[32:35], v[160:163], v[96:111]
	ds_read_b128 v[160:163], v192 offset:24576
	v_add_f32_e32 v215, 1.0, v215
	v_rcp_f32_e32 v200, v200
	v_mfma_f32_32x32x16_f16 v[112:127], a[32:35], v[164:167], v[112:127]
	ds_read_b128 v[164:167], v192 offset:25600
	v_rcp_f32_e32 v201, v201
	s_waitcnt lgkmcnt(6)
	v_mfma_f32_32x32x16_f16 v[96:111], a[36:39], v[168:171], v[96:111]
	ds_read_b128 v[168:171], v192 offset:26624
	v_rcp_f32_e32 v202, v202
	v_mfma_f32_32x32x16_f16 v[112:127], a[36:39], v[172:175], v[112:127]
	ds_read_b128 v[172:175], v192 offset:27648
	global_load_lds_dwordx4 v192, s[44:45] offset:1024 sc1
	v_rcp_f32_e32 v203, v203
	s_waitcnt lgkmcnt(6)
	v_mfma_f32_32x32x16_f16 v[96:111], a[40:43], v[176:179], v[96:111]
	ds_read_b128 v[176:179], v192 offset:28672
	v_rcp_f32_e32 v204, v204
	v_mfma_f32_32x32x16_f16 v[112:127], a[40:43], v[180:183], v[112:127]
	ds_read_b128 v[180:183], v192 offset:29696
	v_rcp_f32_e32 v205, v205
	v_mul_f32_e32 v204, v204, v144
	s_waitcnt lgkmcnt(6)
	v_mfma_f32_32x32x16_f16 v[96:111], a[44:47], v[184:187], v[96:111]
	ds_read_b128 v[184:187], v192 offset:30720
	v_rcp_f32_e32 v206, v206
	v_mul_f32_e32 v205, v205, v145
	v_mfma_f32_32x32x16_f16 v[112:127], a[44:47], v[188:191], v[112:127]
	ds_read_b128 v[188:191], v192 offset:31744
	global_load_lds_dwordx4 v192, s[44:45] offset:2048 sc1
	v_rcp_f32_e32 v207, v207
	v_mul_f32_e32 v206, v206, v146
	s_waitcnt vmcnt(7)
	s_barrier
	s_waitcnt lgkmcnt(6)
	v_mfma_f32_32x32x16_f16 v[96:111], a[48:51], v[160:163], v[96:111]
	ds_read_b128 v[160:163], v192 offset:32768
	v_rcp_f32_e32 v208, v208
	v_mul_f32_e32 v207, v207, v147
	s_add_u32 s46, s42, 0x2000
	s_addc_u32 s47, s43, 0
	global_load_dwordx4 v[32:35], v192, s[46:47] offset:0
	v_mfma_f32_32x32x16_f16 v[112:127], a[48:51], v[164:167], v[112:127]
	ds_read_b128 v[164:167], v192 offset:33792
	v_rcp_f32_e32 v209, v209
	v_fmamk_f32 v208, v208, 0xc0b8aa3b, v198
	global_load_dwordx4 v[36:39], v192, s[46:47] offset:1024
	global_load_dwordx4 v[40:43], v192, s[46:47] offset:2048
	s_waitcnt lgkmcnt(6)
	v_mfma_f32_32x32x16_f16 v[96:111], a[52:55], v[168:171], v[96:111]
	ds_read_b128 v[168:171], v192 offset:34816
	v_rcp_f32_e32 v210, v210
	v_fmamk_f32 v209, v209, 0xc0b8aa3b, v198
	v_fma_f32 v144, v200, v208, v204
	global_load_dwordx4 v[44:47], v192, s[46:47] offset:3072
	s_add_u32 s46, s42, 0x3000
	s_addc_u32 s47, s43, 0
	v_mfma_f32_32x32x16_f16 v[112:127], a[52:55], v[172:175], v[112:127]
	ds_read_b128 v[172:175], v192 offset:35840
	global_load_lds_dwordx4 v192, s[44:45] offset:3072 sc1
	v_rcp_f32_e32 v211, v211
	v_fmamk_f32 v210, v210, 0xc0b8aa3b, v198
	v_fma_f32 v145, v201, v209, v205
	global_load_dwordx4 v[48:51], v192, s[46:47] offset:0
	global_load_dwordx4 v[52:55], v192, s[46:47] offset:1024
	s_waitcnt lgkmcnt(6)
	v_mfma_f32_32x32x16_f16 v[96:111], a[56:59], v[176:179], v[96:111]
	ds_read_b128 v[176:179], v192 offset:36864
	v_rcp_f32_e32 v212, v212
	v_fmamk_f32 v211, v211, 0xc0b8aa3b, v198
	v_fma_f32 v146, v202, v210, v206
	global_load_dwordx4 v[56:59], v192, s[46:47] offset:2048
	global_load_dwordx4 v[60:63], v192, s[46:47] offset:3072
	v_mfma_f32_32x32x16_f16 v[112:127], a[56:59], v[180:183], v[112:127]
	ds_read_b128 v[180:183], v192 offset:37888
	v_rcp_f32_e32 v213, v213
	v_fma_f32 v147, v203, v211, v207
	s_waitcnt lgkmcnt(6)
	v_mfma_f32_32x32x16_f16 v[96:111], a[60:63], v[184:187], v[96:111]
	ds_read_b128 v[184:187], v192 offset:38912
	v_rcp_f32_e32 v214, v214
	v_mfma_f32_32x32x16_f16 v[112:127], a[60:63], v[188:191], v[112:127]
	ds_read_b128 v[188:191], v192 offset:39936
	s_add_u32 s44, s34, 0x18000
	s_addc_u32 s45, s35, 0
	s_mov_b32 m0, s58
	s_nop 0
	global_load_lds_dwordx4 v192, s[44:45] sc1
	v_rcp_f32_e32 v215, v215
	s_waitcnt lgkmcnt(6)
	v_mfma_f32_32x32x16_f16 v[96:111], a[64:67], v[160:163], v[96:111]
	ds_read_b128 v[160:163], v192 offset:40960
	v_exp_f32_e32 v200, v144
	v_mfma_f32_32x32x16_f16 v[112:127], a[64:67], v[164:167], v[112:127]
	ds_read_b128 v[164:167], v192 offset:41984
	v_exp_f32_e32 v201, v145
	v_add_f32_e32 v200, 1.0, v200
	s_waitcnt lgkmcnt(6)
	v_mfma_f32_32x32x16_f16 v[96:111], a[68:71], v[168:171], v[96:111]
	ds_read_b128 v[168:171], v192 offset:43008
	v_exp_f32_e32 v202, v146
	v_add_f32_e32 v201, 1.0, v201
	v_mfma_f32_32x32x16_f16 v[112:127], a[68:71], v[172:175], v[112:127]
	ds_read_b128 v[172:175], v192 offset:44032
	global_load_lds_dwordx4 v192, s[44:45] offset:1024 sc1
	v_exp_f32_e32 v203, v147
	v_add_f32_e32 v202, 1.0, v202
	s_waitcnt lgkmcnt(6)
	v_mfma_f32_32x32x16_f16 v[96:111], a[72:75], v[176:179], v[96:111]
	ds_read_b128 v[176:179], v192 offset:45056
	v_add_f32_e32 v203, 1.0, v203
	v_rcp_f32_e32 v200, v200
	v_mfma_f32_32x32x16_f16 v[112:127], a[72:75], v[180:183], v[112:127]
	ds_read_b128 v[180:183], v192 offset:46080
	v_rcp_f32_e32 v201, v201
	v_fma_f32 v200, v200, 2.0, -1.0
	s_waitcnt lgkmcnt(6)
	v_mfma_f32_32x32x16_f16 v[96:111], a[76:79], v[184:187], v[96:111]
	ds_read_b128 v[184:187], v192 offset:47104
	v_rcp_f32_e32 v202, v202
	v_fma_f32 v201, v201, 2.0, -1.0
	v_mul_f32_e32 v216, v212, v200
	v_mfma_f32_32x32x16_f16 v[112:127], a[76:79], v[188:191], v[112:127]
	ds_read_b128 v[188:191], v192 offset:48128
	global_load_lds_dwordx4 v192, s[44:45] offset:2048 sc1
	v_rcp_f32_e32 v203, v203
	v_fma_f32 v202, v202, 2.0, -1.0
	v_mul_f32_e32 v217, v213, v201
	s_waitcnt lgkmcnt(6)
	v_mfma_f32_32x32x16_f16 v[96:111], a[80:83], v[160:163], v[96:111]
	ds_read_b128 v[160:163], v192 offset:49152
	v_fma_f32 v203, v203, 2.0, -1.0
	v_mul_f32_e32 v218, v214, v202
	v_exp_f32_e32 v200, v80
	v_mfma_f32_32x32x16_f16 v[112:127], a[80:83], v[164:167], v[112:127]
	ds_read_b128 v[164:167], v192 offset:50176
	v_mul_f32_e32 v219, v215, v203
	v_mul_f32_e32 v236, v216, v228
	v_exp_f32_e32 v201, v81
	s_waitcnt lgkmcnt(6)
	v_mfma_f32_32x32x16_f16 v[96:111], a[84:87], v[168:171], v[96:111]
	ds_read_b128 v[168:171], v192 offset:51200
	v_mul_f32_e32 v237, v216, v232
	v_fmac_f32_e32 v236, v217, v229
	v_exp_f32_e32 v202, v82
	v_mfma_f32_32x32x16_f16 v[112:127], a[84:87], v[172:175], v[112:127]
	ds_read_b128 v[172:175], v192 offset:52224
	global_load_lds_dwordx4 v192, s[44:45] offset:3072 sc1
	v_fmac_f32_e32 v237, v217, v233
	v_fmac_f32_e32 v236, v218, v230
	v_exp_f32_e32 v203, v83
	s_waitcnt lgkmcnt(6)
	v_mfma_f32_32x32x16_f16 v[96:111], a[88:91], v[176:179], v[96:111]
	ds_read_b128 v[176:179], v192 offset:53248
	v_fmac_f32_e32 v237, v218, v234
	v_fmac_f32_e32 v236, v219, v231
	v_exp_f32_e32 v204, v84
	v_mfma_f32_32x32x16_f16 v[112:127], a[88:91], v[180:183], v[112:127]
	ds_read_b128 v[180:183], v192 offset:54272
	v_fmac_f32_e32 v237, v219, v235
	v_mov_b32_e32 v238, v236
	v_exp_f32_e32 v205, v85
	s_waitcnt lgkmcnt(6)
	v_mfma_f32_32x32x16_f16 v[96:111], a[92:95], v[184:187], v[96:111]
	ds_read_b128 v[184:187], v192 offset:55296
	v_mov_b32_e32 v239, v236
	v_mov_b32_e32 v240, v237
	v_exp_f32_e32 v206, v86
	v_mfma_f32_32x32x16_f16 v[112:127], a[92:95], v[188:191], v[112:127]
	ds_read_b128 v[188:191], v192 offset:56320
	s_add_u32 s44, s34, 0x19000
	s_addc_u32 s45, s35, 0
	s_mov_b32 m0, s59
	s_nop 0
	global_load_lds_dwordx4 v192, s[44:45] sc1
	s_lshl_b32 s64, s33, 3
	s_add_u32 s64, s64, s29
	s_lshl_b32 s64, s64, 7
	s_add_u32 s38, s8, s64
	s_addc_u32 s39, s9, 0
	global_load_dword v251, v196, s[38:39] sc1
	v_mov_b32_e32 v241, v237
	v_cvt_pk_f16_f32 v220, v216, v217
	v_exp_f32_e32 v207, v87
	s_waitcnt lgkmcnt(6)
	v_mfma_f32_32x32x16_f16 v[96:111], a[96:99], v[160:163], v[96:111]
	ds_read_b128 v[160:163], v192 offset:57344
	s_nop 1
	v_permlane32_swap_b32_e32 v238, v239
	v_permlane32_swap_b32_e32 v240, v241
	v_add_f32_e32 v238, v238, v239
	v_add_f32_e32 v239, v240, v241
	ds_write_b64 v248, v[238:239] offset:1024
	v_exp_f32_e32 v208, v88
	v_mfma_f32_32x32x16_f16 v[112:127], a[96:99], v[164:167], v[112:127]
	ds_read_b128 v[164:167], v192 offset:58368
	v_cvt_pk_f16_f32 v221, v218, v219
	v_exp_f32_e32 v209, v89
	v_add_f32_e32 v200, 1.0, v200
	s_waitcnt lgkmcnt(7)
	v_mfma_f32_32x32x16_f16 v[96:111], a[100:103], v[168:171], v[96:111]
	ds_read_b128 v[168:171], v192 offset:59392
	v_exp_f32_e32 v210, v90
	v_add_f32_e32 v201, 1.0, v201
	v_add_f32_e32 v202, 1.0, v202
	v_mfma_f32_32x32x16_f16 v[112:127], a[100:103], v[172:175], v[112:127]
	ds_read_b128 v[172:175], v192 offset:60416
	global_load_lds_dwordx4 v192, s[44:45] offset:1024 sc1
	v_exp_f32_e32 v211, v91
	v_add_f32_e32 v203, 1.0, v203
	v_add_f32_e32 v204, 1.0, v204
	s_waitcnt lgkmcnt(7)
	v_mfma_f32_32x32x16_f16 v[96:111], a[104:107], v[176:179], v[96:111]
	ds_read_b128 v[176:179], v192 offset:61440
	v_exp_f32_e32 v212, v92
	v_add_f32_e32 v205, 1.0, v205
	v_add_f32_e32 v206, 1.0, v206
	v_mfma_f32_32x32x16_f16 v[112:127], a[104:107], v[180:183], v[112:127]
	ds_read_b128 v[180:183], v192 offset:62464
	v_exp_f32_e32 v213, v93
	v_add_f32_e32 v207, 1.0, v207
	v_add_f32_e32 v208, 1.0, v208
	s_waitcnt lgkmcnt(7)
	v_mfma_f32_32x32x16_f16 v[96:111], a[108:111], v[184:187], v[96:111]
	ds_read_b128 v[184:187], v192 offset:63488
	v_exp_f32_e32 v214, v94
	v_add_f32_e32 v209, 1.0, v209
	v_add_f32_e32 v210, 1.0, v210
	v_mfma_f32_32x32x16_f16 v[112:127], a[108:111], v[188:191], v[112:127]
	ds_read_b128 v[188:191], v192 offset:64512
	global_load_lds_dwordx4 v192, s[44:45] offset:2048 sc1
	v_exp_f32_e32 v215, v95
	v_add_f32_e32 v211, 1.0, v211
	v_add_f32_e32 v212, 1.0, v212
	s_waitcnt vmcnt(12)
	s_barrier
	s_waitcnt lgkmcnt(6)
	v_mfma_f32_32x32x16_f16 v[96:111], a[112:115], v[160:163], v[96:111]
	ds_read_b128 v[160:163], v193 offset:0
	v_add_f32_e32 v213, 1.0, v213
	v_add_f32_e32 v214, 1.0, v214
	v_rcp_f32_e32 v200, v200
	v_mfma_f32_32x32x16_f16 v[112:127], a[112:115], v[164:167], v[112:127]
	ds_read_b128 v[164:167], v193 offset:1024
	v_add_f32_e32 v215, 1.0, v215
	v_rcp_f32_e32 v201, v201
	s_waitcnt lgkmcnt(6)
	v_mfma_f32_32x32x16_f16 v[96:111], a[116:119], v[168:171], v[96:111]
	ds_read_b128 v[168:171], v193 offset:2048
	v_rcp_f32_e32 v202, v202
	v_mfma_f32_32x32x16_f16 v[112:127], a[116:119], v[172:175], v[112:127]
	ds_read_b128 v[172:175], v193 offset:3072
	global_load_lds_dwordx4 v192, s[44:45] offset:3072 sc1
	v_rcp_f32_e32 v203, v203
	s_waitcnt lgkmcnt(6)
	v_mfma_f32_32x32x16_f16 v[96:111], a[120:123], v[176:179], v[96:111]
	ds_read_b128 v[176:179], v193 offset:4096
	v_rcp_f32_e32 v204, v204
	v_mfma_f32_32x32x16_f16 v[112:127], a[120:123], v[180:183], v[112:127]
	ds_read_b128 v[180:183], v193 offset:5120
	v_rcp_f32_e32 v205, v205
	v_mul_f32_e32 v204, v204, v148
	s_waitcnt lgkmcnt(6)
	v_mfma_f32_32x32x16_f16 v[96:111], a[124:127], v[184:187], v[96:111]
	ds_read_b128 v[184:187], v193 offset:6144
	v_rcp_f32_e32 v206, v206
	v_mul_f32_e32 v205, v205, v149
	v_mfma_f32_32x32x16_f16 v[112:127], a[124:127], v[188:191], v[112:127]
	ds_read_b128 v[188:191], v193 offset:7168
	s_waitcnt vmcnt(3)
	v_cmp_gt_u32_e32 vcc, 1, v251
	s_cbranch_vccz .LD_tok38

.LD_tok38:
	s_and_b32 s64, s33, 1
	s_lshl_b32 s64, s64, 22
	s_add_u32 s64, s64, s49
	s_add_u32 s34, s6, s64
	s_addc_u32 s35, s7, 0
	s_add_u32 s44, s34, 0x0
	s_addc_u32 s45, s35, 0
	s_mov_b32 m0, s52
	s_nop 0
	global_load_lds_dwordx4 v192, s[44:45] sc1
	v_rcp_f32_e32 v207, v207
	v_mul_f32_e32 v206, v206, v150
	s_waitcnt lgkmcnt(6)
	v_mfma_f32_32x32x16_f16 v[96:111], a[128:131], v[160:163], v[96:111]
	ds_read_b128 v[160:163], v193 offset:8192
	v_rcp_f32_e32 v208, v208
	v_mul_f32_e32 v207, v207, v151
	v_mfma_f32_32x32x16_f16 v[112:127], a[128:131], v[164:167], v[112:127]
	ds_read_b128 v[164:167], v193 offset:9216
	v_rcp_f32_e32 v209, v209
	v_fmamk_f32 v208, v208, 0xc0b8aa3b, v198
	s_waitcnt lgkmcnt(6)
	v_mfma_f32_32x32x16_f16 v[96:111], a[132:135], v[168:171], v[96:111]
	ds_read_b128 v[168:171], v193 offset:10240
	v_rcp_f32_e32 v210, v210
	v_fmamk_f32 v209, v209, 0xc0b8aa3b, v198
	v_fma_f32 v148, v200, v208, v204
	v_mfma_f32_32x32x16_f16 v[112:127], a[132:135], v[172:175], v[112:127]
	ds_read_b128 v[172:175], v193 offset:11264
	global_load_lds_dwordx4 v192, s[44:45] offset:1024 sc1
	v_rcp_f32_e32 v211, v211
	v_fmamk_f32 v210, v210, 0xc0b8aa3b, v198
	v_fma_f32 v149, v201, v209, v205
	s_waitcnt lgkmcnt(6)
	v_mfma_f32_32x32x16_f16 v[96:111], a[136:139], v[176:179], v[96:111]
	ds_read_b128 v[176:179], v193 offset:12288
	v_rcp_f32_e32 v212, v212
	v_fmamk_f32 v211, v211, 0xc0b8aa3b, v198
	v_fma_f32 v150, v202, v210, v206
	v_mfma_f32_32x32x16_f16 v[112:127], a[136:139], v[180:183], v[112:127]
	ds_read_b128 v[180:183], v193 offset:13312
	v_rcp_f32_e32 v213, v213
	v_fma_f32 v151, v203, v211, v207
	s_waitcnt lgkmcnt(6)
	v_mfma_f32_32x32x16_f16 v[96:111], a[140:143], v[184:187], v[96:111]
	ds_read_b128 v[184:187], v193 offset:14336
	v_rcp_f32_e32 v214, v214
	v_mfma_f32_32x32x16_f16 v[112:127], a[140:143], v[188:191], v[112:127]
	ds_read_b128 v[188:191], v193 offset:15360
	global_load_lds_dwordx4 v192, s[44:45] offset:2048 sc1
	v_rcp_f32_e32 v215, v215
	s_waitcnt lgkmcnt(6)
	v_mfma_f32_32x32x16_f16 v[96:111], a[144:147], v[160:163], v[96:111]
	ds_read_b128 v[160:163], v193 offset:16384
	v_exp_f32_e32 v200, v148
	v_mfma_f32_32x32x16_f16 v[112:127], a[144:147], v[164:167], v[112:127]
	ds_read_b128 v[164:167], v193 offset:17408
	v_exp_f32_e32 v201, v149
	v_add_f32_e32 v200, 1.0, v200
	s_waitcnt lgkmcnt(6)
	v_mfma_f32_32x32x16_f16 v[96:111], a[148:151], v[168:171], v[96:111]
	ds_read_b128 v[168:171], v193 offset:18432
	v_exp_f32_e32 v202, v150
	v_add_f32_e32 v201, 1.0, v201
	v_mfma_f32_32x32x16_f16 v[112:127], a[148:151], v[172:175], v[112:127]
	ds_read_b128 v[172:175], v193 offset:19456
	global_load_lds_dwordx4 v192, s[44:45] offset:3072 sc1
	v_exp_f32_e32 v203, v151
	v_add_f32_e32 v202, 1.0, v202
	s_waitcnt lgkmcnt(6)
	v_mfma_f32_32x32x16_f16 v[96:111], a[152:155], v[176:179], v[96:111]
	ds_read_b128 v[176:179], v193 offset:20480
	v_add_f32_e32 v203, 1.0, v203
	v_rcp_f32_e32 v200, v200
	v_mfma_f32_32x32x16_f16 v[112:127], a[152:155], v[180:183], v[112:127]
	ds_read_b128 v[180:183], v193 offset:21504
	v_rcp_f32_e32 v201, v201
	v_fma_f32 v200, v200, 2.0, -1.0
	s_waitcnt lgkmcnt(6)
	v_mfma_f32_32x32x16_f16 v[96:111], a[156:159], v[184:187], v[96:111]
	ds_read_b128 v[184:187], v193 offset:22528
	v_rcp_f32_e32 v202, v202
	v_fma_f32 v201, v201, 2.0, -1.0
	v_mul_f32_e32 v216, v212, v200
	v_mfma_f32_32x32x16_f16 v[112:127], a[156:159], v[188:191], v[112:127]
	ds_read_b128 v[188:191], v193 offset:23552
	s_add_u32 s44, s34, 0x1000
	s_addc_u32 s45, s35, 0
	s_mov_b32 m0, s53
	s_nop 0
	global_load_lds_dwordx4 v192, s[44:45] sc1
	v_rcp_f32_e32 v203, v203
	v_fma_f32 v202, v202, 2.0, -1.0
	v_mul_f32_e32 v217, v213, v201
	s_waitcnt lgkmcnt(6)
	v_mfma_f32_32x32x16_f16 v[96:111], a[160:163], v[160:163], v[96:111]
	ds_read_b128 v[160:163], v193 offset:24576
	v_fma_f32 v203, v203, 2.0, -1.0
	v_mul_f32_e32 v218, v214, v202
	v_mfma_f32_32x32x16_f16 v[112:127], a[160:163], v[164:167], v[112:127]
	ds_read_b128 v[164:167], v193 offset:25600
	v_mul_f32_e32 v219, v215, v203
	v_mul_f32_e32 v236, v216, v228
	s_waitcnt lgkmcnt(6)
	v_mfma_f32_32x32x16_f16 v[96:111], a[164:167], v[168:171], v[96:111]
	ds_read_b128 v[168:171], v193 offset:26624
	v_mul_f32_e32 v237, v216, v232
	v_fmac_f32_e32 v236, v217, v229
	v_mfma_f32_32x32x16_f16 v[112:127], a[164:167], v[172:175], v[112:127]
	ds_read_b128 v[172:175], v193 offset:27648
	global_load_lds_dwordx4 v192, s[44:45] offset:1024 sc1
	v_fmac_f32_e32 v237, v217, v233
	v_fmac_f32_e32 v236, v218, v230
	s_waitcnt lgkmcnt(6)
	v_mfma_f32_32x32x16_f16 v[96:111], a[168:171], v[176:179], v[96:111]
	ds_read_b128 v[176:179], v193 offset:28672
	v_fmac_f32_e32 v237, v218, v234
	v_fmac_f32_e32 v236, v219, v231
	v_mfma_f32_32x32x16_f16 v[112:127], a[168:171], v[180:183], v[112:127]
	ds_read_b128 v[180:183], v193 offset:29696
	v_fmac_f32_e32 v237, v219, v235
	v_mov_b32_e32 v238, v236
	s_waitcnt lgkmcnt(6)
	v_mfma_f32_32x32x16_f16 v[96:111], a[172:175], v[184:187], v[96:111]
	ds_read_b128 v[184:187], v193 offset:30720
	v_mov_b32_e32 v239, v236
	v_mov_b32_e32 v240, v237
	v_mfma_f32_32x32x16_f16 v[112:127], a[172:175], v[188:191], v[112:127]
	ds_read_b128 v[188:191], v193 offset:31744
	global_load_lds_dwordx4 v192, s[44:45] offset:2048 sc1
	v_mov_b32_e32 v241, v237
	v_cvt_pk_f16_f32 v222, v216, v217
	s_waitcnt vmcnt(7)
	s_barrier
	s_waitcnt lgkmcnt(6)
	v_mfma_f32_32x32x16_f16 v[96:111], a[176:179], v[160:163], v[96:111]
	ds_read_b128 v[160:163], v193 offset:32768
	s_nop 1
	v_permlane32_swap_b32_e32 v238, v239
	v_permlane32_swap_b32_e32 v240, v241
	v_add_f32_e32 v238, v238, v239
	v_add_f32_e32 v239, v240, v241
	ds_write_b64 v248, v[238:239] offset:1280
	v_mfma_f32_32x32x16_f16 v[112:127], a[176:179], v[164:167], v[112:127]
	ds_read_b128 v[164:167], v193 offset:33792
	v_cvt_pk_f16_f32 v223, v218, v219
	s_waitcnt lgkmcnt(7)
	v_mfma_f32_32x32x16_f16 v[96:111], a[180:183], v[168:171], v[96:111]
	ds_read_b128 v[168:171], v193 offset:34816
	s_nop 1
	v_permlane32_swap_b32_e32 v220, v222
	v_permlane32_swap_b32_e32 v221, v223
	s_cmp_eq_u32 s31, 0
	s_cbranch_scc1 .LD_slow40
	global_store_dwordx4 v195, v[220:223], s[36:37] offset:0
	s_branch .LD_join41

.LD_join41:
	v_mfma_f32_32x32x16_f16 v[112:127], a[180:183], v[172:175], v[112:127]
	ds_read_b128 v[172:175], v193 offset:35840
	global_load_lds_dwordx4 v192, s[44:45] offset:3072 sc1
	s_waitcnt lgkmcnt(7)
	v_mfma_f32_32x32x16_f16 v[96:111], a[184:187], v[176:179], v[96:111]
	ds_read_b128 v[176:179], v193 offset:36864
	v_mfma_f32_32x32x16_f16 v[112:127], a[184:187], v[180:183], v[112:127]
	ds_read_b128 v[180:183], v193 offset:37888
	s_waitcnt lgkmcnt(7)
	v_mfma_f32_32x32x16_f16 v[96:111], a[188:191], v[184:187], v[96:111]
	ds_read_b128 v[184:187], v193 offset:38912
	v_mfma_f32_32x32x16_f16 v[112:127], a[188:191], v[188:191], v[112:127]
	ds_read_b128 v[188:191], v193 offset:39936
	s_add_u32 s44, s34, 0x8000
	s_addc_u32 s45, s35, 0
	s_mov_b32 m0, s54
	s_nop 0
	global_load_lds_dwordx4 v192, s[44:45] sc1
	s_waitcnt lgkmcnt(6)
	v_mfma_f32_32x32x16_f16 v[96:111], a[192:195], v[160:163], v[96:111]
	ds_read_b128 v[160:163], v193 offset:40960
	v_mfma_f32_32x32x16_f16 v[112:127], a[192:195], v[164:167], v[112:127]
	ds_read_b128 v[164:167], v193 offset:41984
	s_waitcnt lgkmcnt(6)
	v_mfma_f32_32x32x16_f16 v[96:111], a[196:199], v[168:171], v[96:111]
	ds_read_b128 v[168:171], v193 offset:43008
	v_mfma_f32_32x32x16_f16 v[112:127], a[196:199], v[172:175], v[112:127]
	ds_read_b128 v[172:175], v193 offset:44032
	global_load_lds_dwordx4 v192, s[44:45] offset:1024 sc1
	s_waitcnt lgkmcnt(6)
	v_mfma_f32_32x32x16_f16 v[96:111], a[200:203], v[176:179], v[96:111]
	ds_read_b128 v[176:179], v193 offset:45056
	v_mfma_f32_32x32x16_f16 v[112:127], a[200:203], v[180:183], v[112:127]
	ds_read_b128 v[180:183], v193 offset:46080
	s_waitcnt lgkmcnt(6)
	v_mfma_f32_32x32x16_f16 v[96:111], a[204:207], v[184:187], v[96:111]
	ds_read_b128 v[184:187], v193 offset:47104
	v_mfma_f32_32x32x16_f16 v[112:127], a[204:207], v[188:191], v[112:127]
	ds_read_b128 v[188:191], v193 offset:48128
	global_load_lds_dwordx4 v192, s[44:45] offset:2048 sc1
	s_waitcnt vmcnt(4)
	s_barrier
	v_mov_b32_e32 v199, 3
	s_cmp_eq_u32 s31, 0
	s_cbranch_scc1 .LD_slow42
	global_store_dword v197, v199, s[40:41]
	s_branch .LD_join43

.LD_join43:
	ds_read_b64 v[200:201], v249 offset:1024
	ds_read_b64 v[202:203], v249 offset:3072
	ds_read_b64 v[204:205], v249 offset:5120
	ds_read_b64 v[206:207], v249 offset:7168
	s_waitcnt lgkmcnt(10)
	v_mfma_f32_32x32x16_f16 v[96:111], a[208:211], v[160:163], v[96:111]
	ds_read_b128 v[160:163], v193 offset:49152
	v_mfma_f32_32x32x16_f16 v[112:127], a[208:211], v[164:167], v[112:127]
	ds_read_b128 v[164:167], v193 offset:50176
	s_waitcnt lgkmcnt(10)
	v_mfma_f32_32x32x16_f16 v[96:111], a[212:215], v[168:171], v[96:111]
	ds_read_b128 v[168:171], v193 offset:51200
	v_mfma_f32_32x32x16_f16 v[112:127], a[212:215], v[172:175], v[112:127]
	ds_read_b128 v[172:175], v193 offset:52224
	global_load_lds_dwordx4 v192, s[44:45] offset:3072 sc1
	s_waitcnt lgkmcnt(10)
	v_mfma_f32_32x32x16_f16 v[96:111], a[216:219], v[176:179], v[96:111]
	ds_read_b128 v[176:179], v193 offset:53248
	v_mfma_f32_32x32x16_f16 v[112:127], a[216:219], v[180:183], v[112:127]
	ds_read_b128 v[180:183], v193 offset:54272
	s_waitcnt lgkmcnt(10)
	v_mfma_f32_32x32x16_f16 v[96:111], a[220:223], v[184:187], v[96:111]
	ds_read_b128 v[184:187], v193 offset:55296
	v_mfma_f32_32x32x16_f16 v[112:127], a[220:223], v[188:191], v[112:127]
	ds_read_b128 v[188:191], v193 offset:56320
	s_add_u32 s44, s34, 0x9000
	s_addc_u32 s45, s35, 0
	s_mov_b32 m0, s55
	s_nop 0
	global_load_lds_dwordx4 v192, s[44:45] sc1
	s_waitcnt lgkmcnt(6)
	v_mfma_f32_32x32x16_f16 v[96:111], a[224:227], v[160:163], v[96:111]
	ds_read_b128 v[160:163], v193 offset:57344
	v_mfma_f32_32x32x16_f16 v[112:127], a[224:227], v[164:167], v[112:127]
	ds_read_b128 v[164:167], v193 offset:58368
	s_waitcnt lgkmcnt(6)
	v_mfma_f32_32x32x16_f16 v[96:111], a[228:231], v[168:171], v[96:111]
	ds_read_b128 v[168:171], v193 offset:59392
	v_mfma_f32_32x32x16_f16 v[112:127], a[228:231], v[172:175], v[112:127]
	ds_read_b128 v[172:175], v193 offset:60416
	global_load_lds_dwordx4 v192, s[44:45] offset:1024 sc1
	v_add_f32_e32 v200, v200, v202
	v_add_f32_e32 v201, v201, v203
	v_add_f32_e32 v200, v200, v204
	v_add_f32_e32 v201, v201, v205
	v_add_f32_e32 v200, v200, v206
	v_add_f32_e32 v201, v201, v207
	global_store_dwordx2 v250, v[200:201], s[72:73]
	s_waitcnt lgkmcnt(6)
	v_mfma_f32_32x32x16_f16 v[96:111], a[232:235], v[176:179], v[96:111]
	ds_read_b128 v[176:179], v193 offset:61440
	v_mfma_f32_32x32x16_f16 v[112:127], a[232:235], v[180:183], v[112:127]
	ds_read_b128 v[180:183], v193 offset:62464
	s_waitcnt lgkmcnt(6)
	v_mfma_f32_32x32x16_f16 v[96:111], a[236:239], v[184:187], v[96:111]
	ds_read_b128 v[184:187], v193 offset:63488
	v_mfma_f32_32x32x16_f16 v[112:127], a[236:239], v[188:191], v[112:127]
	ds_read_b128 v[188:191], v193 offset:64512
	global_load_lds_dwordx4 v192, s[44:45] offset:2048 sc1
	s_waitcnt vmcnt(9)
	s_barrier
	s_waitcnt lgkmcnt(6)
	v_mfma_f32_32x32x16_f16 v[96:111], a[240:243], v[160:163], v[96:111]
	ds_read_b128 v[160:163], v192 offset:0
	v_mfma_f32_32x32x16_f16 v[112:127], a[240:243], v[164:167], v[112:127]
	ds_read_b128 v[164:167], v192 offset:1024
	s_waitcnt lgkmcnt(6)
	v_mfma_f32_32x32x16_f16 v[96:111], a[244:247], v[168:171], v[96:111]
	ds_read_b128 v[168:171], v192 offset:2048
	v_mfma_f32_32x32x16_f16 v[112:127], a[244:247], v[172:175], v[112:127]
	ds_read_b128 v[172:175], v192 offset:3072
	global_load_lds_dwordx4 v192, s[44:45] offset:3072 sc1
	s_waitcnt lgkmcnt(6)
	v_mfma_f32_32x32x16_f16 v[96:111], a[248:251], v[176:179], v[96:111]
	ds_read_b128 v[176:179], v192 offset:4096
	v_mfma_f32_32x32x16_f16 v[112:127], a[248:251], v[180:183], v[112:127]
	ds_read_b128 v[180:183], v192 offset:5120
	s_waitcnt lgkmcnt(6)
	v_mfma_f32_32x32x16_f16 v[96:111], a[252:255], v[184:187], v[96:111]
	ds_read_b128 v[184:187], v192 offset:6144
	v_mfma_f32_32x32x16_f16 v[112:127], a[252:255], v[188:191], v[112:127]
	ds_read_b128 v[188:191], v192 offset:7168
	s_add_u32 s44, s34, 0x10000
	s_addc_u32 s45, s35, 0
	s_mov_b32 m0, s56
	s_nop 0
	global_load_lds_dwordx4 v192, s[44:45] sc1
	s_add_u32 s33, s33, 1
	s_cmp_lt_u32 s33, s28
	s_cbranch_scc1 .LD_loop16
.LD_end17:
	s_nop 15
	s_nop 3
	s_sub_u32 s71, s33, 1
	s_and_b32 s64, s71, 1
	s_lshl_b32 s64, s64, 22
	s_add_u32 s64, s64, s50
	s_add_u32 s64, s64, 0x60000
	s_add_u32 s36, s6, s64
	s_addc_u32 s37, s7, 0
	s_lshl_b32 s64, s71, 3
	s_add_u32 s64, s64, s29
	s_lshl_b32 s64, s64, 5
	s_add_u32 s64, s64, s30
	s_lshl_b32 s64, s64, 2
	s_add_u32 s40, s8, s64
	s_addc_u32 s41, s9, 0
	s_lshl_b32 s64, s71, 19
	s_add_u32 s64, s64, 0x600
	s_add_u32 s72, s62, s64
	s_addc_u32 s73, s63, 0
	v_exp_f32_e32 v200, v96
	v_exp_f32_e32 v201, v97
	v_exp_f32_e32 v202, v98
	v_exp_f32_e32 v203, v99
	v_exp_f32_e32 v204, v100
	v_exp_f32_e32 v205, v101
	v_exp_f32_e32 v206, v102
	v_exp_f32_e32 v207, v103
	v_exp_f32_e32 v208, v104
	v_exp_f32_e32 v209, v105
	v_exp_f32_e32 v210, v106
	v_exp_f32_e32 v211, v107
	v_exp_f32_e32 v212, v108
	v_exp_f32_e32 v213, v109
	v_exp_f32_e32 v214, v110
	v_exp_f32_e32 v215, v111
	v_add_f32_e32 v200, 1.0, v200
	v_add_f32_e32 v201, 1.0, v201
	v_add_f32_e32 v202, 1.0, v202
	v_add_f32_e32 v203, 1.0, v203
	v_add_f32_e32 v204, 1.0, v204
	v_add_f32_e32 v205, 1.0, v205
	v_add_f32_e32 v206, 1.0, v206
	v_add_f32_e32 v207, 1.0, v207
	v_add_f32_e32 v208, 1.0, v208
	v_add_f32_e32 v209, 1.0, v209
	v_add_f32_e32 v210, 1.0, v210
	v_add_f32_e32 v211, 1.0, v211
	v_add_f32_e32 v212, 1.0, v212
	v_add_f32_e32 v213, 1.0, v213
	v_add_f32_e32 v214, 1.0, v214
	v_add_f32_e32 v215, 1.0, v215
	v_rcp_f32_e32 v200, v200
	v_rcp_f32_e32 v201, v201
	v_rcp_f32_e32 v202, v202
	v_rcp_f32_e32 v203, v203
	v_rcp_f32_e32 v204, v204
	v_rcp_f32_e32 v205, v205
	v_rcp_f32_e32 v206, v206
	v_rcp_f32_e32 v207, v207
	v_rcp_f32_e32 v208, v208
	v_rcp_f32_e32 v209, v209
	v_rcp_f32_e32 v210, v210
	v_rcp_f32_e32 v211, v211
	v_rcp_f32_e32 v212, v212
	v_rcp_f32_e32 v213, v213
	v_rcp_f32_e32 v214, v214
	v_rcp_f32_e32 v215, v215
	v_fmamk_f32 v208, v208, 0xc0b8aa3b, v198
	v_fmamk_f32 v209, v209, 0xc0b8aa3b, v198
	v_fmamk_f32 v210, v210, 0xc0b8aa3b, v198
	v_fmamk_f32 v211, v211, 0xc0b8aa3b, v198
	v_mul_f32_e32 v204, v204, v152
	v_mul_f32_e32 v205, v205, v153
	v_mul_f32_e32 v206, v206, v154
	v_mul_f32_e32 v207, v207, v155
	v_fma_f32 v152, v200, v208, v204
	v_fma_f32 v153, v201, v209, v205
	v_fma_f32 v154, v202, v210, v206
	v_fma_f32 v155, v203, v211, v207
	v_exp_f32_e32 v200, v152
	v_exp_f32_e32 v201, v153
	v_exp_f32_e32 v202, v154
	v_exp_f32_e32 v203, v155
	v_add_f32_e32 v200, 1.0, v200
	v_add_f32_e32 v201, 1.0, v201
	v_add_f32_e32 v202, 1.0, v202
	v_add_f32_e32 v203, 1.0, v203
	v_rcp_f32_e32 v200, v200
	v_rcp_f32_e32 v201, v201
	v_rcp_f32_e32 v202, v202
	v_rcp_f32_e32 v203, v203
	v_fma_f32 v200, v200, 2.0, -1.0
	v_fma_f32 v201, v201, 2.0, -1.0
	v_fma_f32 v202, v202, 2.0, -1.0
	v_fma_f32 v203, v203, 2.0, -1.0
	v_mul_f32_e32 v216, v212, v200
	v_mul_f32_e32 v217, v213, v201
	v_mul_f32_e32 v218, v214, v202
	v_mul_f32_e32 v219, v215, v203
	v_mul_f32_e32 v236, v216, v228
	v_mul_f32_e32 v237, v216, v232
	v_fmac_f32_e32 v236, v217, v229
	v_fmac_f32_e32 v237, v217, v233
	v_fmac_f32_e32 v236, v218, v230
	v_fmac_f32_e32 v237, v218, v234
	v_fmac_f32_e32 v236, v219, v231
	v_fmac_f32_e32 v237, v219, v235
	v_mov_b32_e32 v238, v236
	v_mov_b32_e32 v239, v236
	v_mov_b32_e32 v240, v237
	v_mov_b32_e32 v241, v237
	s_nop 1
	v_permlane32_swap_b32_e32 v238, v239
	v_permlane32_swap_b32_e32 v240, v241
	v_add_f32_e32 v238, v238, v239
	v_add_f32_e32 v239, v240, v241
	ds_write_b64 v248, v[238:239] offset:1536
	v_cvt_pk_f16_f32 v220, v216, v217
	v_cvt_pk_f16_f32 v221, v218, v219
	v_exp_f32_e32 v200, v112
	v_exp_f32_e32 v201, v113
	v_exp_f32_e32 v202, v114
	v_exp_f32_e32 v203, v115
	v_exp_f32_e32 v204, v116
	v_exp_f32_e32 v205, v117
	v_exp_f32_e32 v206, v118
	v_exp_f32_e32 v207, v119
	v_exp_f32_e32 v208, v120
	v_exp_f32_e32 v209, v121
	v_exp_f32_e32 v210, v122
	v_exp_f32_e32 v211, v123
	v_exp_f32_e32 v212, v124
	v_exp_f32_e32 v213, v125
	v_exp_f32_e32 v214, v126
	v_exp_f32_e32 v215, v127
	v_add_f32_e32 v200, 1.0, v200
	v_add_f32_e32 v201, 1.0, v201
	v_add_f32_e32 v202, 1.0, v202
	v_add_f32_e32 v203, 1.0, v203
	v_add_f32_e32 v204, 1.0, v204
	v_add_f32_e32 v205, 1.0, v205
	v_add_f32_e32 v206, 1.0, v206
	v_add_f32_e32 v207, 1.0, v207
	v_add_f32_e32 v208, 1.0, v208
	v_add_f32_e32 v209, 1.0, v209
	v_add_f32_e32 v210, 1.0, v210
	v_add_f32_e32 v211, 1.0, v211
	v_add_f32_e32 v212, 1.0, v212
	v_add_f32_e32 v213, 1.0, v213
	v_add_f32_e32 v214, 1.0, v214
	v_add_f32_e32 v215, 1.0, v215
	v_rcp_f32_e32 v200, v200
	v_rcp_f32_e32 v201, v201
	v_rcp_f32_e32 v202, v202
	v_rcp_f32_e32 v203, v203
	v_rcp_f32_e32 v204, v204
	v_rcp_f32_e32 v205, v205
	v_rcp_f32_e32 v206, v206
	v_rcp_f32_e32 v207, v207
	v_rcp_f32_e32 v208, v208
	v_rcp_f32_e32 v209, v209
	v_rcp_f32_e32 v210, v210
	v_rcp_f32_e32 v211, v211
	v_rcp_f32_e32 v212, v212
	v_rcp_f32_e32 v213, v213
	v_rcp_f32_e32 v214, v214
	v_rcp_f32_e32 v215, v215
	v_fmamk_f32 v208, v208, 0xc0b8aa3b, v198
	v_fmamk_f32 v209, v209, 0xc0b8aa3b, v198
	v_fmamk_f32 v210, v210, 0xc0b8aa3b, v198
	v_fmamk_f32 v211, v211, 0xc0b8aa3b, v198
	v_mul_f32_e32 v204, v204, v156
	v_mul_f32_e32 v205, v205, v157
	v_mul_f32_e32 v206, v206, v158
	v_mul_f32_e32 v207, v207, v159
	v_fma_f32 v156, v200, v208, v204
	v_fma_f32 v157, v201, v209, v205
	v_fma_f32 v158, v202, v210, v206
	v_fma_f32 v159, v203, v211, v207
	v_exp_f32_e32 v200, v156
	v_exp_f32_e32 v201, v157
	v_exp_f32_e32 v202, v158
	v_exp_f32_e32 v203, v159
	v_add_f32_e32 v200, 1.0, v200
	v_add_f32_e32 v201, 1.0, v201
	v_add_f32_e32 v202, 1.0, v202
	v_add_f32_e32 v203, 1.0, v203
	v_rcp_f32_e32 v200, v200
	v_rcp_f32_e32 v201, v201
	v_rcp_f32_e32 v202, v202
	v_rcp_f32_e32 v203, v203
	v_fma_f32 v200, v200, 2.0, -1.0
	v_fma_f32 v201, v201, 2.0, -1.0
	v_fma_f32 v202, v202, 2.0, -1.0
	v_fma_f32 v203, v203, 2.0, -1.0
	v_mul_f32_e32 v216, v212, v200
	v_mul_f32_e32 v217, v213, v201
	v_mul_f32_e32 v218, v214, v202
	v_mul_f32_e32 v219, v215, v203
	v_mul_f32_e32 v236, v216, v228
	v_mul_f32_e32 v237, v216, v232
	v_fmac_f32_e32 v236, v217, v229
	v_fmac_f32_e32 v237, v217, v233
	v_fmac_f32_e32 v236, v218, v230
	v_fmac_f32_e32 v237, v218, v234
	v_fmac_f32_e32 v236, v219, v231
	v_fmac_f32_e32 v237, v219, v235
	v_mov_b32_e32 v238, v236
	v_mov_b32_e32 v239, v236
	v_mov_b32_e32 v240, v237
	v_mov_b32_e32 v241, v237
	s_nop 1
	v_permlane32_swap_b32_e32 v238, v239
	v_permlane32_swap_b32_e32 v240, v241
	v_add_f32_e32 v238, v238, v239
	v_add_f32_e32 v239, v240, v241
	ds_write_b64 v248, v[238:239] offset:1792
	v_cvt_pk_f16_f32 v222, v216, v217
	v_cvt_pk_f16_f32 v223, v218, v219
	s_nop 1
	v_permlane32_swap_b32_e32 v220, v222
	v_permlane32_swap_b32_e32 v221, v223
	s_cmp_eq_u32 s31, 0
	s_cbranch_scc1 .LD_slow44
	global_store_dwordx4 v195, v[220:223], s[36:37] offset:0
	s_branch .LD_join45

.LD_join45:
	s_waitcnt vmcnt(0)
	s_waitcnt lgkmcnt(0)
	s_barrier
	v_mov_b32_e32 v199, 4
	s_cmp_eq_u32 s31, 0
	s_cbranch_scc1 .LD_slow46
	global_store_dword v197, v199, s[40:41]
	s_branch .LD_join47

.LD_join47:
	ds_read_b64 v[200:201], v249 offset:1536
	ds_read_b64 v[202:203], v249 offset:3584
	ds_read_b64 v[204:205], v249 offset:5632
	ds_read_b64 v[206:207], v249 offset:7680
	s_waitcnt lgkmcnt(0)
	v_add_f32_e32 v200, v200, v202
	v_add_f32_e32 v201, v201, v203
	v_add_f32_e32 v200, v200, v204
	v_add_f32_e32 v201, v201, v205
	v_add_f32_e32 v200, v200, v206
	v_add_f32_e32 v201, v201, v207
	global_store_dwordx2 v250, v[200:201], s[72:73]
	s_waitcnt vmcnt(0) lgkmcnt(0)
	s_endpgm
	.p2align 8
